# v12 plus 4x-pipelined x->bf16/e4m3 conversion loop in the prologue phase (4 loads in flight per thread instead of 1)
# baseline (speedup 1.0000x reference)
; #define LAS __attribute__((address_space(3)))
; DI int tidx() { const int w = __builtin_amdgcn_readfirstlane(((volatile LAS int*)(131072 + 3072))[hw_wave_slot()]); int ln; asm volatile("v_mbcnt_lo_u32_b32 %0, -1, 0\n\tv_mbcnt_hi_u32_b32 %0, -1, %0" : "=v"(ln)); return (w << 6) + ln; }
; __device__ __forceinline__ unsigned xb_add(unsigned* p, unsigned v) { return __hip_atomic_fetch_add(p, v, __ATOMIC_RELAXED, __HIP_MEMORY_SCOPE_AGENT); }
; __device__ __forceinline__ unsigned xb_xcc_id() { return (unsigned)__builtin_amdgcn_s_getreg((3 << 11) | 20) & 0xFu; }
; DI KArgP kargs() { KArgP p = (KArgP)__builtin_amdgcn_kernarg_segment_ptr(); asm volatile("" : "+s"(p)); return p; }
; __device__ __forceinline__ XcdBarrier xcd_barrier_post(unsigned* bar, volatile LAS unsigned* st) {
;     XcdBarrier b; b.bar = bar; b.x = xb_xcc_id(); b.st = st;
;     if (tidx() == 0) (void)xb_add(&bar[XB_XCNT(b.x)], 1u);
;     return b;
; __global__ void __launch_bounds__(512, 2) mk_fwd(FArgs args) {
;     ...
;     __syncthreads();
;     XcdBarrier bar = xcd_barrier_post(ctl + CW_BAR + kargs()->li * XCD_BAR_WORDS, MISC + 8);
.LBB0_12:
	s_or_b64 exec, exec, s[6:7]
	s_mov_b64 s[6:7], s[0:1]
	s_waitcnt lgkmcnt(0)
	s_barrier
	s_getreg_b32 s99, hwreg(HW_REG_HW_ID, 0, 6)
	s_and_b32 s99, s99, 63
	s_lshl_b32 s99, s99, 2
	s_or_b32 s99, s99, 0x20c00
	v_mov_b32_e32 v255, s99
	ds_read_b32 v255, v255
	s_waitcnt lgkmcnt(0)
	v_readfirstlane_b32 s99, v255
	s_nop 3
	s_cmp_lt_u32 s99, 4
	s_cselect_b32 s99, 1, 0
	v_mov_b32_e32 v255, 0x20000
	s_mov_b32 s98, 0
	s_load_dword s3, s[6:7], 0xc0
	s_getreg_b32 s8, hwreg(HW_REG_XCC_ID, 0, 4)
	s_waitcnt lgkmcnt(0)
	s_mul_i32 s6, s3, 0xd80
	s_ashr_i32 s7, s6, 31
	s_lshl_b64 s[6:7], s[6:7], 2
	s_add_u32 s3, s4, s6
	s_addc_u32 s6, s5, s7
	s_add_u32 s30, s3, 0x4000
	s_getreg_b32 s3, hwreg(HW_REG_HW_ID, 0, 6)
	s_addc_u32 s31, s6, 0
	s_and_b32 s3, s3, 63
	s_lshl_b32 s3, s3, 2
	s_or_b32 s3, s3, 0x20c00
	v_mov_b32_e32 v0, s3
	ds_read_b32 v0, v0
	v_mbcnt_lo_u32_b32 v1, -1, 0
	v_mbcnt_hi_u32_b32 v1, -1, v1
	s_and_b32 s33, s8, 15
	s_waitcnt lgkmcnt(0)
	v_readfirstlane_b32 s3, v0
	s_lshl_b32 s3, s3, 6
	v_sub_u32_e32 v0, 0, v1
	v_cmp_eq_u32_e32 vcc, s3, v0
	s_and_saveexec_b64 s[6:7], vcc
	s_cbranch_execz .LBB0_15
	s_mov_b64 s[8:9], exec
	v_mbcnt_lo_u32_b32 v0, s8, 0
	v_mbcnt_hi_u32_b32 v0, s9, v0
	v_cmp_eq_u32_e32 vcc, 0, v0
	s_and_b64 s[10:11], exec, vcc
	s_mov_b64 exec, s[10:11]
	s_cbranch_execz .LBB0_15
	s_lshl_b32 s3, s33, 8
	s_bcnt1_i32_b64 s8, s[8:9]
	v_mov_b32_e32 v0, s3
	v_mov_b32_e32 v1, s8
	global_atomic_add v0, v1, s[30:31] offset:1024

; #define PG8_STAGE(bufoff, gbase, voff) do { _Pragma("unroll") for (int _i = 0; _i < 2; ++_i) { unsigned keep_; \
;         asm volatile("s_mov_b32 %0, m0\n\ts_mov_b32 m0, %3\n\ts_nop 0\n\tglobal_load_lds_dwordx4 %1, %2\n\ts_mov_b32 m0, %0" : "=&s"(keep_) : "v"((voff)[_i]), "s"((const char*)(gbase)), "s"(ldsbase + (unsigned)((bufoff) + _i * 8192)) : "memory"); } } while (0)
; #define PG8_WAIT_V(n) asm volatile("s_waitcnt vmcnt(" #n ")" ::: "memory")
; #define PG8_WAIT_L(n) asm volatile("s_waitcnt lgkmcnt(" #n ")" ::: "memory")
; #define PG8_BAR __builtin_amdgcn_s_barrier()
; #define PG8_SCHED __builtin_amdgcn_sched_barrier(0)
;     DI int nt(const Unit& u) const { return (u.aux & 8) ? PLED / 64 : ((u.aux & 4) ? (D_ / 2) / 64 : D_ / 64); }
; template <class Epi, class Sched, bool ALIGN_EPI, bool FP8 = false>
; DI void gemm_phase(LAS unsigned char* lds, const Gemm g, const Sched& S, const Epi& E) {
;     ...
;         for (int t = 0; t < nt; t += 2) {
;             if constexpr (Epi::MID) { if (t == (nt >> 1)) E.mid(acc, cur, wr, wc, fr, fq); }
;             const bool last = (t == nt - 2);
;             const char* a1 = cA + (size_t)(t + 1) * kstep;
;             const char* a2 = last ? nA : cA + (size_t)(t + 2) * kstep; const char* b2 = last ? nB : cB + (size_t)(t + 2) * kstep;
;             const char* a3 = a2 + kstep; const char* b3 = b2 + kstep;
;             PG8_LDB(B0, 0, 0); PG8_LDB(B1, 0, 1); PG8_SCHED; PG8_LDA(At, 0, 0); PG8_STAGE(PG8_SA(1, 1), a1 + hstepA, voffA);
;             PG8_WAIT_V(8); PG8_WAIT_L(0); PG8_BAR; PG8_MMA(0, 0, At, B0); PG8_MMA(0, 1, At, B1); PG8_BAR; PG8_SCHED;
;             PG8_LDA(At, 0, 1); PG8_STAGE(PG8_SB(0, 0), b2, voffB); PG8_STAGE(PG8_SB(0, 1), b2 + hstepB, voffB); PG8_STAGE(PG8_SA(0, 0), a2, voffA);
;             PG8_WAIT_V(8); PG8_WAIT_L(0); PG8_BAR; PG8_MMA(1, 0, At, B0); PG8_MMA(1, 1, At, B1); PG8_BAR; PG8_SCHED;
;             PG8_LDB(B0, 1, 0); PG8_LDB(B1, 1, 1); PG8_SCHED; PG8_LDA(At, 1, 0); PG8_STAGE(PG8_SA(0, 1), a2 + hstepA, voffA);
;             PG8_WAIT_V(8); PG8_WAIT_L(0); PG8_BAR; PG8_MMA(0, 0, At, B0); PG8_MMA(0, 1, At, B1); PG8_BAR; PG8_SCHED;
.LBB0_255:
	s_cmp_lg_u32 s99, 0
	s_cbranch_scc1 .Lmy_g0_255
	s_add_i32 s53, s51, 2
	s_add_u32 s42, s18, s56
	s_addc_u32 s43, s19, s57
	s_add_u32 s58, s42, 0x100
	v_add_u32_e32 v130, 0x10000, v157
	s_addc_u32 s59, s43, 0
	ds_read_b128 v[146:149], v130
	ds_read_b128 v[150:153], v130 offset:1024
	ds_read_b128 v[160:163], v130 offset:2048
	ds_read_b128 v[164:167], v130 offset:3072
	v_add_u32_e32 v130, 0x14000, v157
	s_add_u32 s60, s22, s56
	ds_read_b128 v[168:171], v130
	ds_read_b128 v[172:175], v130 offset:1024
	ds_read_b128 v[176:179], v130 offset:2048
	ds_read_b128 v[180:183], v130 offset:3072
	s_addc_u32 s61, s23, s57
	s_add_u32 s60, s60, 0x100
	s_addc_u32 s61, s61, 0
	s_cmp_eq_u32 s20, s51
	s_cselect_b32 s62, s8, s58
	s_cselect_b32 s63, s9, s59
	s_cselect_b32 s60, s54, s60
	s_cselect_b32 s61, s55, s61
	s_add_u32 s58, s62, 0x80
	s_addc_u32 s59, s63, 0
	ds_read_b128 v[184:187], v158
	ds_read_b128 v[188:191], v158 offset:1024
	ds_read_b128 v[192:195], v158 offset:2048
	ds_read_b128 v[196:199], v158 offset:3072
	ds_read_b128 v[200:203], v158 offset:4096
	ds_read_b128 v[204:207], v158 offset:5120
	ds_read_b128 v[208:211], v158 offset:6144
	ds_read_b128 v[212:215], v158 offset:7168
	s_add_u32 s42, s42, 0x80080
	s_addc_u32 s43, s43, 0
	s_mov_b32 s51, m0
	s_mov_b32 m0, s89
	s_nop 0
	global_load_lds_dwordx4 v129, s[42:43]
	s_mov_b32 m0, s51
	s_nop 0
	s_mov_b32 s51, m0
	s_mov_b32 m0, s90
	s_nop 0
	global_load_lds_dwordx4 v154, s[42:43]
	s_mov_b32 m0, s51
	s_waitcnt vmcnt(8)
	s_waitcnt lgkmcnt(0)
	s_mov_b64 exec, 1
	ds_add_u32 v255, v255 offset:4096
	s_mov_b64 exec, -1
	s_setprio 1
	v_mfma_f32_16x16x32_bf16 v[124:127], v[146:149], v[184:187], v[124:127]
	v_mfma_f32_16x16x32_bf16 v[120:123], v[160:163], v[184:187], v[120:123]
	v_mfma_f32_16x16x32_bf16 v[116:119], v[146:149], v[192:195], v[116:119]
	v_mfma_f32_16x16x32_bf16 v[112:115], v[160:163], v[192:195], v[112:115]
	v_mfma_f32_16x16x32_bf16 v[108:111], v[146:149], v[200:203], v[108:111]
	v_mfma_f32_16x16x32_bf16 v[104:107], v[160:163], v[200:203], v[104:107]
	v_mfma_f32_16x16x32_bf16 v[100:103], v[146:149], v[208:211], v[100:103]
	v_mfma_f32_16x16x32_bf16 v[96:99], v[160:163], v[208:211], v[96:99]
	v_mfma_f32_16x16x32_bf16 v[124:127], v[150:153], v[188:191], v[124:127]
	v_mfma_f32_16x16x32_bf16 v[120:123], v[164:167], v[188:191], v[120:123]
	v_mfma_f32_16x16x32_bf16 v[116:119], v[150:153], v[196:199], v[116:119]
	v_mfma_f32_16x16x32_bf16 v[112:115], v[164:167], v[196:199], v[112:115]
	v_mfma_f32_16x16x32_bf16 v[108:111], v[150:153], v[204:207], v[108:111]
	v_mfma_f32_16x16x32_bf16 v[104:107], v[164:167], v[204:207], v[104:107]
	v_mfma_f32_16x16x32_bf16 v[100:103], v[150:153], v[212:215], v[100:103]
	v_mfma_f32_16x16x32_bf16 v[96:99], v[164:167], v[212:215], v[96:99]
	v_mfma_f32_16x16x32_bf16 v[92:95], v[168:171], v[184:187], v[92:95]
	v_mfma_f32_16x16x32_bf16 v[88:91], v[176:179], v[184:187], v[88:91]
	v_mfma_f32_16x16x32_bf16 v[84:87], v[168:171], v[192:195], v[84:87]
	v_mfma_f32_16x16x32_bf16 v[80:83], v[176:179], v[192:195], v[80:83]
	v_mfma_f32_16x16x32_bf16 v[76:79], v[168:171], v[200:203], v[76:79]
	v_mfma_f32_16x16x32_bf16 v[72:75], v[176:179], v[200:203], v[72:75]
	v_mfma_f32_16x16x32_bf16 v[68:71], v[168:171], v[208:211], v[68:71]
	v_mfma_f32_16x16x32_bf16 v[64:67], v[176:179], v[208:211], v[64:67]
	v_mfma_f32_16x16x32_bf16 v[92:95], v[172:175], v[188:191], v[92:95]
	v_mfma_f32_16x16x32_bf16 v[88:91], v[180:183], v[188:191], v[88:91]
	v_mfma_f32_16x16x32_bf16 v[84:87], v[172:175], v[196:199], v[84:87]
	v_mfma_f32_16x16x32_bf16 v[80:83], v[180:183], v[196:199], v[80:83]
	v_mfma_f32_16x16x32_bf16 v[76:79], v[172:175], v[204:207], v[76:79]
	v_mfma_f32_16x16x32_bf16 v[72:75], v[180:183], v[204:207], v[72:75]
	v_mfma_f32_16x16x32_bf16 v[68:71], v[172:175], v[212:215], v[68:71]
	v_mfma_f32_16x16x32_bf16 v[64:67], v[180:183], v[212:215], v[64:67]
	s_setprio 0
	s_barrier
	ds_read_b128 v[184:187], v158 offset:16384
	ds_read_b128 v[188:191], v158 offset:17408
	ds_read_b128 v[192:195], v158 offset:18432
	ds_read_b128 v[196:199], v158 offset:19456
	ds_read_b128 v[200:203], v158 offset:20480
	ds_read_b128 v[204:207], v158 offset:21504
	ds_read_b128 v[208:211], v158 offset:22528
	ds_read_b128 v[212:215], v158 offset:23552
	s_mov_b32 s42, m0
	s_mov_b32 m0, s17
	s_nop 0
	global_load_lds_dwordx4 v145, s[60:61]
	s_mov_b32 m0, s42
	s_nop 0
	s_mov_b32 s42, m0
	s_mov_b32 m0, s68
	s_nop 0
	global_load_lds_dwordx4 v155, s[60:61]
	s_mov_b32 m0, s42
	s_add_u32 s42, s60, 0x80000
	s_addc_u32 s43, s61, 0
	s_mov_b32 s51, m0
	s_mov_b32 m0, s69
	s_nop 0
	global_load_lds_dwordx4 v145, s[42:43]
	s_mov_b32 m0, s51
	s_nop 0
	s_mov_b32 s51, m0
	s_mov_b32 m0, s70
	s_nop 0
	global_load_lds_dwordx4 v155, s[42:43]
	s_mov_b32 m0, s51
	s_mov_b32 s42, m0
	s_mov_b32 m0, s15
	s_nop 0
	global_load_lds_dwordx4 v129, s[62:63]
	s_mov_b32 m0, s42
	s_nop 0
	s_mov_b32 s42, m0
	s_mov_b32 m0, s71
	s_nop 0
	global_load_lds_dwordx4 v154, s[62:63]
	s_mov_b32 m0, s42
	s_waitcnt vmcnt(8)
	s_waitcnt lgkmcnt(0)
; #define PG8_STAGE(bufoff, gbase, voff) do { _Pragma("unroll") for (int _i = 0; _i < 2; ++_i) { unsigned keep_; \
;         asm volatile("s_mov_b32 %0, m0\n\ts_mov_b32 m0, %3\n\ts_nop 0\n\tglobal_load_lds_dwordx4 %1, %2\n\ts_mov_b32 m0, %0" : "=&s"(keep_) : "v"((voff)[_i]), "s"((const char*)(gbase)), "s"(ldsbase + (unsigned)((bufoff) + _i * 8192)) : "memory"); } } while (0)
; #define PG8_WAIT_V(n) asm volatile("s_waitcnt vmcnt(" #n ")" ::: "memory")
; #define PG8_WAIT_L(n) asm volatile("s_waitcnt lgkmcnt(" #n ")" ::: "memory")
; #define PG8_BAR __builtin_amdgcn_s_barrier()
; #define PG8_SCHED __builtin_amdgcn_sched_barrier(0)
; template <class Epi, class Sched, bool ALIGN_EPI, bool FP8 = false>
; DI void gemm_phase(LAS unsigned char* lds, const Gemm g, const Sched& S, const Epi& E) {
;     ...
;             PG8_WAIT_V(8); PG8_WAIT_L(0); PG8_BAR; PG8_MMA(0, 0, At, B0); PG8_MMA(0, 1, At, B1); PG8_BAR; PG8_SCHED;
;             PG8_LDA(At, 0, 1); PG8_STAGE(PG8_SB(0, 0), b2, voffB); PG8_STAGE(PG8_SB(0, 1), b2 + hstepB, voffB); PG8_STAGE(PG8_SA(0, 0), a2, voffA);
;             PG8_WAIT_V(8); PG8_WAIT_L(0); PG8_BAR; PG8_MMA(1, 0, At, B0); PG8_MMA(1, 1, At, B1); PG8_BAR; PG8_SCHED;
;             PG8_LDB(B0, 1, 0); PG8_LDB(B1, 1, 1); PG8_SCHED; PG8_LDA(At, 1, 0); PG8_STAGE(PG8_SA(0, 1), a2 + hstepA, voffA);
;             PG8_WAIT_V(8); PG8_WAIT_L(0); PG8_BAR; PG8_MMA(0, 0, At, B0); PG8_MMA(0, 1, At, B1); PG8_BAR; PG8_SCHED;
	s_mov_b64 exec, 1
	ds_add_u32 v255, v255 offset:4096
	s_mov_b64 exec, -1
	s_setprio 1
	v_mfma_f32_16x16x32_bf16 v[60:63], v[146:149], v[184:187], v[60:63]
	v_mfma_f32_16x16x32_bf16 v[56:59], v[160:163], v[184:187], v[56:59]
	v_mfma_f32_16x16x32_bf16 v[52:55], v[146:149], v[192:195], v[52:55]
	v_mfma_f32_16x16x32_bf16 v[48:51], v[160:163], v[192:195], v[48:51]
	v_mfma_f32_16x16x32_bf16 v[44:47], v[146:149], v[200:203], v[44:47]
	v_mfma_f32_16x16x32_bf16 v[40:43], v[160:163], v[200:203], v[40:43]
	v_mfma_f32_16x16x32_bf16 v[36:39], v[146:149], v[208:211], v[36:39]
	v_mfma_f32_16x16x32_bf16 v[32:35], v[160:163], v[208:211], v[32:35]
	v_mfma_f32_16x16x32_bf16 v[60:63], v[150:153], v[188:191], v[60:63]
	v_mfma_f32_16x16x32_bf16 v[56:59], v[164:167], v[188:191], v[56:59]
	v_mfma_f32_16x16x32_bf16 v[52:55], v[150:153], v[196:199], v[52:55]
	v_mfma_f32_16x16x32_bf16 v[48:51], v[164:167], v[196:199], v[48:51]
	v_mfma_f32_16x16x32_bf16 v[44:47], v[150:153], v[204:207], v[44:47]
	v_mfma_f32_16x16x32_bf16 v[40:43], v[164:167], v[204:207], v[40:43]
	v_mfma_f32_16x16x32_bf16 v[36:39], v[150:153], v[212:215], v[36:39]
	v_mfma_f32_16x16x32_bf16 v[32:35], v[164:167], v[212:215], v[32:35]
	v_mfma_f32_16x16x32_bf16 v[28:31], v[168:171], v[184:187], v[28:31]
	v_mfma_f32_16x16x32_bf16 v[24:27], v[176:179], v[184:187], v[24:27]
	v_mfma_f32_16x16x32_bf16 v[20:23], v[168:171], v[192:195], v[20:23]
	v_mfma_f32_16x16x32_bf16 v[16:19], v[176:179], v[192:195], v[16:19]
	v_mfma_f32_16x16x32_bf16 v[12:15], v[168:171], v[200:203], v[12:15]
	v_mfma_f32_16x16x32_bf16 v[8:11], v[176:179], v[200:203], v[8:11]
	v_mfma_f32_16x16x32_bf16 v[4:7], v[168:171], v[208:211], v[4:7]
	v_mfma_f32_16x16x32_bf16 v[0:3], v[176:179], v[208:211], v[0:3]
	v_mfma_f32_16x16x32_bf16 v[28:31], v[172:175], v[188:191], v[28:31]
	v_mfma_f32_16x16x32_bf16 v[24:27], v[180:183], v[188:191], v[24:27]
	v_mfma_f32_16x16x32_bf16 v[20:23], v[172:175], v[196:199], v[20:23]
	v_mfma_f32_16x16x32_bf16 v[16:19], v[180:183], v[196:199], v[16:19]
	v_mfma_f32_16x16x32_bf16 v[12:15], v[172:175], v[204:207], v[12:15]
	v_mfma_f32_16x16x32_bf16 v[8:11], v[180:183], v[204:207], v[8:11]
	v_mfma_f32_16x16x32_bf16 v[4:7], v[172:175], v[212:215], v[4:7]
	v_mfma_f32_16x16x32_bf16 v[0:3], v[180:183], v[212:215], v[0:3]
	s_setprio 0
	s_barrier
	v_add_u32_e32 v130, 0x18000, v157
	ds_read_b128 v[146:149], v130
	ds_read_b128 v[150:153], v130 offset:1024
	ds_read_b128 v[160:163], v130 offset:2048
	ds_read_b128 v[164:167], v130 offset:3072
	v_add_u32_e32 v130, 0x1c000, v157
	ds_read_b128 v[168:171], v130
	ds_read_b128 v[172:175], v130 offset:1024
	ds_read_b128 v[176:179], v130 offset:2048
	ds_read_b128 v[180:183], v130 offset:3072
	ds_read_b128 v[184:187], v158 offset:32768
	ds_read_b128 v[188:191], v158 offset:33792
	ds_read_b128 v[192:195], v158 offset:34816
	ds_read_b128 v[196:199], v158 offset:35840
	ds_read_b128 v[200:203], v158 offset:36864
	ds_read_b128 v[204:207], v158 offset:37888
	ds_read_b128 v[208:211], v158 offset:38912
	ds_read_b128 v[212:215], v158 offset:39936
	s_add_u32 s42, s62, 0x80000
	s_addc_u32 s43, s63, 0
	s_mov_b32 s51, m0
	s_mov_b32 m0, s72
	s_nop 0
	global_load_lds_dwordx4 v129, s[42:43]
	s_mov_b32 m0, s51
	s_nop 0
	s_mov_b32 s51, m0
	s_mov_b32 m0, s73
	s_nop 0
	global_load_lds_dwordx4 v154, s[42:43]
	s_mov_b32 m0, s51
	s_waitcnt vmcnt(8)
	s_waitcnt lgkmcnt(0)
	s_mov_b64 exec, 1
	ds_add_u32 v255, v255 offset:4096
	s_mov_b64 exec, -1
	s_setprio 1
	v_mfma_f32_16x16x32_bf16 v[124:127], v[146:149], v[184:187], v[124:127]
	v_mfma_f32_16x16x32_bf16 v[120:123], v[160:163], v[184:187], v[120:123]
	v_mfma_f32_16x16x32_bf16 v[116:119], v[146:149], v[192:195], v[116:119]
	v_mfma_f32_16x16x32_bf16 v[112:115], v[160:163], v[192:195], v[112:115]
	v_mfma_f32_16x16x32_bf16 v[108:111], v[146:149], v[200:203], v[108:111]
	v_mfma_f32_16x16x32_bf16 v[104:107], v[160:163], v[200:203], v[104:107]
	v_mfma_f32_16x16x32_bf16 v[100:103], v[146:149], v[208:211], v[100:103]
	v_mfma_f32_16x16x32_bf16 v[96:99], v[160:163], v[208:211], v[96:99]
	v_mfma_f32_16x16x32_bf16 v[124:127], v[150:153], v[188:191], v[124:127]
	v_mfma_f32_16x16x32_bf16 v[120:123], v[164:167], v[188:191], v[120:123]
	v_mfma_f32_16x16x32_bf16 v[116:119], v[150:153], v[196:199], v[116:119]
	v_mfma_f32_16x16x32_bf16 v[112:115], v[164:167], v[196:199], v[112:115]
	v_mfma_f32_16x16x32_bf16 v[108:111], v[150:153], v[204:207], v[108:111]
	v_mfma_f32_16x16x32_bf16 v[104:107], v[164:167], v[204:207], v[104:107]
	v_mfma_f32_16x16x32_bf16 v[100:103], v[150:153], v[212:215], v[100:103]
	v_mfma_f32_16x16x32_bf16 v[96:99], v[164:167], v[212:215], v[96:99]
	v_mfma_f32_16x16x32_bf16 v[92:95], v[168:171], v[184:187], v[92:95]
	v_mfma_f32_16x16x32_bf16 v[88:91], v[176:179], v[184:187], v[88:91]
	v_mfma_f32_16x16x32_bf16 v[84:87], v[168:171], v[192:195], v[84:87]
	v_mfma_f32_16x16x32_bf16 v[80:83], v[176:179], v[192:195], v[80:83]
	v_mfma_f32_16x16x32_bf16 v[76:79], v[168:171], v[200:203], v[76:79]
	v_mfma_f32_16x16x32_bf16 v[72:75], v[176:179], v[200:203], v[72:75]
	v_mfma_f32_16x16x32_bf16 v[68:71], v[168:171], v[208:211], v[68:71]
	v_mfma_f32_16x16x32_bf16 v[64:67], v[176:179], v[208:211], v[64:67]
	v_mfma_f32_16x16x32_bf16 v[92:95], v[172:175], v[188:191], v[92:95]
	v_mfma_f32_16x16x32_bf16 v[88:91], v[180:183], v[188:191], v[88:91]
	v_mfma_f32_16x16x32_bf16 v[84:87], v[172:175], v[196:199], v[84:87]
	v_mfma_f32_16x16x32_bf16 v[80:83], v[180:183], v[196:199], v[80:83]
	v_mfma_f32_16x16x32_bf16 v[76:79], v[172:175], v[204:207], v[76:79]
	v_mfma_f32_16x16x32_bf16 v[72:75], v[180:183], v[204:207], v[72:75]
	v_mfma_f32_16x16x32_bf16 v[68:71], v[172:175], v[212:215], v[68:71]
	v_mfma_f32_16x16x32_bf16 v[64:67], v[180:183], v[212:215], v[64:67]
	s_setprio 0
	s_barrier
; #define PG8_STAGE(bufoff, gbase, voff) do { _Pragma("unroll") for (int _i = 0; _i < 2; ++_i) { unsigned keep_; \
;         asm volatile("s_mov_b32 %0, m0\n\ts_mov_b32 m0, %3\n\ts_nop 0\n\tglobal_load_lds_dwordx4 %1, %2\n\ts_mov_b32 m0, %0" : "=&s"(keep_) : "v"((voff)[_i]), "s"((const char*)(gbase)), "s"(ldsbase + (unsigned)((bufoff) + _i * 8192)) : "memory"); } } while (0)
; #define PG8_WAIT_V(n) asm volatile("s_waitcnt vmcnt(" #n ")" ::: "memory")
; #define PG8_WAIT_L(n) asm volatile("s_waitcnt lgkmcnt(" #n ")" ::: "memory")
; #define PG8_BAR __builtin_amdgcn_s_barrier()
; #define PG8_SCHED __builtin_amdgcn_sched_barrier(0)
; template <class Epi, class Sched, bool ALIGN_EPI, bool FP8 = false>
; DI void gemm_phase(LAS unsigned char* lds, const Gemm g, const Sched& S, const Epi& E) {
;     ...
;             PG8_LDB(B0, 1, 0); PG8_LDB(B1, 1, 1); PG8_SCHED; PG8_LDA(At, 1, 0); PG8_STAGE(PG8_SA(0, 1), a2 + hstepA, voffA);
;             PG8_WAIT_V(8); PG8_WAIT_L(0); PG8_BAR; PG8_MMA(0, 0, At, B0); PG8_MMA(0, 1, At, B1); PG8_BAR; PG8_SCHED;
;             PG8_LDA(At, 1, 1); PG8_STAGE(PG8_SB(1, 0), b3, voffB); PG8_STAGE(PG8_SB(1, 1), b3 + hstepB, voffB); PG8_STAGE(PG8_SA(1, 0), a3, voffA);
;             PG8_WAIT_V(8); PG8_WAIT_L(0); PG8_BAR; PG8_MMA(1, 0, At, B0); PG8_MMA(1, 1, At, B1); PG8_BAR; PG8_SCHED;
	ds_read_b128 v[184:187], v158 offset:49152
	ds_read_b128 v[188:191], v158 offset:50176
	ds_read_b128 v[192:195], v158 offset:51200
	ds_read_b128 v[196:199], v158 offset:52224
	ds_read_b128 v[200:203], v158 offset:53248
	ds_read_b128 v[204:207], v158 offset:54272
	ds_read_b128 v[208:211], v158 offset:55296
	ds_read_b128 v[212:215], v158 offset:56320
	s_add_u32 s42, s60, 0x80
	s_addc_u32 s43, s61, 0
	s_mov_b32 s51, m0
	s_mov_b32 m0, s83
	s_nop 0
	global_load_lds_dwordx4 v145, s[42:43]
	s_mov_b32 m0, s51
	s_nop 0
	s_mov_b32 s51, m0
	s_mov_b32 m0, s84
	s_nop 0
	global_load_lds_dwordx4 v155, s[42:43]
	s_mov_b32 m0, s51
	s_add_u32 s42, s60, 0x80080
	s_addc_u32 s43, s61, 0
	s_mov_b32 s51, m0
	s_mov_b32 m0, s87
	s_nop 0
	global_load_lds_dwordx4 v145, s[42:43]
	s_mov_b32 m0, s51
	s_nop 0
	s_mov_b32 s51, m0
	s_mov_b32 m0, s88
	s_nop 0
	global_load_lds_dwordx4 v155, s[42:43]
	s_mov_b32 m0, s51
	s_mov_b32 s42, m0
	s_mov_b32 m0, s85
	s_nop 0
	global_load_lds_dwordx4 v129, s[58:59]
	s_mov_b32 m0, s42
	s_nop 0
	s_mov_b32 s42, m0
	s_mov_b32 m0, s86
	s_nop 0
	global_load_lds_dwordx4 v154, s[58:59]
	s_mov_b32 m0, s42
	s_waitcnt vmcnt(8)
	s_waitcnt lgkmcnt(0)
	s_mov_b64 exec, 1
	ds_add_u32 v255, v255 offset:4096
	s_mov_b64 exec, -1
	s_setprio 1
	v_mfma_f32_16x16x32_bf16 v[60:63], v[146:149], v[184:187], v[60:63]
	v_mfma_f32_16x16x32_bf16 v[56:59], v[160:163], v[184:187], v[56:59]
	v_mfma_f32_16x16x32_bf16 v[52:55], v[146:149], v[192:195], v[52:55]
	v_mfma_f32_16x16x32_bf16 v[48:51], v[160:163], v[192:195], v[48:51]
	v_mfma_f32_16x16x32_bf16 v[44:47], v[146:149], v[200:203], v[44:47]
	v_mfma_f32_16x16x32_bf16 v[40:43], v[160:163], v[200:203], v[40:43]
	v_mfma_f32_16x16x32_bf16 v[36:39], v[146:149], v[208:211], v[36:39]
	v_mfma_f32_16x16x32_bf16 v[32:35], v[160:163], v[208:211], v[32:35]
	v_mfma_f32_16x16x32_bf16 v[60:63], v[150:153], v[188:191], v[60:63]
	v_mfma_f32_16x16x32_bf16 v[56:59], v[164:167], v[188:191], v[56:59]
	v_mfma_f32_16x16x32_bf16 v[52:55], v[150:153], v[196:199], v[52:55]
	v_mfma_f32_16x16x32_bf16 v[48:51], v[164:167], v[196:199], v[48:51]
	v_mfma_f32_16x16x32_bf16 v[44:47], v[150:153], v[204:207], v[44:47]
	v_mfma_f32_16x16x32_bf16 v[40:43], v[164:167], v[204:207], v[40:43]
	v_mfma_f32_16x16x32_bf16 v[36:39], v[150:153], v[212:215], v[36:39]
	v_mfma_f32_16x16x32_bf16 v[32:35], v[164:167], v[212:215], v[32:35]
	v_mfma_f32_16x16x32_bf16 v[28:31], v[168:171], v[184:187], v[28:31]
	v_mfma_f32_16x16x32_bf16 v[24:27], v[176:179], v[184:187], v[24:27]
	v_mfma_f32_16x16x32_bf16 v[20:23], v[168:171], v[192:195], v[20:23]
	v_mfma_f32_16x16x32_bf16 v[16:19], v[176:179], v[192:195], v[16:19]
	v_mfma_f32_16x16x32_bf16 v[12:15], v[168:171], v[200:203], v[12:15]
	v_mfma_f32_16x16x32_bf16 v[8:11], v[176:179], v[200:203], v[8:11]
	v_mfma_f32_16x16x32_bf16 v[4:7], v[168:171], v[208:211], v[4:7]
	v_mfma_f32_16x16x32_bf16 v[0:3], v[176:179], v[208:211], v[0:3]
	v_mfma_f32_16x16x32_bf16 v[28:31], v[172:175], v[188:191], v[28:31]
	v_mfma_f32_16x16x32_bf16 v[24:27], v[180:183], v[188:191], v[24:27]
	v_mfma_f32_16x16x32_bf16 v[20:23], v[172:175], v[196:199], v[20:23]
	v_mfma_f32_16x16x32_bf16 v[16:19], v[180:183], v[196:199], v[16:19]
	v_mfma_f32_16x16x32_bf16 v[12:15], v[172:175], v[204:207], v[12:15]
	v_mfma_f32_16x16x32_bf16 v[8:11], v[180:183], v[204:207], v[8:11]
	v_mfma_f32_16x16x32_bf16 v[4:7], v[172:175], v[212:215], v[4:7]
	v_mfma_f32_16x16x32_bf16 v[0:3], v[180:183], v[212:215], v[0:3]
	s_setprio 0
	s_barrier
	s_add_u32 s56, s56, 0x100
	s_addc_u32 s57, s57, 0
	s_cmp_ge_u32 s53, s81
	s_mov_b32 s51, s53
	s_cbranch_scc0 .LBB0_255
	s_branch .Lmy_ex_255
.Lmy_g0_255:
	s_add_i32 s53, s51, 2
	s_add_u32 s42, s18, s56
	s_addc_u32 s43, s19, s57
	s_add_u32 s58, s42, 0x100
	v_add_u32_e32 v130, 0x10000, v157
	s_addc_u32 s59, s43, 0
	ds_read_b128 v[146:149], v130
	ds_read_b128 v[150:153], v130 offset:1024
	ds_read_b128 v[160:163], v130 offset:2048
	ds_read_b128 v[164:167], v130 offset:3072
	v_add_u32_e32 v130, 0x14000, v157
	s_add_u32 s60, s22, s56
	ds_read_b128 v[168:171], v130
	ds_read_b128 v[172:175], v130 offset:1024
	ds_read_b128 v[176:179], v130 offset:2048
	ds_read_b128 v[180:183], v130 offset:3072
	s_addc_u32 s61, s23, s57
	s_add_u32 s60, s60, 0x100
	s_addc_u32 s61, s61, 0
	s_cmp_eq_u32 s20, s51
	s_cselect_b32 s62, s8, s58
	s_cselect_b32 s63, s9, s59
	s_cselect_b32 s60, s54, s60
	s_cselect_b32 s61, s55, s61
	s_add_u32 s58, s62, 0x80
	s_addc_u32 s59, s63, 0
	ds_read_b128 v[184:187], v158
	ds_read_b128 v[188:191], v158 offset:1024
	ds_read_b128 v[192:195], v158 offset:2048
	ds_read_b128 v[196:199], v158 offset:3072
	ds_read_b128 v[200:203], v158 offset:4096
	ds_read_b128 v[204:207], v158 offset:5120
	ds_read_b128 v[208:211], v158 offset:6144
	ds_read_b128 v[212:215], v158 offset:7168
	s_add_u32 s42, s42, 0x80080
	s_addc_u32 s43, s43, 0
	s_mov_b32 s51, m0
	s_mov_b32 m0, s89
	s_nop 0
	global_load_lds_dwordx4 v129, s[42:43]
	s_mov_b32 m0, s51
	s_nop 0
	s_mov_b32 s51, m0
	s_mov_b32 m0, s90
	s_nop 0
	global_load_lds_dwordx4 v154, s[42:43]
	s_mov_b32 m0, s51
	s_waitcnt vmcnt(8)
	s_waitcnt lgkmcnt(0)
	s_barrier
; #define PG8_STAGE(bufoff, gbase, voff) do { _Pragma("unroll") for (int _i = 0; _i < 2; ++_i) { unsigned keep_; \
;         asm volatile("s_mov_b32 %0, m0\n\ts_mov_b32 m0, %3\n\ts_nop 0\n\tglobal_load_lds_dwordx4 %1, %2\n\ts_mov_b32 m0, %0" : "=&s"(keep_) : "v"((voff)[_i]), "s"((const char*)(gbase)), "s"(ldsbase + (unsigned)((bufoff) + _i * 8192)) : "memory"); } } while (0)
; #define PG8_WAIT_V(n) asm volatile("s_waitcnt vmcnt(" #n ")" ::: "memory")
; #define PG8_WAIT_L(n) asm volatile("s_waitcnt lgkmcnt(" #n ")" ::: "memory")
; #define PG8_BAR __builtin_amdgcn_s_barrier()
; #define PG8_SCHED __builtin_amdgcn_sched_barrier(0)
; template <class Epi, class Sched, bool ALIGN_EPI, bool FP8 = false>
; DI void gemm_phase(LAS unsigned char* lds, const Gemm g, const Sched& S, const Epi& E) {
;     ...
;             PG8_WAIT_V(8); PG8_WAIT_L(0); PG8_BAR; PG8_MMA(0, 0, At, B0); PG8_MMA(0, 1, At, B1); PG8_BAR; PG8_SCHED;
;             PG8_LDA(At, 0, 1); PG8_STAGE(PG8_SB(0, 0), b2, voffB); PG8_STAGE(PG8_SB(0, 1), b2 + hstepB, voffB); PG8_STAGE(PG8_SA(0, 0), a2, voffA);
;             PG8_WAIT_V(8); PG8_WAIT_L(0); PG8_BAR; PG8_MMA(1, 0, At, B0); PG8_MMA(1, 1, At, B1); PG8_BAR; PG8_SCHED;
;             PG8_LDB(B0, 1, 0); PG8_LDB(B1, 1, 1); PG8_SCHED; PG8_LDA(At, 1, 0); PG8_STAGE(PG8_SA(0, 1), a2 + hstepA, voffA);
;             PG8_WAIT_V(8); PG8_WAIT_L(0); PG8_BAR; PG8_MMA(0, 0, At, B0); PG8_MMA(0, 1, At, B1); PG8_BAR; PG8_SCHED;
	s_setprio 1
	v_mfma_f32_16x16x32_bf16 v[124:127], v[146:149], v[184:187], v[124:127]
	v_mfma_f32_16x16x32_bf16 v[120:123], v[160:163], v[184:187], v[120:123]
	v_mfma_f32_16x16x32_bf16 v[116:119], v[146:149], v[192:195], v[116:119]
	v_mfma_f32_16x16x32_bf16 v[112:115], v[160:163], v[192:195], v[112:115]
	v_mfma_f32_16x16x32_bf16 v[108:111], v[146:149], v[200:203], v[108:111]
	v_mfma_f32_16x16x32_bf16 v[104:107], v[160:163], v[200:203], v[104:107]
	v_mfma_f32_16x16x32_bf16 v[100:103], v[146:149], v[208:211], v[100:103]
	v_mfma_f32_16x16x32_bf16 v[96:99], v[160:163], v[208:211], v[96:99]
	v_mfma_f32_16x16x32_bf16 v[124:127], v[150:153], v[188:191], v[124:127]
	v_mfma_f32_16x16x32_bf16 v[120:123], v[164:167], v[188:191], v[120:123]
	v_mfma_f32_16x16x32_bf16 v[116:119], v[150:153], v[196:199], v[116:119]
	v_mfma_f32_16x16x32_bf16 v[112:115], v[164:167], v[196:199], v[112:115]
	v_mfma_f32_16x16x32_bf16 v[108:111], v[150:153], v[204:207], v[108:111]
	v_mfma_f32_16x16x32_bf16 v[104:107], v[164:167], v[204:207], v[104:107]
	v_mfma_f32_16x16x32_bf16 v[100:103], v[150:153], v[212:215], v[100:103]
	v_mfma_f32_16x16x32_bf16 v[96:99], v[164:167], v[212:215], v[96:99]
	v_mfma_f32_16x16x32_bf16 v[92:95], v[168:171], v[184:187], v[92:95]
	v_mfma_f32_16x16x32_bf16 v[88:91], v[176:179], v[184:187], v[88:91]
	v_mfma_f32_16x16x32_bf16 v[84:87], v[168:171], v[192:195], v[84:87]
	v_mfma_f32_16x16x32_bf16 v[80:83], v[176:179], v[192:195], v[80:83]
	v_mfma_f32_16x16x32_bf16 v[76:79], v[168:171], v[200:203], v[76:79]
	v_mfma_f32_16x16x32_bf16 v[72:75], v[176:179], v[200:203], v[72:75]
	v_mfma_f32_16x16x32_bf16 v[68:71], v[168:171], v[208:211], v[68:71]
	v_mfma_f32_16x16x32_bf16 v[64:67], v[176:179], v[208:211], v[64:67]
	v_mfma_f32_16x16x32_bf16 v[92:95], v[172:175], v[188:191], v[92:95]
	v_mfma_f32_16x16x32_bf16 v[88:91], v[180:183], v[188:191], v[88:91]
	v_mfma_f32_16x16x32_bf16 v[84:87], v[172:175], v[196:199], v[84:87]
	v_mfma_f32_16x16x32_bf16 v[80:83], v[180:183], v[196:199], v[80:83]
	ds_read_b32 v255, v255 offset:4096
	v_mfma_f32_16x16x32_bf16 v[76:79], v[172:175], v[204:207], v[76:79]
	v_mfma_f32_16x16x32_bf16 v[72:75], v[180:183], v[204:207], v[72:75]
	v_mfma_f32_16x16x32_bf16 v[68:71], v[172:175], v[212:215], v[68:71]
	v_mfma_f32_16x16x32_bf16 v[64:67], v[180:183], v[212:215], v[64:67]
	s_add_u32 s98, s98, 0x80000
	s_waitcnt lgkmcnt(0)
	v_readfirstlane_b32 s101, v255
	v_mov_b32_e32 v255, 0x20000
	s_cmp_ge_u32 s101, s98
	s_cbranch_scc1 .Lmy_g_0
.Lmy_w_0:
	s_sleep 8
	ds_read_b32 v255, v255 offset:4096
	s_waitcnt lgkmcnt(0)
	v_readfirstlane_b32 s101, v255
	v_mov_b32_e32 v255, 0x20000
	s_cmp_ge_u32 s101, s98
	s_cbranch_scc0 .Lmy_w_0
.Lmy_g_0:
	s_setprio 0
	ds_read_b128 v[184:187], v158 offset:16384
	ds_read_b128 v[188:191], v158 offset:17408
	ds_read_b128 v[192:195], v158 offset:18432
	ds_read_b128 v[196:199], v158 offset:19456
	ds_read_b128 v[200:203], v158 offset:20480
	ds_read_b128 v[204:207], v158 offset:21504
	ds_read_b128 v[208:211], v158 offset:22528
	ds_read_b128 v[212:215], v158 offset:23552
	s_mov_b32 s42, m0
	s_mov_b32 m0, s17
	s_nop 0
	global_load_lds_dwordx4 v145, s[60:61]
	s_mov_b32 m0, s42
	s_nop 0
	s_mov_b32 s42, m0
	s_mov_b32 m0, s68
	s_nop 0
	global_load_lds_dwordx4 v155, s[60:61]
	s_mov_b32 m0, s42
	s_add_u32 s42, s60, 0x80000
	s_addc_u32 s43, s61, 0
	s_mov_b32 s51, m0
	s_mov_b32 m0, s69
	s_nop 0
	global_load_lds_dwordx4 v145, s[42:43]
	s_mov_b32 m0, s51
	s_nop 0
	s_mov_b32 s51, m0
	s_mov_b32 m0, s70
	s_nop 0
	global_load_lds_dwordx4 v155, s[42:43]
	s_mov_b32 m0, s51
	s_mov_b32 s42, m0
	s_mov_b32 m0, s15
	s_nop 0
	global_load_lds_dwordx4 v129, s[62:63]
	s_mov_b32 m0, s42
	s_nop 0
	s_mov_b32 s42, m0
	s_mov_b32 m0, s71
	s_nop 0
	global_load_lds_dwordx4 v154, s[62:63]
	s_mov_b32 m0, s42
	s_waitcnt vmcnt(8)
	s_waitcnt lgkmcnt(0)
	s_barrier
	s_setprio 1
	v_mfma_f32_16x16x32_bf16 v[60:63], v[146:149], v[184:187], v[60:63]
	v_mfma_f32_16x16x32_bf16 v[56:59], v[160:163], v[184:187], v[56:59]
	v_mfma_f32_16x16x32_bf16 v[52:55], v[146:149], v[192:195], v[52:55]
	v_mfma_f32_16x16x32_bf16 v[48:51], v[160:163], v[192:195], v[48:51]
	v_mfma_f32_16x16x32_bf16 v[44:47], v[146:149], v[200:203], v[44:47]
	v_mfma_f32_16x16x32_bf16 v[40:43], v[160:163], v[200:203], v[40:43]
	v_mfma_f32_16x16x32_bf16 v[36:39], v[146:149], v[208:211], v[36:39]
	v_mfma_f32_16x16x32_bf16 v[32:35], v[160:163], v[208:211], v[32:35]
	v_mfma_f32_16x16x32_bf16 v[60:63], v[150:153], v[188:191], v[60:63]
	v_mfma_f32_16x16x32_bf16 v[56:59], v[164:167], v[188:191], v[56:59]
	v_mfma_f32_16x16x32_bf16 v[52:55], v[150:153], v[196:199], v[52:55]
	v_mfma_f32_16x16x32_bf16 v[48:51], v[164:167], v[196:199], v[48:51]
	v_mfma_f32_16x16x32_bf16 v[44:47], v[150:153], v[204:207], v[44:47]
	v_mfma_f32_16x16x32_bf16 v[40:43], v[164:167], v[204:207], v[40:43]
	v_mfma_f32_16x16x32_bf16 v[36:39], v[150:153], v[212:215], v[36:39]
	v_mfma_f32_16x16x32_bf16 v[32:35], v[164:167], v[212:215], v[32:35]
	v_mfma_f32_16x16x32_bf16 v[28:31], v[168:171], v[184:187], v[28:31]
	v_mfma_f32_16x16x32_bf16 v[24:27], v[176:179], v[184:187], v[24:27]
	v_mfma_f32_16x16x32_bf16 v[20:23], v[168:171], v[192:195], v[20:23]
	v_mfma_f32_16x16x32_bf16 v[16:19], v[176:179], v[192:195], v[16:19]
	v_mfma_f32_16x16x32_bf16 v[12:15], v[168:171], v[200:203], v[12:15]
	v_mfma_f32_16x16x32_bf16 v[8:11], v[176:179], v[200:203], v[8:11]
	v_mfma_f32_16x16x32_bf16 v[4:7], v[168:171], v[208:211], v[4:7]
	v_mfma_f32_16x16x32_bf16 v[0:3], v[176:179], v[208:211], v[0:3]
	v_mfma_f32_16x16x32_bf16 v[28:31], v[172:175], v[188:191], v[28:31]
	v_mfma_f32_16x16x32_bf16 v[24:27], v[180:183], v[188:191], v[24:27]
	v_mfma_f32_16x16x32_bf16 v[20:23], v[172:175], v[196:199], v[20:23]
	v_mfma_f32_16x16x32_bf16 v[16:19], v[180:183], v[196:199], v[16:19]
	ds_read_b32 v255, v255 offset:4096
	v_mfma_f32_16x16x32_bf16 v[12:15], v[172:175], v[204:207], v[12:15]
	v_mfma_f32_16x16x32_bf16 v[8:11], v[180:183], v[204:207], v[8:11]
	v_mfma_f32_16x16x32_bf16 v[4:7], v[172:175], v[212:215], v[4:7]
	v_mfma_f32_16x16x32_bf16 v[0:3], v[180:183], v[212:215], v[0:3]
	s_add_u32 s98, s98, 0x80000
	s_waitcnt lgkmcnt(0)
	v_readfirstlane_b32 s101, v255
	v_mov_b32_e32 v255, 0x20000
	s_cmp_ge_u32 s101, s98
	s_cbranch_scc1 .Lmy_g_1

; #define PG8_STAGE(bufoff, gbase, voff) do { _Pragma("unroll") for (int _i = 0; _i < 2; ++_i) { unsigned keep_; \
;         asm volatile("s_mov_b32 %0, m0\n\ts_mov_b32 m0, %3\n\ts_nop 0\n\tglobal_load_lds_dwordx4 %1, %2\n\ts_mov_b32 m0, %0" : "=&s"(keep_) : "v"((voff)[_i]), "s"((const char*)(gbase)), "s"(ldsbase + (unsigned)((bufoff) + _i * 8192)) : "memory"); } } while (0)
; #define PG8_WAIT_V(n) asm volatile("s_waitcnt vmcnt(" #n ")" ::: "memory")
; #define PG8_WAIT_L(n) asm volatile("s_waitcnt lgkmcnt(" #n ")" ::: "memory")
; #define PG8_BAR __builtin_amdgcn_s_barrier()
; #define PG8_SCHED __builtin_amdgcn_sched_barrier(0)
; template <class Epi, class Sched, bool ALIGN_EPI, bool FP8 = false>
; DI void gemm_phase(LAS unsigned char* lds, const Gemm g, const Sched& S, const Epi& E) {
;     ...
;             PG8_LDB(B0, 1, 0); PG8_LDB(B1, 1, 1); PG8_SCHED; PG8_LDA(At, 1, 0); PG8_STAGE(PG8_SA(0, 1), a2 + hstepA, voffA);
;             PG8_WAIT_V(8); PG8_WAIT_L(0); PG8_BAR; PG8_MMA(0, 0, At, B0); PG8_MMA(0, 1, At, B1); PG8_BAR; PG8_SCHED;
.Lmy_g_1:
	s_setprio 0
	v_add_u32_e32 v130, 0x18000, v157
	ds_read_b128 v[146:149], v130
	ds_read_b128 v[150:153], v130 offset:1024
	ds_read_b128 v[160:163], v130 offset:2048
	ds_read_b128 v[164:167], v130 offset:3072
	v_add_u32_e32 v130, 0x1c000, v157
	ds_read_b128 v[168:171], v130
	ds_read_b128 v[172:175], v130 offset:1024
	ds_read_b128 v[176:179], v130 offset:2048
	ds_read_b128 v[180:183], v130 offset:3072
	ds_read_b128 v[184:187], v158 offset:32768
	ds_read_b128 v[188:191], v158 offset:33792
	ds_read_b128 v[192:195], v158 offset:34816
	ds_read_b128 v[196:199], v158 offset:35840
	ds_read_b128 v[200:203], v158 offset:36864
	ds_read_b128 v[204:207], v158 offset:37888
	ds_read_b128 v[208:211], v158 offset:38912
	ds_read_b128 v[212:215], v158 offset:39936
	s_add_u32 s42, s62, 0x80000
	s_addc_u32 s43, s63, 0
	s_mov_b32 s51, m0
	s_mov_b32 m0, s72
	s_nop 0
	global_load_lds_dwordx4 v129, s[42:43]
	s_mov_b32 m0, s51
	s_nop 0
	s_mov_b32 s51, m0
	s_mov_b32 m0, s73
	s_nop 0
	global_load_lds_dwordx4 v154, s[42:43]
	s_mov_b32 m0, s51
	s_waitcnt vmcnt(8)
	s_waitcnt lgkmcnt(0)
	s_barrier
	s_setprio 1
	v_mfma_f32_16x16x32_bf16 v[124:127], v[146:149], v[184:187], v[124:127]
	v_mfma_f32_16x16x32_bf16 v[120:123], v[160:163], v[184:187], v[120:123]
	v_mfma_f32_16x16x32_bf16 v[116:119], v[146:149], v[192:195], v[116:119]
	v_mfma_f32_16x16x32_bf16 v[112:115], v[160:163], v[192:195], v[112:115]
	v_mfma_f32_16x16x32_bf16 v[108:111], v[146:149], v[200:203], v[108:111]
	v_mfma_f32_16x16x32_bf16 v[104:107], v[160:163], v[200:203], v[104:107]
	v_mfma_f32_16x16x32_bf16 v[100:103], v[146:149], v[208:211], v[100:103]
	v_mfma_f32_16x16x32_bf16 v[96:99], v[160:163], v[208:211], v[96:99]
	v_mfma_f32_16x16x32_bf16 v[124:127], v[150:153], v[188:191], v[124:127]
	v_mfma_f32_16x16x32_bf16 v[120:123], v[164:167], v[188:191], v[120:123]
	v_mfma_f32_16x16x32_bf16 v[116:119], v[150:153], v[196:199], v[116:119]
	v_mfma_f32_16x16x32_bf16 v[112:115], v[164:167], v[196:199], v[112:115]
	v_mfma_f32_16x16x32_bf16 v[108:111], v[150:153], v[204:207], v[108:111]
	v_mfma_f32_16x16x32_bf16 v[104:107], v[164:167], v[204:207], v[104:107]
	v_mfma_f32_16x16x32_bf16 v[100:103], v[150:153], v[212:215], v[100:103]
	v_mfma_f32_16x16x32_bf16 v[96:99], v[164:167], v[212:215], v[96:99]
	v_mfma_f32_16x16x32_bf16 v[92:95], v[168:171], v[184:187], v[92:95]
	v_mfma_f32_16x16x32_bf16 v[88:91], v[176:179], v[184:187], v[88:91]
	v_mfma_f32_16x16x32_bf16 v[84:87], v[168:171], v[192:195], v[84:87]
	v_mfma_f32_16x16x32_bf16 v[80:83], v[176:179], v[192:195], v[80:83]
	v_mfma_f32_16x16x32_bf16 v[76:79], v[168:171], v[200:203], v[76:79]
	v_mfma_f32_16x16x32_bf16 v[72:75], v[176:179], v[200:203], v[72:75]
	v_mfma_f32_16x16x32_bf16 v[68:71], v[168:171], v[208:211], v[68:71]
	v_mfma_f32_16x16x32_bf16 v[64:67], v[176:179], v[208:211], v[64:67]
	v_mfma_f32_16x16x32_bf16 v[92:95], v[172:175], v[188:191], v[92:95]
	v_mfma_f32_16x16x32_bf16 v[88:91], v[180:183], v[188:191], v[88:91]
	v_mfma_f32_16x16x32_bf16 v[84:87], v[172:175], v[196:199], v[84:87]
	v_mfma_f32_16x16x32_bf16 v[80:83], v[180:183], v[196:199], v[80:83]
	ds_read_b32 v255, v255 offset:4096
	v_mfma_f32_16x16x32_bf16 v[76:79], v[172:175], v[204:207], v[76:79]
	v_mfma_f32_16x16x32_bf16 v[72:75], v[180:183], v[204:207], v[72:75]
	v_mfma_f32_16x16x32_bf16 v[68:71], v[172:175], v[212:215], v[68:71]
	v_mfma_f32_16x16x32_bf16 v[64:67], v[180:183], v[212:215], v[64:67]
	s_add_u32 s98, s98, 0x80000
	s_waitcnt lgkmcnt(0)
	v_readfirstlane_b32 s101, v255
	v_mov_b32_e32 v255, 0x20000
	s_cmp_ge_u32 s101, s98
	s_cbranch_scc1 .Lmy_g_2

; #define PG8_STAGE(bufoff, gbase, voff) do { _Pragma("unroll") for (int _i = 0; _i < 2; ++_i) { unsigned keep_; \
;         asm volatile("s_mov_b32 %0, m0\n\ts_mov_b32 m0, %3\n\ts_nop 0\n\tglobal_load_lds_dwordx4 %1, %2\n\ts_mov_b32 m0, %0" : "=&s"(keep_) : "v"((voff)[_i]), "s"((const char*)(gbase)), "s"(ldsbase + (unsigned)((bufoff) + _i * 8192)) : "memory"); } } while (0)
; #define PG8_WAIT_V(n) asm volatile("s_waitcnt vmcnt(" #n ")" ::: "memory")
; #define PG8_WAIT_L(n) asm volatile("s_waitcnt lgkmcnt(" #n ")" ::: "memory")
; #define PG8_BAR __builtin_amdgcn_s_barrier()
; #define PG8_SCHED __builtin_amdgcn_sched_barrier(0)
; template <class Epi, class Sched, bool ALIGN_EPI, bool FP8 = false>
; DI void gemm_phase(LAS unsigned char* lds, const Gemm g, const Sched& S, const Epi& E) {
;     ...
;             PG8_LDA(At, 1, 1); PG8_STAGE(PG8_SB(1, 0), b3, voffB); PG8_STAGE(PG8_SB(1, 1), b3 + hstepB, voffB); PG8_STAGE(PG8_SA(1, 0), a3, voffA);
;             PG8_WAIT_V(8); PG8_WAIT_L(0); PG8_BAR; PG8_MMA(1, 0, At, B0); PG8_MMA(1, 1, At, B1); PG8_BAR; PG8_SCHED;
.Lmy_g_2:
	s_setprio 0
	ds_read_b128 v[184:187], v158 offset:49152
	ds_read_b128 v[188:191], v158 offset:50176
	ds_read_b128 v[192:195], v158 offset:51200
	ds_read_b128 v[196:199], v158 offset:52224
	ds_read_b128 v[200:203], v158 offset:53248
	ds_read_b128 v[204:207], v158 offset:54272
	ds_read_b128 v[208:211], v158 offset:55296
	ds_read_b128 v[212:215], v158 offset:56320
	s_add_u32 s42, s60, 0x80
	s_addc_u32 s43, s61, 0
	s_mov_b32 s51, m0
	s_mov_b32 m0, s83
	s_nop 0
	global_load_lds_dwordx4 v145, s[42:43]
	s_mov_b32 m0, s51
	s_nop 0
	s_mov_b32 s51, m0
	s_mov_b32 m0, s84
	s_nop 0
	global_load_lds_dwordx4 v155, s[42:43]
	s_mov_b32 m0, s51
	s_add_u32 s42, s60, 0x80080
	s_addc_u32 s43, s61, 0
	s_mov_b32 s51, m0
	s_mov_b32 m0, s87
	s_nop 0
	global_load_lds_dwordx4 v145, s[42:43]
	s_mov_b32 m0, s51
	s_nop 0
	s_mov_b32 s51, m0
	s_mov_b32 m0, s88
	s_nop 0
	global_load_lds_dwordx4 v155, s[42:43]
	s_mov_b32 m0, s51
	s_mov_b32 s42, m0
	s_mov_b32 m0, s85
	s_nop 0
	global_load_lds_dwordx4 v129, s[58:59]
	s_mov_b32 m0, s42
	s_nop 0
	s_mov_b32 s42, m0
	s_mov_b32 m0, s86
	s_nop 0
	global_load_lds_dwordx4 v154, s[58:59]
	s_mov_b32 m0, s42
	s_waitcnt vmcnt(8)
	s_waitcnt lgkmcnt(0)
	s_barrier
	s_setprio 1
	v_mfma_f32_16x16x32_bf16 v[60:63], v[146:149], v[184:187], v[60:63]
	v_mfma_f32_16x16x32_bf16 v[56:59], v[160:163], v[184:187], v[56:59]
	v_mfma_f32_16x16x32_bf16 v[52:55], v[146:149], v[192:195], v[52:55]
	v_mfma_f32_16x16x32_bf16 v[48:51], v[160:163], v[192:195], v[48:51]
	v_mfma_f32_16x16x32_bf16 v[44:47], v[146:149], v[200:203], v[44:47]
	v_mfma_f32_16x16x32_bf16 v[40:43], v[160:163], v[200:203], v[40:43]
	v_mfma_f32_16x16x32_bf16 v[36:39], v[146:149], v[208:211], v[36:39]
	v_mfma_f32_16x16x32_bf16 v[32:35], v[160:163], v[208:211], v[32:35]
	v_mfma_f32_16x16x32_bf16 v[60:63], v[150:153], v[188:191], v[60:63]
	v_mfma_f32_16x16x32_bf16 v[56:59], v[164:167], v[188:191], v[56:59]
	v_mfma_f32_16x16x32_bf16 v[52:55], v[150:153], v[196:199], v[52:55]
	v_mfma_f32_16x16x32_bf16 v[48:51], v[164:167], v[196:199], v[48:51]
	v_mfma_f32_16x16x32_bf16 v[44:47], v[150:153], v[204:207], v[44:47]
	v_mfma_f32_16x16x32_bf16 v[40:43], v[164:167], v[204:207], v[40:43]
	v_mfma_f32_16x16x32_bf16 v[36:39], v[150:153], v[212:215], v[36:39]
	v_mfma_f32_16x16x32_bf16 v[32:35], v[164:167], v[212:215], v[32:35]
	v_mfma_f32_16x16x32_bf16 v[28:31], v[168:171], v[184:187], v[28:31]
	v_mfma_f32_16x16x32_bf16 v[24:27], v[176:179], v[184:187], v[24:27]
	v_mfma_f32_16x16x32_bf16 v[20:23], v[168:171], v[192:195], v[20:23]
	v_mfma_f32_16x16x32_bf16 v[16:19], v[176:179], v[192:195], v[16:19]
	v_mfma_f32_16x16x32_bf16 v[12:15], v[168:171], v[200:203], v[12:15]
	v_mfma_f32_16x16x32_bf16 v[8:11], v[176:179], v[200:203], v[8:11]
	v_mfma_f32_16x16x32_bf16 v[4:7], v[168:171], v[208:211], v[4:7]
	v_mfma_f32_16x16x32_bf16 v[0:3], v[176:179], v[208:211], v[0:3]
	v_mfma_f32_16x16x32_bf16 v[28:31], v[172:175], v[188:191], v[28:31]
	v_mfma_f32_16x16x32_bf16 v[24:27], v[180:183], v[188:191], v[24:27]
	v_mfma_f32_16x16x32_bf16 v[20:23], v[172:175], v[196:199], v[20:23]
	v_mfma_f32_16x16x32_bf16 v[16:19], v[180:183], v[196:199], v[16:19]
	ds_read_b32 v255, v255 offset:4096
	v_mfma_f32_16x16x32_bf16 v[12:15], v[172:175], v[204:207], v[12:15]
	v_mfma_f32_16x16x32_bf16 v[8:11], v[180:183], v[204:207], v[8:11]
	v_mfma_f32_16x16x32_bf16 v[4:7], v[172:175], v[212:215], v[4:7]
	v_mfma_f32_16x16x32_bf16 v[0:3], v[180:183], v[212:215], v[0:3]
	s_add_u32 s98, s98, 0x80000
	s_waitcnt lgkmcnt(0)
	v_readfirstlane_b32 s101, v255
	v_mov_b32_e32 v255, 0x20000
	s_cmp_ge_u32 s101, s98
	s_cbranch_scc1 .Lmy_g_3

; #define PG8_WAIT_V(n) asm volatile("s_waitcnt vmcnt(" #n ")" ::: "memory")
; #define PG8_WAIT_L(n) asm volatile("s_waitcnt lgkmcnt(" #n ")" ::: "memory")
; #define PG8_BAR __builtin_amdgcn_s_barrier()
; #define PG8_SCHED __builtin_amdgcn_sched_barrier(0)
; template <class Epi, class Sched, bool ALIGN_EPI, bool FP8 = false>
; DI void gemm_phase(LAS unsigned char* lds, const Gemm g, const Sched& S, const Epi& E) {
;     ...
;             PG8_WAIT_V(8); PG8_WAIT_L(0); PG8_BAR; PG8_MMA(1, 0, At, B0); PG8_MMA(1, 1, At, B1); PG8_BAR; PG8_SCHED;
;         }
;         if constexpr (ALIGN_EPI) { if (wr == 0) PG8_BAR; }
;         E(acc, cur, wr, wc, fr, fq);
.Lmy_g_3:
	s_setprio 0
	s_add_u32 s56, s56, 0x100
	s_addc_u32 s57, s57, 0
	s_cmp_ge_u32 s53, s81
	s_mov_b32 s51, s53
	s_cbranch_scc0 .Lmy_g0_255
.Lmy_ex_255:
	s_and_b64 vcc, exec, s[26:27]
	s_cbranch_vccnz .LBB0_265
	s_bitcmp0_b32 s77, 1
	s_mov_b64 s[56:57], -1
	v_lshl_add_u32 v142, s14, 8, v156
	s_cbranch_scc0 .LBB0_266

; #define PG8_STAGE(bufoff, gbase, voff) do { _Pragma("unroll") for (int _i = 0; _i < 2; ++_i) { unsigned keep_; \
;         asm volatile("s_mov_b32 %0, m0\n\ts_mov_b32 m0, %3\n\ts_nop 0\n\tglobal_load_lds_dwordx4 %1, %2\n\ts_mov_b32 m0, %0" : "=&s"(keep_) : "v"((voff)[_i]), "s"((const char*)(gbase)), "s"(ldsbase + (unsigned)((bufoff) + _i * 8192)) : "memory"); } } while (0)
; #define PG8_WAIT_V(n) asm volatile("s_waitcnt vmcnt(" #n ")" ::: "memory")
; #define PG8_WAIT_L(n) asm volatile("s_waitcnt lgkmcnt(" #n ")" ::: "memory")
; #define PG8_BAR __builtin_amdgcn_s_barrier()
; #define PG8_SCHED __builtin_amdgcn_sched_barrier(0)
;     DI int nt(const Unit& u) const { return (u.aux & 8) ? PLED / 64 : ((u.aux & 4) ? (D_ / 2) / 64 : D_ / 64); }
; template <class Epi, class Sched, bool ALIGN_EPI, bool FP8 = false>
; DI void gemm_phase(LAS unsigned char* lds, const Gemm g, const Sched& S, const Epi& E) {
;     ...
;         for (int t = 0; t < nt; t += 2) {
;             if constexpr (Epi::MID) { if (t == (nt >> 1)) E.mid(acc, cur, wr, wc, fr, fq); }
;             const bool last = (t == nt - 2);
;             const char* a1 = cA + (size_t)(t + 1) * kstep;
;             const char* a2 = last ? nA : cA + (size_t)(t + 2) * kstep; const char* b2 = last ? nB : cB + (size_t)(t + 2) * kstep;
;             const char* a3 = a2 + kstep; const char* b3 = b2 + kstep;
;             PG8_LDB(B0, 0, 0); PG8_LDB(B1, 0, 1); PG8_SCHED; PG8_LDA(At, 0, 0); PG8_STAGE(PG8_SA(1, 1), a1 + hstepA, voffA);
;             PG8_WAIT_V(8); PG8_WAIT_L(0); PG8_BAR; PG8_MMA(0, 0, At, B0); PG8_MMA(0, 1, At, B1); PG8_BAR; PG8_SCHED;
;             PG8_LDA(At, 0, 1); PG8_STAGE(PG8_SB(0, 0), b2, voffB); PG8_STAGE(PG8_SB(0, 1), b2 + hstepB, voffB); PG8_STAGE(PG8_SA(0, 0), a2, voffA);
;             PG8_WAIT_V(8); PG8_WAIT_L(0); PG8_BAR; PG8_MMA(1, 0, At, B0); PG8_MMA(1, 1, At, B1); PG8_BAR; PG8_SCHED;
;             PG8_LDB(B0, 1, 0); PG8_LDB(B1, 1, 1); PG8_SCHED; PG8_LDA(At, 1, 0); PG8_STAGE(PG8_SA(0, 1), a2 + hstepA, voffA);
;             PG8_WAIT_V(8); PG8_WAIT_L(0); PG8_BAR; PG8_MMA(0, 0, At, B0); PG8_MMA(0, 1, At, B1); PG8_BAR; PG8_SCHED;
.LBB0_298:
	s_cmp_lg_u32 s99, 0
	s_cbranch_scc1 .Lmy_g0_298
	ds_read_b128 v[104:107], v151
	s_waitcnt vmcnt(8)
	ds_read_b128 v[108:111], v151 offset:16
	ds_read_b128 v[112:115], v151 offset:2048
	ds_read_b128 v[116:119], v151 offset:2064
	ds_read_b128 v[160:163], v151 offset:16384
	ds_read_b128 v[164:167], v151 offset:16400
	ds_read_b128 v[168:171], v151 offset:18432
	ds_read_b128 v[172:175], v151 offset:18448
	s_add_u32 s52, s50, 0x100
	s_addc_u32 s53, s51, 0
	s_cmp_eq_u32 s91, 12
	s_cselect_b32 s58, s87, s52
	s_cselect_b32 s59, s43, s53
	s_cselect_b32 s56, s88, s89
	s_cselect_b32 s57, s41, s90
	s_add_u32 s54, s58, 0x80
	s_addc_u32 s55, s59, 0
	ds_read_b128 v[176:179], v150
	ds_read_b128 v[180:183], v150 offset:16
	ds_read_b128 v[184:187], v150 offset:2048
	ds_read_b128 v[188:191], v150 offset:2064
	ds_read_b128 v[192:195], v150 offset:4096
	ds_read_b128 v[196:199], v150 offset:4112
	ds_read_b128 v[200:203], v150 offset:6144
	ds_read_b128 v[204:207], v150 offset:6160
	s_add_u32 s50, s50, 0x40080
	s_addc_u32 s51, s51, 0
	s_mov_b32 s92, m0
	s_mov_b32 m0, s75
	s_nop 0
	global_load_lds_dwordx4 v152, s[50:51]
	s_mov_b32 m0, s92
	s_nop 0
	s_mov_b32 s92, m0
	s_mov_b32 m0, s77
	s_nop 0
	global_load_lds_dwordx4 v154, s[50:51]
	s_mov_b32 m0, s92
	s_waitcnt vmcnt(8)
	s_waitcnt lgkmcnt(0)
	s_mov_b64 exec, 1
	ds_add_u32 v255, v255 offset:4096
	s_mov_b64 exec, -1
	s_setprio 1
	v_mfma_scale_f32_16x16x128_f8f6f4 v[140:143], v[104:111], v[176:183], v[140:143], v158, v158 op_sel_hi:[0,0,0]
	v_mfma_scale_f32_16x16x128_f8f6f4 v[136:139], v[112:119], v[176:183], v[136:139], v158, v158 op_sel_hi:[0,0,0]
	v_mfma_scale_f32_16x16x128_f8f6f4 v[124:127], v[104:111], v[184:191], v[124:127], v158, v158 op_sel_hi:[0,0,0]
	v_mfma_scale_f32_16x16x128_f8f6f4 v[120:123], v[112:119], v[184:191], v[120:123], v158, v158 op_sel_hi:[0,0,0]
	v_mfma_scale_f32_16x16x128_f8f6f4 v[208:211], v[104:111], v[192:199], v[92:95], v158, v158 op_sel_hi:[0,0,0]
	v_mfma_scale_f32_16x16x128_f8f6f4 v[212:215], v[112:119], v[192:199], v[88:91], v158, v158 op_sel_hi:[0,0,0]
	v_mfma_scale_f32_16x16x128_f8f6f4 v[216:219], v[104:111], v[200:207], v[76:79], v158, v158 op_sel_hi:[0,0,0]
	v_mfma_scale_f32_16x16x128_f8f6f4 v[220:223], v[112:119], v[200:207], v[72:75], v158, v158 op_sel_hi:[0,0,0]
	v_mfma_scale_f32_16x16x128_f8f6f4 v[132:135], v[160:167], v[176:183], v[132:135], v158, v158 op_sel_hi:[0,0,0]
	v_mfma_scale_f32_16x16x128_f8f6f4 v[128:131], v[168:175], v[176:183], v[128:131], v158, v158 op_sel_hi:[0,0,0]
	v_mfma_scale_f32_16x16x128_f8f6f4 v[100:103], v[160:167], v[184:191], v[100:103], v158, v158 op_sel_hi:[0,0,0]
	v_mfma_scale_f32_16x16x128_f8f6f4 v[96:99], v[168:175], v[184:191], v[96:99], v158, v158 op_sel_hi:[0,0,0]
	v_mfma_scale_f32_16x16x128_f8f6f4 v[176:179], v[160:167], v[192:199], v[84:87], v158, v158 op_sel_hi:[0,0,0]
	v_mfma_scale_f32_16x16x128_f8f6f4 v[180:183], v[168:175], v[192:199], v[80:83], v158, v158 op_sel_hi:[0,0,0]
	v_mfma_scale_f32_16x16x128_f8f6f4 v[184:187], v[160:167], v[200:207], v[68:71], v158, v158 op_sel_hi:[0,0,0]
	v_mfma_scale_f32_16x16x128_f8f6f4 v[188:191], v[168:175], v[200:207], v[64:67], v158, v158 op_sel_hi:[0,0,0]
	s_setprio 0
	s_barrier
	s_nop 4
	ds_read_b128 v[64:67], v150 offset:16384
	ds_read_b128 v[68:71], v150 offset:16400
	ds_read_b128 v[72:75], v150 offset:18432
	ds_read_b128 v[76:79], v150 offset:18448
	ds_read_b128 v[80:83], v150 offset:20480
	ds_read_b128 v[84:87], v150 offset:20496
	ds_read_b128 v[88:91], v150 offset:22528
	ds_read_b128 v[92:95], v150 offset:22544
	s_mov_b32 s50, m0
	s_mov_b32 m0, s49
	s_nop 0
	global_load_lds_dwordx4 v153, s[56:57]
	s_mov_b32 m0, s50
	s_nop 0
	s_mov_b32 s50, m0
	s_mov_b32 m0, s63
	s_nop 0
	global_load_lds_dwordx4 v155, s[56:57]
	s_mov_b32 m0, s50
	s_add_u32 s50, s56, 0x40000
	s_addc_u32 s51, s57, 0
	s_mov_b32 s92, m0
	s_mov_b32 m0, s64
	s_nop 0
	global_load_lds_dwordx4 v153, s[50:51]
	s_mov_b32 m0, s92
	s_nop 0
	s_mov_b32 s92, m0
	s_mov_b32 m0, s65
	s_nop 0
	global_load_lds_dwordx4 v155, s[50:51]
	s_mov_b32 m0, s92
	s_mov_b32 s50, m0
	s_mov_b32 m0, s62
	s_nop 0
	global_load_lds_dwordx4 v152, s[58:59]
	s_mov_b32 m0, s50
	s_nop 0
	s_mov_b32 s50, m0
	s_mov_b32 m0, s66
	s_nop 0
	global_load_lds_dwordx4 v154, s[58:59]
	s_mov_b32 m0, s50
	s_waitcnt vmcnt(8)
	s_waitcnt lgkmcnt(0)
	s_mov_b64 exec, 1
	ds_add_u32 v255, v255 offset:4096
	s_mov_b64 exec, -1
	s_setprio 1
	v_mfma_scale_f32_16x16x128_f8f6f4 v[60:63], v[104:111], v[64:71], v[60:63], v158, v158 op_sel_hi:[0,0,0]
	v_mfma_scale_f32_16x16x128_f8f6f4 v[56:59], v[112:119], v[64:71], v[56:59], v158, v158 op_sel_hi:[0,0,0]
	v_mfma_scale_f32_16x16x128_f8f6f4 v[192:195], v[104:111], v[72:79], v[44:47], v158, v158 op_sel_hi:[0,0,0]
	v_mfma_scale_f32_16x16x128_f8f6f4 v[196:199], v[112:119], v[72:79], v[40:43], v158, v158 op_sel_hi:[0,0,0]
	v_mfma_scale_f32_16x16x128_f8f6f4 v[200:203], v[104:111], v[80:87], v[28:31], v158, v158 op_sel_hi:[0,0,0]
	v_mfma_scale_f32_16x16x128_f8f6f4 v[204:207], v[112:119], v[80:87], v[24:27], v158, v158 op_sel_hi:[0,0,0]
	v_mfma_scale_f32_16x16x128_f8f6f4 v[224:227], v[104:111], v[88:95], v[12:15], v158, v158 op_sel_hi:[0,0,0]
	v_mfma_scale_f32_16x16x128_f8f6f4 v[228:231], v[112:119], v[88:95], v[8:11], v158, v158 op_sel_hi:[0,0,0]
	v_mfma_scale_f32_16x16x128_f8f6f4 v[52:55], v[160:167], v[64:71], v[52:55], v158, v158 op_sel_hi:[0,0,0]
	v_mfma_scale_f32_16x16x128_f8f6f4 v[48:51], v[168:175], v[64:71], v[48:51], v158, v158 op_sel_hi:[0,0,0]
	v_mfma_scale_f32_16x16x128_f8f6f4 v[232:235], v[160:167], v[72:79], v[36:39], v158, v158 op_sel_hi:[0,0,0]
	v_mfma_scale_f32_16x16x128_f8f6f4 v[236:239], v[168:175], v[72:79], v[32:35], v158, v158 op_sel_hi:[0,0,0]
	v_mfma_scale_f32_16x16x128_f8f6f4 v[240:243], v[160:167], v[80:87], v[20:23], v158, v158 op_sel_hi:[0,0,0]
	v_mfma_scale_f32_16x16x128_f8f6f4 v[244:247], v[168:175], v[80:87], v[16:19], v158, v158 op_sel_hi:[0,0,0]
	v_mfma_scale_f32_16x16x128_f8f6f4 v[248:251], v[160:167], v[88:95], v[4:7], v158, v158 op_sel_hi:[0,0,0]
	v_mfma_scale_f32_16x16x128_f8f6f4 v[144:147], v[168:175], v[88:95], v[0:3], v158, v158 op_sel_hi:[0,0,0]
	s_setprio 0
	s_barrier
; #define PG8_STAGE(bufoff, gbase, voff) do { _Pragma("unroll") for (int _i = 0; _i < 2; ++_i) { unsigned keep_; \
;         asm volatile("s_mov_b32 %0, m0\n\ts_mov_b32 m0, %3\n\ts_nop 0\n\tglobal_load_lds_dwordx4 %1, %2\n\ts_mov_b32 m0, %0" : "=&s"(keep_) : "v"((voff)[_i]), "s"((const char*)(gbase)), "s"(ldsbase + (unsigned)((bufoff) + _i * 8192)) : "memory"); } } while (0)
; #define PG8_WAIT_V(n) asm volatile("s_waitcnt vmcnt(" #n ")" ::: "memory")
; #define PG8_WAIT_L(n) asm volatile("s_waitcnt lgkmcnt(" #n ")" ::: "memory")
; #define PG8_BAR __builtin_amdgcn_s_barrier()
; #define PG8_SCHED __builtin_amdgcn_sched_barrier(0)
; template <class Epi, class Sched, bool ALIGN_EPI, bool FP8 = false>
; DI void gemm_phase(LAS unsigned char* lds, const Gemm g, const Sched& S, const Epi& E) {
;     ...
;             PG8_LDB(B0, 1, 0); PG8_LDB(B1, 1, 1); PG8_SCHED; PG8_LDA(At, 1, 0); PG8_STAGE(PG8_SA(0, 1), a2 + hstepA, voffA);
;             PG8_WAIT_V(8); PG8_WAIT_L(0); PG8_BAR; PG8_MMA(0, 0, At, B0); PG8_MMA(0, 1, At, B1); PG8_BAR; PG8_SCHED;
;             PG8_LDA(At, 1, 1); PG8_STAGE(PG8_SB(1, 0), b3, voffB); PG8_STAGE(PG8_SB(1, 1), b3 + hstepB, voffB); PG8_STAGE(PG8_SA(1, 0), a3, voffA);
;             PG8_WAIT_V(8); PG8_WAIT_L(0); PG8_BAR; PG8_MMA(1, 0, At, B0); PG8_MMA(1, 1, At, B1); PG8_BAR; PG8_SCHED;
;         }
	s_nop 4
	ds_read_b128 v[0:3], v151 offset:32768
	ds_read_b128 v[4:7], v151 offset:32784
	ds_read_b128 v[16:19], v151 offset:34816
	ds_read_b128 v[20:23], v151 offset:34832
	ds_read_b128 v[104:107], v151 offset:49152
	ds_read_b128 v[108:111], v151 offset:49168
	ds_read_b128 v[112:115], v151 offset:51200
	ds_read_b128 v[116:119], v151 offset:51216
	ds_read_b128 v[8:11], v150 offset:32768
	ds_read_b128 v[12:15], v150 offset:32784
	ds_read_b128 v[24:27], v150 offset:34816
	ds_read_b128 v[28:31], v150 offset:34832
	ds_read_b128 v[32:35], v150 offset:36864
	ds_read_b128 v[36:39], v150 offset:36880
	ds_read_b128 v[40:43], v150 offset:38912
	ds_read_b128 v[44:47], v150 offset:38928
	s_add_u32 s50, s58, 0x40000
	s_addc_u32 s51, s59, 0
	s_mov_b32 s58, m0
	s_mov_b32 m0, s67
	s_nop 0
	global_load_lds_dwordx4 v152, s[50:51]
	s_mov_b32 m0, s58
	s_nop 0
	s_mov_b32 s58, m0
	s_mov_b32 m0, s68
	s_nop 0
	global_load_lds_dwordx4 v154, s[50:51]
	s_mov_b32 m0, s58
	s_waitcnt vmcnt(8)
	s_waitcnt lgkmcnt(0)
	s_mov_b64 exec, 1
	ds_add_u32 v255, v255 offset:4096
	s_mov_b64 exec, -1
	s_setprio 1
	v_mfma_scale_f32_16x16x128_f8f6f4 v[140:143], v[0:7], v[8:15], v[140:143], v158, v158 op_sel_hi:[0,0,0]
	v_mfma_scale_f32_16x16x128_f8f6f4 v[136:139], v[16:23], v[8:15], v[136:139], v158, v158 op_sel_hi:[0,0,0]
	v_mfma_scale_f32_16x16x128_f8f6f4 v[124:127], v[0:7], v[24:31], v[124:127], v158, v158 op_sel_hi:[0,0,0]
	v_mfma_scale_f32_16x16x128_f8f6f4 v[120:123], v[16:23], v[24:31], v[120:123], v158, v158 op_sel_hi:[0,0,0]
	v_mfma_scale_f32_16x16x128_f8f6f4 v[92:95], v[0:7], v[32:39], v[208:211], v158, v158 op_sel_hi:[0,0,0]
	v_mfma_scale_f32_16x16x128_f8f6f4 v[88:91], v[16:23], v[32:39], v[212:215], v158, v158 op_sel_hi:[0,0,0]
	v_mfma_scale_f32_16x16x128_f8f6f4 v[76:79], v[0:7], v[40:47], v[216:219], v158, v158 op_sel_hi:[0,0,0]
	v_mfma_scale_f32_16x16x128_f8f6f4 v[72:75], v[16:23], v[40:47], v[220:223], v158, v158 op_sel_hi:[0,0,0]
	v_mfma_scale_f32_16x16x128_f8f6f4 v[132:135], v[104:111], v[8:15], v[132:135], v158, v158 op_sel_hi:[0,0,0]
	v_mfma_scale_f32_16x16x128_f8f6f4 v[128:131], v[112:119], v[8:15], v[128:131], v158, v158 op_sel_hi:[0,0,0]
	v_mfma_scale_f32_16x16x128_f8f6f4 v[100:103], v[104:111], v[24:31], v[100:103], v158, v158 op_sel_hi:[0,0,0]
	v_mfma_scale_f32_16x16x128_f8f6f4 v[96:99], v[112:119], v[24:31], v[96:99], v158, v158 op_sel_hi:[0,0,0]
	v_mfma_scale_f32_16x16x128_f8f6f4 v[84:87], v[104:111], v[32:39], v[176:179], v158, v158 op_sel_hi:[0,0,0]
	v_mfma_scale_f32_16x16x128_f8f6f4 v[80:83], v[112:119], v[32:39], v[180:183], v158, v158 op_sel_hi:[0,0,0]
	v_mfma_scale_f32_16x16x128_f8f6f4 v[68:71], v[104:111], v[40:47], v[184:187], v158, v158 op_sel_hi:[0,0,0]
	v_mfma_scale_f32_16x16x128_f8f6f4 v[64:67], v[112:119], v[40:47], v[188:191], v158, v158 op_sel_hi:[0,0,0]
	s_setprio 0
	s_barrier
	ds_read_b128 v[32:35], v150 offset:49152
	ds_read_b128 v[36:39], v150 offset:49168
	ds_read_b128 v[160:163], v150 offset:51200
	ds_read_b128 v[164:167], v150 offset:51216
	ds_read_b128 v[168:171], v150 offset:53248
	ds_read_b128 v[172:175], v150 offset:53264
	ds_read_b128 v[176:179], v150 offset:55296
	ds_read_b128 v[180:183], v150 offset:55312
	s_add_u32 s50, s56, 0x80
	s_addc_u32 s51, s57, 0
	s_mov_b32 s58, m0
	s_mov_b32 m0, s69
	s_nop 0
	global_load_lds_dwordx4 v153, s[50:51]
	s_mov_b32 m0, s58
	s_nop 0
	s_mov_b32 s58, m0
	s_mov_b32 m0, s70
	s_nop 0
	global_load_lds_dwordx4 v155, s[50:51]
	s_mov_b32 m0, s58
	s_add_u32 s50, s56, 0x40080
	s_addc_u32 s51, s57, 0
	s_mov_b32 s56, m0
	s_mov_b32 m0, s73
	s_nop 0
	global_load_lds_dwordx4 v153, s[50:51]
	s_mov_b32 m0, s56
	s_nop 0
	s_mov_b32 s56, m0
	s_mov_b32 m0, s74
	s_nop 0
	global_load_lds_dwordx4 v155, s[50:51]
	s_mov_b32 m0, s56
	s_mov_b32 s50, m0
	s_mov_b32 m0, s71
	s_nop 0
	global_load_lds_dwordx4 v152, s[54:55]
	s_mov_b32 m0, s50
	s_nop 0
	s_mov_b32 s50, m0
	s_mov_b32 m0, s72
	s_nop 0
	global_load_lds_dwordx4 v154, s[54:55]
	s_mov_b32 m0, s50
	s_waitcnt vmcnt(8)
	s_waitcnt lgkmcnt(0)
	s_mov_b64 exec, 1
	ds_add_u32 v255, v255 offset:4096
	s_mov_b64 exec, -1
	s_setprio 1
	v_mfma_scale_f32_16x16x128_f8f6f4 v[60:63], v[0:7], v[32:39], v[60:63], v158, v158 op_sel_hi:[0,0,0]
	v_mfma_scale_f32_16x16x128_f8f6f4 v[56:59], v[16:23], v[32:39], v[56:59], v158, v158 op_sel_hi:[0,0,0]
	v_mfma_scale_f32_16x16x128_f8f6f4 v[44:47], v[0:7], v[160:167], v[192:195], v158, v158 op_sel_hi:[0,0,0]
	v_mfma_scale_f32_16x16x128_f8f6f4 v[40:43], v[16:23], v[160:167], v[196:199], v158, v158 op_sel_hi:[0,0,0]
	v_mfma_scale_f32_16x16x128_f8f6f4 v[28:31], v[0:7], v[168:175], v[200:203], v158, v158 op_sel_hi:[0,0,0]
	v_mfma_scale_f32_16x16x128_f8f6f4 v[24:27], v[16:23], v[168:175], v[204:207], v158, v158 op_sel_hi:[0,0,0]
	v_mfma_scale_f32_16x16x128_f8f6f4 v[12:15], v[0:7], v[176:183], v[224:227], v158, v158 op_sel_hi:[0,0,0]
	v_mfma_scale_f32_16x16x128_f8f6f4 v[8:11], v[16:23], v[176:183], v[228:231], v158, v158 op_sel_hi:[0,0,0]
	v_mfma_scale_f32_16x16x128_f8f6f4 v[52:55], v[104:111], v[32:39], v[52:55], v158, v158 op_sel_hi:[0,0,0]
	v_mfma_scale_f32_16x16x128_f8f6f4 v[48:51], v[112:119], v[32:39], v[48:51], v158, v158 op_sel_hi:[0,0,0]
	v_mfma_scale_f32_16x16x128_f8f6f4 v[36:39], v[104:111], v[160:167], v[232:235], v158, v158 op_sel_hi:[0,0,0]
	v_mfma_scale_f32_16x16x128_f8f6f4 v[32:35], v[112:119], v[160:167], v[236:239], v158, v158 op_sel_hi:[0,0,0]
	v_mfma_scale_f32_16x16x128_f8f6f4 v[20:23], v[104:111], v[168:175], v[240:243], v158, v158 op_sel_hi:[0,0,0]
	v_mfma_scale_f32_16x16x128_f8f6f4 v[16:19], v[112:119], v[168:175], v[244:247], v158, v158 op_sel_hi:[0,0,0]
	v_mfma_scale_f32_16x16x128_f8f6f4 v[4:7], v[104:111], v[176:183], v[248:251], v158, v158 op_sel_hi:[0,0,0]
	v_mfma_scale_f32_16x16x128_f8f6f4 v[0:3], v[112:119], v[176:183], v[144:147], v158, v158 op_sel_hi:[0,0,0]
	s_setprio 0
	s_barrier
	s_add_i32 s91, s91, 2
	s_add_u32 s89, s89, 0x100
	s_addc_u32 s90, s90, 0
	s_cmp_gt_u32 s91, 13
	s_mov_b64 s[50:51], s[52:53]
	s_cbranch_scc0 .LBB0_298
	s_branch .Lmy_ex_298
; #define PG8_STAGE(bufoff, gbase, voff) do { _Pragma("unroll") for (int _i = 0; _i < 2; ++_i) { unsigned keep_; \
;         asm volatile("s_mov_b32 %0, m0\n\ts_mov_b32 m0, %3\n\ts_nop 0\n\tglobal_load_lds_dwordx4 %1, %2\n\ts_mov_b32 m0, %0" : "=&s"(keep_) : "v"((voff)[_i]), "s"((const char*)(gbase)), "s"(ldsbase + (unsigned)((bufoff) + _i * 8192)) : "memory"); } } while (0)
; #define PG8_WAIT_V(n) asm volatile("s_waitcnt vmcnt(" #n ")" ::: "memory")
; #define PG8_WAIT_L(n) asm volatile("s_waitcnt lgkmcnt(" #n ")" ::: "memory")
; #define PG8_BAR __builtin_amdgcn_s_barrier()
; #define PG8_SCHED __builtin_amdgcn_sched_barrier(0)
; template <class Epi, class Sched, bool ALIGN_EPI, bool FP8 = false>
; DI void gemm_phase(LAS unsigned char* lds, const Gemm g, const Sched& S, const Epi& E) {
;     ...
;             PG8_LDB(B0, 0, 0); PG8_LDB(B1, 0, 1); PG8_SCHED; PG8_LDA(At, 0, 0); PG8_STAGE(PG8_SA(1, 1), a1 + hstepA, voffA);
;             PG8_WAIT_V(8); PG8_WAIT_L(0); PG8_BAR; PG8_MMA(0, 0, At, B0); PG8_MMA(0, 1, At, B1); PG8_BAR; PG8_SCHED;
.Lmy_g0_298:
	ds_read_b128 v[104:107], v151
	s_waitcnt vmcnt(8)
	ds_read_b128 v[108:111], v151 offset:16
	ds_read_b128 v[112:115], v151 offset:2048
	ds_read_b128 v[116:119], v151 offset:2064
	ds_read_b128 v[160:163], v151 offset:16384
	ds_read_b128 v[164:167], v151 offset:16400
	ds_read_b128 v[168:171], v151 offset:18432
	ds_read_b128 v[172:175], v151 offset:18448
	s_add_u32 s52, s50, 0x100
	s_addc_u32 s53, s51, 0
	s_cmp_eq_u32 s91, 12
	s_cselect_b32 s58, s87, s52
	s_cselect_b32 s59, s43, s53
	s_cselect_b32 s56, s88, s89
	s_cselect_b32 s57, s41, s90
	s_add_u32 s54, s58, 0x80
	s_addc_u32 s55, s59, 0
	ds_read_b128 v[176:179], v150
	ds_read_b128 v[180:183], v150 offset:16
	ds_read_b128 v[184:187], v150 offset:2048
	ds_read_b128 v[188:191], v150 offset:2064
	ds_read_b128 v[192:195], v150 offset:4096
	ds_read_b128 v[196:199], v150 offset:4112
	ds_read_b128 v[200:203], v150 offset:6144
	ds_read_b128 v[204:207], v150 offset:6160
	s_add_u32 s50, s50, 0x40080
	s_addc_u32 s51, s51, 0
	s_mov_b32 s92, m0
	s_mov_b32 m0, s75
	s_nop 0
	global_load_lds_dwordx4 v152, s[50:51]
	s_mov_b32 m0, s92
	s_nop 0
	s_mov_b32 s92, m0
	s_mov_b32 m0, s77
	s_nop 0
	global_load_lds_dwordx4 v154, s[50:51]
	s_mov_b32 m0, s92
	s_waitcnt vmcnt(8)
	s_waitcnt lgkmcnt(0)
	s_barrier
	s_setprio 1
	v_mfma_scale_f32_16x16x128_f8f6f4 v[140:143], v[104:111], v[176:183], v[140:143], v158, v158 op_sel_hi:[0,0,0]
	v_mfma_scale_f32_16x16x128_f8f6f4 v[136:139], v[112:119], v[176:183], v[136:139], v158, v158 op_sel_hi:[0,0,0]
	v_mfma_scale_f32_16x16x128_f8f6f4 v[124:127], v[104:111], v[184:191], v[124:127], v158, v158 op_sel_hi:[0,0,0]
	v_mfma_scale_f32_16x16x128_f8f6f4 v[120:123], v[112:119], v[184:191], v[120:123], v158, v158 op_sel_hi:[0,0,0]
	v_mfma_scale_f32_16x16x128_f8f6f4 v[208:211], v[104:111], v[192:199], v[92:95], v158, v158 op_sel_hi:[0,0,0]
	v_mfma_scale_f32_16x16x128_f8f6f4 v[212:215], v[112:119], v[192:199], v[88:91], v158, v158 op_sel_hi:[0,0,0]
	v_mfma_scale_f32_16x16x128_f8f6f4 v[216:219], v[104:111], v[200:207], v[76:79], v158, v158 op_sel_hi:[0,0,0]
	v_mfma_scale_f32_16x16x128_f8f6f4 v[220:223], v[112:119], v[200:207], v[72:75], v158, v158 op_sel_hi:[0,0,0]
	v_mfma_scale_f32_16x16x128_f8f6f4 v[132:135], v[160:167], v[176:183], v[132:135], v158, v158 op_sel_hi:[0,0,0]
	v_mfma_scale_f32_16x16x128_f8f6f4 v[128:131], v[168:175], v[176:183], v[128:131], v158, v158 op_sel_hi:[0,0,0]
	v_mfma_scale_f32_16x16x128_f8f6f4 v[100:103], v[160:167], v[184:191], v[100:103], v158, v158 op_sel_hi:[0,0,0]
	v_mfma_scale_f32_16x16x128_f8f6f4 v[96:99], v[168:175], v[184:191], v[96:99], v158, v158 op_sel_hi:[0,0,0]
	v_mfma_scale_f32_16x16x128_f8f6f4 v[176:179], v[160:167], v[192:199], v[84:87], v158, v158 op_sel_hi:[0,0,0]
	v_mfma_scale_f32_16x16x128_f8f6f4 v[180:183], v[168:175], v[192:199], v[80:83], v158, v158 op_sel_hi:[0,0,0]
	ds_read_b32 v255, v255 offset:4096
	v_mfma_scale_f32_16x16x128_f8f6f4 v[184:187], v[160:167], v[200:207], v[68:71], v158, v158 op_sel_hi:[0,0,0]
	v_mfma_scale_f32_16x16x128_f8f6f4 v[188:191], v[168:175], v[200:207], v[64:67], v158, v158 op_sel_hi:[0,0,0]
	s_add_u32 s98, s98, 0x80000
	s_waitcnt lgkmcnt(0)
	v_readfirstlane_b32 s101, v255
	v_mov_b32_e32 v255, 0x20000
	s_cmp_ge_u32 s101, s98
	s_cbranch_scc1 .Lmy_g_4

; #define PG8_STAGE(bufoff, gbase, voff) do { _Pragma("unroll") for (int _i = 0; _i < 2; ++_i) { unsigned keep_; \
;         asm volatile("s_mov_b32 %0, m0\n\ts_mov_b32 m0, %3\n\ts_nop 0\n\tglobal_load_lds_dwordx4 %1, %2\n\ts_mov_b32 m0, %0" : "=&s"(keep_) : "v"((voff)[_i]), "s"((const char*)(gbase)), "s"(ldsbase + (unsigned)((bufoff) + _i * 8192)) : "memory"); } } while (0)
; #define PG8_WAIT_V(n) asm volatile("s_waitcnt vmcnt(" #n ")" ::: "memory")
; #define PG8_WAIT_L(n) asm volatile("s_waitcnt lgkmcnt(" #n ")" ::: "memory")
; #define PG8_BAR __builtin_amdgcn_s_barrier()
; #define PG8_SCHED __builtin_amdgcn_sched_barrier(0)
; template <class Epi, class Sched, bool ALIGN_EPI, bool FP8 = false>
; DI void gemm_phase(LAS unsigned char* lds, const Gemm g, const Sched& S, const Epi& E) {
;     ...
;             PG8_LDA(At, 0, 1); PG8_STAGE(PG8_SB(0, 0), b2, voffB); PG8_STAGE(PG8_SB(0, 1), b2 + hstepB, voffB); PG8_STAGE(PG8_SA(0, 0), a2, voffA);
;             PG8_WAIT_V(8); PG8_WAIT_L(0); PG8_BAR; PG8_MMA(1, 0, At, B0); PG8_MMA(1, 1, At, B1); PG8_BAR; PG8_SCHED;
.Lmy_g_4:
	s_setprio 0
	s_nop 4
	ds_read_b128 v[64:67], v150 offset:16384
	ds_read_b128 v[68:71], v150 offset:16400
	ds_read_b128 v[72:75], v150 offset:18432
	ds_read_b128 v[76:79], v150 offset:18448
	ds_read_b128 v[80:83], v150 offset:20480
	ds_read_b128 v[84:87], v150 offset:20496
	ds_read_b128 v[88:91], v150 offset:22528
	ds_read_b128 v[92:95], v150 offset:22544
	s_mov_b32 s50, m0
	s_mov_b32 m0, s49
	s_nop 0
	global_load_lds_dwordx4 v153, s[56:57]
	s_mov_b32 m0, s50
	s_nop 0
	s_mov_b32 s50, m0
	s_mov_b32 m0, s63
	s_nop 0
	global_load_lds_dwordx4 v155, s[56:57]
	s_mov_b32 m0, s50
	s_add_u32 s50, s56, 0x40000
	s_addc_u32 s51, s57, 0
	s_mov_b32 s92, m0
	s_mov_b32 m0, s64
	s_nop 0
	global_load_lds_dwordx4 v153, s[50:51]
	s_mov_b32 m0, s92
	s_nop 0
	s_mov_b32 s92, m0
	s_mov_b32 m0, s65
	s_nop 0
	global_load_lds_dwordx4 v155, s[50:51]
	s_mov_b32 m0, s92
	s_mov_b32 s50, m0
	s_mov_b32 m0, s62
	s_nop 0
	global_load_lds_dwordx4 v152, s[58:59]
	s_mov_b32 m0, s50
	s_nop 0
	s_mov_b32 s50, m0
	s_mov_b32 m0, s66
	s_nop 0
	global_load_lds_dwordx4 v154, s[58:59]
	s_mov_b32 m0, s50
	s_waitcnt vmcnt(8)
	s_waitcnt lgkmcnt(0)
	s_barrier
	s_setprio 1
	v_mfma_scale_f32_16x16x128_f8f6f4 v[60:63], v[104:111], v[64:71], v[60:63], v158, v158 op_sel_hi:[0,0,0]
	v_mfma_scale_f32_16x16x128_f8f6f4 v[56:59], v[112:119], v[64:71], v[56:59], v158, v158 op_sel_hi:[0,0,0]
	v_mfma_scale_f32_16x16x128_f8f6f4 v[192:195], v[104:111], v[72:79], v[44:47], v158, v158 op_sel_hi:[0,0,0]
	v_mfma_scale_f32_16x16x128_f8f6f4 v[196:199], v[112:119], v[72:79], v[40:43], v158, v158 op_sel_hi:[0,0,0]
	v_mfma_scale_f32_16x16x128_f8f6f4 v[200:203], v[104:111], v[80:87], v[28:31], v158, v158 op_sel_hi:[0,0,0]
	v_mfma_scale_f32_16x16x128_f8f6f4 v[204:207], v[112:119], v[80:87], v[24:27], v158, v158 op_sel_hi:[0,0,0]
	v_mfma_scale_f32_16x16x128_f8f6f4 v[224:227], v[104:111], v[88:95], v[12:15], v158, v158 op_sel_hi:[0,0,0]
	v_mfma_scale_f32_16x16x128_f8f6f4 v[228:231], v[112:119], v[88:95], v[8:11], v158, v158 op_sel_hi:[0,0,0]
	v_mfma_scale_f32_16x16x128_f8f6f4 v[52:55], v[160:167], v[64:71], v[52:55], v158, v158 op_sel_hi:[0,0,0]
	v_mfma_scale_f32_16x16x128_f8f6f4 v[48:51], v[168:175], v[64:71], v[48:51], v158, v158 op_sel_hi:[0,0,0]
	v_mfma_scale_f32_16x16x128_f8f6f4 v[232:235], v[160:167], v[72:79], v[36:39], v158, v158 op_sel_hi:[0,0,0]
	v_mfma_scale_f32_16x16x128_f8f6f4 v[236:239], v[168:175], v[72:79], v[32:35], v158, v158 op_sel_hi:[0,0,0]
	v_mfma_scale_f32_16x16x128_f8f6f4 v[240:243], v[160:167], v[80:87], v[20:23], v158, v158 op_sel_hi:[0,0,0]
	v_mfma_scale_f32_16x16x128_f8f6f4 v[244:247], v[168:175], v[80:87], v[16:19], v158, v158 op_sel_hi:[0,0,0]
	ds_read_b32 v255, v255 offset:4096
	v_mfma_scale_f32_16x16x128_f8f6f4 v[248:251], v[160:167], v[88:95], v[4:7], v158, v158 op_sel_hi:[0,0,0]
	v_mfma_scale_f32_16x16x128_f8f6f4 v[144:147], v[168:175], v[88:95], v[0:3], v158, v158 op_sel_hi:[0,0,0]
	s_add_u32 s98, s98, 0x80000
	s_waitcnt lgkmcnt(0)
	v_readfirstlane_b32 s101, v255
	v_mov_b32_e32 v255, 0x20000
	s_cmp_ge_u32 s101, s98
	s_cbranch_scc1 .Lmy_g_5

; #define PG8_STAGE(bufoff, gbase, voff) do { _Pragma("unroll") for (int _i = 0; _i < 2; ++_i) { unsigned keep_; \
;         asm volatile("s_mov_b32 %0, m0\n\ts_mov_b32 m0, %3\n\ts_nop 0\n\tglobal_load_lds_dwordx4 %1, %2\n\ts_mov_b32 m0, %0" : "=&s"(keep_) : "v"((voff)[_i]), "s"((const char*)(gbase)), "s"(ldsbase + (unsigned)((bufoff) + _i * 8192)) : "memory"); } } while (0)
; #define PG8_WAIT_V(n) asm volatile("s_waitcnt vmcnt(" #n ")" ::: "memory")
; #define PG8_WAIT_L(n) asm volatile("s_waitcnt lgkmcnt(" #n ")" ::: "memory")
; #define PG8_BAR __builtin_amdgcn_s_barrier()
; #define PG8_SCHED __builtin_amdgcn_sched_barrier(0)
; template <class Epi, class Sched, bool ALIGN_EPI, bool FP8 = false>
; DI void gemm_phase(LAS unsigned char* lds, const Gemm g, const Sched& S, const Epi& E) {
;     ...
;             PG8_LDB(B0, 1, 0); PG8_LDB(B1, 1, 1); PG8_SCHED; PG8_LDA(At, 1, 0); PG8_STAGE(PG8_SA(0, 1), a2 + hstepA, voffA);
;             PG8_WAIT_V(8); PG8_WAIT_L(0); PG8_BAR; PG8_MMA(0, 0, At, B0); PG8_MMA(0, 1, At, B1); PG8_BAR; PG8_SCHED;
.Lmy_g_5:
	s_setprio 0
	s_nop 4
	ds_read_b128 v[0:3], v151 offset:32768
	ds_read_b128 v[4:7], v151 offset:32784
	ds_read_b128 v[16:19], v151 offset:34816
	ds_read_b128 v[20:23], v151 offset:34832
	ds_read_b128 v[104:107], v151 offset:49152
	ds_read_b128 v[108:111], v151 offset:49168
	ds_read_b128 v[112:115], v151 offset:51200
	ds_read_b128 v[116:119], v151 offset:51216
	ds_read_b128 v[8:11], v150 offset:32768
	ds_read_b128 v[12:15], v150 offset:32784
	ds_read_b128 v[24:27], v150 offset:34816
	ds_read_b128 v[28:31], v150 offset:34832
	ds_read_b128 v[32:35], v150 offset:36864
	ds_read_b128 v[36:39], v150 offset:36880
	ds_read_b128 v[40:43], v150 offset:38912
	ds_read_b128 v[44:47], v150 offset:38928
	s_add_u32 s50, s58, 0x40000
	s_addc_u32 s51, s59, 0
	s_mov_b32 s58, m0
	s_mov_b32 m0, s67
	s_nop 0
	global_load_lds_dwordx4 v152, s[50:51]
	s_mov_b32 m0, s58
	s_nop 0
	s_mov_b32 s58, m0
	s_mov_b32 m0, s68
	s_nop 0
	global_load_lds_dwordx4 v154, s[50:51]
	s_mov_b32 m0, s58
	s_waitcnt vmcnt(8)
	s_waitcnt lgkmcnt(0)
	s_barrier
	s_setprio 1
	v_mfma_scale_f32_16x16x128_f8f6f4 v[140:143], v[0:7], v[8:15], v[140:143], v158, v158 op_sel_hi:[0,0,0]
	v_mfma_scale_f32_16x16x128_f8f6f4 v[136:139], v[16:23], v[8:15], v[136:139], v158, v158 op_sel_hi:[0,0,0]
	v_mfma_scale_f32_16x16x128_f8f6f4 v[124:127], v[0:7], v[24:31], v[124:127], v158, v158 op_sel_hi:[0,0,0]
	v_mfma_scale_f32_16x16x128_f8f6f4 v[120:123], v[16:23], v[24:31], v[120:123], v158, v158 op_sel_hi:[0,0,0]
	v_mfma_scale_f32_16x16x128_f8f6f4 v[92:95], v[0:7], v[32:39], v[208:211], v158, v158 op_sel_hi:[0,0,0]
	v_mfma_scale_f32_16x16x128_f8f6f4 v[88:91], v[16:23], v[32:39], v[212:215], v158, v158 op_sel_hi:[0,0,0]
	v_mfma_scale_f32_16x16x128_f8f6f4 v[76:79], v[0:7], v[40:47], v[216:219], v158, v158 op_sel_hi:[0,0,0]
	v_mfma_scale_f32_16x16x128_f8f6f4 v[72:75], v[16:23], v[40:47], v[220:223], v158, v158 op_sel_hi:[0,0,0]
	v_mfma_scale_f32_16x16x128_f8f6f4 v[132:135], v[104:111], v[8:15], v[132:135], v158, v158 op_sel_hi:[0,0,0]
	v_mfma_scale_f32_16x16x128_f8f6f4 v[128:131], v[112:119], v[8:15], v[128:131], v158, v158 op_sel_hi:[0,0,0]
	v_mfma_scale_f32_16x16x128_f8f6f4 v[100:103], v[104:111], v[24:31], v[100:103], v158, v158 op_sel_hi:[0,0,0]
	v_mfma_scale_f32_16x16x128_f8f6f4 v[96:99], v[112:119], v[24:31], v[96:99], v158, v158 op_sel_hi:[0,0,0]
	v_mfma_scale_f32_16x16x128_f8f6f4 v[84:87], v[104:111], v[32:39], v[176:179], v158, v158 op_sel_hi:[0,0,0]
	v_mfma_scale_f32_16x16x128_f8f6f4 v[80:83], v[112:119], v[32:39], v[180:183], v158, v158 op_sel_hi:[0,0,0]
	ds_read_b32 v255, v255 offset:4096
	v_mfma_scale_f32_16x16x128_f8f6f4 v[68:71], v[104:111], v[40:47], v[184:187], v158, v158 op_sel_hi:[0,0,0]
	v_mfma_scale_f32_16x16x128_f8f6f4 v[64:67], v[112:119], v[40:47], v[188:191], v158, v158 op_sel_hi:[0,0,0]
	s_add_u32 s98, s98, 0x80000
	s_waitcnt lgkmcnt(0)
	v_readfirstlane_b32 s101, v255
	v_mov_b32_e32 v255, 0x20000
	s_cmp_ge_u32 s101, s98
	s_cbranch_scc1 .Lmy_g_6

; #define PG8_STAGE(bufoff, gbase, voff) do { _Pragma("unroll") for (int _i = 0; _i < 2; ++_i) { unsigned keep_; \
;         asm volatile("s_mov_b32 %0, m0\n\ts_mov_b32 m0, %3\n\ts_nop 0\n\tglobal_load_lds_dwordx4 %1, %2\n\ts_mov_b32 m0, %0" : "=&s"(keep_) : "v"((voff)[_i]), "s"((const char*)(gbase)), "s"(ldsbase + (unsigned)((bufoff) + _i * 8192)) : "memory"); } } while (0)
; #define PG8_WAIT_V(n) asm volatile("s_waitcnt vmcnt(" #n ")" ::: "memory")
; #define PG8_WAIT_L(n) asm volatile("s_waitcnt lgkmcnt(" #n ")" ::: "memory")
; #define PG8_BAR __builtin_amdgcn_s_barrier()
; #define PG8_SCHED __builtin_amdgcn_sched_barrier(0)
; template <class Epi, class Sched, bool ALIGN_EPI, bool FP8 = false>
; DI void gemm_phase(LAS unsigned char* lds, const Gemm g, const Sched& S, const Epi& E) {
;     ...
;             PG8_LDA(At, 1, 1); PG8_STAGE(PG8_SB(1, 0), b3, voffB); PG8_STAGE(PG8_SB(1, 1), b3 + hstepB, voffB); PG8_STAGE(PG8_SA(1, 0), a3, voffA);
;             PG8_WAIT_V(8); PG8_WAIT_L(0); PG8_BAR; PG8_MMA(1, 0, At, B0); PG8_MMA(1, 1, At, B1); PG8_BAR; PG8_SCHED;
.Lmy_g_6:
	s_setprio 0
	ds_read_b128 v[32:35], v150 offset:49152
	ds_read_b128 v[36:39], v150 offset:49168
	ds_read_b128 v[160:163], v150 offset:51200
	ds_read_b128 v[164:167], v150 offset:51216
	ds_read_b128 v[168:171], v150 offset:53248
	ds_read_b128 v[172:175], v150 offset:53264
	ds_read_b128 v[176:179], v150 offset:55296
	ds_read_b128 v[180:183], v150 offset:55312
	s_add_u32 s50, s56, 0x80
	s_addc_u32 s51, s57, 0
	s_mov_b32 s58, m0
	s_mov_b32 m0, s69
	s_nop 0
	global_load_lds_dwordx4 v153, s[50:51]
	s_mov_b32 m0, s58
	s_nop 0
	s_mov_b32 s58, m0
	s_mov_b32 m0, s70
	s_nop 0
	global_load_lds_dwordx4 v155, s[50:51]
	s_mov_b32 m0, s58
	s_add_u32 s50, s56, 0x40080
	s_addc_u32 s51, s57, 0
	s_mov_b32 s56, m0
	s_mov_b32 m0, s73
	s_nop 0
	global_load_lds_dwordx4 v153, s[50:51]
	s_mov_b32 m0, s56
	s_nop 0
	s_mov_b32 s56, m0
	s_mov_b32 m0, s74
	s_nop 0
	global_load_lds_dwordx4 v155, s[50:51]
	s_mov_b32 m0, s56
	s_mov_b32 s50, m0
	s_mov_b32 m0, s71
	s_nop 0
	global_load_lds_dwordx4 v152, s[54:55]
	s_mov_b32 m0, s50
	s_nop 0
	s_mov_b32 s50, m0
	s_mov_b32 m0, s72
	s_nop 0
	global_load_lds_dwordx4 v154, s[54:55]
	s_mov_b32 m0, s50
	s_waitcnt vmcnt(8)
	s_waitcnt lgkmcnt(0)
	s_barrier
	s_setprio 1
	v_mfma_scale_f32_16x16x128_f8f6f4 v[60:63], v[0:7], v[32:39], v[60:63], v158, v158 op_sel_hi:[0,0,0]
	v_mfma_scale_f32_16x16x128_f8f6f4 v[56:59], v[16:23], v[32:39], v[56:59], v158, v158 op_sel_hi:[0,0,0]
	v_mfma_scale_f32_16x16x128_f8f6f4 v[44:47], v[0:7], v[160:167], v[192:195], v158, v158 op_sel_hi:[0,0,0]
	v_mfma_scale_f32_16x16x128_f8f6f4 v[40:43], v[16:23], v[160:167], v[196:199], v158, v158 op_sel_hi:[0,0,0]
	v_mfma_scale_f32_16x16x128_f8f6f4 v[28:31], v[0:7], v[168:175], v[200:203], v158, v158 op_sel_hi:[0,0,0]
	v_mfma_scale_f32_16x16x128_f8f6f4 v[24:27], v[16:23], v[168:175], v[204:207], v158, v158 op_sel_hi:[0,0,0]
	v_mfma_scale_f32_16x16x128_f8f6f4 v[12:15], v[0:7], v[176:183], v[224:227], v158, v158 op_sel_hi:[0,0,0]
	v_mfma_scale_f32_16x16x128_f8f6f4 v[8:11], v[16:23], v[176:183], v[228:231], v158, v158 op_sel_hi:[0,0,0]
	v_mfma_scale_f32_16x16x128_f8f6f4 v[52:55], v[104:111], v[32:39], v[52:55], v158, v158 op_sel_hi:[0,0,0]
	v_mfma_scale_f32_16x16x128_f8f6f4 v[48:51], v[112:119], v[32:39], v[48:51], v158, v158 op_sel_hi:[0,0,0]
	v_mfma_scale_f32_16x16x128_f8f6f4 v[36:39], v[104:111], v[160:167], v[232:235], v158, v158 op_sel_hi:[0,0,0]
	v_mfma_scale_f32_16x16x128_f8f6f4 v[32:35], v[112:119], v[160:167], v[236:239], v158, v158 op_sel_hi:[0,0,0]
	v_mfma_scale_f32_16x16x128_f8f6f4 v[20:23], v[104:111], v[168:175], v[240:243], v158, v158 op_sel_hi:[0,0,0]
	v_mfma_scale_f32_16x16x128_f8f6f4 v[16:19], v[112:119], v[168:175], v[244:247], v158, v158 op_sel_hi:[0,0,0]
	ds_read_b32 v255, v255 offset:4096
	v_mfma_scale_f32_16x16x128_f8f6f4 v[4:7], v[104:111], v[176:183], v[248:251], v158, v158 op_sel_hi:[0,0,0]
	v_mfma_scale_f32_16x16x128_f8f6f4 v[0:3], v[112:119], v[176:183], v[144:147], v158, v158 op_sel_hi:[0,0,0]
	s_add_u32 s98, s98, 0x80000
	s_waitcnt lgkmcnt(0)
	v_readfirstlane_b32 s101, v255
	v_mov_b32_e32 v255, 0x20000
	s_cmp_ge_u32 s101, s98
	s_cbranch_scc1 .Lmy_g_7

; #define PG8_WAIT_V(n) asm volatile("s_waitcnt vmcnt(" #n ")" ::: "memory")
; #define PG8_WAIT_L(n) asm volatile("s_waitcnt lgkmcnt(" #n ")" ::: "memory")
; #define PG8_BAR __builtin_amdgcn_s_barrier()
; #define PG8_SCHED __builtin_amdgcn_sched_barrier(0)
; template <class Epi, class Sched, bool ALIGN_EPI, bool FP8 = false>
; DI void gemm_phase(LAS unsigned char* lds, const Gemm g, const Sched& S, const Epi& E) {
;     ...
;             PG8_WAIT_V(8); PG8_WAIT_L(0); PG8_BAR; PG8_MMA(1, 0, At, B0); PG8_MMA(1, 1, At, B1); PG8_BAR; PG8_SCHED;
;         }
;         if constexpr (ALIGN_EPI) { if (wr == 0) PG8_BAR; }
;         E(acc, cur, wr, wc, fr, fq);
.Lmy_g_7:
	s_setprio 0
	s_add_i32 s91, s91, 2
	s_add_u32 s89, s89, 0x100
	s_addc_u32 s90, s90, 0
	s_cmp_gt_u32 s91, 13
	s_mov_b64 s[50:51], s[52:53]
	s_cbranch_scc0 .Lmy_g0_298
.Lmy_ex_298:
	s_and_b64 vcc, exec, s[16:17]
	s_cbranch_vccz .LBB0_301
	s_barrier

; #define PG8_STAGE(bufoff, gbase, voff) do { _Pragma("unroll") for (int _i = 0; _i < 2; ++_i) { unsigned keep_; \
;         asm volatile("s_mov_b32 %0, m0\n\ts_mov_b32 m0, %3\n\ts_nop 0\n\tglobal_load_lds_dwordx4 %1, %2\n\ts_mov_b32 m0, %0" : "=&s"(keep_) : "v"((voff)[_i]), "s"((const char*)(gbase)), "s"(ldsbase + (unsigned)((bufoff) + _i * 8192)) : "memory"); } } while (0)
; #define PG8_WAIT_V(n) asm volatile("s_waitcnt vmcnt(" #n ")" ::: "memory")
; #define PG8_WAIT_L(n) asm volatile("s_waitcnt lgkmcnt(" #n ")" ::: "memory")
; #define PG8_BAR __builtin_amdgcn_s_barrier()
; #define PG8_SCHED __builtin_amdgcn_sched_barrier(0)
;     DI int nt(const Unit& u) const { return (u.aux & 8) ? PLED / 64 : ((u.aux & 4) ? (D_ / 2) / 64 : D_ / 64); }
; template <class Epi, class Sched, bool ALIGN_EPI, bool FP8 = false>
; DI void gemm_phase(LAS unsigned char* lds, const Gemm g, const Sched& S, const Epi& E) {
;     ...
;         for (int t = 0; t < nt; t += 2) {
;             if constexpr (Epi::MID) { if (t == (nt >> 1)) E.mid(acc, cur, wr, wc, fr, fq); }
;             const bool last = (t == nt - 2);
;             const char* a1 = cA + (size_t)(t + 1) * kstep;
;             const char* a2 = last ? nA : cA + (size_t)(t + 2) * kstep; const char* b2 = last ? nB : cB + (size_t)(t + 2) * kstep;
;             const char* a3 = a2 + kstep; const char* b3 = b2 + kstep;
;             PG8_LDB(B0, 0, 0); PG8_LDB(B1, 0, 1); PG8_SCHED; PG8_LDA(At, 0, 0); PG8_STAGE(PG8_SA(1, 1), a1 + hstepA, voffA);
;             PG8_WAIT_V(8); PG8_WAIT_L(0); PG8_BAR; PG8_MMA(0, 0, At, B0); PG8_MMA(0, 1, At, B1); PG8_BAR; PG8_SCHED;
;             PG8_LDA(At, 0, 1); PG8_STAGE(PG8_SB(0, 0), b2, voffB); PG8_STAGE(PG8_SB(0, 1), b2 + hstepB, voffB); PG8_STAGE(PG8_SA(0, 0), a2, voffA);
;             PG8_WAIT_V(8); PG8_WAIT_L(0); PG8_BAR; PG8_MMA(1, 0, At, B0); PG8_MMA(1, 1, At, B1); PG8_BAR; PG8_SCHED;
;             PG8_LDB(B0, 1, 0); PG8_LDB(B1, 1, 1); PG8_SCHED; PG8_LDA(At, 1, 0); PG8_STAGE(PG8_SA(0, 1), a2 + hstepA, voffA);
;             PG8_WAIT_V(8); PG8_WAIT_L(0); PG8_BAR; PG8_MMA(0, 0, At, B0); PG8_MMA(0, 1, At, B1); PG8_BAR; PG8_SCHED;
.LBB0_489:
	s_cmp_lg_u32 s99, 0
	s_cbranch_scc1 .Lmy_g0_489
	v_add_u32_e32 v1, 0x10000, v160
	ds_read_b128 v[132:135], v1
	ds_read_b128 v[136:139], v1 offset:1024
	ds_read_b128 v[140:143], v1 offset:2048
	ds_read_b128 v[162:165], v1 offset:3072
	v_add_u32_e32 v1, 0x14000, v160
	ds_read_b128 v[166:169], v1
	ds_read_b128 v[170:173], v1 offset:1024
	ds_read_b128 v[174:177], v1 offset:2048
	ds_read_b128 v[178:181], v1 offset:3072
	s_add_u32 s28, s26, 0x100
	s_addc_u32 s29, s27, 0
	s_cmp_eq_u32 s69, 28
	s_cselect_b32 s44, s65, s28
	s_cselect_b32 s45, s21, s29
	s_cselect_b32 s42, s66, s67
	s_cselect_b32 s43, s19, s68
	s_add_u32 s40, s44, 0x80
	s_addc_u32 s41, s45, 0
	ds_read_b128 v[182:185], v161
	ds_read_b128 v[186:189], v161 offset:1024
	ds_read_b128 v[190:193], v161 offset:2048
	ds_read_b128 v[194:197], v161 offset:3072
	ds_read_b128 v[198:201], v161 offset:4096
	ds_read_b128 v[202:205], v161 offset:5120
	ds_read_b128 v[206:209], v161 offset:6144
	ds_read_b128 v[210:213], v161 offset:7168
	s_add_u32 s26, s26, 0x80080
	s_addc_u32 s27, s27, 0
	s_mov_b32 s70, m0
	s_mov_b32 m0, s61
	s_nop 0
	global_load_lds_dwordx4 v154, s[26:27]
	s_mov_b32 m0, s70
	s_nop 0
	s_mov_b32 s70, m0
	s_mov_b32 m0, s62
	s_nop 0
	global_load_lds_dwordx4 v156, s[26:27]
	s_mov_b32 m0, s70
	s_waitcnt vmcnt(8)
	s_waitcnt lgkmcnt(0)
	s_mov_b64 exec, 1
	ds_add_u32 v255, v255 offset:4096
	s_mov_b64 exec, -1
	s_setprio 1
	v_mfma_f32_16x16x32_bf16 v[128:131], v[132:135], v[182:185], v[128:131]
	v_mfma_f32_16x16x32_bf16 v[124:127], v[140:143], v[182:185], v[124:127]
	v_mfma_f32_16x16x32_bf16 v[112:115], v[132:135], v[190:193], v[112:115]
	v_mfma_f32_16x16x32_bf16 v[108:111], v[140:143], v[190:193], v[108:111]
	v_mfma_f32_16x16x32_bf16 v[96:99], v[132:135], v[198:201], v[96:99]
	v_mfma_f32_16x16x32_bf16 v[92:95], v[140:143], v[198:201], v[92:95]
	v_mfma_f32_16x16x32_bf16 v[80:83], v[132:135], v[206:209], v[80:83]
	v_mfma_f32_16x16x32_bf16 v[76:79], v[140:143], v[206:209], v[76:79]
	v_mfma_f32_16x16x32_bf16 v[128:131], v[136:139], v[186:189], v[128:131]
	v_mfma_f32_16x16x32_bf16 v[124:127], v[162:165], v[186:189], v[124:127]
	v_mfma_f32_16x16x32_bf16 v[112:115], v[136:139], v[194:197], v[112:115]
	v_mfma_f32_16x16x32_bf16 v[108:111], v[162:165], v[194:197], v[108:111]
	v_mfma_f32_16x16x32_bf16 v[96:99], v[136:139], v[202:205], v[96:99]
	v_mfma_f32_16x16x32_bf16 v[92:95], v[162:165], v[202:205], v[92:95]
	v_mfma_f32_16x16x32_bf16 v[80:83], v[136:139], v[210:213], v[80:83]
	v_mfma_f32_16x16x32_bf16 v[76:79], v[162:165], v[210:213], v[76:79]
	v_mfma_f32_16x16x32_bf16 v[120:123], v[166:169], v[182:185], v[120:123]
	v_mfma_f32_16x16x32_bf16 v[116:119], v[174:177], v[182:185], v[116:119]
	v_mfma_f32_16x16x32_bf16 v[104:107], v[166:169], v[190:193], v[104:107]
	v_mfma_f32_16x16x32_bf16 v[100:103], v[174:177], v[190:193], v[100:103]
	v_mfma_f32_16x16x32_bf16 v[88:91], v[166:169], v[198:201], v[88:91]
	v_mfma_f32_16x16x32_bf16 v[84:87], v[174:177], v[198:201], v[84:87]
	v_mfma_f32_16x16x32_bf16 v[72:75], v[166:169], v[206:209], v[72:75]
	v_mfma_f32_16x16x32_bf16 v[68:71], v[174:177], v[206:209], v[68:71]
	v_mfma_f32_16x16x32_bf16 v[120:123], v[170:173], v[186:189], v[120:123]
	v_mfma_f32_16x16x32_bf16 v[116:119], v[178:181], v[186:189], v[116:119]
	v_mfma_f32_16x16x32_bf16 v[104:107], v[170:173], v[194:197], v[104:107]
	v_mfma_f32_16x16x32_bf16 v[100:103], v[178:181], v[194:197], v[100:103]
	v_mfma_f32_16x16x32_bf16 v[88:91], v[170:173], v[202:205], v[88:91]
	v_mfma_f32_16x16x32_bf16 v[84:87], v[178:181], v[202:205], v[84:87]
	v_mfma_f32_16x16x32_bf16 v[72:75], v[170:173], v[210:213], v[72:75]
	v_mfma_f32_16x16x32_bf16 v[68:71], v[178:181], v[210:213], v[68:71]
	s_setprio 0
	s_barrier
	ds_read_b128 v[182:185], v161 offset:16384
	ds_read_b128 v[186:189], v161 offset:17408
	ds_read_b128 v[190:193], v161 offset:18432
	ds_read_b128 v[194:197], v161 offset:19456
	ds_read_b128 v[198:201], v161 offset:20480
	ds_read_b128 v[202:205], v161 offset:21504
	ds_read_b128 v[206:209], v161 offset:22528
	ds_read_b128 v[210:213], v161 offset:23552
	s_mov_b32 s26, m0
	s_mov_b32 m0, s48
	s_nop 0
	global_load_lds_dwordx4 v155, s[42:43]
	s_mov_b32 m0, s26
	s_nop 0
	s_mov_b32 s26, m0
	s_mov_b32 m0, s49
	s_nop 0
	global_load_lds_dwordx4 v157, s[42:43]
	s_mov_b32 m0, s26
	s_add_u32 s26, s42, 0x80000
	s_addc_u32 s27, s43, 0
	s_mov_b32 s70, m0
	s_mov_b32 m0, s50
	s_nop 0
	global_load_lds_dwordx4 v155, s[26:27]
	s_mov_b32 m0, s70
	s_nop 0
	s_mov_b32 s70, m0
	s_mov_b32 m0, s51
	s_nop 0
	global_load_lds_dwordx4 v157, s[26:27]
	s_mov_b32 m0, s70
	s_mov_b32 s26, m0
	s_mov_b32 m0, s47
	s_nop 0
	global_load_lds_dwordx4 v154, s[44:45]
	s_mov_b32 m0, s26
	s_nop 0
	s_mov_b32 s26, m0
	s_mov_b32 m0, s52
	s_nop 0
	global_load_lds_dwordx4 v156, s[44:45]
	s_mov_b32 m0, s26
	s_waitcnt vmcnt(8)
	s_waitcnt lgkmcnt(0)
; #define PG8_STAGE(bufoff, gbase, voff) do { _Pragma("unroll") for (int _i = 0; _i < 2; ++_i) { unsigned keep_; \
;         asm volatile("s_mov_b32 %0, m0\n\ts_mov_b32 m0, %3\n\ts_nop 0\n\tglobal_load_lds_dwordx4 %1, %2\n\ts_mov_b32 m0, %0" : "=&s"(keep_) : "v"((voff)[_i]), "s"((const char*)(gbase)), "s"(ldsbase + (unsigned)((bufoff) + _i * 8192)) : "memory"); } } while (0)
; #define PG8_WAIT_V(n) asm volatile("s_waitcnt vmcnt(" #n ")" ::: "memory")
; #define PG8_WAIT_L(n) asm volatile("s_waitcnt lgkmcnt(" #n ")" ::: "memory")
; #define PG8_BAR __builtin_amdgcn_s_barrier()
; #define PG8_SCHED __builtin_amdgcn_sched_barrier(0)
; template <class Epi, class Sched, bool ALIGN_EPI, bool FP8 = false>
; DI void gemm_phase(LAS unsigned char* lds, const Gemm g, const Sched& S, const Epi& E) {
;     ...
;             PG8_WAIT_V(8); PG8_WAIT_L(0); PG8_BAR; PG8_MMA(0, 0, At, B0); PG8_MMA(0, 1, At, B1); PG8_BAR; PG8_SCHED;
;             PG8_LDA(At, 0, 1); PG8_STAGE(PG8_SB(0, 0), b2, voffB); PG8_STAGE(PG8_SB(0, 1), b2 + hstepB, voffB); PG8_STAGE(PG8_SA(0, 0), a2, voffA);
;             PG8_WAIT_V(8); PG8_WAIT_L(0); PG8_BAR; PG8_MMA(1, 0, At, B0); PG8_MMA(1, 1, At, B1); PG8_BAR; PG8_SCHED;
;             PG8_LDB(B0, 1, 0); PG8_LDB(B1, 1, 1); PG8_SCHED; PG8_LDA(At, 1, 0); PG8_STAGE(PG8_SA(0, 1), a2 + hstepA, voffA);
;             PG8_WAIT_V(8); PG8_WAIT_L(0); PG8_BAR; PG8_MMA(0, 0, At, B0); PG8_MMA(0, 1, At, B1); PG8_BAR; PG8_SCHED;
	s_mov_b64 exec, 1
	ds_add_u32 v255, v255 offset:4096
	s_mov_b64 exec, -1
	s_setprio 1
	v_mfma_f32_16x16x32_bf16 v[64:67], v[132:135], v[182:185], v[64:67]
	v_mfma_f32_16x16x32_bf16 v[60:63], v[140:143], v[182:185], v[60:63]
	v_mfma_f32_16x16x32_bf16 v[48:51], v[132:135], v[190:193], v[48:51]
	v_mfma_f32_16x16x32_bf16 v[44:47], v[140:143], v[190:193], v[44:47]
	v_mfma_f32_16x16x32_bf16 v[32:35], v[132:135], v[198:201], v[32:35]
	v_mfma_f32_16x16x32_bf16 v[28:31], v[140:143], v[198:201], v[28:31]
	v_mfma_f32_16x16x32_bf16 v[16:19], v[132:135], v[206:209], v[16:19]
	v_mfma_f32_16x16x32_bf16 v[12:15], v[140:143], v[206:209], v[12:15]
	v_mfma_f32_16x16x32_bf16 v[64:67], v[136:139], v[186:189], v[64:67]
	v_mfma_f32_16x16x32_bf16 v[60:63], v[162:165], v[186:189], v[60:63]
	v_mfma_f32_16x16x32_bf16 v[48:51], v[136:139], v[194:197], v[48:51]
	v_mfma_f32_16x16x32_bf16 v[44:47], v[162:165], v[194:197], v[44:47]
	v_mfma_f32_16x16x32_bf16 v[32:35], v[136:139], v[202:205], v[32:35]
	v_mfma_f32_16x16x32_bf16 v[28:31], v[162:165], v[202:205], v[28:31]
	v_mfma_f32_16x16x32_bf16 v[16:19], v[136:139], v[210:213], v[16:19]
	v_mfma_f32_16x16x32_bf16 v[12:15], v[162:165], v[210:213], v[12:15]
	v_mfma_f32_16x16x32_bf16 v[56:59], v[166:169], v[182:185], v[56:59]
	v_mfma_f32_16x16x32_bf16 v[52:55], v[174:177], v[182:185], v[52:55]
	v_mfma_f32_16x16x32_bf16 v[40:43], v[166:169], v[190:193], v[40:43]
	v_mfma_f32_16x16x32_bf16 v[36:39], v[174:177], v[190:193], v[36:39]
	v_mfma_f32_16x16x32_bf16 v[24:27], v[166:169], v[198:201], v[24:27]
	v_mfma_f32_16x16x32_bf16 v[20:23], v[174:177], v[198:201], v[20:23]
	v_mfma_f32_16x16x32_bf16 v[8:11], v[166:169], v[206:209], v[8:11]
	v_mfma_f32_16x16x32_bf16 v[2:5], v[174:177], v[206:209], v[4:7]
	v_mfma_f32_16x16x32_bf16 v[56:59], v[170:173], v[186:189], v[56:59]
	v_mfma_f32_16x16x32_bf16 v[52:55], v[178:181], v[186:189], v[52:55]
	v_mfma_f32_16x16x32_bf16 v[40:43], v[170:173], v[194:197], v[40:43]
	v_mfma_f32_16x16x32_bf16 v[36:39], v[178:181], v[194:197], v[36:39]
	v_mfma_f32_16x16x32_bf16 v[24:27], v[170:173], v[202:205], v[24:27]
	v_mfma_f32_16x16x32_bf16 v[20:23], v[178:181], v[202:205], v[20:23]
	v_mfma_f32_16x16x32_bf16 v[8:11], v[170:173], v[210:213], v[8:11]
	v_mfma_f32_16x16x32_bf16 v[2:5], v[178:181], v[210:213], v[2:5]
	s_setprio 0
	s_barrier
	v_add_u32_e32 v1, 0x18000, v160
	ds_read_b128 v[132:135], v1
	ds_read_b128 v[136:139], v1 offset:1024
	ds_read_b128 v[140:143], v1 offset:2048
	ds_read_b128 v[162:165], v1 offset:3072
	v_add_u32_e32 v1, 0x1c000, v160
	ds_read_b128 v[166:169], v1
	ds_read_b128 v[170:173], v1 offset:1024
	ds_read_b128 v[174:177], v1 offset:2048
	ds_read_b128 v[178:181], v1 offset:3072
	ds_read_b128 v[182:185], v161 offset:32768
	ds_read_b128 v[186:189], v161 offset:33792
	ds_read_b128 v[190:193], v161 offset:34816
	ds_read_b128 v[194:197], v161 offset:35840
	ds_read_b128 v[198:201], v161 offset:36864
	ds_read_b128 v[202:205], v161 offset:37888
	ds_read_b128 v[206:209], v161 offset:38912
	ds_read_b128 v[210:213], v161 offset:39936
	s_add_u32 s26, s44, 0x80000
	s_addc_u32 s27, s45, 0
	s_mov_b32 s44, m0
	s_mov_b32 m0, s53
	s_nop 0
	global_load_lds_dwordx4 v154, s[26:27]
	s_mov_b32 m0, s44
	s_nop 0
	s_mov_b32 s44, m0
	s_mov_b32 m0, s54
	s_nop 0
	global_load_lds_dwordx4 v156, s[26:27]
	s_mov_b32 m0, s44
	s_waitcnt vmcnt(8)
	s_waitcnt lgkmcnt(0)
	s_mov_b64 exec, 1
	ds_add_u32 v255, v255 offset:4096
	s_mov_b64 exec, -1
	s_setprio 1
	v_mfma_f32_16x16x32_bf16 v[128:131], v[132:135], v[182:185], v[128:131]
	v_mfma_f32_16x16x32_bf16 v[124:127], v[140:143], v[182:185], v[124:127]
	v_mfma_f32_16x16x32_bf16 v[112:115], v[132:135], v[190:193], v[112:115]
	v_mfma_f32_16x16x32_bf16 v[108:111], v[140:143], v[190:193], v[108:111]
	v_mfma_f32_16x16x32_bf16 v[96:99], v[132:135], v[198:201], v[96:99]
	v_mfma_f32_16x16x32_bf16 v[92:95], v[140:143], v[198:201], v[92:95]
	v_mfma_f32_16x16x32_bf16 v[80:83], v[132:135], v[206:209], v[80:83]
	v_mfma_f32_16x16x32_bf16 v[76:79], v[140:143], v[206:209], v[76:79]
	v_mfma_f32_16x16x32_bf16 v[128:131], v[136:139], v[186:189], v[128:131]
	v_mfma_f32_16x16x32_bf16 v[124:127], v[162:165], v[186:189], v[124:127]
	v_mfma_f32_16x16x32_bf16 v[112:115], v[136:139], v[194:197], v[112:115]
	v_mfma_f32_16x16x32_bf16 v[108:111], v[162:165], v[194:197], v[108:111]
	v_mfma_f32_16x16x32_bf16 v[96:99], v[136:139], v[202:205], v[96:99]
	v_mfma_f32_16x16x32_bf16 v[92:95], v[162:165], v[202:205], v[92:95]
	v_mfma_f32_16x16x32_bf16 v[80:83], v[136:139], v[210:213], v[80:83]
	v_mfma_f32_16x16x32_bf16 v[76:79], v[162:165], v[210:213], v[76:79]
	v_mfma_f32_16x16x32_bf16 v[120:123], v[166:169], v[182:185], v[120:123]
	v_mfma_f32_16x16x32_bf16 v[116:119], v[174:177], v[182:185], v[116:119]
	v_mfma_f32_16x16x32_bf16 v[104:107], v[166:169], v[190:193], v[104:107]
	v_mfma_f32_16x16x32_bf16 v[100:103], v[174:177], v[190:193], v[100:103]
	v_mfma_f32_16x16x32_bf16 v[88:91], v[166:169], v[198:201], v[88:91]
	v_mfma_f32_16x16x32_bf16 v[84:87], v[174:177], v[198:201], v[84:87]
	v_mfma_f32_16x16x32_bf16 v[72:75], v[166:169], v[206:209], v[72:75]
	v_mfma_f32_16x16x32_bf16 v[68:71], v[174:177], v[206:209], v[68:71]
	v_mfma_f32_16x16x32_bf16 v[120:123], v[170:173], v[186:189], v[120:123]
	v_mfma_f32_16x16x32_bf16 v[116:119], v[178:181], v[186:189], v[116:119]
	v_mfma_f32_16x16x32_bf16 v[104:107], v[170:173], v[194:197], v[104:107]
	v_mfma_f32_16x16x32_bf16 v[100:103], v[178:181], v[194:197], v[100:103]
	v_mfma_f32_16x16x32_bf16 v[88:91], v[170:173], v[202:205], v[88:91]
	v_mfma_f32_16x16x32_bf16 v[84:87], v[178:181], v[202:205], v[84:87]
	v_mfma_f32_16x16x32_bf16 v[72:75], v[170:173], v[210:213], v[72:75]
	v_mfma_f32_16x16x32_bf16 v[68:71], v[178:181], v[210:213], v[68:71]
	s_setprio 0
	s_barrier
; #define PG8_STAGE(bufoff, gbase, voff) do { _Pragma("unroll") for (int _i = 0; _i < 2; ++_i) { unsigned keep_; \
;         asm volatile("s_mov_b32 %0, m0\n\ts_mov_b32 m0, %3\n\ts_nop 0\n\tglobal_load_lds_dwordx4 %1, %2\n\ts_mov_b32 m0, %0" : "=&s"(keep_) : "v"((voff)[_i]), "s"((const char*)(gbase)), "s"(ldsbase + (unsigned)((bufoff) + _i * 8192)) : "memory"); } } while (0)
; #define PG8_WAIT_V(n) asm volatile("s_waitcnt vmcnt(" #n ")" ::: "memory")
; #define PG8_WAIT_L(n) asm volatile("s_waitcnt lgkmcnt(" #n ")" ::: "memory")
; #define PG8_BAR __builtin_amdgcn_s_barrier()
; #define PG8_SCHED __builtin_amdgcn_sched_barrier(0)
;     DI int nt(const Unit& u) const { return (u.aux & 8) ? PLED / 64 : ((u.aux & 4) ? (D_ / 2) / 64 : D_ / 64); }
; template <class Epi, class Sched, bool ALIGN_EPI, bool FP8 = false>
; DI void gemm_phase(LAS unsigned char* lds, const Gemm g, const Sched& S, const Epi& E) {
;     ...
;         for (int t = 0; t < nt; t += 2) {
;             if constexpr (Epi::MID) { if (t == (nt >> 1)) E.mid(acc, cur, wr, wc, fr, fq); }
;     ...
;             PG8_LDA(At, 1, 1); PG8_STAGE(PG8_SB(1, 0), b3, voffB); PG8_STAGE(PG8_SB(1, 1), b3 + hstepB, voffB); PG8_STAGE(PG8_SA(1, 0), a3, voffA);
;             PG8_WAIT_V(8); PG8_WAIT_L(0); PG8_BAR; PG8_MMA(1, 0, At, B0); PG8_MMA(1, 1, At, B1); PG8_BAR; PG8_SCHED;
	ds_read_b128 v[182:185], v161 offset:49152
	ds_read_b128 v[186:189], v161 offset:50176
	ds_read_b128 v[190:193], v161 offset:51200
	ds_read_b128 v[194:197], v161 offset:52224
	ds_read_b128 v[198:201], v161 offset:53248
	ds_read_b128 v[202:205], v161 offset:54272
	ds_read_b128 v[206:209], v161 offset:55296
	ds_read_b128 v[210:213], v161 offset:56320
	s_add_u32 s26, s42, 0x80
	s_addc_u32 s27, s43, 0
	s_mov_b32 s44, m0
	s_mov_b32 m0, s55
	s_nop 0
	global_load_lds_dwordx4 v155, s[26:27]
	s_mov_b32 m0, s44
	s_nop 0
	s_mov_b32 s44, m0
	s_mov_b32 m0, s56
	s_nop 0
	global_load_lds_dwordx4 v157, s[26:27]
	s_mov_b32 m0, s44
	s_add_u32 s26, s42, 0x80080
	s_addc_u32 s27, s43, 0
	s_mov_b32 s42, m0
	s_mov_b32 m0, s59
	s_nop 0
	global_load_lds_dwordx4 v155, s[26:27]
	s_mov_b32 m0, s42
	s_nop 0
	s_mov_b32 s42, m0
	s_mov_b32 m0, s60
	s_nop 0
	global_load_lds_dwordx4 v157, s[26:27]
	s_mov_b32 m0, s42
	s_mov_b32 s26, m0
	s_mov_b32 m0, s57
	s_nop 0
	global_load_lds_dwordx4 v154, s[40:41]
	s_mov_b32 m0, s26
	s_nop 0
	s_mov_b32 s26, m0
	s_mov_b32 m0, s58
	s_nop 0
	global_load_lds_dwordx4 v156, s[40:41]
	s_mov_b32 m0, s26
	s_waitcnt vmcnt(8)
	s_waitcnt lgkmcnt(0)
	s_mov_b64 exec, 1
	ds_add_u32 v255, v255 offset:4096
	s_mov_b64 exec, -1
	s_setprio 1
	v_mfma_f32_16x16x32_bf16 v[64:67], v[132:135], v[182:185], v[64:67]
	v_mfma_f32_16x16x32_bf16 v[60:63], v[140:143], v[182:185], v[60:63]
	v_mfma_f32_16x16x32_bf16 v[48:51], v[132:135], v[190:193], v[48:51]
	v_mfma_f32_16x16x32_bf16 v[44:47], v[140:143], v[190:193], v[44:47]
	v_mfma_f32_16x16x32_bf16 v[32:35], v[132:135], v[198:201], v[32:35]
	v_mfma_f32_16x16x32_bf16 v[28:31], v[140:143], v[198:201], v[28:31]
	v_mfma_f32_16x16x32_bf16 v[16:19], v[132:135], v[206:209], v[16:19]
	v_mfma_f32_16x16x32_bf16 v[12:15], v[140:143], v[206:209], v[12:15]
	v_mfma_f32_16x16x32_bf16 v[64:67], v[136:139], v[186:189], v[64:67]
	v_mfma_f32_16x16x32_bf16 v[60:63], v[162:165], v[186:189], v[60:63]
	v_mfma_f32_16x16x32_bf16 v[48:51], v[136:139], v[194:197], v[48:51]
	v_mfma_f32_16x16x32_bf16 v[44:47], v[162:165], v[194:197], v[44:47]
	v_mfma_f32_16x16x32_bf16 v[32:35], v[136:139], v[202:205], v[32:35]
	v_mfma_f32_16x16x32_bf16 v[28:31], v[162:165], v[202:205], v[28:31]
	v_mfma_f32_16x16x32_bf16 v[16:19], v[136:139], v[210:213], v[16:19]
	v_mfma_f32_16x16x32_bf16 v[12:15], v[162:165], v[210:213], v[12:15]
	v_mfma_f32_16x16x32_bf16 v[56:59], v[166:169], v[182:185], v[56:59]
	v_mfma_f32_16x16x32_bf16 v[52:55], v[174:177], v[182:185], v[52:55]
	v_mfma_f32_16x16x32_bf16 v[40:43], v[166:169], v[190:193], v[40:43]
	v_mfma_f32_16x16x32_bf16 v[36:39], v[174:177], v[190:193], v[36:39]
	v_mfma_f32_16x16x32_bf16 v[24:27], v[166:169], v[198:201], v[24:27]
	v_mfma_f32_16x16x32_bf16 v[20:23], v[174:177], v[198:201], v[20:23]
	v_mfma_f32_16x16x32_bf16 v[6:9], v[166:169], v[206:209], v[8:11]
	v_mfma_f32_16x16x32_bf16 v[2:5], v[174:177], v[206:209], v[2:5]
	v_mfma_f32_16x16x32_bf16 v[56:59], v[170:173], v[186:189], v[56:59]
	v_mfma_f32_16x16x32_bf16 v[52:55], v[178:181], v[186:189], v[52:55]
	v_mfma_f32_16x16x32_bf16 v[40:43], v[170:173], v[194:197], v[40:43]
	v_mfma_f32_16x16x32_bf16 v[36:39], v[178:181], v[194:197], v[36:39]
	v_mfma_f32_16x16x32_bf16 v[24:27], v[170:173], v[202:205], v[24:27]
	v_mfma_f32_16x16x32_bf16 v[20:23], v[178:181], v[202:205], v[20:23]
	v_mfma_f32_16x16x32_bf16 v[8:11], v[170:173], v[210:213], v[6:9]
	v_mfma_f32_16x16x32_bf16 v[4:7], v[178:181], v[210:213], v[2:5]
	s_setprio 0
	s_barrier
	s_add_i32 s69, s69, 2
	s_add_u32 s67, s67, 0x100
	s_addc_u32 s68, s68, 0
	s_cmp_gt_u32 s69, 29
	s_cbranch_scc1 .LBB0_491
	s_mov_b64 s[26:27], s[28:29]
	s_cmp_lg_u32 s69, 14
	s_cbranch_scc0 .LBB0_488
	s_branch .LBB0_489
; #define PG8_STAGE(bufoff, gbase, voff) do { _Pragma("unroll") for (int _i = 0; _i < 2; ++_i) { unsigned keep_; \
;         asm volatile("s_mov_b32 %0, m0\n\ts_mov_b32 m0, %3\n\ts_nop 0\n\tglobal_load_lds_dwordx4 %1, %2\n\ts_mov_b32 m0, %0" : "=&s"(keep_) : "v"((voff)[_i]), "s"((const char*)(gbase)), "s"(ldsbase + (unsigned)((bufoff) + _i * 8192)) : "memory"); } } while (0)
; #define PG8_WAIT_V(n) asm volatile("s_waitcnt vmcnt(" #n ")" ::: "memory")
; #define PG8_WAIT_L(n) asm volatile("s_waitcnt lgkmcnt(" #n ")" ::: "memory")
; #define PG8_BAR __builtin_amdgcn_s_barrier()
; #define PG8_SCHED __builtin_amdgcn_sched_barrier(0)
;     DI int nt(const Unit& u) const { return (u.aux & 8) ? PLED / 64 : ((u.aux & 4) ? (D_ / 2) / 64 : D_ / 64); }
; template <class Epi, class Sched, bool ALIGN_EPI, bool FP8 = false>
; DI void gemm_phase(LAS unsigned char* lds, const Gemm g, const Sched& S, const Epi& E) {
;     ...
;             const bool last = (t == nt - 2);
;             const char* a1 = cA + (size_t)(t + 1) * kstep;
;             const char* a2 = last ? nA : cA + (size_t)(t + 2) * kstep; const char* b2 = last ? nB : cB + (size_t)(t + 2) * kstep;
;             const char* a3 = a2 + kstep; const char* b3 = b2 + kstep;
;             PG8_LDB(B0, 0, 0); PG8_LDB(B1, 0, 1); PG8_SCHED; PG8_LDA(At, 0, 0); PG8_STAGE(PG8_SA(1, 1), a1 + hstepA, voffA);
;             PG8_WAIT_V(8); PG8_WAIT_L(0); PG8_BAR; PG8_MMA(0, 0, At, B0); PG8_MMA(0, 1, At, B1); PG8_BAR; PG8_SCHED;
.Lmy_g0_489:
	v_add_u32_e32 v1, 0x10000, v160
	ds_read_b128 v[132:135], v1
	ds_read_b128 v[136:139], v1 offset:1024
	ds_read_b128 v[140:143], v1 offset:2048
	ds_read_b128 v[162:165], v1 offset:3072
	v_add_u32_e32 v1, 0x14000, v160
	ds_read_b128 v[166:169], v1
	ds_read_b128 v[170:173], v1 offset:1024
	ds_read_b128 v[174:177], v1 offset:2048
	ds_read_b128 v[178:181], v1 offset:3072
	s_add_u32 s28, s26, 0x100
	s_addc_u32 s29, s27, 0
	s_cmp_eq_u32 s69, 28
	s_cselect_b32 s44, s65, s28
	s_cselect_b32 s45, s21, s29
	s_cselect_b32 s42, s66, s67
	s_cselect_b32 s43, s19, s68
	s_add_u32 s40, s44, 0x80
	s_addc_u32 s41, s45, 0
	ds_read_b128 v[182:185], v161
	ds_read_b128 v[186:189], v161 offset:1024
	ds_read_b128 v[190:193], v161 offset:2048
	ds_read_b128 v[194:197], v161 offset:3072
	ds_read_b128 v[198:201], v161 offset:4096
	ds_read_b128 v[202:205], v161 offset:5120
	ds_read_b128 v[206:209], v161 offset:6144
	ds_read_b128 v[210:213], v161 offset:7168
	s_add_u32 s26, s26, 0x80080
	s_addc_u32 s27, s27, 0
	s_mov_b32 s70, m0
	s_mov_b32 m0, s61
	s_nop 0
	global_load_lds_dwordx4 v154, s[26:27]
	s_mov_b32 m0, s70
	s_nop 0
	s_mov_b32 s70, m0
	s_mov_b32 m0, s62
	s_nop 0
	global_load_lds_dwordx4 v156, s[26:27]
	s_mov_b32 m0, s70
	s_waitcnt vmcnt(8)
	s_waitcnt lgkmcnt(0)
	s_barrier
	s_setprio 1
	v_mfma_f32_16x16x32_bf16 v[128:131], v[132:135], v[182:185], v[128:131]
	v_mfma_f32_16x16x32_bf16 v[124:127], v[140:143], v[182:185], v[124:127]
	v_mfma_f32_16x16x32_bf16 v[112:115], v[132:135], v[190:193], v[112:115]
	v_mfma_f32_16x16x32_bf16 v[108:111], v[140:143], v[190:193], v[108:111]
	v_mfma_f32_16x16x32_bf16 v[96:99], v[132:135], v[198:201], v[96:99]
	v_mfma_f32_16x16x32_bf16 v[92:95], v[140:143], v[198:201], v[92:95]
	v_mfma_f32_16x16x32_bf16 v[80:83], v[132:135], v[206:209], v[80:83]
	v_mfma_f32_16x16x32_bf16 v[76:79], v[140:143], v[206:209], v[76:79]
	v_mfma_f32_16x16x32_bf16 v[128:131], v[136:139], v[186:189], v[128:131]
	v_mfma_f32_16x16x32_bf16 v[124:127], v[162:165], v[186:189], v[124:127]
	v_mfma_f32_16x16x32_bf16 v[112:115], v[136:139], v[194:197], v[112:115]
	v_mfma_f32_16x16x32_bf16 v[108:111], v[162:165], v[194:197], v[108:111]
	v_mfma_f32_16x16x32_bf16 v[96:99], v[136:139], v[202:205], v[96:99]
	v_mfma_f32_16x16x32_bf16 v[92:95], v[162:165], v[202:205], v[92:95]
	v_mfma_f32_16x16x32_bf16 v[80:83], v[136:139], v[210:213], v[80:83]
	v_mfma_f32_16x16x32_bf16 v[76:79], v[162:165], v[210:213], v[76:79]
	v_mfma_f32_16x16x32_bf16 v[120:123], v[166:169], v[182:185], v[120:123]
	v_mfma_f32_16x16x32_bf16 v[116:119], v[174:177], v[182:185], v[116:119]
	v_mfma_f32_16x16x32_bf16 v[104:107], v[166:169], v[190:193], v[104:107]
	v_mfma_f32_16x16x32_bf16 v[100:103], v[174:177], v[190:193], v[100:103]
	v_mfma_f32_16x16x32_bf16 v[88:91], v[166:169], v[198:201], v[88:91]
	v_mfma_f32_16x16x32_bf16 v[84:87], v[174:177], v[198:201], v[84:87]
	v_mfma_f32_16x16x32_bf16 v[72:75], v[166:169], v[206:209], v[72:75]
	v_mfma_f32_16x16x32_bf16 v[68:71], v[174:177], v[206:209], v[68:71]
	v_mfma_f32_16x16x32_bf16 v[120:123], v[170:173], v[186:189], v[120:123]
	v_mfma_f32_16x16x32_bf16 v[116:119], v[178:181], v[186:189], v[116:119]
	v_mfma_f32_16x16x32_bf16 v[104:107], v[170:173], v[194:197], v[104:107]
	v_mfma_f32_16x16x32_bf16 v[100:103], v[178:181], v[194:197], v[100:103]
	ds_read_b32 v255, v255 offset:4096
	v_mfma_f32_16x16x32_bf16 v[88:91], v[170:173], v[202:205], v[88:91]
	v_mfma_f32_16x16x32_bf16 v[84:87], v[178:181], v[202:205], v[84:87]
	v_mfma_f32_16x16x32_bf16 v[72:75], v[170:173], v[210:213], v[72:75]
	v_mfma_f32_16x16x32_bf16 v[68:71], v[178:181], v[210:213], v[68:71]
	s_add_u32 s98, s98, 0x80000
	s_waitcnt lgkmcnt(0)
	v_readfirstlane_b32 s101, v255
	v_mov_b32_e32 v255, 0x20000
	s_cmp_ge_u32 s101, s98
	s_cbranch_scc1 .Lmy_g_8

; #define PG8_STAGE(bufoff, gbase, voff) do { _Pragma("unroll") for (int _i = 0; _i < 2; ++_i) { unsigned keep_; \
;         asm volatile("s_mov_b32 %0, m0\n\ts_mov_b32 m0, %3\n\ts_nop 0\n\tglobal_load_lds_dwordx4 %1, %2\n\ts_mov_b32 m0, %0" : "=&s"(keep_) : "v"((voff)[_i]), "s"((const char*)(gbase)), "s"(ldsbase + (unsigned)((bufoff) + _i * 8192)) : "memory"); } } while (0)
; #define PG8_WAIT_V(n) asm volatile("s_waitcnt vmcnt(" #n ")" ::: "memory")
; #define PG8_WAIT_L(n) asm volatile("s_waitcnt lgkmcnt(" #n ")" ::: "memory")
; #define PG8_BAR __builtin_amdgcn_s_barrier()
; #define PG8_SCHED __builtin_amdgcn_sched_barrier(0)
; template <class Epi, class Sched, bool ALIGN_EPI, bool FP8 = false>
; DI void gemm_phase(LAS unsigned char* lds, const Gemm g, const Sched& S, const Epi& E) {
;     ...
;             PG8_LDA(At, 0, 1); PG8_STAGE(PG8_SB(0, 0), b2, voffB); PG8_STAGE(PG8_SB(0, 1), b2 + hstepB, voffB); PG8_STAGE(PG8_SA(0, 0), a2, voffA);
;             PG8_WAIT_V(8); PG8_WAIT_L(0); PG8_BAR; PG8_MMA(1, 0, At, B0); PG8_MMA(1, 1, At, B1); PG8_BAR; PG8_SCHED;
.Lmy_g_8:
	s_setprio 0
	ds_read_b128 v[182:185], v161 offset:16384
	ds_read_b128 v[186:189], v161 offset:17408
	ds_read_b128 v[190:193], v161 offset:18432
	ds_read_b128 v[194:197], v161 offset:19456
	ds_read_b128 v[198:201], v161 offset:20480
	ds_read_b128 v[202:205], v161 offset:21504
	ds_read_b128 v[206:209], v161 offset:22528
	ds_read_b128 v[210:213], v161 offset:23552
	s_mov_b32 s26, m0
	s_mov_b32 m0, s48
	s_nop 0
	global_load_lds_dwordx4 v155, s[42:43]
	s_mov_b32 m0, s26
	s_nop 0
	s_mov_b32 s26, m0
	s_mov_b32 m0, s49
	s_nop 0
	global_load_lds_dwordx4 v157, s[42:43]
	s_mov_b32 m0, s26
	s_add_u32 s26, s42, 0x80000
	s_addc_u32 s27, s43, 0
	s_mov_b32 s70, m0
	s_mov_b32 m0, s50
	s_nop 0
	global_load_lds_dwordx4 v155, s[26:27]
	s_mov_b32 m0, s70
	s_nop 0
	s_mov_b32 s70, m0
	s_mov_b32 m0, s51
	s_nop 0
	global_load_lds_dwordx4 v157, s[26:27]
	s_mov_b32 m0, s70
	s_mov_b32 s26, m0
	s_mov_b32 m0, s47
	s_nop 0
	global_load_lds_dwordx4 v154, s[44:45]
	s_mov_b32 m0, s26
	s_nop 0
	s_mov_b32 s26, m0
	s_mov_b32 m0, s52
	s_nop 0
	global_load_lds_dwordx4 v156, s[44:45]
	s_mov_b32 m0, s26
	s_waitcnt vmcnt(8)
	s_waitcnt lgkmcnt(0)
	s_barrier
	s_setprio 1
	v_mfma_f32_16x16x32_bf16 v[64:67], v[132:135], v[182:185], v[64:67]
	v_mfma_f32_16x16x32_bf16 v[60:63], v[140:143], v[182:185], v[60:63]
	v_mfma_f32_16x16x32_bf16 v[48:51], v[132:135], v[190:193], v[48:51]
	v_mfma_f32_16x16x32_bf16 v[44:47], v[140:143], v[190:193], v[44:47]
	v_mfma_f32_16x16x32_bf16 v[32:35], v[132:135], v[198:201], v[32:35]
	v_mfma_f32_16x16x32_bf16 v[28:31], v[140:143], v[198:201], v[28:31]
	v_mfma_f32_16x16x32_bf16 v[16:19], v[132:135], v[206:209], v[16:19]
	v_mfma_f32_16x16x32_bf16 v[12:15], v[140:143], v[206:209], v[12:15]
	v_mfma_f32_16x16x32_bf16 v[64:67], v[136:139], v[186:189], v[64:67]
	v_mfma_f32_16x16x32_bf16 v[60:63], v[162:165], v[186:189], v[60:63]
	v_mfma_f32_16x16x32_bf16 v[48:51], v[136:139], v[194:197], v[48:51]
	v_mfma_f32_16x16x32_bf16 v[44:47], v[162:165], v[194:197], v[44:47]
	v_mfma_f32_16x16x32_bf16 v[32:35], v[136:139], v[202:205], v[32:35]
	v_mfma_f32_16x16x32_bf16 v[28:31], v[162:165], v[202:205], v[28:31]
	v_mfma_f32_16x16x32_bf16 v[16:19], v[136:139], v[210:213], v[16:19]
	v_mfma_f32_16x16x32_bf16 v[12:15], v[162:165], v[210:213], v[12:15]
	v_mfma_f32_16x16x32_bf16 v[56:59], v[166:169], v[182:185], v[56:59]
	v_mfma_f32_16x16x32_bf16 v[52:55], v[174:177], v[182:185], v[52:55]
	v_mfma_f32_16x16x32_bf16 v[40:43], v[166:169], v[190:193], v[40:43]
	v_mfma_f32_16x16x32_bf16 v[36:39], v[174:177], v[190:193], v[36:39]
	v_mfma_f32_16x16x32_bf16 v[24:27], v[166:169], v[198:201], v[24:27]
	v_mfma_f32_16x16x32_bf16 v[20:23], v[174:177], v[198:201], v[20:23]
	v_mfma_f32_16x16x32_bf16 v[8:11], v[166:169], v[206:209], v[8:11]
	v_mfma_f32_16x16x32_bf16 v[2:5], v[174:177], v[206:209], v[4:7]
	v_mfma_f32_16x16x32_bf16 v[56:59], v[170:173], v[186:189], v[56:59]
	v_mfma_f32_16x16x32_bf16 v[52:55], v[178:181], v[186:189], v[52:55]
	v_mfma_f32_16x16x32_bf16 v[40:43], v[170:173], v[194:197], v[40:43]
	v_mfma_f32_16x16x32_bf16 v[36:39], v[178:181], v[194:197], v[36:39]
	ds_read_b32 v255, v255 offset:4096
	v_mfma_f32_16x16x32_bf16 v[24:27], v[170:173], v[202:205], v[24:27]
	v_mfma_f32_16x16x32_bf16 v[20:23], v[178:181], v[202:205], v[20:23]
	v_mfma_f32_16x16x32_bf16 v[8:11], v[170:173], v[210:213], v[8:11]
	v_mfma_f32_16x16x32_bf16 v[2:5], v[178:181], v[210:213], v[2:5]
	s_add_u32 s98, s98, 0x80000
	s_waitcnt lgkmcnt(0)
	v_readfirstlane_b32 s101, v255
	v_mov_b32_e32 v255, 0x20000
	s_cmp_ge_u32 s101, s98
	s_cbranch_scc1 .Lmy_g_9

; #define PG8_STAGE(bufoff, gbase, voff) do { _Pragma("unroll") for (int _i = 0; _i < 2; ++_i) { unsigned keep_; \
;         asm volatile("s_mov_b32 %0, m0\n\ts_mov_b32 m0, %3\n\ts_nop 0\n\tglobal_load_lds_dwordx4 %1, %2\n\ts_mov_b32 m0, %0" : "=&s"(keep_) : "v"((voff)[_i]), "s"((const char*)(gbase)), "s"(ldsbase + (unsigned)((bufoff) + _i * 8192)) : "memory"); } } while (0)
; #define PG8_WAIT_V(n) asm volatile("s_waitcnt vmcnt(" #n ")" ::: "memory")
; #define PG8_WAIT_L(n) asm volatile("s_waitcnt lgkmcnt(" #n ")" ::: "memory")
; #define PG8_BAR __builtin_amdgcn_s_barrier()
; #define PG8_SCHED __builtin_amdgcn_sched_barrier(0)
; template <class Epi, class Sched, bool ALIGN_EPI, bool FP8 = false>
; DI void gemm_phase(LAS unsigned char* lds, const Gemm g, const Sched& S, const Epi& E) {
;     ...
;             PG8_LDB(B0, 1, 0); PG8_LDB(B1, 1, 1); PG8_SCHED; PG8_LDA(At, 1, 0); PG8_STAGE(PG8_SA(0, 1), a2 + hstepA, voffA);
;             PG8_WAIT_V(8); PG8_WAIT_L(0); PG8_BAR; PG8_MMA(0, 0, At, B0); PG8_MMA(0, 1, At, B1); PG8_BAR; PG8_SCHED;
.Lmy_g_9:
	s_setprio 0
	v_add_u32_e32 v1, 0x18000, v160
	ds_read_b128 v[132:135], v1
	ds_read_b128 v[136:139], v1 offset:1024
	ds_read_b128 v[140:143], v1 offset:2048
	ds_read_b128 v[162:165], v1 offset:3072
	v_add_u32_e32 v1, 0x1c000, v160
	ds_read_b128 v[166:169], v1
	ds_read_b128 v[170:173], v1 offset:1024
	ds_read_b128 v[174:177], v1 offset:2048
	ds_read_b128 v[178:181], v1 offset:3072
	ds_read_b128 v[182:185], v161 offset:32768
	ds_read_b128 v[186:189], v161 offset:33792
	ds_read_b128 v[190:193], v161 offset:34816
	ds_read_b128 v[194:197], v161 offset:35840
	ds_read_b128 v[198:201], v161 offset:36864
	ds_read_b128 v[202:205], v161 offset:37888
	ds_read_b128 v[206:209], v161 offset:38912
	ds_read_b128 v[210:213], v161 offset:39936
	s_add_u32 s26, s44, 0x80000
	s_addc_u32 s27, s45, 0
	s_mov_b32 s44, m0
	s_mov_b32 m0, s53
	s_nop 0
	global_load_lds_dwordx4 v154, s[26:27]
	s_mov_b32 m0, s44
	s_nop 0
	s_mov_b32 s44, m0
	s_mov_b32 m0, s54
	s_nop 0
	global_load_lds_dwordx4 v156, s[26:27]
	s_mov_b32 m0, s44
	s_waitcnt vmcnt(8)
	s_waitcnt lgkmcnt(0)
	s_barrier
	s_setprio 1
	v_mfma_f32_16x16x32_bf16 v[128:131], v[132:135], v[182:185], v[128:131]
	v_mfma_f32_16x16x32_bf16 v[124:127], v[140:143], v[182:185], v[124:127]
	v_mfma_f32_16x16x32_bf16 v[112:115], v[132:135], v[190:193], v[112:115]
	v_mfma_f32_16x16x32_bf16 v[108:111], v[140:143], v[190:193], v[108:111]
	v_mfma_f32_16x16x32_bf16 v[96:99], v[132:135], v[198:201], v[96:99]
	v_mfma_f32_16x16x32_bf16 v[92:95], v[140:143], v[198:201], v[92:95]
	v_mfma_f32_16x16x32_bf16 v[80:83], v[132:135], v[206:209], v[80:83]
	v_mfma_f32_16x16x32_bf16 v[76:79], v[140:143], v[206:209], v[76:79]
	v_mfma_f32_16x16x32_bf16 v[128:131], v[136:139], v[186:189], v[128:131]
	v_mfma_f32_16x16x32_bf16 v[124:127], v[162:165], v[186:189], v[124:127]
	v_mfma_f32_16x16x32_bf16 v[112:115], v[136:139], v[194:197], v[112:115]
	v_mfma_f32_16x16x32_bf16 v[108:111], v[162:165], v[194:197], v[108:111]
	v_mfma_f32_16x16x32_bf16 v[96:99], v[136:139], v[202:205], v[96:99]
	v_mfma_f32_16x16x32_bf16 v[92:95], v[162:165], v[202:205], v[92:95]
	v_mfma_f32_16x16x32_bf16 v[80:83], v[136:139], v[210:213], v[80:83]
	v_mfma_f32_16x16x32_bf16 v[76:79], v[162:165], v[210:213], v[76:79]
	v_mfma_f32_16x16x32_bf16 v[120:123], v[166:169], v[182:185], v[120:123]
	v_mfma_f32_16x16x32_bf16 v[116:119], v[174:177], v[182:185], v[116:119]
	v_mfma_f32_16x16x32_bf16 v[104:107], v[166:169], v[190:193], v[104:107]
	v_mfma_f32_16x16x32_bf16 v[100:103], v[174:177], v[190:193], v[100:103]
	v_mfma_f32_16x16x32_bf16 v[88:91], v[166:169], v[198:201], v[88:91]
	v_mfma_f32_16x16x32_bf16 v[84:87], v[174:177], v[198:201], v[84:87]
	v_mfma_f32_16x16x32_bf16 v[72:75], v[166:169], v[206:209], v[72:75]
	v_mfma_f32_16x16x32_bf16 v[68:71], v[174:177], v[206:209], v[68:71]
	v_mfma_f32_16x16x32_bf16 v[120:123], v[170:173], v[186:189], v[120:123]
	v_mfma_f32_16x16x32_bf16 v[116:119], v[178:181], v[186:189], v[116:119]
	v_mfma_f32_16x16x32_bf16 v[104:107], v[170:173], v[194:197], v[104:107]
	v_mfma_f32_16x16x32_bf16 v[100:103], v[178:181], v[194:197], v[100:103]
	ds_read_b32 v255, v255 offset:4096
	v_mfma_f32_16x16x32_bf16 v[88:91], v[170:173], v[202:205], v[88:91]
	v_mfma_f32_16x16x32_bf16 v[84:87], v[178:181], v[202:205], v[84:87]
	v_mfma_f32_16x16x32_bf16 v[72:75], v[170:173], v[210:213], v[72:75]
	v_mfma_f32_16x16x32_bf16 v[68:71], v[178:181], v[210:213], v[68:71]
	s_add_u32 s98, s98, 0x80000
	s_waitcnt lgkmcnt(0)
	v_readfirstlane_b32 s101, v255
	v_mov_b32_e32 v255, 0x20000
	s_cmp_ge_u32 s101, s98
	s_cbranch_scc1 .Lmy_g_10

; #define PG8_STAGE(bufoff, gbase, voff) do { _Pragma("unroll") for (int _i = 0; _i < 2; ++_i) { unsigned keep_; \
;         asm volatile("s_mov_b32 %0, m0\n\ts_mov_b32 m0, %3\n\ts_nop 0\n\tglobal_load_lds_dwordx4 %1, %2\n\ts_mov_b32 m0, %0" : "=&s"(keep_) : "v"((voff)[_i]), "s"((const char*)(gbase)), "s"(ldsbase + (unsigned)((bufoff) + _i * 8192)) : "memory"); } } while (0)
; #define PG8_WAIT_V(n) asm volatile("s_waitcnt vmcnt(" #n ")" ::: "memory")
; #define PG8_WAIT_L(n) asm volatile("s_waitcnt lgkmcnt(" #n ")" ::: "memory")
; #define PG8_BAR __builtin_amdgcn_s_barrier()
; #define PG8_SCHED __builtin_amdgcn_sched_barrier(0)
; template <class Epi, class Sched, bool ALIGN_EPI, bool FP8 = false>
; DI void gemm_phase(LAS unsigned char* lds, const Gemm g, const Sched& S, const Epi& E) {
;     ...
;             PG8_LDA(At, 1, 1); PG8_STAGE(PG8_SB(1, 0), b3, voffB); PG8_STAGE(PG8_SB(1, 1), b3 + hstepB, voffB); PG8_STAGE(PG8_SA(1, 0), a3, voffA);
;             PG8_WAIT_V(8); PG8_WAIT_L(0); PG8_BAR; PG8_MMA(1, 0, At, B0); PG8_MMA(1, 1, At, B1); PG8_BAR; PG8_SCHED;
.Lmy_g_10:
	s_setprio 0
	ds_read_b128 v[182:185], v161 offset:49152
	ds_read_b128 v[186:189], v161 offset:50176
	ds_read_b128 v[190:193], v161 offset:51200
	ds_read_b128 v[194:197], v161 offset:52224
	ds_read_b128 v[198:201], v161 offset:53248
	ds_read_b128 v[202:205], v161 offset:54272
	ds_read_b128 v[206:209], v161 offset:55296
	ds_read_b128 v[210:213], v161 offset:56320
	s_add_u32 s26, s42, 0x80
	s_addc_u32 s27, s43, 0
	s_mov_b32 s44, m0
	s_mov_b32 m0, s55
	s_nop 0
	global_load_lds_dwordx4 v155, s[26:27]
	s_mov_b32 m0, s44
	s_nop 0
	s_mov_b32 s44, m0
	s_mov_b32 m0, s56
	s_nop 0
	global_load_lds_dwordx4 v157, s[26:27]
	s_mov_b32 m0, s44
	s_add_u32 s26, s42, 0x80080
	s_addc_u32 s27, s43, 0
	s_mov_b32 s42, m0
	s_mov_b32 m0, s59
	s_nop 0
	global_load_lds_dwordx4 v155, s[26:27]
	s_mov_b32 m0, s42
	s_nop 0
	s_mov_b32 s42, m0
	s_mov_b32 m0, s60
	s_nop 0
	global_load_lds_dwordx4 v157, s[26:27]
	s_mov_b32 m0, s42
	s_mov_b32 s26, m0
	s_mov_b32 m0, s57
	s_nop 0
	global_load_lds_dwordx4 v154, s[40:41]
	s_mov_b32 m0, s26
	s_nop 0
	s_mov_b32 s26, m0
	s_mov_b32 m0, s58
	s_nop 0
	global_load_lds_dwordx4 v156, s[40:41]
	s_mov_b32 m0, s26
	s_waitcnt vmcnt(8)
	s_waitcnt lgkmcnt(0)
	s_barrier
	s_setprio 1
	v_mfma_f32_16x16x32_bf16 v[64:67], v[132:135], v[182:185], v[64:67]
	v_mfma_f32_16x16x32_bf16 v[60:63], v[140:143], v[182:185], v[60:63]
	v_mfma_f32_16x16x32_bf16 v[48:51], v[132:135], v[190:193], v[48:51]
	v_mfma_f32_16x16x32_bf16 v[44:47], v[140:143], v[190:193], v[44:47]
	v_mfma_f32_16x16x32_bf16 v[32:35], v[132:135], v[198:201], v[32:35]
	v_mfma_f32_16x16x32_bf16 v[28:31], v[140:143], v[198:201], v[28:31]
	v_mfma_f32_16x16x32_bf16 v[16:19], v[132:135], v[206:209], v[16:19]
	v_mfma_f32_16x16x32_bf16 v[12:15], v[140:143], v[206:209], v[12:15]
	v_mfma_f32_16x16x32_bf16 v[64:67], v[136:139], v[186:189], v[64:67]
	v_mfma_f32_16x16x32_bf16 v[60:63], v[162:165], v[186:189], v[60:63]
	v_mfma_f32_16x16x32_bf16 v[48:51], v[136:139], v[194:197], v[48:51]
	v_mfma_f32_16x16x32_bf16 v[44:47], v[162:165], v[194:197], v[44:47]
	v_mfma_f32_16x16x32_bf16 v[32:35], v[136:139], v[202:205], v[32:35]
	v_mfma_f32_16x16x32_bf16 v[28:31], v[162:165], v[202:205], v[28:31]
	v_mfma_f32_16x16x32_bf16 v[16:19], v[136:139], v[210:213], v[16:19]
	v_mfma_f32_16x16x32_bf16 v[12:15], v[162:165], v[210:213], v[12:15]
	v_mfma_f32_16x16x32_bf16 v[56:59], v[166:169], v[182:185], v[56:59]
	v_mfma_f32_16x16x32_bf16 v[52:55], v[174:177], v[182:185], v[52:55]
	v_mfma_f32_16x16x32_bf16 v[40:43], v[166:169], v[190:193], v[40:43]
	v_mfma_f32_16x16x32_bf16 v[36:39], v[174:177], v[190:193], v[36:39]
	v_mfma_f32_16x16x32_bf16 v[24:27], v[166:169], v[198:201], v[24:27]
	v_mfma_f32_16x16x32_bf16 v[20:23], v[174:177], v[198:201], v[20:23]
	v_mfma_f32_16x16x32_bf16 v[6:9], v[166:169], v[206:209], v[8:11]
	v_mfma_f32_16x16x32_bf16 v[2:5], v[174:177], v[206:209], v[2:5]
	v_mfma_f32_16x16x32_bf16 v[56:59], v[170:173], v[186:189], v[56:59]
	v_mfma_f32_16x16x32_bf16 v[52:55], v[178:181], v[186:189], v[52:55]
	v_mfma_f32_16x16x32_bf16 v[40:43], v[170:173], v[194:197], v[40:43]
	v_mfma_f32_16x16x32_bf16 v[36:39], v[178:181], v[194:197], v[36:39]
	ds_read_b32 v255, v255 offset:4096
	v_mfma_f32_16x16x32_bf16 v[24:27], v[170:173], v[202:205], v[24:27]
	v_mfma_f32_16x16x32_bf16 v[20:23], v[178:181], v[202:205], v[20:23]
	v_mfma_f32_16x16x32_bf16 v[8:11], v[170:173], v[210:213], v[6:9]
	v_mfma_f32_16x16x32_bf16 v[4:7], v[178:181], v[210:213], v[2:5]
	s_add_u32 s98, s98, 0x80000
	s_waitcnt lgkmcnt(0)
	v_readfirstlane_b32 s101, v255
	v_mov_b32_e32 v255, 0x20000
	s_cmp_ge_u32 s101, s98
	s_cbranch_scc1 .Lmy_g_11

;     DI int nt(const Unit& u) const { return (u.aux & 8) ? PLED / 64 : ((u.aux & 4) ? (D_ / 2) / 64 : D_ / 64); }
; template <class Epi, class Sched, bool ALIGN_EPI, bool FP8 = false>
; DI void gemm_phase(LAS unsigned char* lds, const Gemm g, const Sched& S, const Epi& E) {
;     ...
;         for (int t = 0; t < nt; t += 2) {
;             if constexpr (Epi::MID) { if (t == (nt >> 1)) E.mid(acc, cur, wr, wc, fr, fq); }
.Lmy_g_11:
	s_setprio 0
	s_add_i32 s69, s69, 2
	s_add_u32 s67, s67, 0x100
	s_addc_u32 s68, s68, 0
	s_cmp_gt_u32 s69, 29
	s_cbranch_scc1 .LBB0_491
	s_mov_b64 s[26:27], s[28:29]
	s_cmp_lg_u32 s69, 14
	s_cbranch_scc0 .LBB0_488
	s_branch .Lmy_g0_489

; #define PG8_STAGE(bufoff, gbase, voff) do { _Pragma("unroll") for (int _i = 0; _i < 2; ++_i) { unsigned keep_; \
;         asm volatile("s_mov_b32 %0, m0\n\ts_mov_b32 m0, %3\n\ts_nop 0\n\tglobal_load_lds_dwordx4 %1, %2\n\ts_mov_b32 m0, %0" : "=&s"(keep_) : "v"((voff)[_i]), "s"((const char*)(gbase)), "s"(ldsbase + (unsigned)((bufoff) + _i * 8192)) : "memory"); } } while (0)
; #define PG8_WAIT_V(n) asm volatile("s_waitcnt vmcnt(" #n ")" ::: "memory")
; #define PG8_WAIT_L(n) asm volatile("s_waitcnt lgkmcnt(" #n ")" ::: "memory")
; #define PG8_BAR __builtin_amdgcn_s_barrier()
; #define PG8_SCHED __builtin_amdgcn_sched_barrier(0)
;     DI int nt(const Unit& u) const { return (u.aux & 8) ? PLED / 64 : ((u.aux & 4) ? (D_ / 2) / 64 : D_ / 64); }
; template <class Epi, class Sched, bool ALIGN_EPI, bool FP8 = false>
; DI void gemm_phase(LAS unsigned char* lds, const Gemm g, const Sched& S, const Epi& E) {
;     ...
;             const bool last = (t == nt - 2);
;             const char* a1 = cA + (size_t)(t + 1) * kstep;
;             const char* a2 = last ? nA : cA + (size_t)(t + 2) * kstep; const char* b2 = last ? nB : cB + (size_t)(t + 2) * kstep;
;             const char* a3 = a2 + kstep; const char* b3 = b2 + kstep;
;             PG8_LDB(B0, 0, 0); PG8_LDB(B1, 0, 1); PG8_SCHED; PG8_LDA(At, 0, 0); PG8_STAGE(PG8_SA(1, 1), a1 + hstepA, voffA);
;             PG8_WAIT_V(8); PG8_WAIT_L(0); PG8_BAR; PG8_MMA(0, 0, At, B0); PG8_MMA(0, 1, At, B1); PG8_BAR; PG8_SCHED;
;             PG8_LDA(At, 0, 1); PG8_STAGE(PG8_SB(0, 0), b2, voffB); PG8_STAGE(PG8_SB(0, 1), b2 + hstepB, voffB); PG8_STAGE(PG8_SA(0, 0), a2, voffA);
;             PG8_WAIT_V(8); PG8_WAIT_L(0); PG8_BAR; PG8_MMA(1, 0, At, B0); PG8_MMA(1, 1, At, B1); PG8_BAR; PG8_SCHED;
.LBB0_569:
	s_cmp_lg_u32 s99, 0
	s_cbranch_scc1 .Lmy_g0_569
	ds_read_b128 v[146:149], v140
	ds_read_b128 v[150:153], v140 offset:1024
	ds_read_b128 v[154:157], v140 offset:2048
	ds_read_b128 v[158:161], v140 offset:3072
	ds_read_b128 v[162:165], v141
	ds_read_b128 v[166:169], v141 offset:1024
	ds_read_b128 v[170:173], v141 offset:2048
	ds_read_b128 v[174:177], v141 offset:3072
	s_add_u32 s66, s64, 0x100
	s_addc_u32 s67, s65, 0
	s_cmp_eq_u32 s97, 28
	s_cselect_b32 s72, s93, s66
	s_cselect_b32 s73, s57, s67
	s_cselect_b32 s70, s94, s95
	s_cselect_b32 s71, s55, s96
	s_add_u32 s68, s72, 0x80
	s_addc_u32 s69, s73, 0
	ds_read_b128 v[178:181], v142
	ds_read_b128 v[182:185], v142 offset:1024
	ds_read_b128 v[186:189], v142 offset:2048
	ds_read_b128 v[190:193], v142 offset:3072
	ds_read_b128 v[194:197], v142 offset:4096
	ds_read_b128 v[198:201], v142 offset:5120
	ds_read_b128 v[202:205], v142 offset:6144
	ds_read_b128 v[206:209], v142 offset:7168
	s_add_u32 s64, s64, 0x80080
	s_addc_u32 s65, s65, 0
	s_mov_b32 vcc_lo, m0
	s_mov_b32 m0, s89
	s_nop 0
	global_load_lds_dwordx4 v134, s[64:65]
	s_mov_b32 m0, vcc_lo
	s_nop 0
	s_mov_b32 vcc_lo, m0
	s_mov_b32 m0, s90
	s_nop 0
	global_load_lds_dwordx4 v136, s[64:65]
	s_mov_b32 m0, vcc_lo
	s_waitcnt vmcnt(8)
	s_waitcnt lgkmcnt(0)
	s_mov_b64 exec, 1
	ds_add_u32 v255, v255 offset:4096
	s_mov_b64 exec, -1
	s_setprio 1
	v_mfma_f32_16x16x32_bf16 v[124:127], v[146:149], v[178:181], v[124:127]
	v_mfma_f32_16x16x32_bf16 v[120:123], v[154:157], v[178:181], v[120:123]
	v_mfma_f32_16x16x32_bf16 v[108:111], v[146:149], v[186:189], v[108:111]
	v_mfma_f32_16x16x32_bf16 v[104:107], v[154:157], v[186:189], v[104:107]
	v_mfma_f32_16x16x32_bf16 v[92:95], v[146:149], v[194:197], v[92:95]
	v_mfma_f32_16x16x32_bf16 v[88:91], v[154:157], v[194:197], v[88:91]
	v_mfma_f32_16x16x32_bf16 v[76:79], v[146:149], v[202:205], v[76:79]
	v_mfma_f32_16x16x32_bf16 v[72:75], v[154:157], v[202:205], v[72:75]
	v_mfma_f32_16x16x32_bf16 v[124:127], v[150:153], v[182:185], v[124:127]
	v_mfma_f32_16x16x32_bf16 v[120:123], v[158:161], v[182:185], v[120:123]
	v_mfma_f32_16x16x32_bf16 v[108:111], v[150:153], v[190:193], v[108:111]
	v_mfma_f32_16x16x32_bf16 v[104:107], v[158:161], v[190:193], v[104:107]
	v_mfma_f32_16x16x32_bf16 v[92:95], v[150:153], v[198:201], v[92:95]
	v_mfma_f32_16x16x32_bf16 v[88:91], v[158:161], v[198:201], v[88:91]
	v_mfma_f32_16x16x32_bf16 v[76:79], v[150:153], v[206:209], v[76:79]
	v_mfma_f32_16x16x32_bf16 v[72:75], v[158:161], v[206:209], v[72:75]
	v_mfma_f32_16x16x32_bf16 v[116:119], v[162:165], v[178:181], v[116:119]
	v_mfma_f32_16x16x32_bf16 v[112:115], v[170:173], v[178:181], v[112:115]
	v_mfma_f32_16x16x32_bf16 v[100:103], v[162:165], v[186:189], v[100:103]
	v_mfma_f32_16x16x32_bf16 v[96:99], v[170:173], v[186:189], v[96:99]
	v_mfma_f32_16x16x32_bf16 v[84:87], v[162:165], v[194:197], v[84:87]
	v_mfma_f32_16x16x32_bf16 v[80:83], v[170:173], v[194:197], v[80:83]
	v_mfma_f32_16x16x32_bf16 v[68:71], v[162:165], v[202:205], v[68:71]
	v_mfma_f32_16x16x32_bf16 v[64:67], v[170:173], v[202:205], v[64:67]
	v_mfma_f32_16x16x32_bf16 v[116:119], v[166:169], v[182:185], v[116:119]
	v_mfma_f32_16x16x32_bf16 v[112:115], v[174:177], v[182:185], v[112:115]
	v_mfma_f32_16x16x32_bf16 v[100:103], v[166:169], v[190:193], v[100:103]
	v_mfma_f32_16x16x32_bf16 v[96:99], v[174:177], v[190:193], v[96:99]
	v_mfma_f32_16x16x32_bf16 v[84:87], v[166:169], v[198:201], v[84:87]
	v_mfma_f32_16x16x32_bf16 v[80:83], v[174:177], v[198:201], v[80:83]
	v_mfma_f32_16x16x32_bf16 v[68:71], v[166:169], v[206:209], v[68:71]
	v_mfma_f32_16x16x32_bf16 v[64:67], v[174:177], v[206:209], v[64:67]
	s_setprio 0
	s_barrier
	ds_read_b128 v[178:181], v142 offset:16384
	ds_read_b128 v[182:185], v142 offset:17408
	ds_read_b128 v[186:189], v142 offset:18432
	ds_read_b128 v[190:193], v142 offset:19456
	ds_read_b128 v[194:197], v142 offset:20480
	ds_read_b128 v[198:201], v142 offset:21504
	ds_read_b128 v[202:205], v142 offset:22528
	ds_read_b128 v[206:209], v142 offset:23552
	s_mov_b32 s64, m0
	s_mov_b32 m0, s63
	s_nop 0
	global_load_lds_dwordx4 v135, s[70:71]
	s_mov_b32 m0, s64
	s_nop 0
	s_mov_b32 s64, m0
	s_mov_b32 m0, s75
	s_nop 0
	global_load_lds_dwordx4 v137, s[70:71]
	s_mov_b32 m0, s64
	s_add_u32 s64, s70, 0x80000
	s_addc_u32 s65, s71, 0
	s_mov_b32 vcc_lo, m0
	s_mov_b32 m0, s77
	s_nop 0
	global_load_lds_dwordx4 v135, s[64:65]
	s_mov_b32 m0, vcc_lo
	s_nop 0
	s_mov_b32 vcc_lo, m0
	s_mov_b32 m0, s79
	s_nop 0
	global_load_lds_dwordx4 v137, s[64:65]
	s_mov_b32 m0, vcc_lo
	s_mov_b32 s64, m0
	s_mov_b32 m0, s74
	s_nop 0
	global_load_lds_dwordx4 v134, s[72:73]
	s_mov_b32 m0, s64
	s_nop 0
	s_mov_b32 s64, m0
	s_mov_b32 m0, s80
	s_nop 0
	global_load_lds_dwordx4 v136, s[72:73]
	s_mov_b32 m0, s64
	s_waitcnt vmcnt(8)
	s_waitcnt lgkmcnt(0)
; #define PG8_STAGE(bufoff, gbase, voff) do { _Pragma("unroll") for (int _i = 0; _i < 2; ++_i) { unsigned keep_; \
;         asm volatile("s_mov_b32 %0, m0\n\ts_mov_b32 m0, %3\n\ts_nop 0\n\tglobal_load_lds_dwordx4 %1, %2\n\ts_mov_b32 m0, %0" : "=&s"(keep_) : "v"((voff)[_i]), "s"((const char*)(gbase)), "s"(ldsbase + (unsigned)((bufoff) + _i * 8192)) : "memory"); } } while (0)
; #define PG8_WAIT_V(n) asm volatile("s_waitcnt vmcnt(" #n ")" ::: "memory")
; #define PG8_WAIT_L(n) asm volatile("s_waitcnt lgkmcnt(" #n ")" ::: "memory")
; #define PG8_BAR __builtin_amdgcn_s_barrier()
; #define PG8_SCHED __builtin_amdgcn_sched_barrier(0)
; template <class Epi, class Sched, bool ALIGN_EPI, bool FP8 = false>
; DI void gemm_phase(LAS unsigned char* lds, const Gemm g, const Sched& S, const Epi& E) {
;     ...
;             PG8_WAIT_V(8); PG8_WAIT_L(0); PG8_BAR; PG8_MMA(1, 0, At, B0); PG8_MMA(1, 1, At, B1); PG8_BAR; PG8_SCHED;
;             PG8_LDB(B0, 1, 0); PG8_LDB(B1, 1, 1); PG8_SCHED; PG8_LDA(At, 1, 0); PG8_STAGE(PG8_SA(0, 1), a2 + hstepA, voffA);
;             PG8_WAIT_V(8); PG8_WAIT_L(0); PG8_BAR; PG8_MMA(0, 0, At, B0); PG8_MMA(0, 1, At, B1); PG8_BAR; PG8_SCHED;
	s_mov_b64 exec, 1
	ds_add_u32 v255, v255 offset:4096
	s_mov_b64 exec, -1
	s_setprio 1
	v_mfma_f32_16x16x32_bf16 v[60:63], v[146:149], v[178:181], v[60:63]
	v_mfma_f32_16x16x32_bf16 v[56:59], v[154:157], v[178:181], v[56:59]
	v_mfma_f32_16x16x32_bf16 v[44:47], v[146:149], v[186:189], v[44:47]
	v_mfma_f32_16x16x32_bf16 v[40:43], v[154:157], v[186:189], v[40:43]
	v_mfma_f32_16x16x32_bf16 v[28:31], v[146:149], v[194:197], v[28:31]
	v_mfma_f32_16x16x32_bf16 v[24:27], v[154:157], v[194:197], v[24:27]
	v_mfma_f32_16x16x32_bf16 v[12:15], v[146:149], v[202:205], v[12:15]
	v_mfma_f32_16x16x32_bf16 v[8:11], v[154:157], v[202:205], v[8:11]
	v_mfma_f32_16x16x32_bf16 v[60:63], v[150:153], v[182:185], v[60:63]
	v_mfma_f32_16x16x32_bf16 v[56:59], v[158:161], v[182:185], v[56:59]
	v_mfma_f32_16x16x32_bf16 v[44:47], v[150:153], v[190:193], v[44:47]
	v_mfma_f32_16x16x32_bf16 v[40:43], v[158:161], v[190:193], v[40:43]
	v_mfma_f32_16x16x32_bf16 v[28:31], v[150:153], v[198:201], v[28:31]
	v_mfma_f32_16x16x32_bf16 v[24:27], v[158:161], v[198:201], v[24:27]
	v_mfma_f32_16x16x32_bf16 v[12:15], v[150:153], v[206:209], v[12:15]
	v_mfma_f32_16x16x32_bf16 v[8:11], v[158:161], v[206:209], v[8:11]
	v_mfma_f32_16x16x32_bf16 v[52:55], v[162:165], v[178:181], v[52:55]
	v_mfma_f32_16x16x32_bf16 v[48:51], v[170:173], v[178:181], v[48:51]
	v_mfma_f32_16x16x32_bf16 v[36:39], v[162:165], v[186:189], v[36:39]
	v_mfma_f32_16x16x32_bf16 v[32:35], v[170:173], v[186:189], v[32:35]
	v_mfma_f32_16x16x32_bf16 v[20:23], v[162:165], v[194:197], v[20:23]
	v_mfma_f32_16x16x32_bf16 v[16:19], v[170:173], v[194:197], v[16:19]
	v_mfma_f32_16x16x32_bf16 v[4:7], v[162:165], v[202:205], v[4:7]
	v_mfma_f32_16x16x32_bf16 v[0:3], v[170:173], v[202:205], v[0:3]
	v_mfma_f32_16x16x32_bf16 v[52:55], v[166:169], v[182:185], v[52:55]
	v_mfma_f32_16x16x32_bf16 v[48:51], v[174:177], v[182:185], v[48:51]
	v_mfma_f32_16x16x32_bf16 v[36:39], v[166:169], v[190:193], v[36:39]
	v_mfma_f32_16x16x32_bf16 v[32:35], v[174:177], v[190:193], v[32:35]
	v_mfma_f32_16x16x32_bf16 v[20:23], v[166:169], v[198:201], v[20:23]
	v_mfma_f32_16x16x32_bf16 v[16:19], v[174:177], v[198:201], v[16:19]
	v_mfma_f32_16x16x32_bf16 v[4:7], v[166:169], v[206:209], v[4:7]
	v_mfma_f32_16x16x32_bf16 v[0:3], v[174:177], v[206:209], v[0:3]
	s_setprio 0
	s_barrier
	ds_read_b128 v[146:149], v143
	ds_read_b128 v[150:153], v143 offset:1024
	ds_read_b128 v[154:157], v143 offset:2048
	ds_read_b128 v[158:161], v143 offset:3072
	ds_read_b128 v[162:165], v144
	ds_read_b128 v[166:169], v144 offset:1024
	ds_read_b128 v[170:173], v144 offset:2048
	ds_read_b128 v[174:177], v144 offset:3072
	ds_read_b128 v[178:181], v142 offset:32768
	ds_read_b128 v[182:185], v142 offset:33792
	ds_read_b128 v[186:189], v142 offset:34816
	ds_read_b128 v[190:193], v142 offset:35840
	ds_read_b128 v[194:197], v142 offset:36864
	ds_read_b128 v[198:201], v142 offset:37888
	ds_read_b128 v[202:205], v142 offset:38912
	ds_read_b128 v[206:209], v142 offset:39936
	s_add_u32 s64, s72, 0x80000
	s_addc_u32 s65, s73, 0
	s_mov_b32 s72, m0
	s_mov_b32 m0, s81
	s_nop 0
	global_load_lds_dwordx4 v134, s[64:65]
	s_mov_b32 m0, s72
	s_nop 0
	s_mov_b32 s72, m0
	s_mov_b32 m0, s82
	s_nop 0
	global_load_lds_dwordx4 v136, s[64:65]
	s_mov_b32 m0, s72
	s_waitcnt vmcnt(8)
	s_waitcnt lgkmcnt(0)
	s_mov_b64 exec, 1
	ds_add_u32 v255, v255 offset:4096
	s_mov_b64 exec, -1
	s_setprio 1
	v_mfma_f32_16x16x32_bf16 v[124:127], v[146:149], v[178:181], v[124:127]
	v_mfma_f32_16x16x32_bf16 v[120:123], v[154:157], v[178:181], v[120:123]
	v_mfma_f32_16x16x32_bf16 v[108:111], v[146:149], v[186:189], v[108:111]
	v_mfma_f32_16x16x32_bf16 v[104:107], v[154:157], v[186:189], v[104:107]
	v_mfma_f32_16x16x32_bf16 v[92:95], v[146:149], v[194:197], v[92:95]
	v_mfma_f32_16x16x32_bf16 v[88:91], v[154:157], v[194:197], v[88:91]
	v_mfma_f32_16x16x32_bf16 v[76:79], v[146:149], v[202:205], v[76:79]
	v_mfma_f32_16x16x32_bf16 v[72:75], v[154:157], v[202:205], v[72:75]
	v_mfma_f32_16x16x32_bf16 v[124:127], v[150:153], v[182:185], v[124:127]
	v_mfma_f32_16x16x32_bf16 v[120:123], v[158:161], v[182:185], v[120:123]
	v_mfma_f32_16x16x32_bf16 v[108:111], v[150:153], v[190:193], v[108:111]
	v_mfma_f32_16x16x32_bf16 v[104:107], v[158:161], v[190:193], v[104:107]
	v_mfma_f32_16x16x32_bf16 v[92:95], v[150:153], v[198:201], v[92:95]
	v_mfma_f32_16x16x32_bf16 v[88:91], v[158:161], v[198:201], v[88:91]
	v_mfma_f32_16x16x32_bf16 v[76:79], v[150:153], v[206:209], v[76:79]
	v_mfma_f32_16x16x32_bf16 v[72:75], v[158:161], v[206:209], v[72:75]
	v_mfma_f32_16x16x32_bf16 v[116:119], v[162:165], v[178:181], v[116:119]
	v_mfma_f32_16x16x32_bf16 v[112:115], v[170:173], v[178:181], v[112:115]
	v_mfma_f32_16x16x32_bf16 v[100:103], v[162:165], v[186:189], v[100:103]
	v_mfma_f32_16x16x32_bf16 v[96:99], v[170:173], v[186:189], v[96:99]
	v_mfma_f32_16x16x32_bf16 v[84:87], v[162:165], v[194:197], v[84:87]
	v_mfma_f32_16x16x32_bf16 v[80:83], v[170:173], v[194:197], v[80:83]
	v_mfma_f32_16x16x32_bf16 v[68:71], v[162:165], v[202:205], v[68:71]
	v_mfma_f32_16x16x32_bf16 v[64:67], v[170:173], v[202:205], v[64:67]
	v_mfma_f32_16x16x32_bf16 v[116:119], v[166:169], v[182:185], v[116:119]
	v_mfma_f32_16x16x32_bf16 v[112:115], v[174:177], v[182:185], v[112:115]
	v_mfma_f32_16x16x32_bf16 v[100:103], v[166:169], v[190:193], v[100:103]
	v_mfma_f32_16x16x32_bf16 v[96:99], v[174:177], v[190:193], v[96:99]
	v_mfma_f32_16x16x32_bf16 v[84:87], v[166:169], v[198:201], v[84:87]
	v_mfma_f32_16x16x32_bf16 v[80:83], v[174:177], v[198:201], v[80:83]
	v_mfma_f32_16x16x32_bf16 v[68:71], v[166:169], v[206:209], v[68:71]
	v_mfma_f32_16x16x32_bf16 v[64:67], v[174:177], v[206:209], v[64:67]
	s_setprio 0
	s_barrier
; #define PG8_STAGE(bufoff, gbase, voff) do { _Pragma("unroll") for (int _i = 0; _i < 2; ++_i) { unsigned keep_; \
;         asm volatile("s_mov_b32 %0, m0\n\ts_mov_b32 m0, %3\n\ts_nop 0\n\tglobal_load_lds_dwordx4 %1, %2\n\ts_mov_b32 m0, %0" : "=&s"(keep_) : "v"((voff)[_i]), "s"((const char*)(gbase)), "s"(ldsbase + (unsigned)((bufoff) + _i * 8192)) : "memory"); } } while (0)
; #define PG8_WAIT_V(n) asm volatile("s_waitcnt vmcnt(" #n ")" ::: "memory")
; #define PG8_WAIT_L(n) asm volatile("s_waitcnt lgkmcnt(" #n ")" ::: "memory")
; #define PG8_BAR __builtin_amdgcn_s_barrier()
; #define PG8_SCHED __builtin_amdgcn_sched_barrier(0)
;     DI int nt(const Unit& u) const { return (u.aux & 8) ? PLED / 64 : ((u.aux & 4) ? (D_ / 2) / 64 : D_ / 64); }
; template <class Epi, class Sched, bool ALIGN_EPI, bool FP8 = false>
; DI void gemm_phase(LAS unsigned char* lds, const Gemm g, const Sched& S, const Epi& E) {
;     ...
;         for (int t = 0; t < nt; t += 2) {
;     ...
;             PG8_LDA(At, 1, 1); PG8_STAGE(PG8_SB(1, 0), b3, voffB); PG8_STAGE(PG8_SB(1, 1), b3 + hstepB, voffB); PG8_STAGE(PG8_SA(1, 0), a3, voffA);
;             PG8_WAIT_V(8); PG8_WAIT_L(0); PG8_BAR; PG8_MMA(1, 0, At, B0); PG8_MMA(1, 1, At, B1); PG8_BAR; PG8_SCHED;
	ds_read_b128 v[178:181], v142 offset:49152
	ds_read_b128 v[182:185], v142 offset:50176
	ds_read_b128 v[186:189], v142 offset:51200
	ds_read_b128 v[190:193], v142 offset:52224
	ds_read_b128 v[194:197], v142 offset:53248
	ds_read_b128 v[198:201], v142 offset:54272
	ds_read_b128 v[202:205], v142 offset:55296
	ds_read_b128 v[206:209], v142 offset:56320
	s_add_u32 s64, s70, 0x80
	s_addc_u32 s65, s71, 0
	s_mov_b32 s72, m0
	s_mov_b32 m0, s83
	s_nop 0
	global_load_lds_dwordx4 v135, s[64:65]
	s_mov_b32 m0, s72
	s_nop 0
	s_mov_b32 s72, m0
	s_mov_b32 m0, s84
	s_nop 0
	global_load_lds_dwordx4 v137, s[64:65]
	s_mov_b32 m0, s72
	s_add_u32 s64, s70, 0x80080
	s_addc_u32 s65, s71, 0
	s_mov_b32 s70, m0
	s_mov_b32 m0, s87
	s_nop 0
	global_load_lds_dwordx4 v135, s[64:65]
	s_mov_b32 m0, s70
	s_nop 0
	s_mov_b32 s70, m0
	s_mov_b32 m0, s88
	s_nop 0
	global_load_lds_dwordx4 v137, s[64:65]
	s_mov_b32 m0, s70
	s_mov_b32 s64, m0
	s_mov_b32 m0, s85
	s_nop 0
	global_load_lds_dwordx4 v134, s[68:69]
	s_mov_b32 m0, s64
	s_nop 0
	s_mov_b32 s64, m0
	s_mov_b32 m0, s86
	s_nop 0
	global_load_lds_dwordx4 v136, s[68:69]
	s_mov_b32 m0, s64
	s_waitcnt vmcnt(8)
	s_waitcnt lgkmcnt(0)
	s_mov_b64 exec, 1
	ds_add_u32 v255, v255 offset:4096
	s_mov_b64 exec, -1
	s_setprio 1
	v_mfma_f32_16x16x32_bf16 v[60:63], v[146:149], v[178:181], v[60:63]
	v_mfma_f32_16x16x32_bf16 v[56:59], v[154:157], v[178:181], v[56:59]
	v_mfma_f32_16x16x32_bf16 v[44:47], v[146:149], v[186:189], v[44:47]
	v_mfma_f32_16x16x32_bf16 v[40:43], v[154:157], v[186:189], v[40:43]
	v_mfma_f32_16x16x32_bf16 v[28:31], v[146:149], v[194:197], v[28:31]
	v_mfma_f32_16x16x32_bf16 v[24:27], v[154:157], v[194:197], v[24:27]
	v_mfma_f32_16x16x32_bf16 v[12:15], v[146:149], v[202:205], v[12:15]
	v_mfma_f32_16x16x32_bf16 v[8:11], v[154:157], v[202:205], v[8:11]
	v_mfma_f32_16x16x32_bf16 v[60:63], v[150:153], v[182:185], v[60:63]
	v_mfma_f32_16x16x32_bf16 v[56:59], v[158:161], v[182:185], v[56:59]
	v_mfma_f32_16x16x32_bf16 v[44:47], v[150:153], v[190:193], v[44:47]
	v_mfma_f32_16x16x32_bf16 v[40:43], v[158:161], v[190:193], v[40:43]
	v_mfma_f32_16x16x32_bf16 v[28:31], v[150:153], v[198:201], v[28:31]
	v_mfma_f32_16x16x32_bf16 v[24:27], v[158:161], v[198:201], v[24:27]
	v_mfma_f32_16x16x32_bf16 v[12:15], v[150:153], v[206:209], v[12:15]
	v_mfma_f32_16x16x32_bf16 v[8:11], v[158:161], v[206:209], v[8:11]
	v_mfma_f32_16x16x32_bf16 v[52:55], v[162:165], v[178:181], v[52:55]
	v_mfma_f32_16x16x32_bf16 v[48:51], v[170:173], v[178:181], v[48:51]
	v_mfma_f32_16x16x32_bf16 v[36:39], v[162:165], v[186:189], v[36:39]
	v_mfma_f32_16x16x32_bf16 v[32:35], v[170:173], v[186:189], v[32:35]
	v_mfma_f32_16x16x32_bf16 v[20:23], v[162:165], v[194:197], v[20:23]
	v_mfma_f32_16x16x32_bf16 v[16:19], v[170:173], v[194:197], v[16:19]
	v_mfma_f32_16x16x32_bf16 v[4:7], v[162:165], v[202:205], v[4:7]
	v_mfma_f32_16x16x32_bf16 v[0:3], v[170:173], v[202:205], v[0:3]
	v_mfma_f32_16x16x32_bf16 v[52:55], v[166:169], v[182:185], v[52:55]
	v_mfma_f32_16x16x32_bf16 v[48:51], v[174:177], v[182:185], v[48:51]
	v_mfma_f32_16x16x32_bf16 v[36:39], v[166:169], v[190:193], v[36:39]
	v_mfma_f32_16x16x32_bf16 v[32:35], v[174:177], v[190:193], v[32:35]
	v_mfma_f32_16x16x32_bf16 v[20:23], v[166:169], v[198:201], v[20:23]
	v_mfma_f32_16x16x32_bf16 v[16:19], v[174:177], v[198:201], v[16:19]
	v_mfma_f32_16x16x32_bf16 v[4:7], v[166:169], v[206:209], v[4:7]
	v_mfma_f32_16x16x32_bf16 v[0:3], v[174:177], v[206:209], v[0:3]
	s_setprio 0
	s_barrier
	s_add_i32 s97, s97, 2
	s_add_u32 s95, s95, 0x100
	s_addc_u32 s96, s96, 0
	s_cmp_gt_u32 s97, 29
	s_mov_b64 s[64:65], s[66:67]
	s_cbranch_scc0 .LBB0_569
	s_branch .Lmy_ex_569
; #define PG8_STAGE(bufoff, gbase, voff) do { _Pragma("unroll") for (int _i = 0; _i < 2; ++_i) { unsigned keep_; \
;         asm volatile("s_mov_b32 %0, m0\n\ts_mov_b32 m0, %3\n\ts_nop 0\n\tglobal_load_lds_dwordx4 %1, %2\n\ts_mov_b32 m0, %0" : "=&s"(keep_) : "v"((voff)[_i]), "s"((const char*)(gbase)), "s"(ldsbase + (unsigned)((bufoff) + _i * 8192)) : "memory"); } } while (0)
; #define PG8_WAIT_V(n) asm volatile("s_waitcnt vmcnt(" #n ")" ::: "memory")
; #define PG8_WAIT_L(n) asm volatile("s_waitcnt lgkmcnt(" #n ")" ::: "memory")
; #define PG8_BAR __builtin_amdgcn_s_barrier()
; #define PG8_SCHED __builtin_amdgcn_sched_barrier(0)
;     DI int nt(const Unit& u) const { return (u.aux & 8) ? PLED / 64 : ((u.aux & 4) ? (D_ / 2) / 64 : D_ / 64); }
; template <class Epi, class Sched, bool ALIGN_EPI, bool FP8 = false>
; DI void gemm_phase(LAS unsigned char* lds, const Gemm g, const Sched& S, const Epi& E) {
;     ...
;             const bool last = (t == nt - 2);
;             const char* a1 = cA + (size_t)(t + 1) * kstep;
;             const char* a2 = last ? nA : cA + (size_t)(t + 2) * kstep; const char* b2 = last ? nB : cB + (size_t)(t + 2) * kstep;
;             const char* a3 = a2 + kstep; const char* b3 = b2 + kstep;
;             PG8_LDB(B0, 0, 0); PG8_LDB(B1, 0, 1); PG8_SCHED; PG8_LDA(At, 0, 0); PG8_STAGE(PG8_SA(1, 1), a1 + hstepA, voffA);
;             PG8_WAIT_V(8); PG8_WAIT_L(0); PG8_BAR; PG8_MMA(0, 0, At, B0); PG8_MMA(0, 1, At, B1); PG8_BAR; PG8_SCHED;
.Lmy_g0_569:
	ds_read_b128 v[146:149], v140
	ds_read_b128 v[150:153], v140 offset:1024
	ds_read_b128 v[154:157], v140 offset:2048
	ds_read_b128 v[158:161], v140 offset:3072
	ds_read_b128 v[162:165], v141
	ds_read_b128 v[166:169], v141 offset:1024
	ds_read_b128 v[170:173], v141 offset:2048
	ds_read_b128 v[174:177], v141 offset:3072
	s_add_u32 s66, s64, 0x100
	s_addc_u32 s67, s65, 0
	s_cmp_eq_u32 s97, 28
	s_cselect_b32 s72, s93, s66
	s_cselect_b32 s73, s57, s67
	s_cselect_b32 s70, s94, s95
	s_cselect_b32 s71, s55, s96
	s_add_u32 s68, s72, 0x80
	s_addc_u32 s69, s73, 0
	ds_read_b128 v[178:181], v142
	ds_read_b128 v[182:185], v142 offset:1024
	ds_read_b128 v[186:189], v142 offset:2048
	ds_read_b128 v[190:193], v142 offset:3072
	ds_read_b128 v[194:197], v142 offset:4096
	ds_read_b128 v[198:201], v142 offset:5120
	ds_read_b128 v[202:205], v142 offset:6144
	ds_read_b128 v[206:209], v142 offset:7168
	s_add_u32 s64, s64, 0x80080
	s_addc_u32 s65, s65, 0
	s_mov_b32 vcc_lo, m0
	s_mov_b32 m0, s89
	s_nop 0
	global_load_lds_dwordx4 v134, s[64:65]
	s_mov_b32 m0, vcc_lo
	s_nop 0
	s_mov_b32 vcc_lo, m0
	s_mov_b32 m0, s90
	s_nop 0
	global_load_lds_dwordx4 v136, s[64:65]
	s_mov_b32 m0, vcc_lo
	s_waitcnt vmcnt(8)
	s_waitcnt lgkmcnt(0)
	s_barrier
	s_setprio 1
	v_mfma_f32_16x16x32_bf16 v[124:127], v[146:149], v[178:181], v[124:127]
	v_mfma_f32_16x16x32_bf16 v[120:123], v[154:157], v[178:181], v[120:123]
	v_mfma_f32_16x16x32_bf16 v[108:111], v[146:149], v[186:189], v[108:111]
	v_mfma_f32_16x16x32_bf16 v[104:107], v[154:157], v[186:189], v[104:107]
	v_mfma_f32_16x16x32_bf16 v[92:95], v[146:149], v[194:197], v[92:95]
	v_mfma_f32_16x16x32_bf16 v[88:91], v[154:157], v[194:197], v[88:91]
	v_mfma_f32_16x16x32_bf16 v[76:79], v[146:149], v[202:205], v[76:79]
	v_mfma_f32_16x16x32_bf16 v[72:75], v[154:157], v[202:205], v[72:75]
	v_mfma_f32_16x16x32_bf16 v[124:127], v[150:153], v[182:185], v[124:127]
	v_mfma_f32_16x16x32_bf16 v[120:123], v[158:161], v[182:185], v[120:123]
	v_mfma_f32_16x16x32_bf16 v[108:111], v[150:153], v[190:193], v[108:111]
	v_mfma_f32_16x16x32_bf16 v[104:107], v[158:161], v[190:193], v[104:107]
	v_mfma_f32_16x16x32_bf16 v[92:95], v[150:153], v[198:201], v[92:95]
	v_mfma_f32_16x16x32_bf16 v[88:91], v[158:161], v[198:201], v[88:91]
	v_mfma_f32_16x16x32_bf16 v[76:79], v[150:153], v[206:209], v[76:79]
	v_mfma_f32_16x16x32_bf16 v[72:75], v[158:161], v[206:209], v[72:75]
	v_mfma_f32_16x16x32_bf16 v[116:119], v[162:165], v[178:181], v[116:119]
	v_mfma_f32_16x16x32_bf16 v[112:115], v[170:173], v[178:181], v[112:115]
	v_mfma_f32_16x16x32_bf16 v[100:103], v[162:165], v[186:189], v[100:103]
	v_mfma_f32_16x16x32_bf16 v[96:99], v[170:173], v[186:189], v[96:99]
	v_mfma_f32_16x16x32_bf16 v[84:87], v[162:165], v[194:197], v[84:87]
	v_mfma_f32_16x16x32_bf16 v[80:83], v[170:173], v[194:197], v[80:83]
	v_mfma_f32_16x16x32_bf16 v[68:71], v[162:165], v[202:205], v[68:71]
	v_mfma_f32_16x16x32_bf16 v[64:67], v[170:173], v[202:205], v[64:67]
	v_mfma_f32_16x16x32_bf16 v[116:119], v[166:169], v[182:185], v[116:119]
	v_mfma_f32_16x16x32_bf16 v[112:115], v[174:177], v[182:185], v[112:115]
	v_mfma_f32_16x16x32_bf16 v[100:103], v[166:169], v[190:193], v[100:103]
	v_mfma_f32_16x16x32_bf16 v[96:99], v[174:177], v[190:193], v[96:99]
	ds_read_b32 v255, v255 offset:4096
	v_mfma_f32_16x16x32_bf16 v[84:87], v[166:169], v[198:201], v[84:87]
	v_mfma_f32_16x16x32_bf16 v[80:83], v[174:177], v[198:201], v[80:83]
	v_mfma_f32_16x16x32_bf16 v[68:71], v[166:169], v[206:209], v[68:71]
	v_mfma_f32_16x16x32_bf16 v[64:67], v[174:177], v[206:209], v[64:67]
	s_add_u32 s98, s98, 0x80000
	s_waitcnt lgkmcnt(0)
	v_readfirstlane_b32 s101, v255
	v_mov_b32_e32 v255, 0x20000
	s_cmp_ge_u32 s101, s98
	s_cbranch_scc1 .Lmy_g_12

; #define PG8_STAGE(bufoff, gbase, voff) do { _Pragma("unroll") for (int _i = 0; _i < 2; ++_i) { unsigned keep_; \
;         asm volatile("s_mov_b32 %0, m0\n\ts_mov_b32 m0, %3\n\ts_nop 0\n\tglobal_load_lds_dwordx4 %1, %2\n\ts_mov_b32 m0, %0" : "=&s"(keep_) : "v"((voff)[_i]), "s"((const char*)(gbase)), "s"(ldsbase + (unsigned)((bufoff) + _i * 8192)) : "memory"); } } while (0)
; #define PG8_WAIT_V(n) asm volatile("s_waitcnt vmcnt(" #n ")" ::: "memory")
; #define PG8_WAIT_L(n) asm volatile("s_waitcnt lgkmcnt(" #n ")" ::: "memory")
; #define PG8_BAR __builtin_amdgcn_s_barrier()
; #define PG8_SCHED __builtin_amdgcn_sched_barrier(0)
; template <class Epi, class Sched, bool ALIGN_EPI, bool FP8 = false>
; DI void gemm_phase(LAS unsigned char* lds, const Gemm g, const Sched& S, const Epi& E) {
;     ...
;             PG8_LDA(At, 0, 1); PG8_STAGE(PG8_SB(0, 0), b2, voffB); PG8_STAGE(PG8_SB(0, 1), b2 + hstepB, voffB); PG8_STAGE(PG8_SA(0, 0), a2, voffA);
;             PG8_WAIT_V(8); PG8_WAIT_L(0); PG8_BAR; PG8_MMA(1, 0, At, B0); PG8_MMA(1, 1, At, B1); PG8_BAR; PG8_SCHED;
.Lmy_g_12:
	s_setprio 0
	ds_read_b128 v[178:181], v142 offset:16384
	ds_read_b128 v[182:185], v142 offset:17408
	ds_read_b128 v[186:189], v142 offset:18432
	ds_read_b128 v[190:193], v142 offset:19456
	ds_read_b128 v[194:197], v142 offset:20480
	ds_read_b128 v[198:201], v142 offset:21504
	ds_read_b128 v[202:205], v142 offset:22528
	ds_read_b128 v[206:209], v142 offset:23552
	s_mov_b32 s64, m0
	s_mov_b32 m0, s63
	s_nop 0
	global_load_lds_dwordx4 v135, s[70:71]
	s_mov_b32 m0, s64
	s_nop 0
	s_mov_b32 s64, m0
	s_mov_b32 m0, s75
	s_nop 0
	global_load_lds_dwordx4 v137, s[70:71]
	s_mov_b32 m0, s64
	s_add_u32 s64, s70, 0x80000
	s_addc_u32 s65, s71, 0
	s_mov_b32 vcc_lo, m0
	s_mov_b32 m0, s77
	s_nop 0
	global_load_lds_dwordx4 v135, s[64:65]
	s_mov_b32 m0, vcc_lo
	s_nop 0
	s_mov_b32 vcc_lo, m0
	s_mov_b32 m0, s79
	s_nop 0
	global_load_lds_dwordx4 v137, s[64:65]
	s_mov_b32 m0, vcc_lo
	s_mov_b32 s64, m0
	s_mov_b32 m0, s74
	s_nop 0
	global_load_lds_dwordx4 v134, s[72:73]
	s_mov_b32 m0, s64
	s_nop 0
	s_mov_b32 s64, m0
	s_mov_b32 m0, s80
	s_nop 0
	global_load_lds_dwordx4 v136, s[72:73]
	s_mov_b32 m0, s64
	s_waitcnt vmcnt(8)
	s_waitcnt lgkmcnt(0)
	s_barrier
	s_setprio 1
	v_mfma_f32_16x16x32_bf16 v[60:63], v[146:149], v[178:181], v[60:63]
	v_mfma_f32_16x16x32_bf16 v[56:59], v[154:157], v[178:181], v[56:59]
	v_mfma_f32_16x16x32_bf16 v[44:47], v[146:149], v[186:189], v[44:47]
	v_mfma_f32_16x16x32_bf16 v[40:43], v[154:157], v[186:189], v[40:43]
	v_mfma_f32_16x16x32_bf16 v[28:31], v[146:149], v[194:197], v[28:31]
	v_mfma_f32_16x16x32_bf16 v[24:27], v[154:157], v[194:197], v[24:27]
	v_mfma_f32_16x16x32_bf16 v[12:15], v[146:149], v[202:205], v[12:15]
	v_mfma_f32_16x16x32_bf16 v[8:11], v[154:157], v[202:205], v[8:11]
	v_mfma_f32_16x16x32_bf16 v[60:63], v[150:153], v[182:185], v[60:63]
	v_mfma_f32_16x16x32_bf16 v[56:59], v[158:161], v[182:185], v[56:59]
	v_mfma_f32_16x16x32_bf16 v[44:47], v[150:153], v[190:193], v[44:47]
	v_mfma_f32_16x16x32_bf16 v[40:43], v[158:161], v[190:193], v[40:43]
	v_mfma_f32_16x16x32_bf16 v[28:31], v[150:153], v[198:201], v[28:31]
	v_mfma_f32_16x16x32_bf16 v[24:27], v[158:161], v[198:201], v[24:27]
	v_mfma_f32_16x16x32_bf16 v[12:15], v[150:153], v[206:209], v[12:15]
	v_mfma_f32_16x16x32_bf16 v[8:11], v[158:161], v[206:209], v[8:11]
	v_mfma_f32_16x16x32_bf16 v[52:55], v[162:165], v[178:181], v[52:55]
	v_mfma_f32_16x16x32_bf16 v[48:51], v[170:173], v[178:181], v[48:51]
	v_mfma_f32_16x16x32_bf16 v[36:39], v[162:165], v[186:189], v[36:39]
	v_mfma_f32_16x16x32_bf16 v[32:35], v[170:173], v[186:189], v[32:35]
	v_mfma_f32_16x16x32_bf16 v[20:23], v[162:165], v[194:197], v[20:23]
	v_mfma_f32_16x16x32_bf16 v[16:19], v[170:173], v[194:197], v[16:19]
	v_mfma_f32_16x16x32_bf16 v[4:7], v[162:165], v[202:205], v[4:7]
	v_mfma_f32_16x16x32_bf16 v[0:3], v[170:173], v[202:205], v[0:3]
	v_mfma_f32_16x16x32_bf16 v[52:55], v[166:169], v[182:185], v[52:55]
	v_mfma_f32_16x16x32_bf16 v[48:51], v[174:177], v[182:185], v[48:51]
	v_mfma_f32_16x16x32_bf16 v[36:39], v[166:169], v[190:193], v[36:39]
	v_mfma_f32_16x16x32_bf16 v[32:35], v[174:177], v[190:193], v[32:35]
	ds_read_b32 v255, v255 offset:4096
	v_mfma_f32_16x16x32_bf16 v[20:23], v[166:169], v[198:201], v[20:23]
	v_mfma_f32_16x16x32_bf16 v[16:19], v[174:177], v[198:201], v[16:19]
	v_mfma_f32_16x16x32_bf16 v[4:7], v[166:169], v[206:209], v[4:7]
	v_mfma_f32_16x16x32_bf16 v[0:3], v[174:177], v[206:209], v[0:3]
	s_add_u32 s98, s98, 0x80000
	s_waitcnt lgkmcnt(0)
	v_readfirstlane_b32 s101, v255
	v_mov_b32_e32 v255, 0x20000
	s_cmp_ge_u32 s101, s98
	s_cbranch_scc1 .Lmy_g_13

; #define PG8_STAGE(bufoff, gbase, voff) do { _Pragma("unroll") for (int _i = 0; _i < 2; ++_i) { unsigned keep_; \
;         asm volatile("s_mov_b32 %0, m0\n\ts_mov_b32 m0, %3\n\ts_nop 0\n\tglobal_load_lds_dwordx4 %1, %2\n\ts_mov_b32 m0, %0" : "=&s"(keep_) : "v"((voff)[_i]), "s"((const char*)(gbase)), "s"(ldsbase + (unsigned)((bufoff) + _i * 8192)) : "memory"); } } while (0)
; #define PG8_WAIT_V(n) asm volatile("s_waitcnt vmcnt(" #n ")" ::: "memory")
; #define PG8_WAIT_L(n) asm volatile("s_waitcnt lgkmcnt(" #n ")" ::: "memory")
; #define PG8_BAR __builtin_amdgcn_s_barrier()
; #define PG8_SCHED __builtin_amdgcn_sched_barrier(0)
; template <class Epi, class Sched, bool ALIGN_EPI, bool FP8 = false>
; DI void gemm_phase(LAS unsigned char* lds, const Gemm g, const Sched& S, const Epi& E) {
;     ...
;             PG8_LDB(B0, 1, 0); PG8_LDB(B1, 1, 1); PG8_SCHED; PG8_LDA(At, 1, 0); PG8_STAGE(PG8_SA(0, 1), a2 + hstepA, voffA);
;             PG8_WAIT_V(8); PG8_WAIT_L(0); PG8_BAR; PG8_MMA(0, 0, At, B0); PG8_MMA(0, 1, At, B1); PG8_BAR; PG8_SCHED;
.Lmy_g_13:
	s_setprio 0
	ds_read_b128 v[146:149], v143
	ds_read_b128 v[150:153], v143 offset:1024
	ds_read_b128 v[154:157], v143 offset:2048
	ds_read_b128 v[158:161], v143 offset:3072
	ds_read_b128 v[162:165], v144
	ds_read_b128 v[166:169], v144 offset:1024
	ds_read_b128 v[170:173], v144 offset:2048
	ds_read_b128 v[174:177], v144 offset:3072
	ds_read_b128 v[178:181], v142 offset:32768
	ds_read_b128 v[182:185], v142 offset:33792
	ds_read_b128 v[186:189], v142 offset:34816
	ds_read_b128 v[190:193], v142 offset:35840
	ds_read_b128 v[194:197], v142 offset:36864
	ds_read_b128 v[198:201], v142 offset:37888
	ds_read_b128 v[202:205], v142 offset:38912
	ds_read_b128 v[206:209], v142 offset:39936
	s_add_u32 s64, s72, 0x80000
	s_addc_u32 s65, s73, 0
	s_mov_b32 s72, m0
	s_mov_b32 m0, s81
	s_nop 0
	global_load_lds_dwordx4 v134, s[64:65]
	s_mov_b32 m0, s72
	s_nop 0
	s_mov_b32 s72, m0
	s_mov_b32 m0, s82
	s_nop 0
	global_load_lds_dwordx4 v136, s[64:65]
	s_mov_b32 m0, s72
	s_waitcnt vmcnt(8)
	s_waitcnt lgkmcnt(0)
	s_barrier
	s_setprio 1
	v_mfma_f32_16x16x32_bf16 v[124:127], v[146:149], v[178:181], v[124:127]
	v_mfma_f32_16x16x32_bf16 v[120:123], v[154:157], v[178:181], v[120:123]
	v_mfma_f32_16x16x32_bf16 v[108:111], v[146:149], v[186:189], v[108:111]
	v_mfma_f32_16x16x32_bf16 v[104:107], v[154:157], v[186:189], v[104:107]
	v_mfma_f32_16x16x32_bf16 v[92:95], v[146:149], v[194:197], v[92:95]
	v_mfma_f32_16x16x32_bf16 v[88:91], v[154:157], v[194:197], v[88:91]
	v_mfma_f32_16x16x32_bf16 v[76:79], v[146:149], v[202:205], v[76:79]
	v_mfma_f32_16x16x32_bf16 v[72:75], v[154:157], v[202:205], v[72:75]
	v_mfma_f32_16x16x32_bf16 v[124:127], v[150:153], v[182:185], v[124:127]
	v_mfma_f32_16x16x32_bf16 v[120:123], v[158:161], v[182:185], v[120:123]
	v_mfma_f32_16x16x32_bf16 v[108:111], v[150:153], v[190:193], v[108:111]
	v_mfma_f32_16x16x32_bf16 v[104:107], v[158:161], v[190:193], v[104:107]
	v_mfma_f32_16x16x32_bf16 v[92:95], v[150:153], v[198:201], v[92:95]
	v_mfma_f32_16x16x32_bf16 v[88:91], v[158:161], v[198:201], v[88:91]
	v_mfma_f32_16x16x32_bf16 v[76:79], v[150:153], v[206:209], v[76:79]
	v_mfma_f32_16x16x32_bf16 v[72:75], v[158:161], v[206:209], v[72:75]
	v_mfma_f32_16x16x32_bf16 v[116:119], v[162:165], v[178:181], v[116:119]
	v_mfma_f32_16x16x32_bf16 v[112:115], v[170:173], v[178:181], v[112:115]
	v_mfma_f32_16x16x32_bf16 v[100:103], v[162:165], v[186:189], v[100:103]
	v_mfma_f32_16x16x32_bf16 v[96:99], v[170:173], v[186:189], v[96:99]
	v_mfma_f32_16x16x32_bf16 v[84:87], v[162:165], v[194:197], v[84:87]
	v_mfma_f32_16x16x32_bf16 v[80:83], v[170:173], v[194:197], v[80:83]
	v_mfma_f32_16x16x32_bf16 v[68:71], v[162:165], v[202:205], v[68:71]
	v_mfma_f32_16x16x32_bf16 v[64:67], v[170:173], v[202:205], v[64:67]
	v_mfma_f32_16x16x32_bf16 v[116:119], v[166:169], v[182:185], v[116:119]
	v_mfma_f32_16x16x32_bf16 v[112:115], v[174:177], v[182:185], v[112:115]
	v_mfma_f32_16x16x32_bf16 v[100:103], v[166:169], v[190:193], v[100:103]
	v_mfma_f32_16x16x32_bf16 v[96:99], v[174:177], v[190:193], v[96:99]
	ds_read_b32 v255, v255 offset:4096
	v_mfma_f32_16x16x32_bf16 v[84:87], v[166:169], v[198:201], v[84:87]
	v_mfma_f32_16x16x32_bf16 v[80:83], v[174:177], v[198:201], v[80:83]
	v_mfma_f32_16x16x32_bf16 v[68:71], v[166:169], v[206:209], v[68:71]
	v_mfma_f32_16x16x32_bf16 v[64:67], v[174:177], v[206:209], v[64:67]
	s_add_u32 s98, s98, 0x80000
	s_waitcnt lgkmcnt(0)
	v_readfirstlane_b32 s101, v255
	v_mov_b32_e32 v255, 0x20000
	s_cmp_ge_u32 s101, s98
	s_cbranch_scc1 .Lmy_g_14

; #define PG8_STAGE(bufoff, gbase, voff) do { _Pragma("unroll") for (int _i = 0; _i < 2; ++_i) { unsigned keep_; \
;         asm volatile("s_mov_b32 %0, m0\n\ts_mov_b32 m0, %3\n\ts_nop 0\n\tglobal_load_lds_dwordx4 %1, %2\n\ts_mov_b32 m0, %0" : "=&s"(keep_) : "v"((voff)[_i]), "s"((const char*)(gbase)), "s"(ldsbase + (unsigned)((bufoff) + _i * 8192)) : "memory"); } } while (0)
; #define PG8_WAIT_V(n) asm volatile("s_waitcnt vmcnt(" #n ")" ::: "memory")
; #define PG8_WAIT_L(n) asm volatile("s_waitcnt lgkmcnt(" #n ")" ::: "memory")
; #define PG8_BAR __builtin_amdgcn_s_barrier()
; #define PG8_SCHED __builtin_amdgcn_sched_barrier(0)
; template <class Epi, class Sched, bool ALIGN_EPI, bool FP8 = false>
; DI void gemm_phase(LAS unsigned char* lds, const Gemm g, const Sched& S, const Epi& E) {
;     ...
;             PG8_LDA(At, 1, 1); PG8_STAGE(PG8_SB(1, 0), b3, voffB); PG8_STAGE(PG8_SB(1, 1), b3 + hstepB, voffB); PG8_STAGE(PG8_SA(1, 0), a3, voffA);
;             PG8_WAIT_V(8); PG8_WAIT_L(0); PG8_BAR; PG8_MMA(1, 0, At, B0); PG8_MMA(1, 1, At, B1); PG8_BAR; PG8_SCHED;
.Lmy_g_14:
	s_setprio 0
	ds_read_b128 v[178:181], v142 offset:49152
	ds_read_b128 v[182:185], v142 offset:50176
	ds_read_b128 v[186:189], v142 offset:51200
	ds_read_b128 v[190:193], v142 offset:52224
	ds_read_b128 v[194:197], v142 offset:53248
	ds_read_b128 v[198:201], v142 offset:54272
	ds_read_b128 v[202:205], v142 offset:55296
	ds_read_b128 v[206:209], v142 offset:56320
	s_add_u32 s64, s70, 0x80
	s_addc_u32 s65, s71, 0
	s_mov_b32 s72, m0
	s_mov_b32 m0, s83
	s_nop 0
	global_load_lds_dwordx4 v135, s[64:65]
	s_mov_b32 m0, s72
	s_nop 0
	s_mov_b32 s72, m0
	s_mov_b32 m0, s84
	s_nop 0
	global_load_lds_dwordx4 v137, s[64:65]
	s_mov_b32 m0, s72
	s_add_u32 s64, s70, 0x80080
	s_addc_u32 s65, s71, 0
	s_mov_b32 s70, m0
	s_mov_b32 m0, s87
	s_nop 0
	global_load_lds_dwordx4 v135, s[64:65]
	s_mov_b32 m0, s70
	s_nop 0
	s_mov_b32 s70, m0
	s_mov_b32 m0, s88
	s_nop 0
	global_load_lds_dwordx4 v137, s[64:65]
	s_mov_b32 m0, s70
	s_mov_b32 s64, m0
	s_mov_b32 m0, s85
	s_nop 0
	global_load_lds_dwordx4 v134, s[68:69]
	s_mov_b32 m0, s64
	s_nop 0
	s_mov_b32 s64, m0
	s_mov_b32 m0, s86
	s_nop 0
	global_load_lds_dwordx4 v136, s[68:69]
	s_mov_b32 m0, s64
	s_waitcnt vmcnt(8)
	s_waitcnt lgkmcnt(0)
	s_barrier
	s_setprio 1
	v_mfma_f32_16x16x32_bf16 v[60:63], v[146:149], v[178:181], v[60:63]
	v_mfma_f32_16x16x32_bf16 v[56:59], v[154:157], v[178:181], v[56:59]
	v_mfma_f32_16x16x32_bf16 v[44:47], v[146:149], v[186:189], v[44:47]
	v_mfma_f32_16x16x32_bf16 v[40:43], v[154:157], v[186:189], v[40:43]
	v_mfma_f32_16x16x32_bf16 v[28:31], v[146:149], v[194:197], v[28:31]
	v_mfma_f32_16x16x32_bf16 v[24:27], v[154:157], v[194:197], v[24:27]
	v_mfma_f32_16x16x32_bf16 v[12:15], v[146:149], v[202:205], v[12:15]
	v_mfma_f32_16x16x32_bf16 v[8:11], v[154:157], v[202:205], v[8:11]
	v_mfma_f32_16x16x32_bf16 v[60:63], v[150:153], v[182:185], v[60:63]
	v_mfma_f32_16x16x32_bf16 v[56:59], v[158:161], v[182:185], v[56:59]
	v_mfma_f32_16x16x32_bf16 v[44:47], v[150:153], v[190:193], v[44:47]
	v_mfma_f32_16x16x32_bf16 v[40:43], v[158:161], v[190:193], v[40:43]
	v_mfma_f32_16x16x32_bf16 v[28:31], v[150:153], v[198:201], v[28:31]
	v_mfma_f32_16x16x32_bf16 v[24:27], v[158:161], v[198:201], v[24:27]
	v_mfma_f32_16x16x32_bf16 v[12:15], v[150:153], v[206:209], v[12:15]
	v_mfma_f32_16x16x32_bf16 v[8:11], v[158:161], v[206:209], v[8:11]
	v_mfma_f32_16x16x32_bf16 v[52:55], v[162:165], v[178:181], v[52:55]
	v_mfma_f32_16x16x32_bf16 v[48:51], v[170:173], v[178:181], v[48:51]
	v_mfma_f32_16x16x32_bf16 v[36:39], v[162:165], v[186:189], v[36:39]
	v_mfma_f32_16x16x32_bf16 v[32:35], v[170:173], v[186:189], v[32:35]
	v_mfma_f32_16x16x32_bf16 v[20:23], v[162:165], v[194:197], v[20:23]
	v_mfma_f32_16x16x32_bf16 v[16:19], v[170:173], v[194:197], v[16:19]
	v_mfma_f32_16x16x32_bf16 v[4:7], v[162:165], v[202:205], v[4:7]
	v_mfma_f32_16x16x32_bf16 v[0:3], v[170:173], v[202:205], v[0:3]
	v_mfma_f32_16x16x32_bf16 v[52:55], v[166:169], v[182:185], v[52:55]
	v_mfma_f32_16x16x32_bf16 v[48:51], v[174:177], v[182:185], v[48:51]
	v_mfma_f32_16x16x32_bf16 v[36:39], v[166:169], v[190:193], v[36:39]
	v_mfma_f32_16x16x32_bf16 v[32:35], v[174:177], v[190:193], v[32:35]
	ds_read_b32 v255, v255 offset:4096
	v_mfma_f32_16x16x32_bf16 v[20:23], v[166:169], v[198:201], v[20:23]
	v_mfma_f32_16x16x32_bf16 v[16:19], v[174:177], v[198:201], v[16:19]
	v_mfma_f32_16x16x32_bf16 v[4:7], v[166:169], v[206:209], v[4:7]
	v_mfma_f32_16x16x32_bf16 v[0:3], v[174:177], v[206:209], v[0:3]
	s_add_u32 s98, s98, 0x80000
	s_waitcnt lgkmcnt(0)
	v_readfirstlane_b32 s101, v255
	v_mov_b32_e32 v255, 0x20000
	s_cmp_ge_u32 s101, s98
	s_cbranch_scc1 .Lmy_g_15

; DI unsigned cvt_pk_bf16(float lo, float hi) { const f32x2_t v = {lo, hi}; return __builtin_bit_cast(unsigned, __builtin_convertvector(v, bf16x2_t)); }
; #define PG8_BAR __builtin_amdgcn_s_barrier()
; template <class Epi, class Sched, bool ALIGN_EPI, bool FP8 = false>
; DI void gemm_phase(LAS unsigned char* lds, const Gemm g, const Sched& S, const Epi& E) {
;     ...
;         if constexpr (ALIGN_EPI) { if (wr == 0) PG8_BAR; }
;     DI void operator()(const f32x4 (&acc)[2][2][4][2], const Unit& u, int wr, int wc, int fr, int fq) const {
;         int row0 = u.pm * BM + wr * 64 + fr; asm volatile("" : "+v"(row0));
;         const int col0 = u.pn * BM + wc * 32 + 8 * fq;
; #pragma unroll
;         for (int ai = 0; ai < 2; ++ai)
; #pragma unroll
;             for (int m = 0; m < 4; ++m) { const size_t r = (size_t)(row0 + ai * HALF + m * 16);
; #pragma unroll
;                 for (int bj = 0; bj < 2; ++bj) { const size_t o = r * D_ + col0 + bj * HALF; f32x4 x0, x1; unpack8f(*(const u32x4*)(R0 + o), x0, x1);
;                     f32x4 v0 = ALPHA * x0 + acc[ai][bj][m][0], v1 = ALPHA * x1 + acc[ai][bj][m][1];
;                     if (HAS_R1) { f32x4 q0, q1; unpack8f(*(const u32x4*)(R1 + o), q0, q1); v0 = v0 + q0; v1 = v1 + q1; }
;                     u32x4 w; w.x = cvt_pk_bf16(v0[0], v0[1]); w.y = cvt_pk_bf16(v0[2], v0[3]); w.z = cvt_pk_bf16(v1[0], v1[1]); w.w = cvt_pk_bf16(v1[2], v1[3]);
;                     *(u32x4*)(Yo + o) = w; }
;                 if (m & 1) asm volatile("" ::: "memory"); }
;     }
.Lmy_g_15:
	s_setprio 0
	s_add_i32 s97, s97, 2
	s_add_u32 s95, s95, 0x100
	s_addc_u32 s96, s96, 0
	s_cmp_gt_u32 s97, 29
	s_mov_b64 s[64:65], s[66:67]
	s_cbranch_scc0 .Lmy_g0_569
.Lmy_ex_569:
	s_and_b64 vcc, exec, s[14:15]
	s_cbranch_vccz .LBB0_572
	s_barrier
.LBB0_572:
	v_lshl_add_u32 v132, s62, 8, v138
	v_lshl_or_b32 v146, s92, 8, v139
	v_ashrrev_i32_e32 v133, 31, v132
	v_ashrrev_i32_e32 v147, 31, v146
	v_lshlrev_b64 v[132:133], 11, v[132:133]
	v_lshl_add_u64 v[132:133], v[132:133], 0, v[146:147]
	v_lshlrev_b64 v[132:133], 1, v[132:133]
	v_lshl_add_u64 v[146:147], s[10:11], 0, v[132:133]
	v_or_b32_e32 v154, 0x100, v132
	v_mov_b32_e32 v155, v133
	global_load_dwordx4 v[146:149], v[146:147], off
	v_lshl_add_u64 v[150:151], s[10:11], 0, v[154:155]
	global_load_dwordx4 v[150:153], v[150:151], off
	v_lshl_add_u64 v[156:157], s[12:13], 0, v[132:133]
	v_lshl_add_u64 v[158:159], v[132:133], 0, s[18:19]
	v_lshl_add_u64 v[154:155], s[12:13], 0, v[154:155]
	v_lshl_add_u64 v[160:161], s[10:11], 0, v[158:159]
	s_mov_b64 s[64:65], 0x80000
	s_andn2_b64 vcc, exec, s[4:5]
	s_mov_b64 s[4:5], -1
	s_waitcnt vmcnt(1)
	v_lshlrev_b32_e32 v162, 16, v146
	v_and_b32_e32 v163, 0xffff0000, v146
	v_lshlrev_b32_e32 v146, 16, v147
	v_and_b32_e32 v147, 0xffff0000, v147
	v_lshlrev_b32_e32 v164, 16, v148
	v_and_b32_e32 v165, 0xffff0000, v148
	v_lshlrev_b32_e32 v148, 16, v149
	v_and_b32_e32 v149, 0xffff0000, v149
	v_pk_fma_f32 v[126:127], v[146:147], s[16:17], v[126:127] op_sel_hi:[1,0,1]
	v_pk_fma_f32 v[124:125], v[162:163], s[16:17], v[124:125] op_sel_hi:[1,0,1]
	v_pk_fma_f32 v[146:147], v[148:149], s[16:17], v[122:123] op_sel_hi:[1,0,1]
	s_waitcnt vmcnt(0)
	v_lshlrev_b32_e32 v148, 16, v150
	v_and_b32_e32 v149, 0xffff0000, v150
	v_lshlrev_b32_e32 v150, 16, v151
	v_and_b32_e32 v151, 0xffff0000, v151
	v_lshlrev_b32_e32 v162, 16, v152
	v_and_b32_e32 v163, 0xffff0000, v152
	v_lshlrev_b32_e32 v152, 16, v153
	v_and_b32_e32 v153, 0xffff0000, v153
	v_pk_fma_f32 v[122:123], v[164:165], s[16:17], v[120:121] op_sel_hi:[1,0,1]
	v_cvt_pk_bf16_f32 v120, v124, v125
	v_pk_fma_f32 v[118:119], v[150:151], s[16:17], v[118:119] op_sel_hi:[1,0,1]
	v_pk_fma_f32 v[116:117], v[148:149], s[16:17], v[116:117] op_sel_hi:[1,0,1]
	v_pk_fma_f32 v[124:125], v[152:153], s[16:17], v[114:115] op_sel_hi:[1,0,1]
	v_pk_fma_f32 v[114:115], v[162:163], s[16:17], v[112:113] op_sel_hi:[1,0,1]
	v_cvt_pk_bf16_f32 v121, v126, v127
	v_cvt_pk_bf16_f32 v122, v122, v123
	v_cvt_pk_bf16_f32 v123, v146, v147
	v_cvt_pk_bf16_f32 v112, v116, v117
	v_cvt_pk_bf16_f32 v113, v118, v119
	v_cvt_pk_bf16_f32 v114, v114, v115
	v_cvt_pk_bf16_f32 v115, v124, v125
	global_store_dwordx4 v[156:157], v[120:123], off
	global_store_dwordx4 v[154:155], v[112:115], off
	global_load_dwordx4 v[112:115], v[160:161], off
	v_lshl_add_u64 v[120:121], v[132:133], 0, s[20:21]
	v_lshl_add_u64 v[116:117], s[10:11], 0, v[120:121]
	global_load_dwordx4 v[116:119], v[116:117], off
	v_lshl_add_u64 v[124:125], s[12:13], 0, v[158:159]
	v_lshl_add_u64 v[122:123], v[132:133], 0, s[22:23]
	v_lshl_add_u64 v[120:121], s[12:13], 0, v[120:121]
	v_lshl_add_u64 v[126:127], s[10:11], 0, v[122:123]
	s_waitcnt vmcnt(1)
	v_lshlrev_b32_e32 v146, 16, v112
	v_and_b32_e32 v147, 0xffff0000, v112
	v_lshlrev_b32_e32 v112, 16, v113
	v_and_b32_e32 v113, 0xffff0000, v113
	v_lshlrev_b32_e32 v148, 16, v114
	v_and_b32_e32 v149, 0xffff0000, v114
	v_lshlrev_b32_e32 v114, 16, v115
	v_and_b32_e32 v115, 0xffff0000, v115
	s_waitcnt vmcnt(0)
	v_lshlrev_b32_e32 v150, 16, v116
	v_and_b32_e32 v151, 0xffff0000, v116
	v_lshlrev_b32_e32 v116, 16, v117
	v_and_b32_e32 v117, 0xffff0000, v117
	v_lshlrev_b32_e32 v152, 16, v118
	v_and_b32_e32 v153, 0xffff0000, v118
	v_lshlrev_b32_e32 v118, 16, v119
	v_and_b32_e32 v119, 0xffff0000, v119
	v_pk_fma_f32 v[110:111], v[112:113], s[16:17], v[110:111] op_sel_hi:[1,0,1]
	v_pk_fma_f32 v[108:109], v[146:147], s[16:17], v[108:109] op_sel_hi:[1,0,1]
	v_pk_fma_f32 v[106:107], v[114:115], s[16:17], v[106:107] op_sel_hi:[1,0,1]
	v_pk_fma_f32 v[104:105], v[148:149], s[16:17], v[104:105] op_sel_hi:[1,0,1]
	v_pk_fma_f32 v[102:103], v[116:117], s[16:17], v[102:103] op_sel_hi:[1,0,1]
	v_pk_fma_f32 v[100:101], v[150:151], s[16:17], v[100:101] op_sel_hi:[1,0,1]
	v_pk_fma_f32 v[112:113], v[118:119], s[16:17], v[98:99] op_sel_hi:[1,0,1]
	v_pk_fma_f32 v[114:115], v[152:153], s[16:17], v[96:97] op_sel_hi:[1,0,1]
	v_cvt_pk_bf16_f32 v96, v108, v109
	v_cvt_pk_bf16_f32 v97, v110, v111
	v_cvt_pk_bf16_f32 v98, v104, v105
	v_cvt_pk_bf16_f32 v99, v106, v107
	v_cvt_pk_bf16_f32 v100, v100, v101
	v_cvt_pk_bf16_f32 v101, v102, v103
	v_cvt_pk_bf16_f32 v102, v114, v115
	v_cvt_pk_bf16_f32 v103, v112, v113
	global_store_dwordx4 v[124:125], v[96:99], off
	global_store_dwordx4 v[120:121], v[100:103], off
	v_lshl_add_u64 v[104:105], v[132:133], 0, s[24:25]
	global_load_dwordx4 v[96:99], v[126:127], off
	v_lshl_add_u64 v[100:101], s[10:11], 0, v[104:105]
	global_load_dwordx4 v[100:103], v[100:101], off
	v_lshl_add_u64 v[106:107], v[132:133], 0, s[26:27]
	v_lshl_add_u64 v[108:109], s[12:13], 0, v[122:123]
	v_lshl_add_u64 v[104:105], s[12:13], 0, v[104:105]
	v_lshl_add_u64 v[110:111], s[10:11], 0, v[106:107]
	s_waitcnt vmcnt(1)
	v_lshlrev_b32_e32 v112, 16, v96
	v_and_b32_e32 v113, 0xffff0000, v96
	v_lshlrev_b32_e32 v96, 16, v97
	v_and_b32_e32 v97, 0xffff0000, v97
	v_lshlrev_b32_e32 v114, 16, v98
	v_and_b32_e32 v115, 0xffff0000, v98
	v_lshlrev_b32_e32 v98, 16, v99
	v_and_b32_e32 v99, 0xffff0000, v99
	s_waitcnt vmcnt(0)
; DI unsigned cvt_pk_bf16(float lo, float hi) { const f32x2_t v = {lo, hi}; return __builtin_bit_cast(unsigned, __builtin_convertvector(v, bf16x2_t)); }
;     DI void operator()(const f32x4 (&acc)[2][2][4][2], const Unit& u, int wr, int wc, int fr, int fq) const {
;         int row0 = u.pm * BM + wr * 64 + fr; asm volatile("" : "+v"(row0));
;         const int col0 = u.pn * BM + wc * 32 + 8 * fq;
; #pragma unroll
;         for (int ai = 0; ai < 2; ++ai)
; #pragma unroll
;             for (int m = 0; m < 4; ++m) { const size_t r = (size_t)(row0 + ai * HALF + m * 16);
; #pragma unroll
;                 for (int bj = 0; bj < 2; ++bj) { const size_t o = r * D_ + col0 + bj * HALF; f32x4 x0, x1; unpack8f(*(const u32x4*)(R0 + o), x0, x1);
;                     f32x4 v0 = ALPHA * x0 + acc[ai][bj][m][0], v1 = ALPHA * x1 + acc[ai][bj][m][1];
;                     if (HAS_R1) { f32x4 q0, q1; unpack8f(*(const u32x4*)(R1 + o), q0, q1); v0 = v0 + q0; v1 = v1 + q1; }
;                     u32x4 w; w.x = cvt_pk_bf16(v0[0], v0[1]); w.y = cvt_pk_bf16(v0[2], v0[3]); w.z = cvt_pk_bf16(v1[0], v1[1]); w.w = cvt_pk_bf16(v1[2], v1[3]);
;                     *(u32x4*)(Yo + o) = w; }
;                 if (m & 1) asm volatile("" ::: "memory"); }
;     }
	v_lshlrev_b32_e32 v116, 16, v100
	v_and_b32_e32 v117, 0xffff0000, v100
	v_lshlrev_b32_e32 v100, 16, v101
	v_and_b32_e32 v101, 0xffff0000, v101
	v_lshlrev_b32_e32 v118, 16, v102
	v_and_b32_e32 v119, 0xffff0000, v102
	v_lshlrev_b32_e32 v102, 16, v103
	v_and_b32_e32 v103, 0xffff0000, v103
	v_pk_fma_f32 v[94:95], v[96:97], s[16:17], v[94:95] op_sel_hi:[1,0,1]
	v_pk_fma_f32 v[92:93], v[112:113], s[16:17], v[92:93] op_sel_hi:[1,0,1]
	v_pk_fma_f32 v[90:91], v[98:99], s[16:17], v[90:91] op_sel_hi:[1,0,1]
	v_pk_fma_f32 v[88:89], v[114:115], s[16:17], v[88:89] op_sel_hi:[1,0,1]
	v_pk_fma_f32 v[86:87], v[100:101], s[16:17], v[86:87] op_sel_hi:[1,0,1]
	v_pk_fma_f32 v[84:85], v[116:117], s[16:17], v[84:85] op_sel_hi:[1,0,1]
	v_pk_fma_f32 v[96:97], v[102:103], s[16:17], v[82:83] op_sel_hi:[1,0,1]
	v_pk_fma_f32 v[98:99], v[118:119], s[16:17], v[80:81] op_sel_hi:[1,0,1]
	v_cvt_pk_bf16_f32 v80, v92, v93
	v_cvt_pk_bf16_f32 v81, v94, v95
	v_cvt_pk_bf16_f32 v82, v88, v89
	v_cvt_pk_bf16_f32 v83, v90, v91
	v_cvt_pk_bf16_f32 v84, v84, v85
	v_cvt_pk_bf16_f32 v85, v86, v87
	v_cvt_pk_bf16_f32 v86, v98, v99
	v_cvt_pk_bf16_f32 v87, v96, v97
	global_store_dwordx4 v[108:109], v[80:83], off
	global_store_dwordx4 v[104:105], v[84:87], off
	v_lshl_add_u64 v[88:89], v[132:133], 0, s[28:29]
	global_load_dwordx4 v[80:83], v[110:111], off
	v_lshl_add_u64 v[84:85], s[10:11], 0, v[88:89]
	global_load_dwordx4 v[84:87], v[84:85], off
	v_lshl_add_u64 v[92:93], s[12:13], 0, v[106:107]
	v_lshl_add_u64 v[90:91], v[132:133], 0, s[64:65]
	v_lshl_add_u64 v[88:89], s[12:13], 0, v[88:89]
	v_lshl_add_u64 v[94:95], s[10:11], 0, v[90:91]
	s_waitcnt vmcnt(1)
	v_lshlrev_b32_e32 v96, 16, v80
	v_and_b32_e32 v97, 0xffff0000, v80
	v_lshlrev_b32_e32 v80, 16, v81
	v_and_b32_e32 v81, 0xffff0000, v81
	v_lshlrev_b32_e32 v98, 16, v82
	v_and_b32_e32 v99, 0xffff0000, v82
	v_lshlrev_b32_e32 v82, 16, v83
	v_and_b32_e32 v83, 0xffff0000, v83
	s_waitcnt vmcnt(0)
	v_lshlrev_b32_e32 v100, 16, v84
	v_and_b32_e32 v101, 0xffff0000, v84
	v_lshlrev_b32_e32 v84, 16, v85
	v_and_b32_e32 v85, 0xffff0000, v85
	v_lshlrev_b32_e32 v102, 16, v86
	v_and_b32_e32 v103, 0xffff0000, v86
	v_lshlrev_b32_e32 v86, 16, v87
	v_and_b32_e32 v87, 0xffff0000, v87
	v_pk_fma_f32 v[78:79], v[80:81], s[16:17], v[78:79] op_sel_hi:[1,0,1]
	v_pk_fma_f32 v[76:77], v[96:97], s[16:17], v[76:77] op_sel_hi:[1,0,1]
	v_pk_fma_f32 v[74:75], v[82:83], s[16:17], v[74:75] op_sel_hi:[1,0,1]
	v_pk_fma_f32 v[72:73], v[98:99], s[16:17], v[72:73] op_sel_hi:[1,0,1]
	v_pk_fma_f32 v[70:71], v[84:85], s[16:17], v[70:71] op_sel_hi:[1,0,1]
	v_pk_fma_f32 v[68:69], v[100:101], s[16:17], v[68:69] op_sel_hi:[1,0,1]
	v_pk_fma_f32 v[80:81], v[86:87], s[16:17], v[66:67] op_sel_hi:[1,0,1]
	v_pk_fma_f32 v[82:83], v[102:103], s[16:17], v[64:65] op_sel_hi:[1,0,1]
	v_cvt_pk_bf16_f32 v64, v76, v77
	v_cvt_pk_bf16_f32 v65, v78, v79
	v_cvt_pk_bf16_f32 v66, v72, v73
	v_cvt_pk_bf16_f32 v67, v74, v75
	v_cvt_pk_bf16_f32 v68, v68, v69
	v_cvt_pk_bf16_f32 v69, v70, v71
	v_cvt_pk_bf16_f32 v70, v82, v83
	v_cvt_pk_bf16_f32 v71, v80, v81
	global_store_dwordx4 v[92:93], v[64:67], off
	global_store_dwordx4 v[88:89], v[68:71], off
	v_lshl_add_u64 v[72:73], v[132:133], 0, s[40:41]
	global_load_dwordx4 v[64:67], v[94:95], off
	v_lshl_add_u64 v[68:69], s[10:11], 0, v[72:73]
	global_load_dwordx4 v[68:71], v[68:69], off
	v_lshl_add_u64 v[74:75], v[132:133], 0, s[42:43]
	v_lshl_add_u64 v[76:77], s[12:13], 0, v[90:91]
	v_lshl_add_u64 v[72:73], s[12:13], 0, v[72:73]
	v_lshl_add_u64 v[78:79], s[10:11], 0, v[74:75]
	s_waitcnt vmcnt(1)
	v_lshlrev_b32_e32 v80, 16, v64
	v_and_b32_e32 v81, 0xffff0000, v64
	v_lshlrev_b32_e32 v64, 16, v65
	v_and_b32_e32 v65, 0xffff0000, v65
	v_lshlrev_b32_e32 v82, 16, v66
	v_and_b32_e32 v83, 0xffff0000, v66
	v_lshlrev_b32_e32 v66, 16, v67
	v_and_b32_e32 v67, 0xffff0000, v67
	s_waitcnt vmcnt(0)
	v_lshlrev_b32_e32 v84, 16, v68
	v_and_b32_e32 v85, 0xffff0000, v68
	v_lshlrev_b32_e32 v68, 16, v69
	v_and_b32_e32 v69, 0xffff0000, v69
	v_lshlrev_b32_e32 v86, 16, v70
	v_and_b32_e32 v87, 0xffff0000, v70
	v_lshlrev_b32_e32 v70, 16, v71
	v_and_b32_e32 v71, 0xffff0000, v71
	v_pk_fma_f32 v[62:63], v[64:65], s[16:17], v[62:63] op_sel_hi:[1,0,1]
	v_pk_fma_f32 v[60:61], v[80:81], s[16:17], v[60:61] op_sel_hi:[1,0,1]
	v_pk_fma_f32 v[58:59], v[66:67], s[16:17], v[58:59] op_sel_hi:[1,0,1]
	v_pk_fma_f32 v[56:57], v[82:83], s[16:17], v[56:57] op_sel_hi:[1,0,1]
	v_pk_fma_f32 v[54:55], v[68:69], s[16:17], v[54:55] op_sel_hi:[1,0,1]
	v_pk_fma_f32 v[52:53], v[84:85], s[16:17], v[52:53] op_sel_hi:[1,0,1]
	v_pk_fma_f32 v[64:65], v[70:71], s[16:17], v[50:51] op_sel_hi:[1,0,1]
	v_pk_fma_f32 v[66:67], v[86:87], s[16:17], v[48:49] op_sel_hi:[1,0,1]
	v_cvt_pk_bf16_f32 v48, v60, v61
	v_cvt_pk_bf16_f32 v49, v62, v63
	v_cvt_pk_bf16_f32 v50, v56, v57
	v_cvt_pk_bf16_f32 v51, v58, v59
	v_cvt_pk_bf16_f32 v52, v52, v53
	v_cvt_pk_bf16_f32 v53, v54, v55
	v_cvt_pk_bf16_f32 v54, v66, v67
	v_cvt_pk_bf16_f32 v55, v64, v65
	global_store_dwordx4 v[76:77], v[48:51], off
	global_store_dwordx4 v[72:73], v[52:55], off
	v_lshl_add_u64 v[56:57], v[132:133], 0, s[44:45]
	global_load_dwordx4 v[48:51], v[78:79], off
	v_lshl_add_u64 v[52:53], s[10:11], 0, v[56:57]
	global_load_dwordx4 v[52:55], v[52:53], off
	v_lshl_add_u64 v[60:61], s[12:13], 0, v[74:75]
	v_lshl_add_u64 v[58:59], v[132:133], 0, s[46:47]
	v_lshl_add_u64 v[56:57], s[12:13], 0, v[56:57]
	v_lshl_add_u64 v[62:63], s[10:11], 0, v[58:59]
	s_waitcnt vmcnt(1)
; DI unsigned cvt_pk_bf16(float lo, float hi) { const f32x2_t v = {lo, hi}; return __builtin_bit_cast(unsigned, __builtin_convertvector(v, bf16x2_t)); }
; #define PG8_BAR __builtin_amdgcn_s_barrier()
;     DI int nt(const Unit& u) const { return (u.aux & 8) ? PLED / 64 : ((u.aux & 4) ? (D_ / 2) / 64 : D_ / 64); }
; template <class Epi, class Sched, bool ALIGN_EPI, bool FP8 = false>
; DI void gemm_phase(LAS unsigned char* lds, const Gemm g, const Sched& S, const Epi& E) {
;     ...
;         if (!has_next) break;
; #pragma unroll
;         for (int a = 0; a < 2; ++a)
; #pragma unroll
;             for (int b = 0; b < 2; ++b)
; #pragma unroll
;                 for (int m = 0; m < 4; ++m)
; #pragma unroll
;                     for (int n = 0; n < 2; ++n) acc[a][b][m][n] = (f32x4){0.f, 0.f, 0.f, 0.f};
;         cur = nxt; cA = nA; cB = nB; ++ui;
;         if constexpr (sched_vark<Sched>::value) nt = S.nt(cur);
;         if constexpr (ALIGN_EPI) { if (wr == 1) PG8_BAR; }
;     DI void operator()(const f32x4 (&acc)[2][2][4][2], const Unit& u, int wr, int wc, int fr, int fq) const {
;         int row0 = u.pm * BM + wr * 64 + fr; asm volatile("" : "+v"(row0));
;         const int col0 = u.pn * BM + wc * 32 + 8 * fq;
; #pragma unroll
;         for (int ai = 0; ai < 2; ++ai)
; #pragma unroll
;             for (int m = 0; m < 4; ++m) { const size_t r = (size_t)(row0 + ai * HALF + m * 16);
; #pragma unroll
;                 for (int bj = 0; bj < 2; ++bj) { const size_t o = r * D_ + col0 + bj * HALF; f32x4 x0, x1; unpack8f(*(const u32x4*)(R0 + o), x0, x1);
;                     f32x4 v0 = ALPHA * x0 + acc[ai][bj][m][0], v1 = ALPHA * x1 + acc[ai][bj][m][1];
;                     if (HAS_R1) { f32x4 q0, q1; unpack8f(*(const u32x4*)(R1 + o), q0, q1); v0 = v0 + q0; v1 = v1 + q1; }
;                     u32x4 w; w.x = cvt_pk_bf16(v0[0], v0[1]); w.y = cvt_pk_bf16(v0[2], v0[3]); w.z = cvt_pk_bf16(v1[0], v1[1]); w.w = cvt_pk_bf16(v1[2], v1[3]);
;                     *(u32x4*)(Yo + o) = w; }
;                 if (m & 1) asm volatile("" ::: "memory"); }
;     }
	v_lshlrev_b32_e32 v64, 16, v48
	v_and_b32_e32 v65, 0xffff0000, v48
	v_lshlrev_b32_e32 v48, 16, v49
	v_and_b32_e32 v49, 0xffff0000, v49
	v_lshlrev_b32_e32 v66, 16, v50
	v_and_b32_e32 v67, 0xffff0000, v50
	v_lshlrev_b32_e32 v50, 16, v51
	v_and_b32_e32 v51, 0xffff0000, v51
	s_waitcnt vmcnt(0)
	v_lshlrev_b32_e32 v68, 16, v52
	v_and_b32_e32 v69, 0xffff0000, v52
	v_lshlrev_b32_e32 v52, 16, v53
	v_and_b32_e32 v53, 0xffff0000, v53
	v_lshlrev_b32_e32 v70, 16, v54
	v_and_b32_e32 v71, 0xffff0000, v54
	v_lshlrev_b32_e32 v54, 16, v55
	v_and_b32_e32 v55, 0xffff0000, v55
	v_pk_fma_f32 v[46:47], v[48:49], s[16:17], v[46:47] op_sel_hi:[1,0,1]
	v_pk_fma_f32 v[44:45], v[64:65], s[16:17], v[44:45] op_sel_hi:[1,0,1]
	v_pk_fma_f32 v[42:43], v[50:51], s[16:17], v[42:43] op_sel_hi:[1,0,1]
	v_pk_fma_f32 v[40:41], v[66:67], s[16:17], v[40:41] op_sel_hi:[1,0,1]
	v_pk_fma_f32 v[38:39], v[52:53], s[16:17], v[38:39] op_sel_hi:[1,0,1]
	v_pk_fma_f32 v[36:37], v[68:69], s[16:17], v[36:37] op_sel_hi:[1,0,1]
	v_pk_fma_f32 v[48:49], v[54:55], s[16:17], v[34:35] op_sel_hi:[1,0,1]
	v_pk_fma_f32 v[50:51], v[70:71], s[16:17], v[32:33] op_sel_hi:[1,0,1]
	v_cvt_pk_bf16_f32 v32, v44, v45
	v_cvt_pk_bf16_f32 v33, v46, v47
	v_cvt_pk_bf16_f32 v34, v40, v41
	v_cvt_pk_bf16_f32 v35, v42, v43
	v_cvt_pk_bf16_f32 v36, v36, v37
	v_cvt_pk_bf16_f32 v37, v38, v39
	v_cvt_pk_bf16_f32 v38, v50, v51
	v_cvt_pk_bf16_f32 v39, v48, v49
	global_store_dwordx4 v[60:61], v[32:35], off
	global_store_dwordx4 v[56:57], v[36:39], off
	v_lshl_add_u64 v[40:41], v[132:133], 0, s[48:49]
	global_load_dwordx4 v[32:35], v[62:63], off
	v_lshl_add_u64 v[36:37], s[10:11], 0, v[40:41]
	global_load_dwordx4 v[36:39], v[36:37], off
	v_lshl_add_u64 v[42:43], v[132:133], 0, s[50:51]
	v_lshl_add_u64 v[44:45], s[12:13], 0, v[58:59]
	v_lshl_add_u64 v[40:41], s[12:13], 0, v[40:41]
	v_lshl_add_u64 v[46:47], s[10:11], 0, v[42:43]
	s_waitcnt vmcnt(1)
	v_lshlrev_b32_e32 v48, 16, v32
	v_and_b32_e32 v49, 0xffff0000, v32
	v_lshlrev_b32_e32 v32, 16, v33
	v_and_b32_e32 v33, 0xffff0000, v33
	v_lshlrev_b32_e32 v50, 16, v34
	v_and_b32_e32 v51, 0xffff0000, v34
	v_lshlrev_b32_e32 v34, 16, v35
	v_and_b32_e32 v35, 0xffff0000, v35
	s_waitcnt vmcnt(0)
	v_lshlrev_b32_e32 v52, 16, v36
	v_and_b32_e32 v53, 0xffff0000, v36
	v_lshlrev_b32_e32 v36, 16, v37
	v_and_b32_e32 v37, 0xffff0000, v37
	v_lshlrev_b32_e32 v54, 16, v38
	v_and_b32_e32 v55, 0xffff0000, v38
	v_lshlrev_b32_e32 v38, 16, v39
	v_and_b32_e32 v39, 0xffff0000, v39
	v_pk_fma_f32 v[30:31], v[32:33], s[16:17], v[30:31] op_sel_hi:[1,0,1]
	v_pk_fma_f32 v[28:29], v[48:49], s[16:17], v[28:29] op_sel_hi:[1,0,1]
	v_pk_fma_f32 v[26:27], v[34:35], s[16:17], v[26:27] op_sel_hi:[1,0,1]
	v_pk_fma_f32 v[24:25], v[50:51], s[16:17], v[24:25] op_sel_hi:[1,0,1]
	v_pk_fma_f32 v[22:23], v[36:37], s[16:17], v[22:23] op_sel_hi:[1,0,1]
	v_pk_fma_f32 v[20:21], v[52:53], s[16:17], v[20:21] op_sel_hi:[1,0,1]
	v_pk_fma_f32 v[32:33], v[38:39], s[16:17], v[18:19] op_sel_hi:[1,0,1]
	v_pk_fma_f32 v[34:35], v[54:55], s[16:17], v[16:17] op_sel_hi:[1,0,1]
	v_cvt_pk_bf16_f32 v16, v28, v29
	v_cvt_pk_bf16_f32 v17, v30, v31
	v_cvt_pk_bf16_f32 v18, v24, v25
	v_cvt_pk_bf16_f32 v19, v26, v27
	v_cvt_pk_bf16_f32 v20, v20, v21
	v_cvt_pk_bf16_f32 v21, v22, v23
	v_cvt_pk_bf16_f32 v22, v34, v35
	v_cvt_pk_bf16_f32 v23, v32, v33
	global_store_dwordx4 v[44:45], v[16:19], off
	global_store_dwordx4 v[40:41], v[20:23], off
	v_lshl_add_u64 v[24:25], v[132:133], 0, s[52:53]
	global_load_dwordx4 v[16:19], v[46:47], off
	v_lshl_add_u64 v[20:21], s[10:11], 0, v[24:25]
	global_load_dwordx4 v[20:23], v[20:21], off
	v_lshl_add_u64 v[26:27], s[12:13], 0, v[42:43]
	v_lshl_add_u64 v[24:25], s[12:13], 0, v[24:25]
	s_waitcnt vmcnt(1)
	v_lshlrev_b32_e32 v28, 16, v16
	v_and_b32_e32 v29, 0xffff0000, v16
	v_lshlrev_b32_e32 v16, 16, v17
	v_and_b32_e32 v17, 0xffff0000, v17
	v_lshlrev_b32_e32 v30, 16, v18
	v_and_b32_e32 v31, 0xffff0000, v18
	v_lshlrev_b32_e32 v18, 16, v19
	v_and_b32_e32 v19, 0xffff0000, v19
	s_waitcnt vmcnt(0)
	v_lshlrev_b32_e32 v32, 16, v20
	v_and_b32_e32 v33, 0xffff0000, v20
	v_lshlrev_b32_e32 v20, 16, v21
	v_and_b32_e32 v21, 0xffff0000, v21
	v_lshlrev_b32_e32 v34, 16, v22
	v_and_b32_e32 v35, 0xffff0000, v22
	v_lshlrev_b32_e32 v22, 16, v23
	v_and_b32_e32 v23, 0xffff0000, v23
	v_pk_fma_f32 v[14:15], v[16:17], s[16:17], v[14:15] op_sel_hi:[1,0,1]
	v_pk_fma_f32 v[12:13], v[28:29], s[16:17], v[12:13] op_sel_hi:[1,0,1]
	v_pk_fma_f32 v[10:11], v[18:19], s[16:17], v[10:11] op_sel_hi:[1,0,1]
	v_pk_fma_f32 v[8:9], v[30:31], s[16:17], v[8:9] op_sel_hi:[1,0,1]
	v_pk_fma_f32 v[6:7], v[20:21], s[16:17], v[6:7] op_sel_hi:[1,0,1]
	v_pk_fma_f32 v[4:5], v[32:33], s[16:17], v[4:5] op_sel_hi:[1,0,1]
	v_pk_fma_f32 v[16:17], v[22:23], s[16:17], v[2:3] op_sel_hi:[1,0,1]
	v_pk_fma_f32 v[18:19], v[34:35], s[16:17], v[0:1] op_sel_hi:[1,0,1]
	v_cvt_pk_bf16_f32 v0, v12, v13
	v_cvt_pk_bf16_f32 v1, v14, v15
	v_cvt_pk_bf16_f32 v2, v8, v9
	v_cvt_pk_bf16_f32 v3, v10, v11
	v_cvt_pk_bf16_f32 v4, v4, v5
	v_cvt_pk_bf16_f32 v5, v6, v7
	v_cvt_pk_bf16_f32 v6, v18, v19
	v_cvt_pk_bf16_f32 v7, v16, v17
	global_store_dwordx4 v[26:27], v[0:3], off
	global_store_dwordx4 v[24:25], v[4:7], off
	s_cbranch_vccnz .LBB0_561
	s_andn2_b64 vcc, exec, s[8:9]
	s_cbranch_vccnz .LBB0_560
	s_barrier
	s_branch .LBB0_560

; #define PG8_STAGE(bufoff, gbase, voff) do { _Pragma("unroll") for (int _i = 0; _i < 2; ++_i) { unsigned keep_; \
;         asm volatile("s_mov_b32 %0, m0\n\ts_mov_b32 m0, %3\n\ts_nop 0\n\tglobal_load_lds_dwordx4 %1, %2\n\ts_mov_b32 m0, %0" : "=&s"(keep_) : "v"((voff)[_i]), "s"((const char*)(gbase)), "s"(ldsbase + (unsigned)((bufoff) + _i * 8192)) : "memory"); } } while (0)
; #define PG8_WAIT_V(n) asm volatile("s_waitcnt vmcnt(" #n ")" ::: "memory")
; #define PG8_WAIT_L(n) asm volatile("s_waitcnt lgkmcnt(" #n ")" ::: "memory")
; #define PG8_BAR __builtin_amdgcn_s_barrier()
; #define PG8_SCHED __builtin_amdgcn_sched_barrier(0)
;     DI int nt(const Unit& u) const { return (u.aux & 8) ? PLED / 64 : ((u.aux & 4) ? (D_ / 2) / 64 : D_ / 64); }
; template <class Epi, class Sched, bool ALIGN_EPI, bool FP8 = false>
; DI void gemm_phase(LAS unsigned char* lds, const Gemm g, const Sched& S, const Epi& E) {
;     ...
;             const bool last = (t == nt - 2);
;             const char* a1 = cA + (size_t)(t + 1) * kstep;
;             const char* a2 = last ? nA : cA + (size_t)(t + 2) * kstep; const char* b2 = last ? nB : cB + (size_t)(t + 2) * kstep;
;             const char* a3 = a2 + kstep; const char* b3 = b2 + kstep;
;             PG8_LDB(B0, 0, 0); PG8_LDB(B1, 0, 1); PG8_SCHED; PG8_LDA(At, 0, 0); PG8_STAGE(PG8_SA(1, 1), a1 + hstepA, voffA);
;             PG8_WAIT_V(8); PG8_WAIT_L(0); PG8_BAR; PG8_MMA(0, 0, At, B0); PG8_MMA(0, 1, At, B1); PG8_BAR; PG8_SCHED;
;             PG8_LDA(At, 0, 1); PG8_STAGE(PG8_SB(0, 0), b2, voffB); PG8_STAGE(PG8_SB(0, 1), b2 + hstepB, voffB); PG8_STAGE(PG8_SA(0, 0), a2, voffA);
;             PG8_WAIT_V(8); PG8_WAIT_L(0); PG8_BAR; PG8_MMA(1, 0, At, B0); PG8_MMA(1, 1, At, B1); PG8_BAR; PG8_SCHED;
.LBB0_700:
	s_cmp_lg_u32 s99, 0
	s_cbranch_scc1 .Lmy_g0_700
	ds_read_b128 v[148:151], v142
	ds_read_b128 v[152:155], v142 offset:1024
	ds_read_b128 v[156:159], v142 offset:2048
	ds_read_b128 v[160:163], v142 offset:3072
	ds_read_b128 v[164:167], v143
	ds_read_b128 v[168:171], v143 offset:1024
	ds_read_b128 v[172:175], v143 offset:2048
	ds_read_b128 v[176:179], v143 offset:3072
	s_add_u32 s26, s24, 0x100
	s_addc_u32 s27, s25, 0
	s_cmp_eq_u32 s71, 28
	s_cselect_b32 s42, s67, s26
	s_cselect_b32 s43, s17, s27
	s_cselect_b32 s40, s68, s69
	s_cselect_b32 s41, s13, s70
	s_add_u32 s28, s42, 0x80
	s_addc_u32 s29, s43, 0
	ds_read_b128 v[180:183], v144
	ds_read_b128 v[184:187], v144 offset:1024
	ds_read_b128 v[188:191], v144 offset:2048
	ds_read_b128 v[192:195], v144 offset:3072
	ds_read_b128 v[196:199], v144 offset:4096
	ds_read_b128 v[200:203], v144 offset:5120
	ds_read_b128 v[204:207], v144 offset:6144
	ds_read_b128 v[208:211], v144 offset:7168
	s_add_u32 s24, s24, 0x80080
	s_addc_u32 s25, s25, 0
	s_mov_b32 s72, m0
	s_mov_b32 m0, s61
	s_nop 0
	global_load_lds_dwordx4 v136, s[24:25]
	s_mov_b32 m0, s72
	s_nop 0
	s_mov_b32 s72, m0
	s_mov_b32 m0, s62
	s_nop 0
	global_load_lds_dwordx4 v138, s[24:25]
	s_mov_b32 m0, s72
	s_waitcnt vmcnt(8)
	s_waitcnt lgkmcnt(0)
	s_mov_b64 exec, 1
	ds_add_u32 v255, v255 offset:4096
	s_mov_b64 exec, -1
	s_setprio 1
	v_mfma_f32_16x16x32_bf16 v[124:127], v[148:151], v[180:183], v[124:127]
	v_mfma_f32_16x16x32_bf16 v[116:119], v[156:159], v[180:183], v[116:119]
	v_mfma_f32_16x16x32_bf16 v[108:111], v[148:151], v[188:191], v[108:111]
	v_mfma_f32_16x16x32_bf16 v[100:103], v[156:159], v[188:191], v[100:103]
	v_mfma_f32_16x16x32_bf16 v[92:95], v[148:151], v[196:199], v[92:95]
	v_mfma_f32_16x16x32_bf16 v[84:87], v[156:159], v[196:199], v[84:87]
	v_mfma_f32_16x16x32_bf16 v[76:79], v[148:151], v[204:207], v[76:79]
	v_mfma_f32_16x16x32_bf16 v[68:71], v[156:159], v[204:207], v[68:71]
	v_mfma_f32_16x16x32_bf16 v[124:127], v[152:155], v[184:187], v[124:127]
	v_mfma_f32_16x16x32_bf16 v[116:119], v[160:163], v[184:187], v[116:119]
	v_mfma_f32_16x16x32_bf16 v[108:111], v[152:155], v[192:195], v[108:111]
	v_mfma_f32_16x16x32_bf16 v[100:103], v[160:163], v[192:195], v[100:103]
	v_mfma_f32_16x16x32_bf16 v[92:95], v[152:155], v[200:203], v[92:95]
	v_mfma_f32_16x16x32_bf16 v[84:87], v[160:163], v[200:203], v[84:87]
	v_mfma_f32_16x16x32_bf16 v[76:79], v[152:155], v[208:211], v[76:79]
	v_mfma_f32_16x16x32_bf16 v[68:71], v[160:163], v[208:211], v[68:71]
	v_mfma_f32_16x16x32_bf16 v[120:123], v[164:167], v[180:183], v[120:123]
	v_mfma_f32_16x16x32_bf16 v[112:115], v[172:175], v[180:183], v[112:115]
	v_mfma_f32_16x16x32_bf16 v[104:107], v[164:167], v[188:191], v[104:107]
	v_mfma_f32_16x16x32_bf16 v[96:99], v[172:175], v[188:191], v[96:99]
	v_mfma_f32_16x16x32_bf16 v[88:91], v[164:167], v[196:199], v[88:91]
	v_mfma_f32_16x16x32_bf16 v[80:83], v[172:175], v[196:199], v[80:83]
	v_mfma_f32_16x16x32_bf16 v[72:75], v[164:167], v[204:207], v[72:75]
	v_mfma_f32_16x16x32_bf16 v[64:67], v[172:175], v[204:207], v[64:67]
	v_mfma_f32_16x16x32_bf16 v[120:123], v[168:171], v[184:187], v[120:123]
	v_mfma_f32_16x16x32_bf16 v[112:115], v[176:179], v[184:187], v[112:115]
	v_mfma_f32_16x16x32_bf16 v[104:107], v[168:171], v[192:195], v[104:107]
	v_mfma_f32_16x16x32_bf16 v[96:99], v[176:179], v[192:195], v[96:99]
	v_mfma_f32_16x16x32_bf16 v[88:91], v[168:171], v[200:203], v[88:91]
	v_mfma_f32_16x16x32_bf16 v[80:83], v[176:179], v[200:203], v[80:83]
	v_mfma_f32_16x16x32_bf16 v[72:75], v[168:171], v[208:211], v[72:75]
	v_mfma_f32_16x16x32_bf16 v[64:67], v[176:179], v[208:211], v[64:67]
	s_setprio 0
	s_barrier
	ds_read_b128 v[180:183], v144 offset:16384
	ds_read_b128 v[184:187], v144 offset:17408
	ds_read_b128 v[188:191], v144 offset:18432
	ds_read_b128 v[192:195], v144 offset:19456
	ds_read_b128 v[196:199], v144 offset:20480
	ds_read_b128 v[200:203], v144 offset:21504
	ds_read_b128 v[204:207], v144 offset:22528
	ds_read_b128 v[208:211], v144 offset:23552
	s_mov_b32 s24, m0
	s_mov_b32 m0, s23
	s_nop 0
	global_load_lds_dwordx4 v137, s[40:41]
	s_mov_b32 m0, s24
	s_nop 0
	s_mov_b32 s24, m0
	s_mov_b32 m0, s47
	s_nop 0
	global_load_lds_dwordx4 v139, s[40:41]
	s_mov_b32 m0, s24
	s_add_u32 s24, s40, 0x80000
	s_addc_u32 s25, s41, 0
	s_mov_b32 s72, m0
	s_mov_b32 m0, s48
	s_nop 0
	global_load_lds_dwordx4 v137, s[24:25]
	s_mov_b32 m0, s72
	s_nop 0
	s_mov_b32 s72, m0
	s_mov_b32 m0, s49
	s_nop 0
	global_load_lds_dwordx4 v139, s[24:25]
	s_mov_b32 m0, s72
	s_mov_b32 s24, m0
	s_mov_b32 m0, s44
	s_nop 0
	global_load_lds_dwordx4 v136, s[42:43]
	s_mov_b32 m0, s24
	s_nop 0
	s_mov_b32 s24, m0
	s_mov_b32 m0, s50
	s_nop 0
	global_load_lds_dwordx4 v138, s[42:43]
	s_mov_b32 m0, s24
	s_waitcnt vmcnt(8)
	s_waitcnt lgkmcnt(0)
; #define PG8_STAGE(bufoff, gbase, voff) do { _Pragma("unroll") for (int _i = 0; _i < 2; ++_i) { unsigned keep_; \
;         asm volatile("s_mov_b32 %0, m0\n\ts_mov_b32 m0, %3\n\ts_nop 0\n\tglobal_load_lds_dwordx4 %1, %2\n\ts_mov_b32 m0, %0" : "=&s"(keep_) : "v"((voff)[_i]), "s"((const char*)(gbase)), "s"(ldsbase + (unsigned)((bufoff) + _i * 8192)) : "memory"); } } while (0)
; #define PG8_WAIT_V(n) asm volatile("s_waitcnt vmcnt(" #n ")" ::: "memory")
; #define PG8_WAIT_L(n) asm volatile("s_waitcnt lgkmcnt(" #n ")" ::: "memory")
; #define PG8_BAR __builtin_amdgcn_s_barrier()
; #define PG8_SCHED __builtin_amdgcn_sched_barrier(0)
; template <class Epi, class Sched, bool ALIGN_EPI, bool FP8 = false>
; DI void gemm_phase(LAS unsigned char* lds, const Gemm g, const Sched& S, const Epi& E) {
;     ...
;             PG8_WAIT_V(8); PG8_WAIT_L(0); PG8_BAR; PG8_MMA(1, 0, At, B0); PG8_MMA(1, 1, At, B1); PG8_BAR; PG8_SCHED;
;             PG8_LDB(B0, 1, 0); PG8_LDB(B1, 1, 1); PG8_SCHED; PG8_LDA(At, 1, 0); PG8_STAGE(PG8_SA(0, 1), a2 + hstepA, voffA);
;             PG8_WAIT_V(8); PG8_WAIT_L(0); PG8_BAR; PG8_MMA(0, 0, At, B0); PG8_MMA(0, 1, At, B1); PG8_BAR; PG8_SCHED;
	s_mov_b64 exec, 1
	ds_add_u32 v255, v255 offset:4096
	s_mov_b64 exec, -1
	s_setprio 1
	v_mfma_f32_16x16x32_bf16 v[60:63], v[148:151], v[180:183], v[60:63]
	v_mfma_f32_16x16x32_bf16 v[52:55], v[156:159], v[180:183], v[52:55]
	v_mfma_f32_16x16x32_bf16 v[44:47], v[148:151], v[188:191], v[44:47]
	v_mfma_f32_16x16x32_bf16 v[36:39], v[156:159], v[188:191], v[36:39]
	v_mfma_f32_16x16x32_bf16 v[28:31], v[148:151], v[196:199], v[28:31]
	v_mfma_f32_16x16x32_bf16 v[20:23], v[156:159], v[196:199], v[20:23]
	v_mfma_f32_16x16x32_bf16 v[12:15], v[148:151], v[204:207], v[12:15]
	v_mfma_f32_16x16x32_bf16 v[4:7], v[156:159], v[204:207], v[4:7]
	v_mfma_f32_16x16x32_bf16 v[60:63], v[152:155], v[184:187], v[60:63]
	v_mfma_f32_16x16x32_bf16 v[52:55], v[160:163], v[184:187], v[52:55]
	v_mfma_f32_16x16x32_bf16 v[44:47], v[152:155], v[192:195], v[44:47]
	v_mfma_f32_16x16x32_bf16 v[36:39], v[160:163], v[192:195], v[36:39]
	v_mfma_f32_16x16x32_bf16 v[28:31], v[152:155], v[200:203], v[28:31]
	v_mfma_f32_16x16x32_bf16 v[20:23], v[160:163], v[200:203], v[20:23]
	v_mfma_f32_16x16x32_bf16 v[12:15], v[152:155], v[208:211], v[12:15]
	v_mfma_f32_16x16x32_bf16 v[4:7], v[160:163], v[208:211], v[4:7]
	v_mfma_f32_16x16x32_bf16 v[56:59], v[164:167], v[180:183], v[56:59]
	v_mfma_f32_16x16x32_bf16 v[48:51], v[172:175], v[180:183], v[48:51]
	v_mfma_f32_16x16x32_bf16 v[40:43], v[164:167], v[188:191], v[40:43]
	v_mfma_f32_16x16x32_bf16 v[32:35], v[172:175], v[188:191], v[32:35]
	v_mfma_f32_16x16x32_bf16 v[24:27], v[164:167], v[196:199], v[24:27]
	v_mfma_f32_16x16x32_bf16 v[16:19], v[172:175], v[196:199], v[16:19]
	v_mfma_f32_16x16x32_bf16 v[8:11], v[164:167], v[204:207], v[8:11]
	v_mfma_f32_16x16x32_bf16 v[0:3], v[172:175], v[204:207], v[0:3]
	v_mfma_f32_16x16x32_bf16 v[56:59], v[168:171], v[184:187], v[56:59]
	v_mfma_f32_16x16x32_bf16 v[48:51], v[176:179], v[184:187], v[48:51]
	v_mfma_f32_16x16x32_bf16 v[40:43], v[168:171], v[192:195], v[40:43]
	v_mfma_f32_16x16x32_bf16 v[32:35], v[176:179], v[192:195], v[32:35]
	v_mfma_f32_16x16x32_bf16 v[24:27], v[168:171], v[200:203], v[24:27]
	v_mfma_f32_16x16x32_bf16 v[16:19], v[176:179], v[200:203], v[16:19]
	v_mfma_f32_16x16x32_bf16 v[8:11], v[168:171], v[208:211], v[8:11]
	v_mfma_f32_16x16x32_bf16 v[0:3], v[176:179], v[208:211], v[0:3]
	s_setprio 0
	s_barrier
	ds_read_b128 v[148:151], v145
	ds_read_b128 v[152:155], v145 offset:1024
	ds_read_b128 v[156:159], v145 offset:2048
	ds_read_b128 v[160:163], v145 offset:3072
	ds_read_b128 v[164:167], v146
	ds_read_b128 v[168:171], v146 offset:1024
	ds_read_b128 v[172:175], v146 offset:2048
	ds_read_b128 v[176:179], v146 offset:3072
	ds_read_b128 v[180:183], v144 offset:32768
	ds_read_b128 v[184:187], v144 offset:33792
	ds_read_b128 v[188:191], v144 offset:34816
	ds_read_b128 v[192:195], v144 offset:35840
	ds_read_b128 v[196:199], v144 offset:36864
	ds_read_b128 v[200:203], v144 offset:37888
	ds_read_b128 v[204:207], v144 offset:38912
	ds_read_b128 v[208:211], v144 offset:39936
	s_add_u32 s24, s42, 0x80000
	s_addc_u32 s25, s43, 0
	s_mov_b32 s42, m0
	s_mov_b32 m0, s51
	s_nop 0
	global_load_lds_dwordx4 v136, s[24:25]
	s_mov_b32 m0, s42
	s_nop 0
	s_mov_b32 s42, m0
	s_mov_b32 m0, s52
	s_nop 0
	global_load_lds_dwordx4 v138, s[24:25]
	s_mov_b32 m0, s42
	s_waitcnt vmcnt(8)
	s_waitcnt lgkmcnt(0)
	s_mov_b64 exec, 1
	ds_add_u32 v255, v255 offset:4096
	s_mov_b64 exec, -1
	s_setprio 1
	v_mfma_f32_16x16x32_bf16 v[124:127], v[148:151], v[180:183], v[124:127]
	v_mfma_f32_16x16x32_bf16 v[116:119], v[156:159], v[180:183], v[116:119]
	v_mfma_f32_16x16x32_bf16 v[108:111], v[148:151], v[188:191], v[108:111]
	v_mfma_f32_16x16x32_bf16 v[100:103], v[156:159], v[188:191], v[100:103]
	v_mfma_f32_16x16x32_bf16 v[92:95], v[148:151], v[196:199], v[92:95]
	v_mfma_f32_16x16x32_bf16 v[84:87], v[156:159], v[196:199], v[84:87]
	v_mfma_f32_16x16x32_bf16 v[76:79], v[148:151], v[204:207], v[76:79]
	v_mfma_f32_16x16x32_bf16 v[68:71], v[156:159], v[204:207], v[68:71]
	v_mfma_f32_16x16x32_bf16 v[124:127], v[152:155], v[184:187], v[124:127]
	v_mfma_f32_16x16x32_bf16 v[116:119], v[160:163], v[184:187], v[116:119]
	v_mfma_f32_16x16x32_bf16 v[108:111], v[152:155], v[192:195], v[108:111]
	v_mfma_f32_16x16x32_bf16 v[100:103], v[160:163], v[192:195], v[100:103]
	v_mfma_f32_16x16x32_bf16 v[92:95], v[152:155], v[200:203], v[92:95]
	v_mfma_f32_16x16x32_bf16 v[84:87], v[160:163], v[200:203], v[84:87]
	v_mfma_f32_16x16x32_bf16 v[76:79], v[152:155], v[208:211], v[76:79]
	v_mfma_f32_16x16x32_bf16 v[68:71], v[160:163], v[208:211], v[68:71]
	v_mfma_f32_16x16x32_bf16 v[120:123], v[164:167], v[180:183], v[120:123]
	v_mfma_f32_16x16x32_bf16 v[112:115], v[172:175], v[180:183], v[112:115]
	v_mfma_f32_16x16x32_bf16 v[104:107], v[164:167], v[188:191], v[104:107]
	v_mfma_f32_16x16x32_bf16 v[96:99], v[172:175], v[188:191], v[96:99]
	v_mfma_f32_16x16x32_bf16 v[88:91], v[164:167], v[196:199], v[88:91]
	v_mfma_f32_16x16x32_bf16 v[80:83], v[172:175], v[196:199], v[80:83]
	v_mfma_f32_16x16x32_bf16 v[72:75], v[164:167], v[204:207], v[72:75]
	v_mfma_f32_16x16x32_bf16 v[64:67], v[172:175], v[204:207], v[64:67]
	v_mfma_f32_16x16x32_bf16 v[120:123], v[168:171], v[184:187], v[120:123]
	v_mfma_f32_16x16x32_bf16 v[112:115], v[176:179], v[184:187], v[112:115]
	v_mfma_f32_16x16x32_bf16 v[104:107], v[168:171], v[192:195], v[104:107]
	v_mfma_f32_16x16x32_bf16 v[96:99], v[176:179], v[192:195], v[96:99]
	v_mfma_f32_16x16x32_bf16 v[88:91], v[168:171], v[200:203], v[88:91]
	v_mfma_f32_16x16x32_bf16 v[80:83], v[176:179], v[200:203], v[80:83]
	v_mfma_f32_16x16x32_bf16 v[72:75], v[168:171], v[208:211], v[72:75]
	v_mfma_f32_16x16x32_bf16 v[64:67], v[176:179], v[208:211], v[64:67]
	s_setprio 0
	s_barrier
; #define PG8_STAGE(bufoff, gbase, voff) do { _Pragma("unroll") for (int _i = 0; _i < 2; ++_i) { unsigned keep_; \
;         asm volatile("s_mov_b32 %0, m0\n\ts_mov_b32 m0, %3\n\ts_nop 0\n\tglobal_load_lds_dwordx4 %1, %2\n\ts_mov_b32 m0, %0" : "=&s"(keep_) : "v"((voff)[_i]), "s"((const char*)(gbase)), "s"(ldsbase + (unsigned)((bufoff) + _i * 8192)) : "memory"); } } while (0)
; #define PG8_WAIT_V(n) asm volatile("s_waitcnt vmcnt(" #n ")" ::: "memory")
; #define PG8_WAIT_L(n) asm volatile("s_waitcnt lgkmcnt(" #n ")" ::: "memory")
; #define PG8_BAR __builtin_amdgcn_s_barrier()
; #define PG8_SCHED __builtin_amdgcn_sched_barrier(0)
;     DI int nt(const Unit& u) const { return (u.aux & 8) ? PLED / 64 : ((u.aux & 4) ? (D_ / 2) / 64 : D_ / 64); }
; template <class Epi, class Sched, bool ALIGN_EPI, bool FP8 = false>
; DI void gemm_phase(LAS unsigned char* lds, const Gemm g, const Sched& S, const Epi& E) {
;     ...
;         for (int t = 0; t < nt; t += 2) {
;     ...
;             PG8_LDA(At, 1, 1); PG8_STAGE(PG8_SB(1, 0), b3, voffB); PG8_STAGE(PG8_SB(1, 1), b3 + hstepB, voffB); PG8_STAGE(PG8_SA(1, 0), a3, voffA);
;             PG8_WAIT_V(8); PG8_WAIT_L(0); PG8_BAR; PG8_MMA(1, 0, At, B0); PG8_MMA(1, 1, At, B1); PG8_BAR; PG8_SCHED;
	ds_read_b128 v[180:183], v144 offset:49152
	ds_read_b128 v[184:187], v144 offset:50176
	ds_read_b128 v[188:191], v144 offset:51200
	ds_read_b128 v[192:195], v144 offset:52224
	ds_read_b128 v[196:199], v144 offset:53248
	ds_read_b128 v[200:203], v144 offset:54272
	ds_read_b128 v[204:207], v144 offset:55296
	ds_read_b128 v[208:211], v144 offset:56320
	s_add_u32 s24, s40, 0x80
	s_addc_u32 s25, s41, 0
	s_mov_b32 s42, m0
	s_mov_b32 m0, s55
	s_nop 0
	global_load_lds_dwordx4 v137, s[24:25]
	s_mov_b32 m0, s42
	s_nop 0
	s_mov_b32 s42, m0
	s_mov_b32 m0, s56
	s_nop 0
	global_load_lds_dwordx4 v139, s[24:25]
	s_mov_b32 m0, s42
	s_add_u32 s24, s40, 0x80080
	s_addc_u32 s25, s41, 0
	s_mov_b32 s40, m0
	s_mov_b32 m0, s59
	s_nop 0
	global_load_lds_dwordx4 v137, s[24:25]
	s_mov_b32 m0, s40
	s_nop 0
	s_mov_b32 s40, m0
	s_mov_b32 m0, s60
	s_nop 0
	global_load_lds_dwordx4 v139, s[24:25]
	s_mov_b32 m0, s40
	s_mov_b32 s24, m0
	s_mov_b32 m0, s57
	s_nop 0
	global_load_lds_dwordx4 v136, s[28:29]
	s_mov_b32 m0, s24
	s_nop 0
	s_mov_b32 s24, m0
	s_mov_b32 m0, s58
	s_nop 0
	global_load_lds_dwordx4 v138, s[28:29]
	s_mov_b32 m0, s24
	s_waitcnt vmcnt(8)
	s_waitcnt lgkmcnt(0)
	s_mov_b64 exec, 1
	ds_add_u32 v255, v255 offset:4096
	s_mov_b64 exec, -1
	s_setprio 1
	v_mfma_f32_16x16x32_bf16 v[60:63], v[148:151], v[180:183], v[60:63]
	v_mfma_f32_16x16x32_bf16 v[52:55], v[156:159], v[180:183], v[52:55]
	v_mfma_f32_16x16x32_bf16 v[44:47], v[148:151], v[188:191], v[44:47]
	v_mfma_f32_16x16x32_bf16 v[36:39], v[156:159], v[188:191], v[36:39]
	v_mfma_f32_16x16x32_bf16 v[28:31], v[148:151], v[196:199], v[28:31]
	v_mfma_f32_16x16x32_bf16 v[20:23], v[156:159], v[196:199], v[20:23]
	v_mfma_f32_16x16x32_bf16 v[12:15], v[148:151], v[204:207], v[12:15]
	v_mfma_f32_16x16x32_bf16 v[4:7], v[156:159], v[204:207], v[4:7]
	v_mfma_f32_16x16x32_bf16 v[60:63], v[152:155], v[184:187], v[60:63]
	v_mfma_f32_16x16x32_bf16 v[52:55], v[160:163], v[184:187], v[52:55]
	v_mfma_f32_16x16x32_bf16 v[44:47], v[152:155], v[192:195], v[44:47]
	v_mfma_f32_16x16x32_bf16 v[36:39], v[160:163], v[192:195], v[36:39]
	v_mfma_f32_16x16x32_bf16 v[28:31], v[152:155], v[200:203], v[28:31]
	v_mfma_f32_16x16x32_bf16 v[20:23], v[160:163], v[200:203], v[20:23]
	v_mfma_f32_16x16x32_bf16 v[12:15], v[152:155], v[208:211], v[12:15]
	v_mfma_f32_16x16x32_bf16 v[4:7], v[160:163], v[208:211], v[4:7]
	v_mfma_f32_16x16x32_bf16 v[56:59], v[164:167], v[180:183], v[56:59]
	v_mfma_f32_16x16x32_bf16 v[48:51], v[172:175], v[180:183], v[48:51]
	v_mfma_f32_16x16x32_bf16 v[40:43], v[164:167], v[188:191], v[40:43]
	v_mfma_f32_16x16x32_bf16 v[32:35], v[172:175], v[188:191], v[32:35]
	v_mfma_f32_16x16x32_bf16 v[24:27], v[164:167], v[196:199], v[24:27]
	v_mfma_f32_16x16x32_bf16 v[16:19], v[172:175], v[196:199], v[16:19]
	v_mfma_f32_16x16x32_bf16 v[8:11], v[164:167], v[204:207], v[8:11]
	v_mfma_f32_16x16x32_bf16 v[0:3], v[172:175], v[204:207], v[0:3]
	v_mfma_f32_16x16x32_bf16 v[56:59], v[168:171], v[184:187], v[56:59]
	v_mfma_f32_16x16x32_bf16 v[48:51], v[176:179], v[184:187], v[48:51]
	v_mfma_f32_16x16x32_bf16 v[40:43], v[168:171], v[192:195], v[40:43]
	v_mfma_f32_16x16x32_bf16 v[32:35], v[176:179], v[192:195], v[32:35]
	v_mfma_f32_16x16x32_bf16 v[24:27], v[168:171], v[200:203], v[24:27]
	v_mfma_f32_16x16x32_bf16 v[16:19], v[176:179], v[200:203], v[16:19]
	v_mfma_f32_16x16x32_bf16 v[8:11], v[168:171], v[208:211], v[8:11]
	v_mfma_f32_16x16x32_bf16 v[0:3], v[176:179], v[208:211], v[0:3]
	s_setprio 0
	s_barrier
	s_add_i32 s71, s71, 2
	s_add_u32 s69, s69, 0x100
	s_addc_u32 s70, s70, 0
	s_cmp_gt_u32 s71, 29
	s_mov_b64 s[24:25], s[26:27]
	s_cbranch_scc0 .LBB0_700
	s_branch .Lmy_ex_700
; #define PG8_STAGE(bufoff, gbase, voff) do { _Pragma("unroll") for (int _i = 0; _i < 2; ++_i) { unsigned keep_; \
;         asm volatile("s_mov_b32 %0, m0\n\ts_mov_b32 m0, %3\n\ts_nop 0\n\tglobal_load_lds_dwordx4 %1, %2\n\ts_mov_b32 m0, %0" : "=&s"(keep_) : "v"((voff)[_i]), "s"((const char*)(gbase)), "s"(ldsbase + (unsigned)((bufoff) + _i * 8192)) : "memory"); } } while (0)
; #define PG8_WAIT_V(n) asm volatile("s_waitcnt vmcnt(" #n ")" ::: "memory")
; #define PG8_WAIT_L(n) asm volatile("s_waitcnt lgkmcnt(" #n ")" ::: "memory")
; #define PG8_BAR __builtin_amdgcn_s_barrier()
; #define PG8_SCHED __builtin_amdgcn_sched_barrier(0)
;     DI int nt(const Unit& u) const { return (u.aux & 8) ? PLED / 64 : ((u.aux & 4) ? (D_ / 2) / 64 : D_ / 64); }
; template <class Epi, class Sched, bool ALIGN_EPI, bool FP8 = false>
; DI void gemm_phase(LAS unsigned char* lds, const Gemm g, const Sched& S, const Epi& E) {
;     ...
;             const bool last = (t == nt - 2);
;             const char* a1 = cA + (size_t)(t + 1) * kstep;
;             const char* a2 = last ? nA : cA + (size_t)(t + 2) * kstep; const char* b2 = last ? nB : cB + (size_t)(t + 2) * kstep;
;             const char* a3 = a2 + kstep; const char* b3 = b2 + kstep;
;             PG8_LDB(B0, 0, 0); PG8_LDB(B1, 0, 1); PG8_SCHED; PG8_LDA(At, 0, 0); PG8_STAGE(PG8_SA(1, 1), a1 + hstepA, voffA);
;             PG8_WAIT_V(8); PG8_WAIT_L(0); PG8_BAR; PG8_MMA(0, 0, At, B0); PG8_MMA(0, 1, At, B1); PG8_BAR; PG8_SCHED;
.Lmy_g0_700:
	ds_read_b128 v[148:151], v142
	ds_read_b128 v[152:155], v142 offset:1024
	ds_read_b128 v[156:159], v142 offset:2048
	ds_read_b128 v[160:163], v142 offset:3072
	ds_read_b128 v[164:167], v143
	ds_read_b128 v[168:171], v143 offset:1024
	ds_read_b128 v[172:175], v143 offset:2048
	ds_read_b128 v[176:179], v143 offset:3072
	s_add_u32 s26, s24, 0x100
	s_addc_u32 s27, s25, 0
	s_cmp_eq_u32 s71, 28
	s_cselect_b32 s42, s67, s26
	s_cselect_b32 s43, s17, s27
	s_cselect_b32 s40, s68, s69
	s_cselect_b32 s41, s13, s70
	s_add_u32 s28, s42, 0x80
	s_addc_u32 s29, s43, 0
	ds_read_b128 v[180:183], v144
	ds_read_b128 v[184:187], v144 offset:1024
	ds_read_b128 v[188:191], v144 offset:2048
	ds_read_b128 v[192:195], v144 offset:3072
	ds_read_b128 v[196:199], v144 offset:4096
	ds_read_b128 v[200:203], v144 offset:5120
	ds_read_b128 v[204:207], v144 offset:6144
	ds_read_b128 v[208:211], v144 offset:7168
	s_add_u32 s24, s24, 0x80080
	s_addc_u32 s25, s25, 0
	s_mov_b32 s72, m0
	s_mov_b32 m0, s61
	s_nop 0
	global_load_lds_dwordx4 v136, s[24:25]
	s_mov_b32 m0, s72
	s_nop 0
	s_mov_b32 s72, m0
	s_mov_b32 m0, s62
	s_nop 0
	global_load_lds_dwordx4 v138, s[24:25]
	s_mov_b32 m0, s72
	s_waitcnt vmcnt(8)
	s_waitcnt lgkmcnt(0)
	s_barrier
	s_setprio 1
	v_mfma_f32_16x16x32_bf16 v[124:127], v[148:151], v[180:183], v[124:127]
	v_mfma_f32_16x16x32_bf16 v[116:119], v[156:159], v[180:183], v[116:119]
	v_mfma_f32_16x16x32_bf16 v[108:111], v[148:151], v[188:191], v[108:111]
	v_mfma_f32_16x16x32_bf16 v[100:103], v[156:159], v[188:191], v[100:103]
	v_mfma_f32_16x16x32_bf16 v[92:95], v[148:151], v[196:199], v[92:95]
	v_mfma_f32_16x16x32_bf16 v[84:87], v[156:159], v[196:199], v[84:87]
	v_mfma_f32_16x16x32_bf16 v[76:79], v[148:151], v[204:207], v[76:79]
	v_mfma_f32_16x16x32_bf16 v[68:71], v[156:159], v[204:207], v[68:71]
	v_mfma_f32_16x16x32_bf16 v[124:127], v[152:155], v[184:187], v[124:127]
	v_mfma_f32_16x16x32_bf16 v[116:119], v[160:163], v[184:187], v[116:119]
	v_mfma_f32_16x16x32_bf16 v[108:111], v[152:155], v[192:195], v[108:111]
	v_mfma_f32_16x16x32_bf16 v[100:103], v[160:163], v[192:195], v[100:103]
	v_mfma_f32_16x16x32_bf16 v[92:95], v[152:155], v[200:203], v[92:95]
	v_mfma_f32_16x16x32_bf16 v[84:87], v[160:163], v[200:203], v[84:87]
	v_mfma_f32_16x16x32_bf16 v[76:79], v[152:155], v[208:211], v[76:79]
	v_mfma_f32_16x16x32_bf16 v[68:71], v[160:163], v[208:211], v[68:71]
	v_mfma_f32_16x16x32_bf16 v[120:123], v[164:167], v[180:183], v[120:123]
	v_mfma_f32_16x16x32_bf16 v[112:115], v[172:175], v[180:183], v[112:115]
	v_mfma_f32_16x16x32_bf16 v[104:107], v[164:167], v[188:191], v[104:107]
	v_mfma_f32_16x16x32_bf16 v[96:99], v[172:175], v[188:191], v[96:99]
	v_mfma_f32_16x16x32_bf16 v[88:91], v[164:167], v[196:199], v[88:91]
	v_mfma_f32_16x16x32_bf16 v[80:83], v[172:175], v[196:199], v[80:83]
	v_mfma_f32_16x16x32_bf16 v[72:75], v[164:167], v[204:207], v[72:75]
	v_mfma_f32_16x16x32_bf16 v[64:67], v[172:175], v[204:207], v[64:67]
	v_mfma_f32_16x16x32_bf16 v[120:123], v[168:171], v[184:187], v[120:123]
	v_mfma_f32_16x16x32_bf16 v[112:115], v[176:179], v[184:187], v[112:115]
	v_mfma_f32_16x16x32_bf16 v[104:107], v[168:171], v[192:195], v[104:107]
	v_mfma_f32_16x16x32_bf16 v[96:99], v[176:179], v[192:195], v[96:99]
	ds_read_b32 v255, v255 offset:4096
	v_mfma_f32_16x16x32_bf16 v[88:91], v[168:171], v[200:203], v[88:91]
	v_mfma_f32_16x16x32_bf16 v[80:83], v[176:179], v[200:203], v[80:83]
	v_mfma_f32_16x16x32_bf16 v[72:75], v[168:171], v[208:211], v[72:75]
	v_mfma_f32_16x16x32_bf16 v[64:67], v[176:179], v[208:211], v[64:67]
	s_add_u32 s98, s98, 0x80000
	s_waitcnt lgkmcnt(0)
	v_readfirstlane_b32 s101, v255
	v_mov_b32_e32 v255, 0x20000
	s_cmp_ge_u32 s101, s98
	s_cbranch_scc1 .Lmy_g_16

; #define PG8_STAGE(bufoff, gbase, voff) do { _Pragma("unroll") for (int _i = 0; _i < 2; ++_i) { unsigned keep_; \
;         asm volatile("s_mov_b32 %0, m0\n\ts_mov_b32 m0, %3\n\ts_nop 0\n\tglobal_load_lds_dwordx4 %1, %2\n\ts_mov_b32 m0, %0" : "=&s"(keep_) : "v"((voff)[_i]), "s"((const char*)(gbase)), "s"(ldsbase + (unsigned)((bufoff) + _i * 8192)) : "memory"); } } while (0)
; #define PG8_WAIT_V(n) asm volatile("s_waitcnt vmcnt(" #n ")" ::: "memory")
; #define PG8_WAIT_L(n) asm volatile("s_waitcnt lgkmcnt(" #n ")" ::: "memory")
; #define PG8_BAR __builtin_amdgcn_s_barrier()
; #define PG8_SCHED __builtin_amdgcn_sched_barrier(0)
; template <class Epi, class Sched, bool ALIGN_EPI, bool FP8 = false>
; DI void gemm_phase(LAS unsigned char* lds, const Gemm g, const Sched& S, const Epi& E) {
;     ...
;             PG8_LDA(At, 0, 1); PG8_STAGE(PG8_SB(0, 0), b2, voffB); PG8_STAGE(PG8_SB(0, 1), b2 + hstepB, voffB); PG8_STAGE(PG8_SA(0, 0), a2, voffA);
;             PG8_WAIT_V(8); PG8_WAIT_L(0); PG8_BAR; PG8_MMA(1, 0, At, B0); PG8_MMA(1, 1, At, B1); PG8_BAR; PG8_SCHED;
.Lmy_g_16:
	s_setprio 0
	ds_read_b128 v[180:183], v144 offset:16384
	ds_read_b128 v[184:187], v144 offset:17408
	ds_read_b128 v[188:191], v144 offset:18432
	ds_read_b128 v[192:195], v144 offset:19456
	ds_read_b128 v[196:199], v144 offset:20480
	ds_read_b128 v[200:203], v144 offset:21504
	ds_read_b128 v[204:207], v144 offset:22528
	ds_read_b128 v[208:211], v144 offset:23552
	s_mov_b32 s24, m0
	s_mov_b32 m0, s23
	s_nop 0
	global_load_lds_dwordx4 v137, s[40:41]
	s_mov_b32 m0, s24
	s_nop 0
	s_mov_b32 s24, m0
	s_mov_b32 m0, s47
	s_nop 0
	global_load_lds_dwordx4 v139, s[40:41]
	s_mov_b32 m0, s24
	s_add_u32 s24, s40, 0x80000
	s_addc_u32 s25, s41, 0
	s_mov_b32 s72, m0
	s_mov_b32 m0, s48
	s_nop 0
	global_load_lds_dwordx4 v137, s[24:25]
	s_mov_b32 m0, s72
	s_nop 0
	s_mov_b32 s72, m0
	s_mov_b32 m0, s49
	s_nop 0
	global_load_lds_dwordx4 v139, s[24:25]
	s_mov_b32 m0, s72
	s_mov_b32 s24, m0
	s_mov_b32 m0, s44
	s_nop 0
	global_load_lds_dwordx4 v136, s[42:43]
	s_mov_b32 m0, s24
	s_nop 0
	s_mov_b32 s24, m0
	s_mov_b32 m0, s50
	s_nop 0
	global_load_lds_dwordx4 v138, s[42:43]
	s_mov_b32 m0, s24
	s_waitcnt vmcnt(8)
	s_waitcnt lgkmcnt(0)
	s_barrier
	s_setprio 1
	v_mfma_f32_16x16x32_bf16 v[60:63], v[148:151], v[180:183], v[60:63]
	v_mfma_f32_16x16x32_bf16 v[52:55], v[156:159], v[180:183], v[52:55]
	v_mfma_f32_16x16x32_bf16 v[44:47], v[148:151], v[188:191], v[44:47]
	v_mfma_f32_16x16x32_bf16 v[36:39], v[156:159], v[188:191], v[36:39]
	v_mfma_f32_16x16x32_bf16 v[28:31], v[148:151], v[196:199], v[28:31]
	v_mfma_f32_16x16x32_bf16 v[20:23], v[156:159], v[196:199], v[20:23]
	v_mfma_f32_16x16x32_bf16 v[12:15], v[148:151], v[204:207], v[12:15]
	v_mfma_f32_16x16x32_bf16 v[4:7], v[156:159], v[204:207], v[4:7]
	v_mfma_f32_16x16x32_bf16 v[60:63], v[152:155], v[184:187], v[60:63]
	v_mfma_f32_16x16x32_bf16 v[52:55], v[160:163], v[184:187], v[52:55]
	v_mfma_f32_16x16x32_bf16 v[44:47], v[152:155], v[192:195], v[44:47]
	v_mfma_f32_16x16x32_bf16 v[36:39], v[160:163], v[192:195], v[36:39]
	v_mfma_f32_16x16x32_bf16 v[28:31], v[152:155], v[200:203], v[28:31]
	v_mfma_f32_16x16x32_bf16 v[20:23], v[160:163], v[200:203], v[20:23]
	v_mfma_f32_16x16x32_bf16 v[12:15], v[152:155], v[208:211], v[12:15]
	v_mfma_f32_16x16x32_bf16 v[4:7], v[160:163], v[208:211], v[4:7]
	v_mfma_f32_16x16x32_bf16 v[56:59], v[164:167], v[180:183], v[56:59]
	v_mfma_f32_16x16x32_bf16 v[48:51], v[172:175], v[180:183], v[48:51]
	v_mfma_f32_16x16x32_bf16 v[40:43], v[164:167], v[188:191], v[40:43]
	v_mfma_f32_16x16x32_bf16 v[32:35], v[172:175], v[188:191], v[32:35]
	v_mfma_f32_16x16x32_bf16 v[24:27], v[164:167], v[196:199], v[24:27]
	v_mfma_f32_16x16x32_bf16 v[16:19], v[172:175], v[196:199], v[16:19]
	v_mfma_f32_16x16x32_bf16 v[8:11], v[164:167], v[204:207], v[8:11]
	v_mfma_f32_16x16x32_bf16 v[0:3], v[172:175], v[204:207], v[0:3]
	v_mfma_f32_16x16x32_bf16 v[56:59], v[168:171], v[184:187], v[56:59]
	v_mfma_f32_16x16x32_bf16 v[48:51], v[176:179], v[184:187], v[48:51]
	v_mfma_f32_16x16x32_bf16 v[40:43], v[168:171], v[192:195], v[40:43]
	v_mfma_f32_16x16x32_bf16 v[32:35], v[176:179], v[192:195], v[32:35]
	ds_read_b32 v255, v255 offset:4096
	v_mfma_f32_16x16x32_bf16 v[24:27], v[168:171], v[200:203], v[24:27]
	v_mfma_f32_16x16x32_bf16 v[16:19], v[176:179], v[200:203], v[16:19]
	v_mfma_f32_16x16x32_bf16 v[8:11], v[168:171], v[208:211], v[8:11]
	v_mfma_f32_16x16x32_bf16 v[0:3], v[176:179], v[208:211], v[0:3]
	s_add_u32 s98, s98, 0x80000
	s_waitcnt lgkmcnt(0)
	v_readfirstlane_b32 s101, v255
	v_mov_b32_e32 v255, 0x20000
	s_cmp_ge_u32 s101, s98
	s_cbranch_scc1 .Lmy_g_17

; #define PG8_STAGE(bufoff, gbase, voff) do { _Pragma("unroll") for (int _i = 0; _i < 2; ++_i) { unsigned keep_; \
;         asm volatile("s_mov_b32 %0, m0\n\ts_mov_b32 m0, %3\n\ts_nop 0\n\tglobal_load_lds_dwordx4 %1, %2\n\ts_mov_b32 m0, %0" : "=&s"(keep_) : "v"((voff)[_i]), "s"((const char*)(gbase)), "s"(ldsbase + (unsigned)((bufoff) + _i * 8192)) : "memory"); } } while (0)
; #define PG8_WAIT_V(n) asm volatile("s_waitcnt vmcnt(" #n ")" ::: "memory")
; #define PG8_WAIT_L(n) asm volatile("s_waitcnt lgkmcnt(" #n ")" ::: "memory")
; #define PG8_BAR __builtin_amdgcn_s_barrier()
; #define PG8_SCHED __builtin_amdgcn_sched_barrier(0)
; template <class Epi, class Sched, bool ALIGN_EPI, bool FP8 = false>
; DI void gemm_phase(LAS unsigned char* lds, const Gemm g, const Sched& S, const Epi& E) {
;     ...
;             PG8_LDB(B0, 1, 0); PG8_LDB(B1, 1, 1); PG8_SCHED; PG8_LDA(At, 1, 0); PG8_STAGE(PG8_SA(0, 1), a2 + hstepA, voffA);
;             PG8_WAIT_V(8); PG8_WAIT_L(0); PG8_BAR; PG8_MMA(0, 0, At, B0); PG8_MMA(0, 1, At, B1); PG8_BAR; PG8_SCHED;
.Lmy_g_17:
	s_setprio 0
	ds_read_b128 v[148:151], v145
	ds_read_b128 v[152:155], v145 offset:1024
	ds_read_b128 v[156:159], v145 offset:2048
	ds_read_b128 v[160:163], v145 offset:3072
	ds_read_b128 v[164:167], v146
	ds_read_b128 v[168:171], v146 offset:1024
	ds_read_b128 v[172:175], v146 offset:2048
	ds_read_b128 v[176:179], v146 offset:3072
	ds_read_b128 v[180:183], v144 offset:32768
	ds_read_b128 v[184:187], v144 offset:33792
	ds_read_b128 v[188:191], v144 offset:34816
	ds_read_b128 v[192:195], v144 offset:35840
	ds_read_b128 v[196:199], v144 offset:36864
	ds_read_b128 v[200:203], v144 offset:37888
	ds_read_b128 v[204:207], v144 offset:38912
	ds_read_b128 v[208:211], v144 offset:39936
	s_add_u32 s24, s42, 0x80000
	s_addc_u32 s25, s43, 0
	s_mov_b32 s42, m0
	s_mov_b32 m0, s51
	s_nop 0
	global_load_lds_dwordx4 v136, s[24:25]
	s_mov_b32 m0, s42
	s_nop 0
	s_mov_b32 s42, m0
	s_mov_b32 m0, s52
	s_nop 0
	global_load_lds_dwordx4 v138, s[24:25]
	s_mov_b32 m0, s42
	s_waitcnt vmcnt(8)
	s_waitcnt lgkmcnt(0)
	s_barrier
	s_setprio 1
	v_mfma_f32_16x16x32_bf16 v[124:127], v[148:151], v[180:183], v[124:127]
	v_mfma_f32_16x16x32_bf16 v[116:119], v[156:159], v[180:183], v[116:119]
	v_mfma_f32_16x16x32_bf16 v[108:111], v[148:151], v[188:191], v[108:111]
	v_mfma_f32_16x16x32_bf16 v[100:103], v[156:159], v[188:191], v[100:103]
	v_mfma_f32_16x16x32_bf16 v[92:95], v[148:151], v[196:199], v[92:95]
	v_mfma_f32_16x16x32_bf16 v[84:87], v[156:159], v[196:199], v[84:87]
	v_mfma_f32_16x16x32_bf16 v[76:79], v[148:151], v[204:207], v[76:79]
	v_mfma_f32_16x16x32_bf16 v[68:71], v[156:159], v[204:207], v[68:71]
	v_mfma_f32_16x16x32_bf16 v[124:127], v[152:155], v[184:187], v[124:127]
	v_mfma_f32_16x16x32_bf16 v[116:119], v[160:163], v[184:187], v[116:119]
	v_mfma_f32_16x16x32_bf16 v[108:111], v[152:155], v[192:195], v[108:111]
	v_mfma_f32_16x16x32_bf16 v[100:103], v[160:163], v[192:195], v[100:103]
	v_mfma_f32_16x16x32_bf16 v[92:95], v[152:155], v[200:203], v[92:95]
	v_mfma_f32_16x16x32_bf16 v[84:87], v[160:163], v[200:203], v[84:87]
	v_mfma_f32_16x16x32_bf16 v[76:79], v[152:155], v[208:211], v[76:79]
	v_mfma_f32_16x16x32_bf16 v[68:71], v[160:163], v[208:211], v[68:71]
	v_mfma_f32_16x16x32_bf16 v[120:123], v[164:167], v[180:183], v[120:123]
	v_mfma_f32_16x16x32_bf16 v[112:115], v[172:175], v[180:183], v[112:115]
	v_mfma_f32_16x16x32_bf16 v[104:107], v[164:167], v[188:191], v[104:107]
	v_mfma_f32_16x16x32_bf16 v[96:99], v[172:175], v[188:191], v[96:99]
	v_mfma_f32_16x16x32_bf16 v[88:91], v[164:167], v[196:199], v[88:91]
	v_mfma_f32_16x16x32_bf16 v[80:83], v[172:175], v[196:199], v[80:83]
	v_mfma_f32_16x16x32_bf16 v[72:75], v[164:167], v[204:207], v[72:75]
	v_mfma_f32_16x16x32_bf16 v[64:67], v[172:175], v[204:207], v[64:67]
	v_mfma_f32_16x16x32_bf16 v[120:123], v[168:171], v[184:187], v[120:123]
	v_mfma_f32_16x16x32_bf16 v[112:115], v[176:179], v[184:187], v[112:115]
	v_mfma_f32_16x16x32_bf16 v[104:107], v[168:171], v[192:195], v[104:107]
	v_mfma_f32_16x16x32_bf16 v[96:99], v[176:179], v[192:195], v[96:99]
	ds_read_b32 v255, v255 offset:4096
	v_mfma_f32_16x16x32_bf16 v[88:91], v[168:171], v[200:203], v[88:91]
	v_mfma_f32_16x16x32_bf16 v[80:83], v[176:179], v[200:203], v[80:83]
	v_mfma_f32_16x16x32_bf16 v[72:75], v[168:171], v[208:211], v[72:75]
	v_mfma_f32_16x16x32_bf16 v[64:67], v[176:179], v[208:211], v[64:67]
	s_add_u32 s98, s98, 0x80000
	s_waitcnt lgkmcnt(0)
	v_readfirstlane_b32 s101, v255
	v_mov_b32_e32 v255, 0x20000
	s_cmp_ge_u32 s101, s98
	s_cbranch_scc1 .Lmy_g_18

; #define PG8_STAGE(bufoff, gbase, voff) do { _Pragma("unroll") for (int _i = 0; _i < 2; ++_i) { unsigned keep_; \
;         asm volatile("s_mov_b32 %0, m0\n\ts_mov_b32 m0, %3\n\ts_nop 0\n\tglobal_load_lds_dwordx4 %1, %2\n\ts_mov_b32 m0, %0" : "=&s"(keep_) : "v"((voff)[_i]), "s"((const char*)(gbase)), "s"(ldsbase + (unsigned)((bufoff) + _i * 8192)) : "memory"); } } while (0)
; #define PG8_WAIT_V(n) asm volatile("s_waitcnt vmcnt(" #n ")" ::: "memory")
; #define PG8_WAIT_L(n) asm volatile("s_waitcnt lgkmcnt(" #n ")" ::: "memory")
; #define PG8_BAR __builtin_amdgcn_s_barrier()
; #define PG8_SCHED __builtin_amdgcn_sched_barrier(0)
; template <class Epi, class Sched, bool ALIGN_EPI, bool FP8 = false>
; DI void gemm_phase(LAS unsigned char* lds, const Gemm g, const Sched& S, const Epi& E) {
;     ...
;             PG8_LDA(At, 1, 1); PG8_STAGE(PG8_SB(1, 0), b3, voffB); PG8_STAGE(PG8_SB(1, 1), b3 + hstepB, voffB); PG8_STAGE(PG8_SA(1, 0), a3, voffA);
;             PG8_WAIT_V(8); PG8_WAIT_L(0); PG8_BAR; PG8_MMA(1, 0, At, B0); PG8_MMA(1, 1, At, B1); PG8_BAR; PG8_SCHED;
.Lmy_g_18:
	s_setprio 0
	ds_read_b128 v[180:183], v144 offset:49152
	ds_read_b128 v[184:187], v144 offset:50176
	ds_read_b128 v[188:191], v144 offset:51200
	ds_read_b128 v[192:195], v144 offset:52224
	ds_read_b128 v[196:199], v144 offset:53248
	ds_read_b128 v[200:203], v144 offset:54272
	ds_read_b128 v[204:207], v144 offset:55296
	ds_read_b128 v[208:211], v144 offset:56320
	s_add_u32 s24, s40, 0x80
	s_addc_u32 s25, s41, 0
	s_mov_b32 s42, m0
	s_mov_b32 m0, s55
	s_nop 0
	global_load_lds_dwordx4 v137, s[24:25]
	s_mov_b32 m0, s42
	s_nop 0
	s_mov_b32 s42, m0
	s_mov_b32 m0, s56
	s_nop 0
	global_load_lds_dwordx4 v139, s[24:25]
	s_mov_b32 m0, s42
	s_add_u32 s24, s40, 0x80080
	s_addc_u32 s25, s41, 0
	s_mov_b32 s40, m0
	s_mov_b32 m0, s59
	s_nop 0
	global_load_lds_dwordx4 v137, s[24:25]
	s_mov_b32 m0, s40
	s_nop 0
	s_mov_b32 s40, m0
	s_mov_b32 m0, s60
	s_nop 0
	global_load_lds_dwordx4 v139, s[24:25]
	s_mov_b32 m0, s40
	s_mov_b32 s24, m0
	s_mov_b32 m0, s57
	s_nop 0
	global_load_lds_dwordx4 v136, s[28:29]
	s_mov_b32 m0, s24
	s_nop 0
	s_mov_b32 s24, m0
	s_mov_b32 m0, s58
	s_nop 0
	global_load_lds_dwordx4 v138, s[28:29]
	s_mov_b32 m0, s24
	s_waitcnt vmcnt(8)
	s_waitcnt lgkmcnt(0)
	s_barrier
	s_setprio 1
	v_mfma_f32_16x16x32_bf16 v[60:63], v[148:151], v[180:183], v[60:63]
	v_mfma_f32_16x16x32_bf16 v[52:55], v[156:159], v[180:183], v[52:55]
	v_mfma_f32_16x16x32_bf16 v[44:47], v[148:151], v[188:191], v[44:47]
	v_mfma_f32_16x16x32_bf16 v[36:39], v[156:159], v[188:191], v[36:39]
	v_mfma_f32_16x16x32_bf16 v[28:31], v[148:151], v[196:199], v[28:31]
	v_mfma_f32_16x16x32_bf16 v[20:23], v[156:159], v[196:199], v[20:23]
	v_mfma_f32_16x16x32_bf16 v[12:15], v[148:151], v[204:207], v[12:15]
	v_mfma_f32_16x16x32_bf16 v[4:7], v[156:159], v[204:207], v[4:7]
	v_mfma_f32_16x16x32_bf16 v[60:63], v[152:155], v[184:187], v[60:63]
	v_mfma_f32_16x16x32_bf16 v[52:55], v[160:163], v[184:187], v[52:55]
	v_mfma_f32_16x16x32_bf16 v[44:47], v[152:155], v[192:195], v[44:47]
	v_mfma_f32_16x16x32_bf16 v[36:39], v[160:163], v[192:195], v[36:39]
	v_mfma_f32_16x16x32_bf16 v[28:31], v[152:155], v[200:203], v[28:31]
	v_mfma_f32_16x16x32_bf16 v[20:23], v[160:163], v[200:203], v[20:23]
	v_mfma_f32_16x16x32_bf16 v[12:15], v[152:155], v[208:211], v[12:15]
	v_mfma_f32_16x16x32_bf16 v[4:7], v[160:163], v[208:211], v[4:7]
	v_mfma_f32_16x16x32_bf16 v[56:59], v[164:167], v[180:183], v[56:59]
	v_mfma_f32_16x16x32_bf16 v[48:51], v[172:175], v[180:183], v[48:51]
	v_mfma_f32_16x16x32_bf16 v[40:43], v[164:167], v[188:191], v[40:43]
	v_mfma_f32_16x16x32_bf16 v[32:35], v[172:175], v[188:191], v[32:35]
	v_mfma_f32_16x16x32_bf16 v[24:27], v[164:167], v[196:199], v[24:27]
	v_mfma_f32_16x16x32_bf16 v[16:19], v[172:175], v[196:199], v[16:19]
	v_mfma_f32_16x16x32_bf16 v[8:11], v[164:167], v[204:207], v[8:11]
	v_mfma_f32_16x16x32_bf16 v[0:3], v[172:175], v[204:207], v[0:3]
	v_mfma_f32_16x16x32_bf16 v[56:59], v[168:171], v[184:187], v[56:59]
	v_mfma_f32_16x16x32_bf16 v[48:51], v[176:179], v[184:187], v[48:51]
	v_mfma_f32_16x16x32_bf16 v[40:43], v[168:171], v[192:195], v[40:43]
	v_mfma_f32_16x16x32_bf16 v[32:35], v[176:179], v[192:195], v[32:35]
	ds_read_b32 v255, v255 offset:4096
	v_mfma_f32_16x16x32_bf16 v[24:27], v[168:171], v[200:203], v[24:27]
	v_mfma_f32_16x16x32_bf16 v[16:19], v[176:179], v[200:203], v[16:19]
	v_mfma_f32_16x16x32_bf16 v[8:11], v[168:171], v[208:211], v[8:11]
	v_mfma_f32_16x16x32_bf16 v[0:3], v[176:179], v[208:211], v[0:3]
	s_add_u32 s98, s98, 0x80000
	s_waitcnt lgkmcnt(0)
	v_readfirstlane_b32 s101, v255
	v_mov_b32_e32 v255, 0x20000
	s_cmp_ge_u32 s101, s98
	s_cbranch_scc1 .Lmy_g_19

; #define PG8_BAR __builtin_amdgcn_s_barrier()
;     DI int nt(const Unit& u) const { return (u.aux & 8) ? PLED / 64 : ((u.aux & 4) ? (D_ / 2) / 64 : D_ / 64); }
; template <class Epi, class Sched, bool ALIGN_EPI, bool FP8 = false>
; DI void gemm_phase(LAS unsigned char* lds, const Gemm g, const Sched& S, const Epi& E) {
;     ...
;         for (int t = 0; t < nt; t += 2) {
;     ...
;         if constexpr (ALIGN_EPI) { if (wr == 0) PG8_BAR; }
.Lmy_g_19:
	s_setprio 0
	s_add_i32 s71, s71, 2
	s_add_u32 s69, s69, 0x100
	s_addc_u32 s70, s70, 0
	s_cmp_gt_u32 s71, 29
	s_mov_b64 s[24:25], s[26:27]
	s_cbranch_scc0 .Lmy_g0_700
.Lmy_ex_700:
	s_and_b64 vcc, exec, s[10:11]
	s_cbranch_vccz .LBB0_703
	s_barrier

; #define PG8_STAGE(bufoff, gbase, voff) do { _Pragma("unroll") for (int _i = 0; _i < 2; ++_i) { unsigned keep_; \
;         asm volatile("s_mov_b32 %0, m0\n\ts_mov_b32 m0, %3\n\ts_nop 0\n\tglobal_load_lds_dwordx4 %1, %2\n\ts_mov_b32 m0, %0" : "=&s"(keep_) : "v"((voff)[_i]), "s"((const char*)(gbase)), "s"(ldsbase + (unsigned)((bufoff) + _i * 8192)) : "memory"); } } while (0)
; #define PG8_WAIT_V(n) asm volatile("s_waitcnt vmcnt(" #n ")" ::: "memory")
; #define PG8_WAIT_L(n) asm volatile("s_waitcnt lgkmcnt(" #n ")" ::: "memory")
; #define PG8_BAR __builtin_amdgcn_s_barrier()
; #define PG8_SCHED __builtin_amdgcn_sched_barrier(0)
;     DI int nt(const Unit& u) const { return (u.aux & 8) ? PLED / 64 : ((u.aux & 4) ? (D_ / 2) / 64 : D_ / 64); }
; template <class Epi, class Sched, bool ALIGN_EPI, bool FP8 = false>
; DI void gemm_phase(LAS unsigned char* lds, const Gemm g, const Sched& S, const Epi& E) {
;     ...
;             const bool last = (t == nt - 2);
;             const char* a1 = cA + (size_t)(t + 1) * kstep;
;             const char* a2 = last ? nA : cA + (size_t)(t + 2) * kstep; const char* b2 = last ? nB : cB + (size_t)(t + 2) * kstep;
;             const char* a3 = a2 + kstep; const char* b3 = b2 + kstep;
;             PG8_LDB(B0, 0, 0); PG8_LDB(B1, 0, 1); PG8_SCHED; PG8_LDA(At, 0, 0); PG8_STAGE(PG8_SA(1, 1), a1 + hstepA, voffA);
;             PG8_WAIT_V(8); PG8_WAIT_L(0); PG8_BAR; PG8_MMA(0, 0, At, B0); PG8_MMA(0, 1, At, B1); PG8_BAR; PG8_SCHED;
;             PG8_LDA(At, 0, 1); PG8_STAGE(PG8_SB(0, 0), b2, voffB); PG8_STAGE(PG8_SB(0, 1), b2 + hstepB, voffB); PG8_STAGE(PG8_SA(0, 0), a2, voffA);
;             PG8_WAIT_V(8); PG8_WAIT_L(0); PG8_BAR; PG8_MMA(1, 0, At, B0); PG8_MMA(1, 1, At, B1); PG8_BAR; PG8_SCHED;
.LBB0_724:
	s_cmp_lg_u32 s99, 0
	s_cbranch_scc1 .Lmy_g0_724
	ds_read_b128 v[146:149], v140
	ds_read_b128 v[150:153], v140 offset:1024
	ds_read_b128 v[154:157], v140 offset:2048
	ds_read_b128 v[158:161], v140 offset:3072
	ds_read_b128 v[162:165], v141
	ds_read_b128 v[166:169], v141 offset:1024
	ds_read_b128 v[170:173], v141 offset:2048
	ds_read_b128 v[174:177], v141 offset:3072
	s_add_u32 s66, s64, 0x100
	s_addc_u32 s67, s65, 0
	s_cmp_eq_u32 vcc_lo, 28
	s_cselect_b32 s72, s94, s66
	s_cselect_b32 s73, s57, s67
	s_cselect_b32 s70, s95, s96
	s_cselect_b32 s71, s55, s97
	s_add_u32 s68, s72, 0x80
	s_addc_u32 s69, s73, 0
	ds_read_b128 v[178:181], v142
	ds_read_b128 v[182:185], v142 offset:1024
	ds_read_b128 v[186:189], v142 offset:2048
	ds_read_b128 v[190:193], v142 offset:3072
	ds_read_b128 v[194:197], v142 offset:4096
	ds_read_b128 v[198:201], v142 offset:5120
	ds_read_b128 v[202:205], v142 offset:6144
	ds_read_b128 v[206:209], v142 offset:7168
	s_add_u32 s64, s64, 0x80080
	s_addc_u32 s65, s65, 0
	s_mov_b32 vcc_hi, m0
	s_mov_b32 m0, s90
	s_nop 0
	global_load_lds_dwordx4 v134, s[64:65]
	s_mov_b32 m0, vcc_hi
	s_nop 0
	s_mov_b32 vcc_hi, m0
	s_mov_b32 m0, s91
	s_nop 0
	global_load_lds_dwordx4 v136, s[64:65]
	s_mov_b32 m0, vcc_hi
	s_waitcnt vmcnt(8)
	s_waitcnt lgkmcnt(0)
	s_mov_b64 exec, 1
	ds_add_u32 v255, v255 offset:4096
	s_mov_b64 exec, -1
	s_setprio 1
	v_mfma_f32_16x16x32_bf16 v[124:127], v[146:149], v[178:181], v[124:127]
	v_mfma_f32_16x16x32_bf16 v[120:123], v[154:157], v[178:181], v[120:123]
	v_mfma_f32_16x16x32_bf16 v[108:111], v[146:149], v[186:189], v[108:111]
	v_mfma_f32_16x16x32_bf16 v[104:107], v[154:157], v[186:189], v[104:107]
	v_mfma_f32_16x16x32_bf16 v[92:95], v[146:149], v[194:197], v[92:95]
	v_mfma_f32_16x16x32_bf16 v[88:91], v[154:157], v[194:197], v[88:91]
	v_mfma_f32_16x16x32_bf16 v[76:79], v[146:149], v[202:205], v[76:79]
	v_mfma_f32_16x16x32_bf16 v[72:75], v[154:157], v[202:205], v[72:75]
	v_mfma_f32_16x16x32_bf16 v[124:127], v[150:153], v[182:185], v[124:127]
	v_mfma_f32_16x16x32_bf16 v[120:123], v[158:161], v[182:185], v[120:123]
	v_mfma_f32_16x16x32_bf16 v[108:111], v[150:153], v[190:193], v[108:111]
	v_mfma_f32_16x16x32_bf16 v[104:107], v[158:161], v[190:193], v[104:107]
	v_mfma_f32_16x16x32_bf16 v[92:95], v[150:153], v[198:201], v[92:95]
	v_mfma_f32_16x16x32_bf16 v[88:91], v[158:161], v[198:201], v[88:91]
	v_mfma_f32_16x16x32_bf16 v[76:79], v[150:153], v[206:209], v[76:79]
	v_mfma_f32_16x16x32_bf16 v[72:75], v[158:161], v[206:209], v[72:75]
	v_mfma_f32_16x16x32_bf16 v[116:119], v[162:165], v[178:181], v[116:119]
	v_mfma_f32_16x16x32_bf16 v[112:115], v[170:173], v[178:181], v[112:115]
	v_mfma_f32_16x16x32_bf16 v[100:103], v[162:165], v[186:189], v[100:103]
	v_mfma_f32_16x16x32_bf16 v[96:99], v[170:173], v[186:189], v[96:99]
	v_mfma_f32_16x16x32_bf16 v[84:87], v[162:165], v[194:197], v[84:87]
	v_mfma_f32_16x16x32_bf16 v[80:83], v[170:173], v[194:197], v[80:83]
	v_mfma_f32_16x16x32_bf16 v[68:71], v[162:165], v[202:205], v[68:71]
	v_mfma_f32_16x16x32_bf16 v[64:67], v[170:173], v[202:205], v[64:67]
	v_mfma_f32_16x16x32_bf16 v[116:119], v[166:169], v[182:185], v[116:119]
	v_mfma_f32_16x16x32_bf16 v[112:115], v[174:177], v[182:185], v[112:115]
	v_mfma_f32_16x16x32_bf16 v[100:103], v[166:169], v[190:193], v[100:103]
	v_mfma_f32_16x16x32_bf16 v[96:99], v[174:177], v[190:193], v[96:99]
	v_mfma_f32_16x16x32_bf16 v[84:87], v[166:169], v[198:201], v[84:87]
	v_mfma_f32_16x16x32_bf16 v[80:83], v[174:177], v[198:201], v[80:83]
	v_mfma_f32_16x16x32_bf16 v[68:71], v[166:169], v[206:209], v[68:71]
	v_mfma_f32_16x16x32_bf16 v[64:67], v[174:177], v[206:209], v[64:67]
	s_setprio 0
	s_barrier
	ds_read_b128 v[178:181], v142 offset:16384
	ds_read_b128 v[182:185], v142 offset:17408
	ds_read_b128 v[186:189], v142 offset:18432
	ds_read_b128 v[190:193], v142 offset:19456
	ds_read_b128 v[194:197], v142 offset:20480
	ds_read_b128 v[198:201], v142 offset:21504
	ds_read_b128 v[202:205], v142 offset:22528
	ds_read_b128 v[206:209], v142 offset:23552
	s_mov_b32 s64, m0
	s_mov_b32 m0, s63
	s_nop 0
	global_load_lds_dwordx4 v135, s[70:71]
	s_mov_b32 m0, s64
	s_nop 0
	s_mov_b32 s64, m0
	s_mov_b32 m0, s77
	s_nop 0
	global_load_lds_dwordx4 v137, s[70:71]
	s_mov_b32 m0, s64
	s_add_u32 s64, s70, 0x80000
	s_addc_u32 s65, s71, 0
	s_mov_b32 vcc_hi, m0
	s_mov_b32 m0, s79
	s_nop 0
	global_load_lds_dwordx4 v135, s[64:65]
	s_mov_b32 m0, vcc_hi
	s_nop 0
	s_mov_b32 vcc_hi, m0
	s_mov_b32 m0, s80
	s_nop 0
	global_load_lds_dwordx4 v137, s[64:65]
	s_mov_b32 m0, vcc_hi
	s_mov_b32 s64, m0
	s_mov_b32 m0, s75
	s_nop 0
	global_load_lds_dwordx4 v134, s[72:73]
	s_mov_b32 m0, s64
	s_nop 0
	s_mov_b32 s64, m0
	s_mov_b32 m0, s81
	s_nop 0
	global_load_lds_dwordx4 v136, s[72:73]
	s_mov_b32 m0, s64
	s_waitcnt vmcnt(8)
	s_waitcnt lgkmcnt(0)
; #define PG8_STAGE(bufoff, gbase, voff) do { _Pragma("unroll") for (int _i = 0; _i < 2; ++_i) { unsigned keep_; \
;         asm volatile("s_mov_b32 %0, m0\n\ts_mov_b32 m0, %3\n\ts_nop 0\n\tglobal_load_lds_dwordx4 %1, %2\n\ts_mov_b32 m0, %0" : "=&s"(keep_) : "v"((voff)[_i]), "s"((const char*)(gbase)), "s"(ldsbase + (unsigned)((bufoff) + _i * 8192)) : "memory"); } } while (0)
; #define PG8_WAIT_V(n) asm volatile("s_waitcnt vmcnt(" #n ")" ::: "memory")
; #define PG8_WAIT_L(n) asm volatile("s_waitcnt lgkmcnt(" #n ")" ::: "memory")
; #define PG8_BAR __builtin_amdgcn_s_barrier()
; #define PG8_SCHED __builtin_amdgcn_sched_barrier(0)
; template <class Epi, class Sched, bool ALIGN_EPI, bool FP8 = false>
; DI void gemm_phase(LAS unsigned char* lds, const Gemm g, const Sched& S, const Epi& E) {
;     ...
;             PG8_WAIT_V(8); PG8_WAIT_L(0); PG8_BAR; PG8_MMA(1, 0, At, B0); PG8_MMA(1, 1, At, B1); PG8_BAR; PG8_SCHED;
;             PG8_LDB(B0, 1, 0); PG8_LDB(B1, 1, 1); PG8_SCHED; PG8_LDA(At, 1, 0); PG8_STAGE(PG8_SA(0, 1), a2 + hstepA, voffA);
;             PG8_WAIT_V(8); PG8_WAIT_L(0); PG8_BAR; PG8_MMA(0, 0, At, B0); PG8_MMA(0, 1, At, B1); PG8_BAR; PG8_SCHED;
	s_mov_b64 exec, 1
	ds_add_u32 v255, v255 offset:4096
	s_mov_b64 exec, -1
	s_setprio 1
	v_mfma_f32_16x16x32_bf16 v[60:63], v[146:149], v[178:181], v[60:63]
	v_mfma_f32_16x16x32_bf16 v[56:59], v[154:157], v[178:181], v[56:59]
	v_mfma_f32_16x16x32_bf16 v[44:47], v[146:149], v[186:189], v[44:47]
	v_mfma_f32_16x16x32_bf16 v[40:43], v[154:157], v[186:189], v[40:43]
	v_mfma_f32_16x16x32_bf16 v[28:31], v[146:149], v[194:197], v[28:31]
	v_mfma_f32_16x16x32_bf16 v[24:27], v[154:157], v[194:197], v[24:27]
	v_mfma_f32_16x16x32_bf16 v[12:15], v[146:149], v[202:205], v[12:15]
	v_mfma_f32_16x16x32_bf16 v[8:11], v[154:157], v[202:205], v[8:11]
	v_mfma_f32_16x16x32_bf16 v[60:63], v[150:153], v[182:185], v[60:63]
	v_mfma_f32_16x16x32_bf16 v[56:59], v[158:161], v[182:185], v[56:59]
	v_mfma_f32_16x16x32_bf16 v[44:47], v[150:153], v[190:193], v[44:47]
	v_mfma_f32_16x16x32_bf16 v[40:43], v[158:161], v[190:193], v[40:43]
	v_mfma_f32_16x16x32_bf16 v[28:31], v[150:153], v[198:201], v[28:31]
	v_mfma_f32_16x16x32_bf16 v[24:27], v[158:161], v[198:201], v[24:27]
	v_mfma_f32_16x16x32_bf16 v[12:15], v[150:153], v[206:209], v[12:15]
	v_mfma_f32_16x16x32_bf16 v[8:11], v[158:161], v[206:209], v[8:11]
	v_mfma_f32_16x16x32_bf16 v[52:55], v[162:165], v[178:181], v[52:55]
	v_mfma_f32_16x16x32_bf16 v[48:51], v[170:173], v[178:181], v[48:51]
	v_mfma_f32_16x16x32_bf16 v[36:39], v[162:165], v[186:189], v[36:39]
	v_mfma_f32_16x16x32_bf16 v[32:35], v[170:173], v[186:189], v[32:35]
	v_mfma_f32_16x16x32_bf16 v[20:23], v[162:165], v[194:197], v[20:23]
	v_mfma_f32_16x16x32_bf16 v[16:19], v[170:173], v[194:197], v[16:19]
	v_mfma_f32_16x16x32_bf16 v[4:7], v[162:165], v[202:205], v[4:7]
	v_mfma_f32_16x16x32_bf16 v[0:3], v[170:173], v[202:205], v[0:3]
	v_mfma_f32_16x16x32_bf16 v[52:55], v[166:169], v[182:185], v[52:55]
	v_mfma_f32_16x16x32_bf16 v[48:51], v[174:177], v[182:185], v[48:51]
	v_mfma_f32_16x16x32_bf16 v[36:39], v[166:169], v[190:193], v[36:39]
	v_mfma_f32_16x16x32_bf16 v[32:35], v[174:177], v[190:193], v[32:35]
	v_mfma_f32_16x16x32_bf16 v[20:23], v[166:169], v[198:201], v[20:23]
	v_mfma_f32_16x16x32_bf16 v[16:19], v[174:177], v[198:201], v[16:19]
	v_mfma_f32_16x16x32_bf16 v[4:7], v[166:169], v[206:209], v[4:7]
	v_mfma_f32_16x16x32_bf16 v[0:3], v[174:177], v[206:209], v[0:3]
	s_setprio 0
	s_barrier
	ds_read_b128 v[146:149], v143
	ds_read_b128 v[150:153], v143 offset:1024
	ds_read_b128 v[154:157], v143 offset:2048
	ds_read_b128 v[158:161], v143 offset:3072
	ds_read_b128 v[162:165], v144
	ds_read_b128 v[166:169], v144 offset:1024
	ds_read_b128 v[170:173], v144 offset:2048
	ds_read_b128 v[174:177], v144 offset:3072
	ds_read_b128 v[178:181], v142 offset:32768
	ds_read_b128 v[182:185], v142 offset:33792
	ds_read_b128 v[186:189], v142 offset:34816
	ds_read_b128 v[190:193], v142 offset:35840
	ds_read_b128 v[194:197], v142 offset:36864
	ds_read_b128 v[198:201], v142 offset:37888
	ds_read_b128 v[202:205], v142 offset:38912
	ds_read_b128 v[206:209], v142 offset:39936
	s_add_u32 s64, s72, 0x80000
	s_addc_u32 s65, s73, 0
	s_mov_b32 s72, m0
	s_mov_b32 m0, s82
	s_nop 0
	global_load_lds_dwordx4 v134, s[64:65]
	s_mov_b32 m0, s72
	s_nop 0
	s_mov_b32 s72, m0
	s_mov_b32 m0, s83
	s_nop 0
	global_load_lds_dwordx4 v136, s[64:65]
	s_mov_b32 m0, s72
	s_waitcnt vmcnt(8)
	s_waitcnt lgkmcnt(0)
	s_mov_b64 exec, 1
	ds_add_u32 v255, v255 offset:4096
	s_mov_b64 exec, -1
	s_setprio 1
	v_mfma_f32_16x16x32_bf16 v[124:127], v[146:149], v[178:181], v[124:127]
	v_mfma_f32_16x16x32_bf16 v[120:123], v[154:157], v[178:181], v[120:123]
	v_mfma_f32_16x16x32_bf16 v[108:111], v[146:149], v[186:189], v[108:111]
	v_mfma_f32_16x16x32_bf16 v[104:107], v[154:157], v[186:189], v[104:107]
	v_mfma_f32_16x16x32_bf16 v[92:95], v[146:149], v[194:197], v[92:95]
	v_mfma_f32_16x16x32_bf16 v[88:91], v[154:157], v[194:197], v[88:91]
	v_mfma_f32_16x16x32_bf16 v[76:79], v[146:149], v[202:205], v[76:79]
	v_mfma_f32_16x16x32_bf16 v[72:75], v[154:157], v[202:205], v[72:75]
	v_mfma_f32_16x16x32_bf16 v[124:127], v[150:153], v[182:185], v[124:127]
	v_mfma_f32_16x16x32_bf16 v[120:123], v[158:161], v[182:185], v[120:123]
	v_mfma_f32_16x16x32_bf16 v[108:111], v[150:153], v[190:193], v[108:111]
	v_mfma_f32_16x16x32_bf16 v[104:107], v[158:161], v[190:193], v[104:107]
	v_mfma_f32_16x16x32_bf16 v[92:95], v[150:153], v[198:201], v[92:95]
	v_mfma_f32_16x16x32_bf16 v[88:91], v[158:161], v[198:201], v[88:91]
	v_mfma_f32_16x16x32_bf16 v[76:79], v[150:153], v[206:209], v[76:79]
	v_mfma_f32_16x16x32_bf16 v[72:75], v[158:161], v[206:209], v[72:75]
	v_mfma_f32_16x16x32_bf16 v[116:119], v[162:165], v[178:181], v[116:119]
	v_mfma_f32_16x16x32_bf16 v[112:115], v[170:173], v[178:181], v[112:115]
	v_mfma_f32_16x16x32_bf16 v[100:103], v[162:165], v[186:189], v[100:103]
	v_mfma_f32_16x16x32_bf16 v[96:99], v[170:173], v[186:189], v[96:99]
	v_mfma_f32_16x16x32_bf16 v[84:87], v[162:165], v[194:197], v[84:87]
	v_mfma_f32_16x16x32_bf16 v[80:83], v[170:173], v[194:197], v[80:83]
	v_mfma_f32_16x16x32_bf16 v[68:71], v[162:165], v[202:205], v[68:71]
	v_mfma_f32_16x16x32_bf16 v[64:67], v[170:173], v[202:205], v[64:67]
	v_mfma_f32_16x16x32_bf16 v[116:119], v[166:169], v[182:185], v[116:119]
	v_mfma_f32_16x16x32_bf16 v[112:115], v[174:177], v[182:185], v[112:115]
	v_mfma_f32_16x16x32_bf16 v[100:103], v[166:169], v[190:193], v[100:103]
	v_mfma_f32_16x16x32_bf16 v[96:99], v[174:177], v[190:193], v[96:99]
	v_mfma_f32_16x16x32_bf16 v[84:87], v[166:169], v[198:201], v[84:87]
	v_mfma_f32_16x16x32_bf16 v[80:83], v[174:177], v[198:201], v[80:83]
	v_mfma_f32_16x16x32_bf16 v[68:71], v[166:169], v[206:209], v[68:71]
	v_mfma_f32_16x16x32_bf16 v[64:67], v[174:177], v[206:209], v[64:67]
	s_setprio 0
	s_barrier
; #define PG8_STAGE(bufoff, gbase, voff) do { _Pragma("unroll") for (int _i = 0; _i < 2; ++_i) { unsigned keep_; \
;         asm volatile("s_mov_b32 %0, m0\n\ts_mov_b32 m0, %3\n\ts_nop 0\n\tglobal_load_lds_dwordx4 %1, %2\n\ts_mov_b32 m0, %0" : "=&s"(keep_) : "v"((voff)[_i]), "s"((const char*)(gbase)), "s"(ldsbase + (unsigned)((bufoff) + _i * 8192)) : "memory"); } } while (0)
; #define PG8_WAIT_V(n) asm volatile("s_waitcnt vmcnt(" #n ")" ::: "memory")
; #define PG8_WAIT_L(n) asm volatile("s_waitcnt lgkmcnt(" #n ")" ::: "memory")
; #define PG8_BAR __builtin_amdgcn_s_barrier()
; #define PG8_SCHED __builtin_amdgcn_sched_barrier(0)
;     DI int nt(const Unit& u) const { return (u.aux & 8) ? PLED / 64 : ((u.aux & 4) ? (D_ / 2) / 64 : D_ / 64); }
; template <class Epi, class Sched, bool ALIGN_EPI, bool FP8 = false>
; DI void gemm_phase(LAS unsigned char* lds, const Gemm g, const Sched& S, const Epi& E) {
;     ...
;         for (int t = 0; t < nt; t += 2) {
;     ...
;             PG8_LDA(At, 1, 1); PG8_STAGE(PG8_SB(1, 0), b3, voffB); PG8_STAGE(PG8_SB(1, 1), b3 + hstepB, voffB); PG8_STAGE(PG8_SA(1, 0), a3, voffA);
;             PG8_WAIT_V(8); PG8_WAIT_L(0); PG8_BAR; PG8_MMA(1, 0, At, B0); PG8_MMA(1, 1, At, B1); PG8_BAR; PG8_SCHED;
	ds_read_b128 v[178:181], v142 offset:49152
	ds_read_b128 v[182:185], v142 offset:50176
	ds_read_b128 v[186:189], v142 offset:51200
	ds_read_b128 v[190:193], v142 offset:52224
	ds_read_b128 v[194:197], v142 offset:53248
	ds_read_b128 v[198:201], v142 offset:54272
	ds_read_b128 v[202:205], v142 offset:55296
	ds_read_b128 v[206:209], v142 offset:56320
	s_add_u32 s64, s70, 0x80
	s_addc_u32 s65, s71, 0
	s_mov_b32 s72, m0
	s_mov_b32 m0, s84
	s_nop 0
	global_load_lds_dwordx4 v135, s[64:65]
	s_mov_b32 m0, s72
	s_nop 0
	s_mov_b32 s72, m0
	s_mov_b32 m0, s85
	s_nop 0
	global_load_lds_dwordx4 v137, s[64:65]
	s_mov_b32 m0, s72
	s_add_u32 s64, s70, 0x80080
	s_addc_u32 s65, s71, 0
	s_mov_b32 s70, m0
	s_mov_b32 m0, s88
	s_nop 0
	global_load_lds_dwordx4 v135, s[64:65]
	s_mov_b32 m0, s70
	s_nop 0
	s_mov_b32 s70, m0
	s_mov_b32 m0, s89
	s_nop 0
	global_load_lds_dwordx4 v137, s[64:65]
	s_mov_b32 m0, s70
	s_mov_b32 s64, m0
	s_mov_b32 m0, s86
	s_nop 0
	global_load_lds_dwordx4 v134, s[68:69]
	s_mov_b32 m0, s64
	s_nop 0
	s_mov_b32 s64, m0
	s_mov_b32 m0, s87
	s_nop 0
	global_load_lds_dwordx4 v136, s[68:69]
	s_mov_b32 m0, s64
	s_waitcnt vmcnt(8)
	s_waitcnt lgkmcnt(0)
	s_mov_b64 exec, 1
	ds_add_u32 v255, v255 offset:4096
	s_mov_b64 exec, -1
	s_setprio 1
	v_mfma_f32_16x16x32_bf16 v[60:63], v[146:149], v[178:181], v[60:63]
	v_mfma_f32_16x16x32_bf16 v[56:59], v[154:157], v[178:181], v[56:59]
	v_mfma_f32_16x16x32_bf16 v[44:47], v[146:149], v[186:189], v[44:47]
	v_mfma_f32_16x16x32_bf16 v[40:43], v[154:157], v[186:189], v[40:43]
	v_mfma_f32_16x16x32_bf16 v[28:31], v[146:149], v[194:197], v[28:31]
	v_mfma_f32_16x16x32_bf16 v[24:27], v[154:157], v[194:197], v[24:27]
	v_mfma_f32_16x16x32_bf16 v[12:15], v[146:149], v[202:205], v[12:15]
	v_mfma_f32_16x16x32_bf16 v[8:11], v[154:157], v[202:205], v[8:11]
	v_mfma_f32_16x16x32_bf16 v[60:63], v[150:153], v[182:185], v[60:63]
	v_mfma_f32_16x16x32_bf16 v[56:59], v[158:161], v[182:185], v[56:59]
	v_mfma_f32_16x16x32_bf16 v[44:47], v[150:153], v[190:193], v[44:47]
	v_mfma_f32_16x16x32_bf16 v[40:43], v[158:161], v[190:193], v[40:43]
	v_mfma_f32_16x16x32_bf16 v[28:31], v[150:153], v[198:201], v[28:31]
	v_mfma_f32_16x16x32_bf16 v[24:27], v[158:161], v[198:201], v[24:27]
	v_mfma_f32_16x16x32_bf16 v[12:15], v[150:153], v[206:209], v[12:15]
	v_mfma_f32_16x16x32_bf16 v[8:11], v[158:161], v[206:209], v[8:11]
	v_mfma_f32_16x16x32_bf16 v[52:55], v[162:165], v[178:181], v[52:55]
	v_mfma_f32_16x16x32_bf16 v[48:51], v[170:173], v[178:181], v[48:51]
	v_mfma_f32_16x16x32_bf16 v[36:39], v[162:165], v[186:189], v[36:39]
	v_mfma_f32_16x16x32_bf16 v[32:35], v[170:173], v[186:189], v[32:35]
	v_mfma_f32_16x16x32_bf16 v[20:23], v[162:165], v[194:197], v[20:23]
	v_mfma_f32_16x16x32_bf16 v[16:19], v[170:173], v[194:197], v[16:19]
	v_mfma_f32_16x16x32_bf16 v[4:7], v[162:165], v[202:205], v[4:7]
	v_mfma_f32_16x16x32_bf16 v[0:3], v[170:173], v[202:205], v[0:3]
	v_mfma_f32_16x16x32_bf16 v[52:55], v[166:169], v[182:185], v[52:55]
	v_mfma_f32_16x16x32_bf16 v[48:51], v[174:177], v[182:185], v[48:51]
	v_mfma_f32_16x16x32_bf16 v[36:39], v[166:169], v[190:193], v[36:39]
	v_mfma_f32_16x16x32_bf16 v[32:35], v[174:177], v[190:193], v[32:35]
	v_mfma_f32_16x16x32_bf16 v[20:23], v[166:169], v[198:201], v[20:23]
	v_mfma_f32_16x16x32_bf16 v[16:19], v[174:177], v[198:201], v[16:19]
	v_mfma_f32_16x16x32_bf16 v[4:7], v[166:169], v[206:209], v[4:7]
	v_mfma_f32_16x16x32_bf16 v[0:3], v[174:177], v[206:209], v[0:3]
	s_setprio 0
	s_barrier
	s_add_i32 vcc_lo, vcc_lo, 2
	s_add_u32 s96, s96, 0x100
	s_addc_u32 s97, s97, 0
	s_cmp_gt_u32 vcc_lo, 29
	s_mov_b64 s[64:65], s[66:67]
	s_cbranch_scc0 .LBB0_724
	s_branch .Lmy_ex_724
; #define PG8_STAGE(bufoff, gbase, voff) do { _Pragma("unroll") for (int _i = 0; _i < 2; ++_i) { unsigned keep_; \
;         asm volatile("s_mov_b32 %0, m0\n\ts_mov_b32 m0, %3\n\ts_nop 0\n\tglobal_load_lds_dwordx4 %1, %2\n\ts_mov_b32 m0, %0" : "=&s"(keep_) : "v"((voff)[_i]), "s"((const char*)(gbase)), "s"(ldsbase + (unsigned)((bufoff) + _i * 8192)) : "memory"); } } while (0)
; #define PG8_WAIT_V(n) asm volatile("s_waitcnt vmcnt(" #n ")" ::: "memory")
; #define PG8_WAIT_L(n) asm volatile("s_waitcnt lgkmcnt(" #n ")" ::: "memory")
; #define PG8_BAR __builtin_amdgcn_s_barrier()
; #define PG8_SCHED __builtin_amdgcn_sched_barrier(0)
;     DI int nt(const Unit& u) const { return (u.aux & 8) ? PLED / 64 : ((u.aux & 4) ? (D_ / 2) / 64 : D_ / 64); }
; template <class Epi, class Sched, bool ALIGN_EPI, bool FP8 = false>
; DI void gemm_phase(LAS unsigned char* lds, const Gemm g, const Sched& S, const Epi& E) {
;     ...
;             const bool last = (t == nt - 2);
;             const char* a1 = cA + (size_t)(t + 1) * kstep;
;             const char* a2 = last ? nA : cA + (size_t)(t + 2) * kstep; const char* b2 = last ? nB : cB + (size_t)(t + 2) * kstep;
;             const char* a3 = a2 + kstep; const char* b3 = b2 + kstep;
;             PG8_LDB(B0, 0, 0); PG8_LDB(B1, 0, 1); PG8_SCHED; PG8_LDA(At, 0, 0); PG8_STAGE(PG8_SA(1, 1), a1 + hstepA, voffA);
;             PG8_WAIT_V(8); PG8_WAIT_L(0); PG8_BAR; PG8_MMA(0, 0, At, B0); PG8_MMA(0, 1, At, B1); PG8_BAR; PG8_SCHED;
.Lmy_g0_724:
	ds_read_b128 v[146:149], v140
	ds_read_b128 v[150:153], v140 offset:1024
	ds_read_b128 v[154:157], v140 offset:2048
	ds_read_b128 v[158:161], v140 offset:3072
	ds_read_b128 v[162:165], v141
	ds_read_b128 v[166:169], v141 offset:1024
	ds_read_b128 v[170:173], v141 offset:2048
	ds_read_b128 v[174:177], v141 offset:3072
	s_add_u32 s66, s64, 0x100
	s_addc_u32 s67, s65, 0
	s_cmp_eq_u32 vcc_lo, 28
	s_cselect_b32 s72, s94, s66
	s_cselect_b32 s73, s57, s67
	s_cselect_b32 s70, s95, s96
	s_cselect_b32 s71, s55, s97
	s_add_u32 s68, s72, 0x80
	s_addc_u32 s69, s73, 0
	ds_read_b128 v[178:181], v142
	ds_read_b128 v[182:185], v142 offset:1024
	ds_read_b128 v[186:189], v142 offset:2048
	ds_read_b128 v[190:193], v142 offset:3072
	ds_read_b128 v[194:197], v142 offset:4096
	ds_read_b128 v[198:201], v142 offset:5120
	ds_read_b128 v[202:205], v142 offset:6144
	ds_read_b128 v[206:209], v142 offset:7168
	s_add_u32 s64, s64, 0x80080
	s_addc_u32 s65, s65, 0
	s_mov_b32 vcc_hi, m0
	s_mov_b32 m0, s90
	s_nop 0
	global_load_lds_dwordx4 v134, s[64:65]
	s_mov_b32 m0, vcc_hi
	s_nop 0
	s_mov_b32 vcc_hi, m0
	s_mov_b32 m0, s91
	s_nop 0
	global_load_lds_dwordx4 v136, s[64:65]
	s_mov_b32 m0, vcc_hi
	s_waitcnt vmcnt(8)
	s_waitcnt lgkmcnt(0)
	s_barrier
	s_setprio 1
	v_mfma_f32_16x16x32_bf16 v[124:127], v[146:149], v[178:181], v[124:127]
	v_mfma_f32_16x16x32_bf16 v[120:123], v[154:157], v[178:181], v[120:123]
	v_mfma_f32_16x16x32_bf16 v[108:111], v[146:149], v[186:189], v[108:111]
	v_mfma_f32_16x16x32_bf16 v[104:107], v[154:157], v[186:189], v[104:107]
	v_mfma_f32_16x16x32_bf16 v[92:95], v[146:149], v[194:197], v[92:95]
	v_mfma_f32_16x16x32_bf16 v[88:91], v[154:157], v[194:197], v[88:91]
	v_mfma_f32_16x16x32_bf16 v[76:79], v[146:149], v[202:205], v[76:79]
	v_mfma_f32_16x16x32_bf16 v[72:75], v[154:157], v[202:205], v[72:75]
	v_mfma_f32_16x16x32_bf16 v[124:127], v[150:153], v[182:185], v[124:127]
	v_mfma_f32_16x16x32_bf16 v[120:123], v[158:161], v[182:185], v[120:123]
	v_mfma_f32_16x16x32_bf16 v[108:111], v[150:153], v[190:193], v[108:111]
	v_mfma_f32_16x16x32_bf16 v[104:107], v[158:161], v[190:193], v[104:107]
	v_mfma_f32_16x16x32_bf16 v[92:95], v[150:153], v[198:201], v[92:95]
	v_mfma_f32_16x16x32_bf16 v[88:91], v[158:161], v[198:201], v[88:91]
	v_mfma_f32_16x16x32_bf16 v[76:79], v[150:153], v[206:209], v[76:79]
	v_mfma_f32_16x16x32_bf16 v[72:75], v[158:161], v[206:209], v[72:75]
	v_mfma_f32_16x16x32_bf16 v[116:119], v[162:165], v[178:181], v[116:119]
	v_mfma_f32_16x16x32_bf16 v[112:115], v[170:173], v[178:181], v[112:115]
	v_mfma_f32_16x16x32_bf16 v[100:103], v[162:165], v[186:189], v[100:103]
	v_mfma_f32_16x16x32_bf16 v[96:99], v[170:173], v[186:189], v[96:99]
	v_mfma_f32_16x16x32_bf16 v[84:87], v[162:165], v[194:197], v[84:87]
	v_mfma_f32_16x16x32_bf16 v[80:83], v[170:173], v[194:197], v[80:83]
	v_mfma_f32_16x16x32_bf16 v[68:71], v[162:165], v[202:205], v[68:71]
	v_mfma_f32_16x16x32_bf16 v[64:67], v[170:173], v[202:205], v[64:67]
	v_mfma_f32_16x16x32_bf16 v[116:119], v[166:169], v[182:185], v[116:119]
	v_mfma_f32_16x16x32_bf16 v[112:115], v[174:177], v[182:185], v[112:115]
	v_mfma_f32_16x16x32_bf16 v[100:103], v[166:169], v[190:193], v[100:103]
	v_mfma_f32_16x16x32_bf16 v[96:99], v[174:177], v[190:193], v[96:99]
	ds_read_b32 v255, v255 offset:4096
	v_mfma_f32_16x16x32_bf16 v[84:87], v[166:169], v[198:201], v[84:87]
	v_mfma_f32_16x16x32_bf16 v[80:83], v[174:177], v[198:201], v[80:83]
	v_mfma_f32_16x16x32_bf16 v[68:71], v[166:169], v[206:209], v[68:71]
	v_mfma_f32_16x16x32_bf16 v[64:67], v[174:177], v[206:209], v[64:67]
	s_add_u32 s98, s98, 0x80000
	s_waitcnt lgkmcnt(0)
	v_readfirstlane_b32 s101, v255
	v_mov_b32_e32 v255, 0x20000
	s_cmp_ge_u32 s101, s98
	s_cbranch_scc1 .Lmy_g_20

; #define PG8_STAGE(bufoff, gbase, voff) do { _Pragma("unroll") for (int _i = 0; _i < 2; ++_i) { unsigned keep_; \
;         asm volatile("s_mov_b32 %0, m0\n\ts_mov_b32 m0, %3\n\ts_nop 0\n\tglobal_load_lds_dwordx4 %1, %2\n\ts_mov_b32 m0, %0" : "=&s"(keep_) : "v"((voff)[_i]), "s"((const char*)(gbase)), "s"(ldsbase + (unsigned)((bufoff) + _i * 8192)) : "memory"); } } while (0)
; #define PG8_WAIT_V(n) asm volatile("s_waitcnt vmcnt(" #n ")" ::: "memory")
; #define PG8_WAIT_L(n) asm volatile("s_waitcnt lgkmcnt(" #n ")" ::: "memory")
; #define PG8_BAR __builtin_amdgcn_s_barrier()
; #define PG8_SCHED __builtin_amdgcn_sched_barrier(0)
; template <class Epi, class Sched, bool ALIGN_EPI, bool FP8 = false>
; DI void gemm_phase(LAS unsigned char* lds, const Gemm g, const Sched& S, const Epi& E) {
;     ...
;             PG8_LDA(At, 0, 1); PG8_STAGE(PG8_SB(0, 0), b2, voffB); PG8_STAGE(PG8_SB(0, 1), b2 + hstepB, voffB); PG8_STAGE(PG8_SA(0, 0), a2, voffA);
;             PG8_WAIT_V(8); PG8_WAIT_L(0); PG8_BAR; PG8_MMA(1, 0, At, B0); PG8_MMA(1, 1, At, B1); PG8_BAR; PG8_SCHED;
.Lmy_g_20:
	s_setprio 0
	ds_read_b128 v[178:181], v142 offset:16384
	ds_read_b128 v[182:185], v142 offset:17408
	ds_read_b128 v[186:189], v142 offset:18432
	ds_read_b128 v[190:193], v142 offset:19456
	ds_read_b128 v[194:197], v142 offset:20480
	ds_read_b128 v[198:201], v142 offset:21504
	ds_read_b128 v[202:205], v142 offset:22528
	ds_read_b128 v[206:209], v142 offset:23552
	s_mov_b32 s64, m0
	s_mov_b32 m0, s63
	s_nop 0
	global_load_lds_dwordx4 v135, s[70:71]
	s_mov_b32 m0, s64
	s_nop 0
	s_mov_b32 s64, m0
	s_mov_b32 m0, s77
	s_nop 0
	global_load_lds_dwordx4 v137, s[70:71]
	s_mov_b32 m0, s64
	s_add_u32 s64, s70, 0x80000
	s_addc_u32 s65, s71, 0
	s_mov_b32 vcc_hi, m0
	s_mov_b32 m0, s79
	s_nop 0
	global_load_lds_dwordx4 v135, s[64:65]
	s_mov_b32 m0, vcc_hi
	s_nop 0
	s_mov_b32 vcc_hi, m0
	s_mov_b32 m0, s80
	s_nop 0
	global_load_lds_dwordx4 v137, s[64:65]
	s_mov_b32 m0, vcc_hi
	s_mov_b32 s64, m0
	s_mov_b32 m0, s75
	s_nop 0
	global_load_lds_dwordx4 v134, s[72:73]
	s_mov_b32 m0, s64
	s_nop 0
	s_mov_b32 s64, m0
	s_mov_b32 m0, s81
	s_nop 0
	global_load_lds_dwordx4 v136, s[72:73]
	s_mov_b32 m0, s64
	s_waitcnt vmcnt(8)
	s_waitcnt lgkmcnt(0)
	s_barrier
	s_setprio 1
	v_mfma_f32_16x16x32_bf16 v[60:63], v[146:149], v[178:181], v[60:63]
	v_mfma_f32_16x16x32_bf16 v[56:59], v[154:157], v[178:181], v[56:59]
	v_mfma_f32_16x16x32_bf16 v[44:47], v[146:149], v[186:189], v[44:47]
	v_mfma_f32_16x16x32_bf16 v[40:43], v[154:157], v[186:189], v[40:43]
	v_mfma_f32_16x16x32_bf16 v[28:31], v[146:149], v[194:197], v[28:31]
	v_mfma_f32_16x16x32_bf16 v[24:27], v[154:157], v[194:197], v[24:27]
	v_mfma_f32_16x16x32_bf16 v[12:15], v[146:149], v[202:205], v[12:15]
	v_mfma_f32_16x16x32_bf16 v[8:11], v[154:157], v[202:205], v[8:11]
	v_mfma_f32_16x16x32_bf16 v[60:63], v[150:153], v[182:185], v[60:63]
	v_mfma_f32_16x16x32_bf16 v[56:59], v[158:161], v[182:185], v[56:59]
	v_mfma_f32_16x16x32_bf16 v[44:47], v[150:153], v[190:193], v[44:47]
	v_mfma_f32_16x16x32_bf16 v[40:43], v[158:161], v[190:193], v[40:43]
	v_mfma_f32_16x16x32_bf16 v[28:31], v[150:153], v[198:201], v[28:31]
	v_mfma_f32_16x16x32_bf16 v[24:27], v[158:161], v[198:201], v[24:27]
	v_mfma_f32_16x16x32_bf16 v[12:15], v[150:153], v[206:209], v[12:15]
	v_mfma_f32_16x16x32_bf16 v[8:11], v[158:161], v[206:209], v[8:11]
	v_mfma_f32_16x16x32_bf16 v[52:55], v[162:165], v[178:181], v[52:55]
	v_mfma_f32_16x16x32_bf16 v[48:51], v[170:173], v[178:181], v[48:51]
	v_mfma_f32_16x16x32_bf16 v[36:39], v[162:165], v[186:189], v[36:39]
	v_mfma_f32_16x16x32_bf16 v[32:35], v[170:173], v[186:189], v[32:35]
	v_mfma_f32_16x16x32_bf16 v[20:23], v[162:165], v[194:197], v[20:23]
	v_mfma_f32_16x16x32_bf16 v[16:19], v[170:173], v[194:197], v[16:19]
	v_mfma_f32_16x16x32_bf16 v[4:7], v[162:165], v[202:205], v[4:7]
	v_mfma_f32_16x16x32_bf16 v[0:3], v[170:173], v[202:205], v[0:3]
	v_mfma_f32_16x16x32_bf16 v[52:55], v[166:169], v[182:185], v[52:55]
	v_mfma_f32_16x16x32_bf16 v[48:51], v[174:177], v[182:185], v[48:51]
	v_mfma_f32_16x16x32_bf16 v[36:39], v[166:169], v[190:193], v[36:39]
	v_mfma_f32_16x16x32_bf16 v[32:35], v[174:177], v[190:193], v[32:35]
	ds_read_b32 v255, v255 offset:4096
	v_mfma_f32_16x16x32_bf16 v[20:23], v[166:169], v[198:201], v[20:23]
	v_mfma_f32_16x16x32_bf16 v[16:19], v[174:177], v[198:201], v[16:19]
	v_mfma_f32_16x16x32_bf16 v[4:7], v[166:169], v[206:209], v[4:7]
	v_mfma_f32_16x16x32_bf16 v[0:3], v[174:177], v[206:209], v[0:3]
	s_add_u32 s98, s98, 0x80000
	s_waitcnt lgkmcnt(0)
	v_readfirstlane_b32 s101, v255
	v_mov_b32_e32 v255, 0x20000
	s_cmp_ge_u32 s101, s98
	s_cbranch_scc1 .Lmy_g_21

; #define PG8_STAGE(bufoff, gbase, voff) do { _Pragma("unroll") for (int _i = 0; _i < 2; ++_i) { unsigned keep_; \
;         asm volatile("s_mov_b32 %0, m0\n\ts_mov_b32 m0, %3\n\ts_nop 0\n\tglobal_load_lds_dwordx4 %1, %2\n\ts_mov_b32 m0, %0" : "=&s"(keep_) : "v"((voff)[_i]), "s"((const char*)(gbase)), "s"(ldsbase + (unsigned)((bufoff) + _i * 8192)) : "memory"); } } while (0)
; #define PG8_WAIT_V(n) asm volatile("s_waitcnt vmcnt(" #n ")" ::: "memory")
; #define PG8_WAIT_L(n) asm volatile("s_waitcnt lgkmcnt(" #n ")" ::: "memory")
; #define PG8_BAR __builtin_amdgcn_s_barrier()
; #define PG8_SCHED __builtin_amdgcn_sched_barrier(0)
; template <class Epi, class Sched, bool ALIGN_EPI, bool FP8 = false>
; DI void gemm_phase(LAS unsigned char* lds, const Gemm g, const Sched& S, const Epi& E) {
;     ...
;             PG8_LDB(B0, 1, 0); PG8_LDB(B1, 1, 1); PG8_SCHED; PG8_LDA(At, 1, 0); PG8_STAGE(PG8_SA(0, 1), a2 + hstepA, voffA);
;             PG8_WAIT_V(8); PG8_WAIT_L(0); PG8_BAR; PG8_MMA(0, 0, At, B0); PG8_MMA(0, 1, At, B1); PG8_BAR; PG8_SCHED;
.Lmy_g_21:
	s_setprio 0
	ds_read_b128 v[146:149], v143
	ds_read_b128 v[150:153], v143 offset:1024
	ds_read_b128 v[154:157], v143 offset:2048
	ds_read_b128 v[158:161], v143 offset:3072
	ds_read_b128 v[162:165], v144
	ds_read_b128 v[166:169], v144 offset:1024
	ds_read_b128 v[170:173], v144 offset:2048
	ds_read_b128 v[174:177], v144 offset:3072
	ds_read_b128 v[178:181], v142 offset:32768
	ds_read_b128 v[182:185], v142 offset:33792
	ds_read_b128 v[186:189], v142 offset:34816
	ds_read_b128 v[190:193], v142 offset:35840
	ds_read_b128 v[194:197], v142 offset:36864
	ds_read_b128 v[198:201], v142 offset:37888
	ds_read_b128 v[202:205], v142 offset:38912
	ds_read_b128 v[206:209], v142 offset:39936
	s_add_u32 s64, s72, 0x80000
	s_addc_u32 s65, s73, 0
	s_mov_b32 s72, m0
	s_mov_b32 m0, s82
	s_nop 0
	global_load_lds_dwordx4 v134, s[64:65]
	s_mov_b32 m0, s72
	s_nop 0
	s_mov_b32 s72, m0
	s_mov_b32 m0, s83
	s_nop 0
	global_load_lds_dwordx4 v136, s[64:65]
	s_mov_b32 m0, s72
	s_waitcnt vmcnt(8)
	s_waitcnt lgkmcnt(0)
	s_barrier
	s_setprio 1
	v_mfma_f32_16x16x32_bf16 v[124:127], v[146:149], v[178:181], v[124:127]
	v_mfma_f32_16x16x32_bf16 v[120:123], v[154:157], v[178:181], v[120:123]
	v_mfma_f32_16x16x32_bf16 v[108:111], v[146:149], v[186:189], v[108:111]
	v_mfma_f32_16x16x32_bf16 v[104:107], v[154:157], v[186:189], v[104:107]
	v_mfma_f32_16x16x32_bf16 v[92:95], v[146:149], v[194:197], v[92:95]
	v_mfma_f32_16x16x32_bf16 v[88:91], v[154:157], v[194:197], v[88:91]
	v_mfma_f32_16x16x32_bf16 v[76:79], v[146:149], v[202:205], v[76:79]
	v_mfma_f32_16x16x32_bf16 v[72:75], v[154:157], v[202:205], v[72:75]
	v_mfma_f32_16x16x32_bf16 v[124:127], v[150:153], v[182:185], v[124:127]
	v_mfma_f32_16x16x32_bf16 v[120:123], v[158:161], v[182:185], v[120:123]
	v_mfma_f32_16x16x32_bf16 v[108:111], v[150:153], v[190:193], v[108:111]
	v_mfma_f32_16x16x32_bf16 v[104:107], v[158:161], v[190:193], v[104:107]
	v_mfma_f32_16x16x32_bf16 v[92:95], v[150:153], v[198:201], v[92:95]
	v_mfma_f32_16x16x32_bf16 v[88:91], v[158:161], v[198:201], v[88:91]
	v_mfma_f32_16x16x32_bf16 v[76:79], v[150:153], v[206:209], v[76:79]
	v_mfma_f32_16x16x32_bf16 v[72:75], v[158:161], v[206:209], v[72:75]
	v_mfma_f32_16x16x32_bf16 v[116:119], v[162:165], v[178:181], v[116:119]
	v_mfma_f32_16x16x32_bf16 v[112:115], v[170:173], v[178:181], v[112:115]
	v_mfma_f32_16x16x32_bf16 v[100:103], v[162:165], v[186:189], v[100:103]
	v_mfma_f32_16x16x32_bf16 v[96:99], v[170:173], v[186:189], v[96:99]
	v_mfma_f32_16x16x32_bf16 v[84:87], v[162:165], v[194:197], v[84:87]
	v_mfma_f32_16x16x32_bf16 v[80:83], v[170:173], v[194:197], v[80:83]
	v_mfma_f32_16x16x32_bf16 v[68:71], v[162:165], v[202:205], v[68:71]
	v_mfma_f32_16x16x32_bf16 v[64:67], v[170:173], v[202:205], v[64:67]
	v_mfma_f32_16x16x32_bf16 v[116:119], v[166:169], v[182:185], v[116:119]
	v_mfma_f32_16x16x32_bf16 v[112:115], v[174:177], v[182:185], v[112:115]
	v_mfma_f32_16x16x32_bf16 v[100:103], v[166:169], v[190:193], v[100:103]
	v_mfma_f32_16x16x32_bf16 v[96:99], v[174:177], v[190:193], v[96:99]
	ds_read_b32 v255, v255 offset:4096
	v_mfma_f32_16x16x32_bf16 v[84:87], v[166:169], v[198:201], v[84:87]
	v_mfma_f32_16x16x32_bf16 v[80:83], v[174:177], v[198:201], v[80:83]
	v_mfma_f32_16x16x32_bf16 v[68:71], v[166:169], v[206:209], v[68:71]
	v_mfma_f32_16x16x32_bf16 v[64:67], v[174:177], v[206:209], v[64:67]
	s_add_u32 s98, s98, 0x80000
	s_waitcnt lgkmcnt(0)
	v_readfirstlane_b32 s101, v255
	v_mov_b32_e32 v255, 0x20000
	s_cmp_ge_u32 s101, s98
	s_cbranch_scc1 .Lmy_g_22

; #define PG8_STAGE(bufoff, gbase, voff) do { _Pragma("unroll") for (int _i = 0; _i < 2; ++_i) { unsigned keep_; \
;         asm volatile("s_mov_b32 %0, m0\n\ts_mov_b32 m0, %3\n\ts_nop 0\n\tglobal_load_lds_dwordx4 %1, %2\n\ts_mov_b32 m0, %0" : "=&s"(keep_) : "v"((voff)[_i]), "s"((const char*)(gbase)), "s"(ldsbase + (unsigned)((bufoff) + _i * 8192)) : "memory"); } } while (0)
; #define PG8_WAIT_V(n) asm volatile("s_waitcnt vmcnt(" #n ")" ::: "memory")
; #define PG8_WAIT_L(n) asm volatile("s_waitcnt lgkmcnt(" #n ")" ::: "memory")
; #define PG8_BAR __builtin_amdgcn_s_barrier()
; #define PG8_SCHED __builtin_amdgcn_sched_barrier(0)
; template <class Epi, class Sched, bool ALIGN_EPI, bool FP8 = false>
; DI void gemm_phase(LAS unsigned char* lds, const Gemm g, const Sched& S, const Epi& E) {
;     ...
;             PG8_LDA(At, 1, 1); PG8_STAGE(PG8_SB(1, 0), b3, voffB); PG8_STAGE(PG8_SB(1, 1), b3 + hstepB, voffB); PG8_STAGE(PG8_SA(1, 0), a3, voffA);
;             PG8_WAIT_V(8); PG8_WAIT_L(0); PG8_BAR; PG8_MMA(1, 0, At, B0); PG8_MMA(1, 1, At, B1); PG8_BAR; PG8_SCHED;
.Lmy_g_22:
	s_setprio 0
	ds_read_b128 v[178:181], v142 offset:49152
	ds_read_b128 v[182:185], v142 offset:50176
	ds_read_b128 v[186:189], v142 offset:51200
	ds_read_b128 v[190:193], v142 offset:52224
	ds_read_b128 v[194:197], v142 offset:53248
	ds_read_b128 v[198:201], v142 offset:54272
	ds_read_b128 v[202:205], v142 offset:55296
	ds_read_b128 v[206:209], v142 offset:56320
	s_add_u32 s64, s70, 0x80
	s_addc_u32 s65, s71, 0
	s_mov_b32 s72, m0
	s_mov_b32 m0, s84
	s_nop 0
	global_load_lds_dwordx4 v135, s[64:65]
	s_mov_b32 m0, s72
	s_nop 0
	s_mov_b32 s72, m0
	s_mov_b32 m0, s85
	s_nop 0
	global_load_lds_dwordx4 v137, s[64:65]
	s_mov_b32 m0, s72
	s_add_u32 s64, s70, 0x80080
	s_addc_u32 s65, s71, 0
	s_mov_b32 s70, m0
	s_mov_b32 m0, s88
	s_nop 0
	global_load_lds_dwordx4 v135, s[64:65]
	s_mov_b32 m0, s70
	s_nop 0
	s_mov_b32 s70, m0
	s_mov_b32 m0, s89
	s_nop 0
	global_load_lds_dwordx4 v137, s[64:65]
	s_mov_b32 m0, s70
	s_mov_b32 s64, m0
	s_mov_b32 m0, s86
	s_nop 0
	global_load_lds_dwordx4 v134, s[68:69]
	s_mov_b32 m0, s64
	s_nop 0
	s_mov_b32 s64, m0
	s_mov_b32 m0, s87
	s_nop 0
	global_load_lds_dwordx4 v136, s[68:69]
	s_mov_b32 m0, s64
	s_waitcnt vmcnt(8)
	s_waitcnt lgkmcnt(0)
	s_barrier
	s_setprio 1
	v_mfma_f32_16x16x32_bf16 v[60:63], v[146:149], v[178:181], v[60:63]
	v_mfma_f32_16x16x32_bf16 v[56:59], v[154:157], v[178:181], v[56:59]
	v_mfma_f32_16x16x32_bf16 v[44:47], v[146:149], v[186:189], v[44:47]
	v_mfma_f32_16x16x32_bf16 v[40:43], v[154:157], v[186:189], v[40:43]
	v_mfma_f32_16x16x32_bf16 v[28:31], v[146:149], v[194:197], v[28:31]
	v_mfma_f32_16x16x32_bf16 v[24:27], v[154:157], v[194:197], v[24:27]
	v_mfma_f32_16x16x32_bf16 v[12:15], v[146:149], v[202:205], v[12:15]
	v_mfma_f32_16x16x32_bf16 v[8:11], v[154:157], v[202:205], v[8:11]
	v_mfma_f32_16x16x32_bf16 v[60:63], v[150:153], v[182:185], v[60:63]
	v_mfma_f32_16x16x32_bf16 v[56:59], v[158:161], v[182:185], v[56:59]
	v_mfma_f32_16x16x32_bf16 v[44:47], v[150:153], v[190:193], v[44:47]
	v_mfma_f32_16x16x32_bf16 v[40:43], v[158:161], v[190:193], v[40:43]
	v_mfma_f32_16x16x32_bf16 v[28:31], v[150:153], v[198:201], v[28:31]
	v_mfma_f32_16x16x32_bf16 v[24:27], v[158:161], v[198:201], v[24:27]
	v_mfma_f32_16x16x32_bf16 v[12:15], v[150:153], v[206:209], v[12:15]
	v_mfma_f32_16x16x32_bf16 v[8:11], v[158:161], v[206:209], v[8:11]
	v_mfma_f32_16x16x32_bf16 v[52:55], v[162:165], v[178:181], v[52:55]
	v_mfma_f32_16x16x32_bf16 v[48:51], v[170:173], v[178:181], v[48:51]
	v_mfma_f32_16x16x32_bf16 v[36:39], v[162:165], v[186:189], v[36:39]
	v_mfma_f32_16x16x32_bf16 v[32:35], v[170:173], v[186:189], v[32:35]
	v_mfma_f32_16x16x32_bf16 v[20:23], v[162:165], v[194:197], v[20:23]
	v_mfma_f32_16x16x32_bf16 v[16:19], v[170:173], v[194:197], v[16:19]
	v_mfma_f32_16x16x32_bf16 v[4:7], v[162:165], v[202:205], v[4:7]
	v_mfma_f32_16x16x32_bf16 v[0:3], v[170:173], v[202:205], v[0:3]
	v_mfma_f32_16x16x32_bf16 v[52:55], v[166:169], v[182:185], v[52:55]
	v_mfma_f32_16x16x32_bf16 v[48:51], v[174:177], v[182:185], v[48:51]
	v_mfma_f32_16x16x32_bf16 v[36:39], v[166:169], v[190:193], v[36:39]
	v_mfma_f32_16x16x32_bf16 v[32:35], v[174:177], v[190:193], v[32:35]
	ds_read_b32 v255, v255 offset:4096
	v_mfma_f32_16x16x32_bf16 v[20:23], v[166:169], v[198:201], v[20:23]
	v_mfma_f32_16x16x32_bf16 v[16:19], v[174:177], v[198:201], v[16:19]
	v_mfma_f32_16x16x32_bf16 v[4:7], v[166:169], v[206:209], v[4:7]
	v_mfma_f32_16x16x32_bf16 v[0:3], v[174:177], v[206:209], v[0:3]
	s_add_u32 s98, s98, 0x80000
	s_waitcnt lgkmcnt(0)
	v_readfirstlane_b32 s101, v255
	v_mov_b32_e32 v255, 0x20000
	s_cmp_ge_u32 s101, s98
	s_cbranch_scc1 .Lmy_g_23

;     DI int nt(const Unit& u) const { return (u.aux & 8) ? PLED / 64 : ((u.aux & 4) ? (D_ / 2) / 64 : D_ / 64); }
; template <class Epi, class Sched, bool ALIGN_EPI, bool FP8 = false>
; DI void gemm_phase(LAS unsigned char* lds, const Gemm g, const Sched& S, const Epi& E) {
;     ...
;         for (int t = 0; t < nt; t += 2) {
.Lmy_g_23:
	s_setprio 0
	s_add_i32 vcc_lo, vcc_lo, 2
	s_add_u32 s96, s96, 0x100
	s_addc_u32 s97, s97, 0
	s_cmp_gt_u32 vcc_lo, 29
	s_mov_b64 s[64:65], s[66:67]
	s_cbranch_scc0 .Lmy_g0_724

; #define PG8_STAGE(bufoff, gbase, voff) do { _Pragma("unroll") for (int _i = 0; _i < 2; ++_i) { unsigned keep_; \
;         asm volatile("s_mov_b32 %0, m0\n\ts_mov_b32 m0, %3\n\ts_nop 0\n\tglobal_load_lds_dwordx4 %1, %2\n\ts_mov_b32 m0, %0" : "=&s"(keep_) : "v"((voff)[_i]), "s"((const char*)(gbase)), "s"(ldsbase + (unsigned)((bufoff) + _i * 8192)) : "memory"); } } while (0)
; #define PG8_WAIT_V(n) asm volatile("s_waitcnt vmcnt(" #n ")" ::: "memory")
; #define PG8_WAIT_L(n) asm volatile("s_waitcnt lgkmcnt(" #n ")" ::: "memory")
; #define PG8_BAR __builtin_amdgcn_s_barrier()
; #define PG8_SCHED __builtin_amdgcn_sched_barrier(0)
;     DI int nt(const Unit& u) const { return (u.aux & 8) ? PLED / 64 : ((u.aux & 4) ? (D_ / 2) / 64 : D_ / 64); }
; template <class Epi, class Sched, bool ALIGN_EPI, bool FP8 = false>
; DI void gemm_phase(LAS unsigned char* lds, const Gemm g, const Sched& S, const Epi& E) {
;     ...
;             const bool last = (t == nt - 2);
;             const char* a1 = cA + (size_t)(t + 1) * kstep;
;             const char* a2 = last ? nA : cA + (size_t)(t + 2) * kstep; const char* b2 = last ? nB : cB + (size_t)(t + 2) * kstep;
;             const char* a3 = a2 + kstep; const char* b3 = b2 + kstep;
;             PG8_LDB(B0, 0, 0); PG8_LDB(B1, 0, 1); PG8_SCHED; PG8_LDA(At, 0, 0); PG8_STAGE(PG8_SA(1, 1), a1 + hstepA, voffA);
;             PG8_WAIT_V(8); PG8_WAIT_L(0); PG8_BAR; PG8_MMA(0, 0, At, B0); PG8_MMA(0, 1, At, B1); PG8_BAR; PG8_SCHED;
;             PG8_LDA(At, 0, 1); PG8_STAGE(PG8_SB(0, 0), b2, voffB); PG8_STAGE(PG8_SB(0, 1), b2 + hstepB, voffB); PG8_STAGE(PG8_SA(0, 0), a2, voffA);
;             PG8_WAIT_V(8); PG8_WAIT_L(0); PG8_BAR; PG8_MMA(1, 0, At, B0); PG8_MMA(1, 1, At, B1); PG8_BAR; PG8_SCHED;
.LBB0_809:
	s_cmp_lg_u32 s99, 0
	s_cbranch_scc1 .Lmy_g0_809
	ds_read_b128 v[144:147], v135
	ds_read_b128 v[148:151], v135 offset:16
	ds_read_b128 v[152:155], v135 offset:2048
	ds_read_b128 v[156:159], v135 offset:2064
	ds_read_b128 v[160:163], v135 offset:16384
	ds_read_b128 v[164:167], v135 offset:16400
	ds_read_b128 v[168:171], v135 offset:18432
	ds_read_b128 v[172:175], v135 offset:18448
	s_add_u32 s50, s48, 0x100
	s_addc_u32 s51, s49, 0
	s_cmp_eq_u32 s83, 40
	s_cselect_b32 s56, s6, s50
	s_cselect_b32 s57, s7, s51
	s_cselect_b32 s54, s46, s81
	s_cselect_b32 s55, s47, s82
	s_add_u32 s52, s56, 0x80
	s_addc_u32 s53, s57, 0
	ds_read_b128 v[176:179], v134
	ds_read_b128 v[180:183], v134 offset:16
	ds_read_b128 v[184:187], v134 offset:2048
	ds_read_b128 v[188:191], v134 offset:2064
	ds_read_b128 v[192:195], v134 offset:4096
	ds_read_b128 v[196:199], v134 offset:4112
	ds_read_b128 v[200:203], v134 offset:6144
	ds_read_b128 v[204:207], v134 offset:6160
	s_add_u32 s48, s48, 0xb0080
	s_addc_u32 s49, s49, 0
	s_mov_b32 s84, m0
	s_mov_b32 m0, s72
	s_nop 0
	global_load_lds_dwordx4 v136, s[48:49]
	s_mov_b32 m0, s84
	s_nop 0
	s_mov_b32 s84, m0
	s_mov_b32 m0, s73
	s_nop 0
	global_load_lds_dwordx4 v138, s[48:49]
	s_mov_b32 m0, s84
	s_waitcnt vmcnt(8)
	s_waitcnt lgkmcnt(0)
	s_mov_b64 exec, 1
	ds_add_u32 v255, v255 offset:4096
	s_mov_b64 exec, -1
	s_setprio 1
	v_mfma_scale_f32_16x16x128_f8f6f4 v[124:127], v[144:151], v[176:183], v[124:127], v142, v142 op_sel_hi:[0,0,0]
	v_mfma_scale_f32_16x16x128_f8f6f4 v[120:123], v[152:159], v[176:183], v[120:123], v142, v142 op_sel_hi:[0,0,0]
	v_mfma_scale_f32_16x16x128_f8f6f4 v[108:111], v[144:151], v[184:191], v[108:111], v142, v142 op_sel_hi:[0,0,0]
	v_mfma_scale_f32_16x16x128_f8f6f4 v[104:107], v[152:159], v[184:191], v[104:107], v142, v142 op_sel_hi:[0,0,0]
	v_mfma_scale_f32_16x16x128_f8f6f4 v[208:211], v[144:151], v[192:199], v[92:95], v142, v142 op_sel_hi:[0,0,0]
	v_mfma_scale_f32_16x16x128_f8f6f4 v[212:215], v[152:159], v[192:199], v[88:91], v142, v142 op_sel_hi:[0,0,0]
	v_mfma_scale_f32_16x16x128_f8f6f4 v[216:219], v[144:151], v[200:207], v[76:79], v142, v142 op_sel_hi:[0,0,0]
	v_mfma_scale_f32_16x16x128_f8f6f4 v[220:223], v[152:159], v[200:207], v[72:75], v142, v142 op_sel_hi:[0,0,0]
	v_mfma_scale_f32_16x16x128_f8f6f4 v[116:119], v[160:167], v[176:183], v[116:119], v142, v142 op_sel_hi:[0,0,0]
	v_mfma_scale_f32_16x16x128_f8f6f4 v[112:115], v[168:175], v[176:183], v[112:115], v142, v142 op_sel_hi:[0,0,0]
	v_mfma_scale_f32_16x16x128_f8f6f4 v[100:103], v[160:167], v[184:191], v[100:103], v142, v142 op_sel_hi:[0,0,0]
	v_mfma_scale_f32_16x16x128_f8f6f4 v[96:99], v[168:175], v[184:191], v[96:99], v142, v142 op_sel_hi:[0,0,0]
	v_mfma_scale_f32_16x16x128_f8f6f4 v[176:179], v[160:167], v[192:199], v[84:87], v142, v142 op_sel_hi:[0,0,0]
	v_mfma_scale_f32_16x16x128_f8f6f4 v[180:183], v[168:175], v[192:199], v[80:83], v142, v142 op_sel_hi:[0,0,0]
	v_mfma_scale_f32_16x16x128_f8f6f4 v[184:187], v[160:167], v[200:207], v[68:71], v142, v142 op_sel_hi:[0,0,0]
	v_mfma_scale_f32_16x16x128_f8f6f4 v[188:191], v[168:175], v[200:207], v[64:67], v142, v142 op_sel_hi:[0,0,0]
	s_setprio 0
	s_barrier
	s_nop 4
	ds_read_b128 v[64:67], v134 offset:16384
	ds_read_b128 v[68:71], v134 offset:16400
	ds_read_b128 v[72:75], v134 offset:18432
	ds_read_b128 v[76:79], v134 offset:18448
	ds_read_b128 v[80:83], v134 offset:20480
	ds_read_b128 v[84:87], v134 offset:20496
	ds_read_b128 v[88:91], v134 offset:22528
	ds_read_b128 v[92:95], v134 offset:22544
	s_mov_b32 s48, m0
	s_mov_b32 m0, s59
	s_nop 0
	global_load_lds_dwordx4 v137, s[54:55]
	s_mov_b32 m0, s48
	s_nop 0
	s_mov_b32 s48, m0
	s_mov_b32 m0, s60
	s_nop 0
	global_load_lds_dwordx4 v139, s[54:55]
	s_mov_b32 m0, s48
	s_add_u32 s48, s54, 0xb0000
	s_addc_u32 s49, s55, 0
	s_mov_b32 s84, m0
	s_mov_b32 m0, s61
	s_nop 0
	global_load_lds_dwordx4 v137, s[48:49]
	s_mov_b32 m0, s84
	s_nop 0
	s_mov_b32 s84, m0
	s_mov_b32 m0, s62
	s_nop 0
	global_load_lds_dwordx4 v139, s[48:49]
	s_mov_b32 m0, s84
	s_mov_b32 s48, m0
	s_mov_b32 m0, s58
	s_nop 0
	global_load_lds_dwordx4 v136, s[56:57]
	s_mov_b32 m0, s48
	s_nop 0
	s_mov_b32 s48, m0
	s_mov_b32 m0, s63
	s_nop 0
	global_load_lds_dwordx4 v138, s[56:57]
	s_mov_b32 m0, s48
	s_waitcnt vmcnt(8)
	s_waitcnt lgkmcnt(0)
	s_mov_b64 exec, 1
	ds_add_u32 v255, v255 offset:4096
	s_mov_b64 exec, -1
	s_setprio 1
	v_mfma_scale_f32_16x16x128_f8f6f4 v[60:63], v[144:151], v[64:71], v[60:63], v142, v142 op_sel_hi:[0,0,0]
	v_mfma_scale_f32_16x16x128_f8f6f4 v[56:59], v[152:159], v[64:71], v[56:59], v142, v142 op_sel_hi:[0,0,0]
	v_mfma_scale_f32_16x16x128_f8f6f4 v[192:195], v[144:151], v[72:79], v[44:47], v142, v142 op_sel_hi:[0,0,0]
	v_mfma_scale_f32_16x16x128_f8f6f4 v[196:199], v[152:159], v[72:79], v[40:43], v142, v142 op_sel_hi:[0,0,0]
	v_mfma_scale_f32_16x16x128_f8f6f4 v[200:203], v[144:151], v[80:87], v[28:31], v142, v142 op_sel_hi:[0,0,0]
	v_mfma_scale_f32_16x16x128_f8f6f4 v[204:207], v[152:159], v[80:87], v[24:27], v142, v142 op_sel_hi:[0,0,0]
	v_mfma_scale_f32_16x16x128_f8f6f4 v[224:227], v[144:151], v[88:95], v[12:15], v142, v142 op_sel_hi:[0,0,0]
	v_mfma_scale_f32_16x16x128_f8f6f4 v[228:231], v[152:159], v[88:95], v[8:11], v142, v142 op_sel_hi:[0,0,0]
	v_mfma_scale_f32_16x16x128_f8f6f4 v[52:55], v[160:167], v[64:71], v[52:55], v142, v142 op_sel_hi:[0,0,0]
	v_mfma_scale_f32_16x16x128_f8f6f4 v[48:51], v[168:175], v[64:71], v[48:51], v142, v142 op_sel_hi:[0,0,0]
	v_mfma_scale_f32_16x16x128_f8f6f4 v[232:235], v[160:167], v[72:79], v[36:39], v142, v142 op_sel_hi:[0,0,0]
	v_mfma_scale_f32_16x16x128_f8f6f4 v[236:239], v[168:175], v[72:79], v[32:35], v142, v142 op_sel_hi:[0,0,0]
	v_mfma_scale_f32_16x16x128_f8f6f4 v[240:243], v[160:167], v[80:87], v[20:23], v142, v142 op_sel_hi:[0,0,0]
	v_mfma_scale_f32_16x16x128_f8f6f4 v[244:247], v[168:175], v[80:87], v[16:19], v142, v142 op_sel_hi:[0,0,0]
	v_mfma_scale_f32_16x16x128_f8f6f4 v[248:251], v[160:167], v[88:95], v[4:7], v142, v142 op_sel_hi:[0,0,0]
	v_mfma_scale_f32_16x16x128_f8f6f4 v[128:131], v[168:175], v[88:95], v[0:3], v142, v142 op_sel_hi:[0,0,0]
	s_setprio 0
	s_barrier
; #define PG8_STAGE(bufoff, gbase, voff) do { _Pragma("unroll") for (int _i = 0; _i < 2; ++_i) { unsigned keep_; \
;         asm volatile("s_mov_b32 %0, m0\n\ts_mov_b32 m0, %3\n\ts_nop 0\n\tglobal_load_lds_dwordx4 %1, %2\n\ts_mov_b32 m0, %0" : "=&s"(keep_) : "v"((voff)[_i]), "s"((const char*)(gbase)), "s"(ldsbase + (unsigned)((bufoff) + _i * 8192)) : "memory"); } } while (0)
; #define PG8_WAIT_V(n) asm volatile("s_waitcnt vmcnt(" #n ")" ::: "memory")
; #define PG8_WAIT_L(n) asm volatile("s_waitcnt lgkmcnt(" #n ")" ::: "memory")
; #define PG8_BAR __builtin_amdgcn_s_barrier()
; #define PG8_SCHED __builtin_amdgcn_sched_barrier(0)
; template <class Epi, class Sched, bool ALIGN_EPI, bool FP8 = false>
; DI void gemm_phase(LAS unsigned char* lds, const Gemm g, const Sched& S, const Epi& E) {
;     ...
;             PG8_LDB(B0, 1, 0); PG8_LDB(B1, 1, 1); PG8_SCHED; PG8_LDA(At, 1, 0); PG8_STAGE(PG8_SA(0, 1), a2 + hstepA, voffA);
;             PG8_WAIT_V(8); PG8_WAIT_L(0); PG8_BAR; PG8_MMA(0, 0, At, B0); PG8_MMA(0, 1, At, B1); PG8_BAR; PG8_SCHED;
;             PG8_LDA(At, 1, 1); PG8_STAGE(PG8_SB(1, 0), b3, voffB); PG8_STAGE(PG8_SB(1, 1), b3 + hstepB, voffB); PG8_STAGE(PG8_SA(1, 0), a3, voffA);
;             PG8_WAIT_V(8); PG8_WAIT_L(0); PG8_BAR; PG8_MMA(1, 0, At, B0); PG8_MMA(1, 1, At, B1); PG8_BAR; PG8_SCHED;
;         }
	s_nop 4
	ds_read_b128 v[0:3], v135 offset:32768
	ds_read_b128 v[4:7], v135 offset:32784
	ds_read_b128 v[16:19], v135 offset:34816
	ds_read_b128 v[20:23], v135 offset:34832
	ds_read_b128 v[144:147], v135 offset:49152
	ds_read_b128 v[148:151], v135 offset:49168
	ds_read_b128 v[152:155], v135 offset:51200
	ds_read_b128 v[156:159], v135 offset:51216
	ds_read_b128 v[8:11], v134 offset:32768
	ds_read_b128 v[12:15], v134 offset:32784
	ds_read_b128 v[24:27], v134 offset:34816
	ds_read_b128 v[28:31], v134 offset:34832
	ds_read_b128 v[32:35], v134 offset:36864
	ds_read_b128 v[36:39], v134 offset:36880
	ds_read_b128 v[40:43], v134 offset:38912
	ds_read_b128 v[44:47], v134 offset:38928
	s_add_u32 s48, s56, 0xb0000
	s_addc_u32 s49, s57, 0
	s_mov_b32 s56, m0
	s_mov_b32 m0, s64
	s_nop 0
	global_load_lds_dwordx4 v136, s[48:49]
	s_mov_b32 m0, s56
	s_nop 0
	s_mov_b32 s56, m0
	s_mov_b32 m0, s65
	s_nop 0
	global_load_lds_dwordx4 v138, s[48:49]
	s_mov_b32 m0, s56
	s_waitcnt vmcnt(8)
	s_waitcnt lgkmcnt(0)
	s_mov_b64 exec, 1
	ds_add_u32 v255, v255 offset:4096
	s_mov_b64 exec, -1
	s_setprio 1
	v_mfma_scale_f32_16x16x128_f8f6f4 v[124:127], v[0:7], v[8:15], v[124:127], v142, v142 op_sel_hi:[0,0,0]
	v_mfma_scale_f32_16x16x128_f8f6f4 v[120:123], v[16:23], v[8:15], v[120:123], v142, v142 op_sel_hi:[0,0,0]
	v_mfma_scale_f32_16x16x128_f8f6f4 v[108:111], v[0:7], v[24:31], v[108:111], v142, v142 op_sel_hi:[0,0,0]
	v_mfma_scale_f32_16x16x128_f8f6f4 v[104:107], v[16:23], v[24:31], v[104:107], v142, v142 op_sel_hi:[0,0,0]
	v_mfma_scale_f32_16x16x128_f8f6f4 v[92:95], v[0:7], v[32:39], v[208:211], v142, v142 op_sel_hi:[0,0,0]
	v_mfma_scale_f32_16x16x128_f8f6f4 v[88:91], v[16:23], v[32:39], v[212:215], v142, v142 op_sel_hi:[0,0,0]
	v_mfma_scale_f32_16x16x128_f8f6f4 v[76:79], v[0:7], v[40:47], v[216:219], v142, v142 op_sel_hi:[0,0,0]
	v_mfma_scale_f32_16x16x128_f8f6f4 v[72:75], v[16:23], v[40:47], v[220:223], v142, v142 op_sel_hi:[0,0,0]
	v_mfma_scale_f32_16x16x128_f8f6f4 v[116:119], v[144:151], v[8:15], v[116:119], v142, v142 op_sel_hi:[0,0,0]
	v_mfma_scale_f32_16x16x128_f8f6f4 v[112:115], v[152:159], v[8:15], v[112:115], v142, v142 op_sel_hi:[0,0,0]
	v_mfma_scale_f32_16x16x128_f8f6f4 v[100:103], v[144:151], v[24:31], v[100:103], v142, v142 op_sel_hi:[0,0,0]
	v_mfma_scale_f32_16x16x128_f8f6f4 v[96:99], v[152:159], v[24:31], v[96:99], v142, v142 op_sel_hi:[0,0,0]
	v_mfma_scale_f32_16x16x128_f8f6f4 v[84:87], v[144:151], v[32:39], v[176:179], v142, v142 op_sel_hi:[0,0,0]
	v_mfma_scale_f32_16x16x128_f8f6f4 v[80:83], v[152:159], v[32:39], v[180:183], v142, v142 op_sel_hi:[0,0,0]
	v_mfma_scale_f32_16x16x128_f8f6f4 v[68:71], v[144:151], v[40:47], v[184:187], v142, v142 op_sel_hi:[0,0,0]
	v_mfma_scale_f32_16x16x128_f8f6f4 v[64:67], v[152:159], v[40:47], v[188:191], v142, v142 op_sel_hi:[0,0,0]
	s_setprio 0
	s_barrier
	ds_read_b128 v[32:35], v134 offset:49152
	ds_read_b128 v[36:39], v134 offset:49168
	ds_read_b128 v[160:163], v134 offset:51200
	ds_read_b128 v[164:167], v134 offset:51216
	ds_read_b128 v[168:171], v134 offset:53248
	ds_read_b128 v[172:175], v134 offset:53264
	ds_read_b128 v[176:179], v134 offset:55296
	ds_read_b128 v[180:183], v134 offset:55312
	s_add_u32 s48, s54, 0x80
	s_addc_u32 s49, s55, 0
	s_mov_b32 s56, m0
	s_mov_b32 m0, s66
	s_nop 0
	global_load_lds_dwordx4 v137, s[48:49]
	s_mov_b32 m0, s56
	s_nop 0
	s_mov_b32 s56, m0
	s_mov_b32 m0, s67
	s_nop 0
	global_load_lds_dwordx4 v139, s[48:49]
	s_mov_b32 m0, s56
	s_add_u32 s48, s54, 0xb0080
	s_addc_u32 s49, s55, 0
	s_mov_b32 s54, m0
	s_mov_b32 m0, s70
	s_nop 0
	global_load_lds_dwordx4 v137, s[48:49]
	s_mov_b32 m0, s54
	s_nop 0
	s_mov_b32 s54, m0
	s_mov_b32 m0, s71
	s_nop 0
	global_load_lds_dwordx4 v139, s[48:49]
	s_mov_b32 m0, s54
	s_mov_b32 s48, m0
	s_mov_b32 m0, s68
	s_nop 0
	global_load_lds_dwordx4 v136, s[52:53]
	s_mov_b32 m0, s48
	s_nop 0
	s_mov_b32 s48, m0
	s_mov_b32 m0, s69
	s_nop 0
	global_load_lds_dwordx4 v138, s[52:53]
	s_mov_b32 m0, s48
	s_waitcnt vmcnt(8)
	s_waitcnt lgkmcnt(0)
	s_mov_b64 exec, 1
	ds_add_u32 v255, v255 offset:4096
	s_mov_b64 exec, -1
	s_setprio 1
	v_mfma_scale_f32_16x16x128_f8f6f4 v[60:63], v[0:7], v[32:39], v[60:63], v142, v142 op_sel_hi:[0,0,0]
	v_mfma_scale_f32_16x16x128_f8f6f4 v[56:59], v[16:23], v[32:39], v[56:59], v142, v142 op_sel_hi:[0,0,0]
	v_mfma_scale_f32_16x16x128_f8f6f4 v[44:47], v[0:7], v[160:167], v[192:195], v142, v142 op_sel_hi:[0,0,0]
	v_mfma_scale_f32_16x16x128_f8f6f4 v[40:43], v[16:23], v[160:167], v[196:199], v142, v142 op_sel_hi:[0,0,0]
	v_mfma_scale_f32_16x16x128_f8f6f4 v[28:31], v[0:7], v[168:175], v[200:203], v142, v142 op_sel_hi:[0,0,0]
	v_mfma_scale_f32_16x16x128_f8f6f4 v[24:27], v[16:23], v[168:175], v[204:207], v142, v142 op_sel_hi:[0,0,0]
	v_mfma_scale_f32_16x16x128_f8f6f4 v[12:15], v[0:7], v[176:183], v[224:227], v142, v142 op_sel_hi:[0,0,0]
	v_mfma_scale_f32_16x16x128_f8f6f4 v[8:11], v[16:23], v[176:183], v[228:231], v142, v142 op_sel_hi:[0,0,0]
	v_mfma_scale_f32_16x16x128_f8f6f4 v[52:55], v[144:151], v[32:39], v[52:55], v142, v142 op_sel_hi:[0,0,0]
	v_mfma_scale_f32_16x16x128_f8f6f4 v[48:51], v[152:159], v[32:39], v[48:51], v142, v142 op_sel_hi:[0,0,0]
	v_mfma_scale_f32_16x16x128_f8f6f4 v[36:39], v[144:151], v[160:167], v[232:235], v142, v142 op_sel_hi:[0,0,0]
	v_mfma_scale_f32_16x16x128_f8f6f4 v[32:35], v[152:159], v[160:167], v[236:239], v142, v142 op_sel_hi:[0,0,0]
	v_mfma_scale_f32_16x16x128_f8f6f4 v[20:23], v[144:151], v[168:175], v[240:243], v142, v142 op_sel_hi:[0,0,0]
	v_mfma_scale_f32_16x16x128_f8f6f4 v[16:19], v[152:159], v[168:175], v[244:247], v142, v142 op_sel_hi:[0,0,0]
	v_mfma_scale_f32_16x16x128_f8f6f4 v[4:7], v[144:151], v[176:183], v[248:251], v142, v142 op_sel_hi:[0,0,0]
	v_mfma_scale_f32_16x16x128_f8f6f4 v[0:3], v[152:159], v[176:183], v[128:131], v142, v142 op_sel_hi:[0,0,0]
	s_setprio 0
	s_barrier
	s_add_i32 s83, s83, 2
	s_add_u32 s81, s81, 0x100
	s_addc_u32 s82, s82, 0
	s_cmp_gt_u32 s83, 41
	s_mov_b64 s[48:49], s[50:51]
	s_cbranch_scc0 .LBB0_809
	s_branch .Lmy_ex_809
; #define PG8_STAGE(bufoff, gbase, voff) do { _Pragma("unroll") for (int _i = 0; _i < 2; ++_i) { unsigned keep_; \
;         asm volatile("s_mov_b32 %0, m0\n\ts_mov_b32 m0, %3\n\ts_nop 0\n\tglobal_load_lds_dwordx4 %1, %2\n\ts_mov_b32 m0, %0" : "=&s"(keep_) : "v"((voff)[_i]), "s"((const char*)(gbase)), "s"(ldsbase + (unsigned)((bufoff) + _i * 8192)) : "memory"); } } while (0)
; #define PG8_WAIT_V(n) asm volatile("s_waitcnt vmcnt(" #n ")" ::: "memory")
; #define PG8_WAIT_L(n) asm volatile("s_waitcnt lgkmcnt(" #n ")" ::: "memory")
; #define PG8_BAR __builtin_amdgcn_s_barrier()
; #define PG8_SCHED __builtin_amdgcn_sched_barrier(0)
;     DI int nt(const Unit& u) const { return (u.aux & 8) ? PLED / 64 : ((u.aux & 4) ? (D_ / 2) / 64 : D_ / 64); }
; template <class Epi, class Sched, bool ALIGN_EPI, bool FP8 = false>
; DI void gemm_phase(LAS unsigned char* lds, const Gemm g, const Sched& S, const Epi& E) {
;     ...
;             const bool last = (t == nt - 2);
;             const char* a1 = cA + (size_t)(t + 1) * kstep;
;             const char* a2 = last ? nA : cA + (size_t)(t + 2) * kstep; const char* b2 = last ? nB : cB + (size_t)(t + 2) * kstep;
;             const char* a3 = a2 + kstep; const char* b3 = b2 + kstep;
;             PG8_LDB(B0, 0, 0); PG8_LDB(B1, 0, 1); PG8_SCHED; PG8_LDA(At, 0, 0); PG8_STAGE(PG8_SA(1, 1), a1 + hstepA, voffA);
;             PG8_WAIT_V(8); PG8_WAIT_L(0); PG8_BAR; PG8_MMA(0, 0, At, B0); PG8_MMA(0, 1, At, B1); PG8_BAR; PG8_SCHED;
.Lmy_g0_809:
	ds_read_b128 v[144:147], v135
	ds_read_b128 v[148:151], v135 offset:16
	ds_read_b128 v[152:155], v135 offset:2048
	ds_read_b128 v[156:159], v135 offset:2064
	ds_read_b128 v[160:163], v135 offset:16384
	ds_read_b128 v[164:167], v135 offset:16400
	ds_read_b128 v[168:171], v135 offset:18432
	ds_read_b128 v[172:175], v135 offset:18448
	s_add_u32 s50, s48, 0x100
	s_addc_u32 s51, s49, 0
	s_cmp_eq_u32 s83, 40
	s_cselect_b32 s56, s6, s50
	s_cselect_b32 s57, s7, s51
	s_cselect_b32 s54, s46, s81
	s_cselect_b32 s55, s47, s82
	s_add_u32 s52, s56, 0x80
	s_addc_u32 s53, s57, 0
	ds_read_b128 v[176:179], v134
	ds_read_b128 v[180:183], v134 offset:16
	ds_read_b128 v[184:187], v134 offset:2048
	ds_read_b128 v[188:191], v134 offset:2064
	ds_read_b128 v[192:195], v134 offset:4096
	ds_read_b128 v[196:199], v134 offset:4112
	ds_read_b128 v[200:203], v134 offset:6144
	ds_read_b128 v[204:207], v134 offset:6160
	s_add_u32 s48, s48, 0xb0080
	s_addc_u32 s49, s49, 0
	s_mov_b32 s84, m0
	s_mov_b32 m0, s72
	s_nop 0
	global_load_lds_dwordx4 v136, s[48:49]
	s_mov_b32 m0, s84
	s_nop 0
	s_mov_b32 s84, m0
	s_mov_b32 m0, s73
	s_nop 0
	global_load_lds_dwordx4 v138, s[48:49]
	s_mov_b32 m0, s84
	s_waitcnt vmcnt(8)
	s_waitcnt lgkmcnt(0)
	s_barrier
	s_setprio 1
	v_mfma_scale_f32_16x16x128_f8f6f4 v[124:127], v[144:151], v[176:183], v[124:127], v142, v142 op_sel_hi:[0,0,0]
	v_mfma_scale_f32_16x16x128_f8f6f4 v[120:123], v[152:159], v[176:183], v[120:123], v142, v142 op_sel_hi:[0,0,0]
	v_mfma_scale_f32_16x16x128_f8f6f4 v[108:111], v[144:151], v[184:191], v[108:111], v142, v142 op_sel_hi:[0,0,0]
	v_mfma_scale_f32_16x16x128_f8f6f4 v[104:107], v[152:159], v[184:191], v[104:107], v142, v142 op_sel_hi:[0,0,0]
	v_mfma_scale_f32_16x16x128_f8f6f4 v[208:211], v[144:151], v[192:199], v[92:95], v142, v142 op_sel_hi:[0,0,0]
	v_mfma_scale_f32_16x16x128_f8f6f4 v[212:215], v[152:159], v[192:199], v[88:91], v142, v142 op_sel_hi:[0,0,0]
	v_mfma_scale_f32_16x16x128_f8f6f4 v[216:219], v[144:151], v[200:207], v[76:79], v142, v142 op_sel_hi:[0,0,0]
	v_mfma_scale_f32_16x16x128_f8f6f4 v[220:223], v[152:159], v[200:207], v[72:75], v142, v142 op_sel_hi:[0,0,0]
	v_mfma_scale_f32_16x16x128_f8f6f4 v[116:119], v[160:167], v[176:183], v[116:119], v142, v142 op_sel_hi:[0,0,0]
	v_mfma_scale_f32_16x16x128_f8f6f4 v[112:115], v[168:175], v[176:183], v[112:115], v142, v142 op_sel_hi:[0,0,0]
	v_mfma_scale_f32_16x16x128_f8f6f4 v[100:103], v[160:167], v[184:191], v[100:103], v142, v142 op_sel_hi:[0,0,0]
	v_mfma_scale_f32_16x16x128_f8f6f4 v[96:99], v[168:175], v[184:191], v[96:99], v142, v142 op_sel_hi:[0,0,0]
	v_mfma_scale_f32_16x16x128_f8f6f4 v[176:179], v[160:167], v[192:199], v[84:87], v142, v142 op_sel_hi:[0,0,0]
	v_mfma_scale_f32_16x16x128_f8f6f4 v[180:183], v[168:175], v[192:199], v[80:83], v142, v142 op_sel_hi:[0,0,0]
	ds_read_b32 v255, v255 offset:4096
	v_mfma_scale_f32_16x16x128_f8f6f4 v[184:187], v[160:167], v[200:207], v[68:71], v142, v142 op_sel_hi:[0,0,0]
	v_mfma_scale_f32_16x16x128_f8f6f4 v[188:191], v[168:175], v[200:207], v[64:67], v142, v142 op_sel_hi:[0,0,0]
	s_add_u32 s98, s98, 0x80000
	s_waitcnt lgkmcnt(0)
	v_readfirstlane_b32 s101, v255
	v_mov_b32_e32 v255, 0x20000
	s_cmp_ge_u32 s101, s98
	s_cbranch_scc1 .Lmy_g_24

; #define PG8_STAGE(bufoff, gbase, voff) do { _Pragma("unroll") for (int _i = 0; _i < 2; ++_i) { unsigned keep_; \
;         asm volatile("s_mov_b32 %0, m0\n\ts_mov_b32 m0, %3\n\ts_nop 0\n\tglobal_load_lds_dwordx4 %1, %2\n\ts_mov_b32 m0, %0" : "=&s"(keep_) : "v"((voff)[_i]), "s"((const char*)(gbase)), "s"(ldsbase + (unsigned)((bufoff) + _i * 8192)) : "memory"); } } while (0)
; #define PG8_WAIT_V(n) asm volatile("s_waitcnt vmcnt(" #n ")" ::: "memory")
; #define PG8_WAIT_L(n) asm volatile("s_waitcnt lgkmcnt(" #n ")" ::: "memory")
; #define PG8_BAR __builtin_amdgcn_s_barrier()
; #define PG8_SCHED __builtin_amdgcn_sched_barrier(0)
; template <class Epi, class Sched, bool ALIGN_EPI, bool FP8 = false>
; DI void gemm_phase(LAS unsigned char* lds, const Gemm g, const Sched& S, const Epi& E) {
;     ...
;             PG8_LDA(At, 0, 1); PG8_STAGE(PG8_SB(0, 0), b2, voffB); PG8_STAGE(PG8_SB(0, 1), b2 + hstepB, voffB); PG8_STAGE(PG8_SA(0, 0), a2, voffA);
;             PG8_WAIT_V(8); PG8_WAIT_L(0); PG8_BAR; PG8_MMA(1, 0, At, B0); PG8_MMA(1, 1, At, B1); PG8_BAR; PG8_SCHED;
.Lmy_g_24:
	s_setprio 0
	s_nop 4
	ds_read_b128 v[64:67], v134 offset:16384
	ds_read_b128 v[68:71], v134 offset:16400
	ds_read_b128 v[72:75], v134 offset:18432
	ds_read_b128 v[76:79], v134 offset:18448
	ds_read_b128 v[80:83], v134 offset:20480
	ds_read_b128 v[84:87], v134 offset:20496
	ds_read_b128 v[88:91], v134 offset:22528
	ds_read_b128 v[92:95], v134 offset:22544
	s_mov_b32 s48, m0
	s_mov_b32 m0, s59
	s_nop 0
	global_load_lds_dwordx4 v137, s[54:55]
	s_mov_b32 m0, s48
	s_nop 0
	s_mov_b32 s48, m0
	s_mov_b32 m0, s60
	s_nop 0
	global_load_lds_dwordx4 v139, s[54:55]
	s_mov_b32 m0, s48
	s_add_u32 s48, s54, 0xb0000
	s_addc_u32 s49, s55, 0
	s_mov_b32 s84, m0
	s_mov_b32 m0, s61
	s_nop 0
	global_load_lds_dwordx4 v137, s[48:49]
	s_mov_b32 m0, s84
	s_nop 0
	s_mov_b32 s84, m0
	s_mov_b32 m0, s62
	s_nop 0
	global_load_lds_dwordx4 v139, s[48:49]
	s_mov_b32 m0, s84
	s_mov_b32 s48, m0
	s_mov_b32 m0, s58
	s_nop 0
	global_load_lds_dwordx4 v136, s[56:57]
	s_mov_b32 m0, s48
	s_nop 0
	s_mov_b32 s48, m0
	s_mov_b32 m0, s63
	s_nop 0
	global_load_lds_dwordx4 v138, s[56:57]
	s_mov_b32 m0, s48
	s_waitcnt vmcnt(8)
	s_waitcnt lgkmcnt(0)
	s_barrier
	s_setprio 1
	v_mfma_scale_f32_16x16x128_f8f6f4 v[60:63], v[144:151], v[64:71], v[60:63], v142, v142 op_sel_hi:[0,0,0]
	v_mfma_scale_f32_16x16x128_f8f6f4 v[56:59], v[152:159], v[64:71], v[56:59], v142, v142 op_sel_hi:[0,0,0]
	v_mfma_scale_f32_16x16x128_f8f6f4 v[192:195], v[144:151], v[72:79], v[44:47], v142, v142 op_sel_hi:[0,0,0]
	v_mfma_scale_f32_16x16x128_f8f6f4 v[196:199], v[152:159], v[72:79], v[40:43], v142, v142 op_sel_hi:[0,0,0]
	v_mfma_scale_f32_16x16x128_f8f6f4 v[200:203], v[144:151], v[80:87], v[28:31], v142, v142 op_sel_hi:[0,0,0]
	v_mfma_scale_f32_16x16x128_f8f6f4 v[204:207], v[152:159], v[80:87], v[24:27], v142, v142 op_sel_hi:[0,0,0]
	v_mfma_scale_f32_16x16x128_f8f6f4 v[224:227], v[144:151], v[88:95], v[12:15], v142, v142 op_sel_hi:[0,0,0]
	v_mfma_scale_f32_16x16x128_f8f6f4 v[228:231], v[152:159], v[88:95], v[8:11], v142, v142 op_sel_hi:[0,0,0]
	v_mfma_scale_f32_16x16x128_f8f6f4 v[52:55], v[160:167], v[64:71], v[52:55], v142, v142 op_sel_hi:[0,0,0]
	v_mfma_scale_f32_16x16x128_f8f6f4 v[48:51], v[168:175], v[64:71], v[48:51], v142, v142 op_sel_hi:[0,0,0]
	v_mfma_scale_f32_16x16x128_f8f6f4 v[232:235], v[160:167], v[72:79], v[36:39], v142, v142 op_sel_hi:[0,0,0]
	v_mfma_scale_f32_16x16x128_f8f6f4 v[236:239], v[168:175], v[72:79], v[32:35], v142, v142 op_sel_hi:[0,0,0]
	v_mfma_scale_f32_16x16x128_f8f6f4 v[240:243], v[160:167], v[80:87], v[20:23], v142, v142 op_sel_hi:[0,0,0]
	v_mfma_scale_f32_16x16x128_f8f6f4 v[244:247], v[168:175], v[80:87], v[16:19], v142, v142 op_sel_hi:[0,0,0]
	ds_read_b32 v255, v255 offset:4096
	v_mfma_scale_f32_16x16x128_f8f6f4 v[248:251], v[160:167], v[88:95], v[4:7], v142, v142 op_sel_hi:[0,0,0]
	v_mfma_scale_f32_16x16x128_f8f6f4 v[128:131], v[168:175], v[88:95], v[0:3], v142, v142 op_sel_hi:[0,0,0]
	s_add_u32 s98, s98, 0x80000
	s_waitcnt lgkmcnt(0)
	v_readfirstlane_b32 s101, v255
	v_mov_b32_e32 v255, 0x20000
	s_cmp_ge_u32 s101, s98
	s_cbranch_scc1 .Lmy_g_25

; #define PG8_STAGE(bufoff, gbase, voff) do { _Pragma("unroll") for (int _i = 0; _i < 2; ++_i) { unsigned keep_; \
;         asm volatile("s_mov_b32 %0, m0\n\ts_mov_b32 m0, %3\n\ts_nop 0\n\tglobal_load_lds_dwordx4 %1, %2\n\ts_mov_b32 m0, %0" : "=&s"(keep_) : "v"((voff)[_i]), "s"((const char*)(gbase)), "s"(ldsbase + (unsigned)((bufoff) + _i * 8192)) : "memory"); } } while (0)
; #define PG8_WAIT_V(n) asm volatile("s_waitcnt vmcnt(" #n ")" ::: "memory")
; #define PG8_WAIT_L(n) asm volatile("s_waitcnt lgkmcnt(" #n ")" ::: "memory")
; #define PG8_BAR __builtin_amdgcn_s_barrier()
; #define PG8_SCHED __builtin_amdgcn_sched_barrier(0)
; template <class Epi, class Sched, bool ALIGN_EPI, bool FP8 = false>
; DI void gemm_phase(LAS unsigned char* lds, const Gemm g, const Sched& S, const Epi& E) {
;     ...
;             PG8_LDB(B0, 1, 0); PG8_LDB(B1, 1, 1); PG8_SCHED; PG8_LDA(At, 1, 0); PG8_STAGE(PG8_SA(0, 1), a2 + hstepA, voffA);
;             PG8_WAIT_V(8); PG8_WAIT_L(0); PG8_BAR; PG8_MMA(0, 0, At, B0); PG8_MMA(0, 1, At, B1); PG8_BAR; PG8_SCHED;
.Lmy_g_25:
	s_setprio 0
	s_nop 4
	ds_read_b128 v[0:3], v135 offset:32768
	ds_read_b128 v[4:7], v135 offset:32784
	ds_read_b128 v[16:19], v135 offset:34816
	ds_read_b128 v[20:23], v135 offset:34832
	ds_read_b128 v[144:147], v135 offset:49152
	ds_read_b128 v[148:151], v135 offset:49168
	ds_read_b128 v[152:155], v135 offset:51200
	ds_read_b128 v[156:159], v135 offset:51216
	ds_read_b128 v[8:11], v134 offset:32768
	ds_read_b128 v[12:15], v134 offset:32784
	ds_read_b128 v[24:27], v134 offset:34816
	ds_read_b128 v[28:31], v134 offset:34832
	ds_read_b128 v[32:35], v134 offset:36864
	ds_read_b128 v[36:39], v134 offset:36880
	ds_read_b128 v[40:43], v134 offset:38912
	ds_read_b128 v[44:47], v134 offset:38928
	s_add_u32 s48, s56, 0xb0000
	s_addc_u32 s49, s57, 0
	s_mov_b32 s56, m0
	s_mov_b32 m0, s64
	s_nop 0
	global_load_lds_dwordx4 v136, s[48:49]
	s_mov_b32 m0, s56
	s_nop 0
	s_mov_b32 s56, m0
	s_mov_b32 m0, s65
	s_nop 0
	global_load_lds_dwordx4 v138, s[48:49]
	s_mov_b32 m0, s56
	s_waitcnt vmcnt(8)
	s_waitcnt lgkmcnt(0)
	s_barrier
	s_setprio 1
	v_mfma_scale_f32_16x16x128_f8f6f4 v[124:127], v[0:7], v[8:15], v[124:127], v142, v142 op_sel_hi:[0,0,0]
	v_mfma_scale_f32_16x16x128_f8f6f4 v[120:123], v[16:23], v[8:15], v[120:123], v142, v142 op_sel_hi:[0,0,0]
	v_mfma_scale_f32_16x16x128_f8f6f4 v[108:111], v[0:7], v[24:31], v[108:111], v142, v142 op_sel_hi:[0,0,0]
	v_mfma_scale_f32_16x16x128_f8f6f4 v[104:107], v[16:23], v[24:31], v[104:107], v142, v142 op_sel_hi:[0,0,0]
	v_mfma_scale_f32_16x16x128_f8f6f4 v[92:95], v[0:7], v[32:39], v[208:211], v142, v142 op_sel_hi:[0,0,0]
	v_mfma_scale_f32_16x16x128_f8f6f4 v[88:91], v[16:23], v[32:39], v[212:215], v142, v142 op_sel_hi:[0,0,0]
	v_mfma_scale_f32_16x16x128_f8f6f4 v[76:79], v[0:7], v[40:47], v[216:219], v142, v142 op_sel_hi:[0,0,0]
	v_mfma_scale_f32_16x16x128_f8f6f4 v[72:75], v[16:23], v[40:47], v[220:223], v142, v142 op_sel_hi:[0,0,0]
	v_mfma_scale_f32_16x16x128_f8f6f4 v[116:119], v[144:151], v[8:15], v[116:119], v142, v142 op_sel_hi:[0,0,0]
	v_mfma_scale_f32_16x16x128_f8f6f4 v[112:115], v[152:159], v[8:15], v[112:115], v142, v142 op_sel_hi:[0,0,0]
	v_mfma_scale_f32_16x16x128_f8f6f4 v[100:103], v[144:151], v[24:31], v[100:103], v142, v142 op_sel_hi:[0,0,0]
	v_mfma_scale_f32_16x16x128_f8f6f4 v[96:99], v[152:159], v[24:31], v[96:99], v142, v142 op_sel_hi:[0,0,0]
	v_mfma_scale_f32_16x16x128_f8f6f4 v[84:87], v[144:151], v[32:39], v[176:179], v142, v142 op_sel_hi:[0,0,0]
	v_mfma_scale_f32_16x16x128_f8f6f4 v[80:83], v[152:159], v[32:39], v[180:183], v142, v142 op_sel_hi:[0,0,0]
	ds_read_b32 v255, v255 offset:4096
	v_mfma_scale_f32_16x16x128_f8f6f4 v[68:71], v[144:151], v[40:47], v[184:187], v142, v142 op_sel_hi:[0,0,0]
	v_mfma_scale_f32_16x16x128_f8f6f4 v[64:67], v[152:159], v[40:47], v[188:191], v142, v142 op_sel_hi:[0,0,0]
	s_add_u32 s98, s98, 0x80000
	s_waitcnt lgkmcnt(0)
	v_readfirstlane_b32 s101, v255
	v_mov_b32_e32 v255, 0x20000
	s_cmp_ge_u32 s101, s98
	s_cbranch_scc1 .Lmy_g_26

; #define PG8_STAGE(bufoff, gbase, voff) do { _Pragma("unroll") for (int _i = 0; _i < 2; ++_i) { unsigned keep_; \
;         asm volatile("s_mov_b32 %0, m0\n\ts_mov_b32 m0, %3\n\ts_nop 0\n\tglobal_load_lds_dwordx4 %1, %2\n\ts_mov_b32 m0, %0" : "=&s"(keep_) : "v"((voff)[_i]), "s"((const char*)(gbase)), "s"(ldsbase + (unsigned)((bufoff) + _i * 8192)) : "memory"); } } while (0)
; #define PG8_WAIT_V(n) asm volatile("s_waitcnt vmcnt(" #n ")" ::: "memory")
; #define PG8_WAIT_L(n) asm volatile("s_waitcnt lgkmcnt(" #n ")" ::: "memory")
; #define PG8_BAR __builtin_amdgcn_s_barrier()
; #define PG8_SCHED __builtin_amdgcn_sched_barrier(0)
; template <class Epi, class Sched, bool ALIGN_EPI, bool FP8 = false>
; DI void gemm_phase(LAS unsigned char* lds, const Gemm g, const Sched& S, const Epi& E) {
;     ...
;             PG8_LDA(At, 1, 1); PG8_STAGE(PG8_SB(1, 0), b3, voffB); PG8_STAGE(PG8_SB(1, 1), b3 + hstepB, voffB); PG8_STAGE(PG8_SA(1, 0), a3, voffA);
;             PG8_WAIT_V(8); PG8_WAIT_L(0); PG8_BAR; PG8_MMA(1, 0, At, B0); PG8_MMA(1, 1, At, B1); PG8_BAR; PG8_SCHED;
.Lmy_g_26:
	s_setprio 0
	ds_read_b128 v[32:35], v134 offset:49152
	ds_read_b128 v[36:39], v134 offset:49168
	ds_read_b128 v[160:163], v134 offset:51200
	ds_read_b128 v[164:167], v134 offset:51216
	ds_read_b128 v[168:171], v134 offset:53248
	ds_read_b128 v[172:175], v134 offset:53264
	ds_read_b128 v[176:179], v134 offset:55296
	ds_read_b128 v[180:183], v134 offset:55312
	s_add_u32 s48, s54, 0x80
	s_addc_u32 s49, s55, 0
	s_mov_b32 s56, m0
	s_mov_b32 m0, s66
	s_nop 0
	global_load_lds_dwordx4 v137, s[48:49]
	s_mov_b32 m0, s56
	s_nop 0
	s_mov_b32 s56, m0
	s_mov_b32 m0, s67
	s_nop 0
	global_load_lds_dwordx4 v139, s[48:49]
	s_mov_b32 m0, s56
	s_add_u32 s48, s54, 0xb0080
	s_addc_u32 s49, s55, 0
	s_mov_b32 s54, m0
	s_mov_b32 m0, s70
	s_nop 0
	global_load_lds_dwordx4 v137, s[48:49]
	s_mov_b32 m0, s54
	s_nop 0
	s_mov_b32 s54, m0
	s_mov_b32 m0, s71
	s_nop 0
	global_load_lds_dwordx4 v139, s[48:49]
	s_mov_b32 m0, s54
	s_mov_b32 s48, m0
	s_mov_b32 m0, s68
	s_nop 0
	global_load_lds_dwordx4 v136, s[52:53]
	s_mov_b32 m0, s48
	s_nop 0
	s_mov_b32 s48, m0
	s_mov_b32 m0, s69
	s_nop 0
	global_load_lds_dwordx4 v138, s[52:53]
	s_mov_b32 m0, s48
	s_waitcnt vmcnt(8)
	s_waitcnt lgkmcnt(0)
	s_barrier
	s_setprio 1
	v_mfma_scale_f32_16x16x128_f8f6f4 v[60:63], v[0:7], v[32:39], v[60:63], v142, v142 op_sel_hi:[0,0,0]
	v_mfma_scale_f32_16x16x128_f8f6f4 v[56:59], v[16:23], v[32:39], v[56:59], v142, v142 op_sel_hi:[0,0,0]
	v_mfma_scale_f32_16x16x128_f8f6f4 v[44:47], v[0:7], v[160:167], v[192:195], v142, v142 op_sel_hi:[0,0,0]
	v_mfma_scale_f32_16x16x128_f8f6f4 v[40:43], v[16:23], v[160:167], v[196:199], v142, v142 op_sel_hi:[0,0,0]
	v_mfma_scale_f32_16x16x128_f8f6f4 v[28:31], v[0:7], v[168:175], v[200:203], v142, v142 op_sel_hi:[0,0,0]
	v_mfma_scale_f32_16x16x128_f8f6f4 v[24:27], v[16:23], v[168:175], v[204:207], v142, v142 op_sel_hi:[0,0,0]
	v_mfma_scale_f32_16x16x128_f8f6f4 v[12:15], v[0:7], v[176:183], v[224:227], v142, v142 op_sel_hi:[0,0,0]
	v_mfma_scale_f32_16x16x128_f8f6f4 v[8:11], v[16:23], v[176:183], v[228:231], v142, v142 op_sel_hi:[0,0,0]
	v_mfma_scale_f32_16x16x128_f8f6f4 v[52:55], v[144:151], v[32:39], v[52:55], v142, v142 op_sel_hi:[0,0,0]
	v_mfma_scale_f32_16x16x128_f8f6f4 v[48:51], v[152:159], v[32:39], v[48:51], v142, v142 op_sel_hi:[0,0,0]
	v_mfma_scale_f32_16x16x128_f8f6f4 v[36:39], v[144:151], v[160:167], v[232:235], v142, v142 op_sel_hi:[0,0,0]
	v_mfma_scale_f32_16x16x128_f8f6f4 v[32:35], v[152:159], v[160:167], v[236:239], v142, v142 op_sel_hi:[0,0,0]
	v_mfma_scale_f32_16x16x128_f8f6f4 v[20:23], v[144:151], v[168:175], v[240:243], v142, v142 op_sel_hi:[0,0,0]
	v_mfma_scale_f32_16x16x128_f8f6f4 v[16:19], v[152:159], v[168:175], v[244:247], v142, v142 op_sel_hi:[0,0,0]
	ds_read_b32 v255, v255 offset:4096
	v_mfma_scale_f32_16x16x128_f8f6f4 v[4:7], v[144:151], v[176:183], v[248:251], v142, v142 op_sel_hi:[0,0,0]
	v_mfma_scale_f32_16x16x128_f8f6f4 v[0:3], v[152:159], v[176:183], v[128:131], v142, v142 op_sel_hi:[0,0,0]
	s_add_u32 s98, s98, 0x80000
	s_waitcnt lgkmcnt(0)
	v_readfirstlane_b32 s101, v255
	v_mov_b32_e32 v255, 0x20000
	s_cmp_ge_u32 s101, s98
	s_cbranch_scc1 .Lmy_g_27

; #define PG8_WAIT_V(n) asm volatile("s_waitcnt vmcnt(" #n ")" ::: "memory")
; #define PG8_WAIT_L(n) asm volatile("s_waitcnt lgkmcnt(" #n ")" ::: "memory")
; #define PG8_BAR __builtin_amdgcn_s_barrier()
; #define PG8_SCHED __builtin_amdgcn_sched_barrier(0)
; template <class Epi, class Sched, bool ALIGN_EPI, bool FP8 = false>
; DI void gemm_phase(LAS unsigned char* lds, const Gemm g, const Sched& S, const Epi& E) {
;     ...
;             PG8_WAIT_V(8); PG8_WAIT_L(0); PG8_BAR; PG8_MMA(1, 0, At, B0); PG8_MMA(1, 1, At, B1); PG8_BAR; PG8_SCHED;
;         }
;         if constexpr (ALIGN_EPI) { if (wr == 0) PG8_BAR; }
;         E(acc, cur, wr, wc, fr, fq);
.Lmy_g_27:
	s_setprio 0
	s_add_i32 s83, s83, 2
	s_add_u32 s81, s81, 0x100
	s_addc_u32 s82, s82, 0
	s_cmp_gt_u32 s83, 41
	s_mov_b64 s[48:49], s[50:51]
	s_cbranch_scc0 .Lmy_g0_809
.Lmy_ex_809:
	s_and_b64 vcc, exec, s[20:21]
	s_cbranch_vccz .LBB0_812
	s_barrier

; #define PG8_BAR __builtin_amdgcn_s_barrier()
; template <class Epi, class Sched, bool ALIGN_EPI, bool FP8 = false>
; DI void gemm_phase(LAS unsigned char* lds, const Gemm g, const Sched& S, const Epi& E) {
;     ...
;         if constexpr (ALIGN_EPI) { if (wr == 0) PG8_BAR; }
;         E(acc, cur, wr, wc, fr, fq);
;     DI void operator()(const f32x4 (&acc)[2][2][4][2], const Unit& u, int wr, int wc, int fr, int fq) const {
;         if (u.aux & 2) { const EpiBf16 e{VTp, NTOK}; e(acc, u, wr, wc, fr, fq); }
;         else if (u.aux & 8) { const EpiBf16 e{PWp, D_}; e(acc, u, wr, wc, fr, fq); }
;         else if (u.aux & 4) { const EpiBf16 e{RG0 + (long)(u.aux & 1) * rgd, 1024}; e(acc, u, wr, wc, fr, fq); }
;         else { const EpiA1 e{H5, (bf16*)nullptr, (const float*)nullptr, cosT, sinT}; e(acc, u, wr, wc, fr, fq); }
.Lmy_ex_991:
	s_and_b64 vcc, exec, s[26:27]
	s_cbranch_vccnz .LBB0_1001
	s_bitcmp0_b32 s67, 1
	s_mov_b64 s[56:57], -1
	v_lshl_add_u32 v142, s14, 8, v156
	s_cbranch_scc0 .LBB0_1002

; DI unsigned cvt_pk_bf16(float lo, float hi) { const f32x2_t v = {lo, hi}; return __builtin_bit_cast(unsigned, __builtin_convertvector(v, bf16x2_t)); }
; #define PG8_BAR __builtin_amdgcn_s_barrier()
; template <class Epi, class Sched, bool ALIGN_EPI, bool FP8 = false>
; DI void gemm_phase(LAS unsigned char* lds, const Gemm g, const Sched& S, const Epi& E) {
;     ...
;         if constexpr (ALIGN_EPI) { if (wr == 0) PG8_BAR; }
;         E(acc, cur, wr, wc, fr, fq);
;     DI void operator()(const f32x4 (&acc)[2][2][4][2], const Unit& u, int wr, int wc, int fr, int fq) const {
;         int row0 = u.pm * BM + wr * 64 + fr; asm volatile("" : "+v"(row0));
;         const int col0 = u.pn * BM + wc * 32 + 8 * fq;
; #pragma unroll
;         for (int ai = 0; ai < 2; ++ai)
; #pragma unroll
;             for (int m = 0; m < 4; ++m) { const size_t r = (size_t)(row0 + ai * HALF + m * 16);
; #pragma unroll
;                 for (int bj = 0; bj < 2; ++bj) { const size_t o = r * D_ + col0 + bj * HALF; f32x4 x0, x1; unpack8f(*(const u32x4*)(R0 + o), x0, x1);
;                     f32x4 v0 = ALPHA * x0 + acc[ai][bj][m][0], v1 = ALPHA * x1 + acc[ai][bj][m][1];
;                     if (HAS_R1) { f32x4 q0, q1; unpack8f(*(const u32x4*)(R1 + o), q0, q1); v0 = v0 + q0; v1 = v1 + q1; }
;                     u32x4 w; w.x = cvt_pk_bf16(v0[0], v0[1]); w.y = cvt_pk_bf16(v0[2], v0[3]); w.z = cvt_pk_bf16(v1[0], v1[1]); w.w = cvt_pk_bf16(v1[2], v1[3]);
;                     *(u32x4*)(Yo + o) = w; }
;                 if (m & 1) asm volatile("" ::: "memory"); }
;     }
.Lmy_ex_1305:
	s_and_b64 vcc, exec, s[14:15]
	s_cbranch_vccz .LBB0_1308
	s_barrier
.LBB0_1308:
	v_lshl_add_u32 v132, s62, 8, v138
	v_lshl_or_b32 v146, s92, 8, v139
	v_ashrrev_i32_e32 v133, 31, v132
	v_ashrrev_i32_e32 v147, 31, v146
	v_lshlrev_b64 v[132:133], 11, v[132:133]
	v_lshl_add_u64 v[132:133], v[132:133], 0, v[146:147]
	v_lshlrev_b64 v[132:133], 1, v[132:133]
	v_lshl_add_u64 v[146:147], s[10:11], 0, v[132:133]
	v_or_b32_e32 v154, 0x100, v132
	v_mov_b32_e32 v155, v133
	global_load_dwordx4 v[146:149], v[146:147], off
	v_lshl_add_u64 v[150:151], s[10:11], 0, v[154:155]
	global_load_dwordx4 v[150:153], v[150:151], off
	v_lshl_add_u64 v[156:157], s[12:13], 0, v[132:133]
	v_lshl_add_u64 v[158:159], v[132:133], 0, s[18:19]
	v_lshl_add_u64 v[154:155], s[12:13], 0, v[154:155]
	v_lshl_add_u64 v[160:161], s[10:11], 0, v[158:159]
	s_mov_b64 s[64:65], 0x80000
	s_andn2_b64 vcc, exec, s[4:5]
	s_mov_b64 s[4:5], -1
	s_waitcnt vmcnt(1)
	v_lshlrev_b32_e32 v162, 16, v146
	v_and_b32_e32 v163, 0xffff0000, v146
	v_lshlrev_b32_e32 v146, 16, v147
	v_and_b32_e32 v147, 0xffff0000, v147
	v_lshlrev_b32_e32 v164, 16, v148
	v_and_b32_e32 v165, 0xffff0000, v148
	v_lshlrev_b32_e32 v148, 16, v149
	v_and_b32_e32 v149, 0xffff0000, v149
	v_pk_fma_f32 v[126:127], v[146:147], s[16:17], v[126:127] op_sel_hi:[1,0,1]
	v_pk_fma_f32 v[124:125], v[162:163], s[16:17], v[124:125] op_sel_hi:[1,0,1]
	v_pk_fma_f32 v[146:147], v[148:149], s[16:17], v[122:123] op_sel_hi:[1,0,1]
	s_waitcnt vmcnt(0)
	v_lshlrev_b32_e32 v148, 16, v150
	v_and_b32_e32 v149, 0xffff0000, v150
	v_lshlrev_b32_e32 v150, 16, v151
	v_and_b32_e32 v151, 0xffff0000, v151
	v_lshlrev_b32_e32 v162, 16, v152
	v_and_b32_e32 v163, 0xffff0000, v152
	v_lshlrev_b32_e32 v152, 16, v153
	v_and_b32_e32 v153, 0xffff0000, v153
	v_pk_fma_f32 v[122:123], v[164:165], s[16:17], v[120:121] op_sel_hi:[1,0,1]
	v_cvt_pk_bf16_f32 v120, v124, v125
	v_pk_fma_f32 v[118:119], v[150:151], s[16:17], v[118:119] op_sel_hi:[1,0,1]
	v_pk_fma_f32 v[116:117], v[148:149], s[16:17], v[116:117] op_sel_hi:[1,0,1]
	v_pk_fma_f32 v[124:125], v[152:153], s[16:17], v[114:115] op_sel_hi:[1,0,1]
	v_pk_fma_f32 v[114:115], v[162:163], s[16:17], v[112:113] op_sel_hi:[1,0,1]
	v_cvt_pk_bf16_f32 v121, v126, v127
	v_cvt_pk_bf16_f32 v122, v122, v123
	v_cvt_pk_bf16_f32 v123, v146, v147
	v_cvt_pk_bf16_f32 v112, v116, v117
	v_cvt_pk_bf16_f32 v113, v118, v119
	v_cvt_pk_bf16_f32 v114, v114, v115
	v_cvt_pk_bf16_f32 v115, v124, v125
	global_store_dwordx4 v[156:157], v[120:123], off
	global_store_dwordx4 v[154:155], v[112:115], off
	global_load_dwordx4 v[112:115], v[160:161], off
	v_lshl_add_u64 v[120:121], v[132:133], 0, s[20:21]
	v_lshl_add_u64 v[116:117], s[10:11], 0, v[120:121]
	global_load_dwordx4 v[116:119], v[116:117], off
	v_lshl_add_u64 v[124:125], s[12:13], 0, v[158:159]
	v_lshl_add_u64 v[122:123], v[132:133], 0, s[22:23]
	v_lshl_add_u64 v[120:121], s[12:13], 0, v[120:121]
	v_lshl_add_u64 v[126:127], s[10:11], 0, v[122:123]
	s_waitcnt vmcnt(1)
	v_lshlrev_b32_e32 v146, 16, v112
	v_and_b32_e32 v147, 0xffff0000, v112
	v_lshlrev_b32_e32 v112, 16, v113
	v_and_b32_e32 v113, 0xffff0000, v113
	v_lshlrev_b32_e32 v148, 16, v114
	v_and_b32_e32 v149, 0xffff0000, v114
	v_lshlrev_b32_e32 v114, 16, v115
	v_and_b32_e32 v115, 0xffff0000, v115
	s_waitcnt vmcnt(0)
	v_lshlrev_b32_e32 v150, 16, v116
	v_and_b32_e32 v151, 0xffff0000, v116
	v_lshlrev_b32_e32 v116, 16, v117
	v_and_b32_e32 v117, 0xffff0000, v117
	v_lshlrev_b32_e32 v152, 16, v118
	v_and_b32_e32 v153, 0xffff0000, v118
	v_lshlrev_b32_e32 v118, 16, v119
	v_and_b32_e32 v119, 0xffff0000, v119
	v_pk_fma_f32 v[110:111], v[112:113], s[16:17], v[110:111] op_sel_hi:[1,0,1]
	v_pk_fma_f32 v[108:109], v[146:147], s[16:17], v[108:109] op_sel_hi:[1,0,1]
	v_pk_fma_f32 v[106:107], v[114:115], s[16:17], v[106:107] op_sel_hi:[1,0,1]
	v_pk_fma_f32 v[104:105], v[148:149], s[16:17], v[104:105] op_sel_hi:[1,0,1]
	v_pk_fma_f32 v[102:103], v[116:117], s[16:17], v[102:103] op_sel_hi:[1,0,1]
	v_pk_fma_f32 v[100:101], v[150:151], s[16:17], v[100:101] op_sel_hi:[1,0,1]
	v_pk_fma_f32 v[112:113], v[118:119], s[16:17], v[98:99] op_sel_hi:[1,0,1]
	v_pk_fma_f32 v[114:115], v[152:153], s[16:17], v[96:97] op_sel_hi:[1,0,1]
	v_cvt_pk_bf16_f32 v96, v108, v109
	v_cvt_pk_bf16_f32 v97, v110, v111
	v_cvt_pk_bf16_f32 v98, v104, v105
	v_cvt_pk_bf16_f32 v99, v106, v107
	v_cvt_pk_bf16_f32 v100, v100, v101
	v_cvt_pk_bf16_f32 v101, v102, v103
	v_cvt_pk_bf16_f32 v102, v114, v115
	v_cvt_pk_bf16_f32 v103, v112, v113
	global_store_dwordx4 v[124:125], v[96:99], off
	global_store_dwordx4 v[120:121], v[100:103], off
	v_lshl_add_u64 v[104:105], v[132:133], 0, s[24:25]
	global_load_dwordx4 v[96:99], v[126:127], off
	v_lshl_add_u64 v[100:101], s[10:11], 0, v[104:105]
	global_load_dwordx4 v[100:103], v[100:101], off
	v_lshl_add_u64 v[106:107], v[132:133], 0, s[26:27]
	v_lshl_add_u64 v[108:109], s[12:13], 0, v[122:123]
	v_lshl_add_u64 v[104:105], s[12:13], 0, v[104:105]
	v_lshl_add_u64 v[110:111], s[10:11], 0, v[106:107]
	s_waitcnt vmcnt(1)
	v_lshlrev_b32_e32 v112, 16, v96
	v_and_b32_e32 v113, 0xffff0000, v96
	v_lshlrev_b32_e32 v96, 16, v97
	v_and_b32_e32 v97, 0xffff0000, v97
	v_lshlrev_b32_e32 v114, 16, v98
	v_and_b32_e32 v115, 0xffff0000, v98
	v_lshlrev_b32_e32 v98, 16, v99
	v_and_b32_e32 v99, 0xffff0000, v99
	s_waitcnt vmcnt(0)
; DI unsigned cvt_pk_bf16(float lo, float hi) { const f32x2_t v = {lo, hi}; return __builtin_bit_cast(unsigned, __builtin_convertvector(v, bf16x2_t)); }
;     DI void operator()(const f32x4 (&acc)[2][2][4][2], const Unit& u, int wr, int wc, int fr, int fq) const {
;     ...
;             for (int m = 0; m < 4; ++m) { const size_t r = (size_t)(row0 + ai * HALF + m * 16);
; #pragma unroll
;                 for (int bj = 0; bj < 2; ++bj) { const size_t o = r * D_ + col0 + bj * HALF; f32x4 x0, x1; unpack8f(*(const u32x4*)(R0 + o), x0, x1);
;                     f32x4 v0 = ALPHA * x0 + acc[ai][bj][m][0], v1 = ALPHA * x1 + acc[ai][bj][m][1];
;                     if (HAS_R1) { f32x4 q0, q1; unpack8f(*(const u32x4*)(R1 + o), q0, q1); v0 = v0 + q0; v1 = v1 + q1; }
;                     u32x4 w; w.x = cvt_pk_bf16(v0[0], v0[1]); w.y = cvt_pk_bf16(v0[2], v0[3]); w.z = cvt_pk_bf16(v1[0], v1[1]); w.w = cvt_pk_bf16(v1[2], v1[3]);
;                     *(u32x4*)(Yo + o) = w; }
;                 if (m & 1) asm volatile("" ::: "memory"); }
	v_lshlrev_b32_e32 v116, 16, v100
	v_and_b32_e32 v117, 0xffff0000, v100
	v_lshlrev_b32_e32 v100, 16, v101
	v_and_b32_e32 v101, 0xffff0000, v101
	v_lshlrev_b32_e32 v118, 16, v102
	v_and_b32_e32 v119, 0xffff0000, v102
	v_lshlrev_b32_e32 v102, 16, v103
	v_and_b32_e32 v103, 0xffff0000, v103
	v_pk_fma_f32 v[94:95], v[96:97], s[16:17], v[94:95] op_sel_hi:[1,0,1]
	v_pk_fma_f32 v[92:93], v[112:113], s[16:17], v[92:93] op_sel_hi:[1,0,1]
	v_pk_fma_f32 v[90:91], v[98:99], s[16:17], v[90:91] op_sel_hi:[1,0,1]
	v_pk_fma_f32 v[88:89], v[114:115], s[16:17], v[88:89] op_sel_hi:[1,0,1]
	v_pk_fma_f32 v[86:87], v[100:101], s[16:17], v[86:87] op_sel_hi:[1,0,1]
	v_pk_fma_f32 v[84:85], v[116:117], s[16:17], v[84:85] op_sel_hi:[1,0,1]
	v_pk_fma_f32 v[96:97], v[102:103], s[16:17], v[82:83] op_sel_hi:[1,0,1]
	v_pk_fma_f32 v[98:99], v[118:119], s[16:17], v[80:81] op_sel_hi:[1,0,1]
	v_cvt_pk_bf16_f32 v80, v92, v93
	v_cvt_pk_bf16_f32 v81, v94, v95
	v_cvt_pk_bf16_f32 v82, v88, v89
	v_cvt_pk_bf16_f32 v83, v90, v91
	v_cvt_pk_bf16_f32 v84, v84, v85
	v_cvt_pk_bf16_f32 v85, v86, v87
	v_cvt_pk_bf16_f32 v86, v98, v99
	v_cvt_pk_bf16_f32 v87, v96, v97
	global_store_dwordx4 v[108:109], v[80:83], off
	global_store_dwordx4 v[104:105], v[84:87], off
	v_lshl_add_u64 v[88:89], v[132:133], 0, s[28:29]
	global_load_dwordx4 v[80:83], v[110:111], off
	v_lshl_add_u64 v[84:85], s[10:11], 0, v[88:89]
	global_load_dwordx4 v[84:87], v[84:85], off
	v_lshl_add_u64 v[92:93], s[12:13], 0, v[106:107]
	v_lshl_add_u64 v[90:91], v[132:133], 0, s[64:65]
	v_lshl_add_u64 v[88:89], s[12:13], 0, v[88:89]
	v_lshl_add_u64 v[94:95], s[10:11], 0, v[90:91]
	s_waitcnt vmcnt(1)
	v_lshlrev_b32_e32 v96, 16, v80
	v_and_b32_e32 v97, 0xffff0000, v80
	v_lshlrev_b32_e32 v80, 16, v81
	v_and_b32_e32 v81, 0xffff0000, v81
	v_lshlrev_b32_e32 v98, 16, v82
	v_and_b32_e32 v99, 0xffff0000, v82
	v_lshlrev_b32_e32 v82, 16, v83
	v_and_b32_e32 v83, 0xffff0000, v83
	s_waitcnt vmcnt(0)
	v_lshlrev_b32_e32 v100, 16, v84
	v_and_b32_e32 v101, 0xffff0000, v84
	v_lshlrev_b32_e32 v84, 16, v85
	v_and_b32_e32 v85, 0xffff0000, v85
	v_lshlrev_b32_e32 v102, 16, v86
	v_and_b32_e32 v103, 0xffff0000, v86
	v_lshlrev_b32_e32 v86, 16, v87
	v_and_b32_e32 v87, 0xffff0000, v87
	v_pk_fma_f32 v[78:79], v[80:81], s[16:17], v[78:79] op_sel_hi:[1,0,1]
	v_pk_fma_f32 v[76:77], v[96:97], s[16:17], v[76:77] op_sel_hi:[1,0,1]
	v_pk_fma_f32 v[74:75], v[82:83], s[16:17], v[74:75] op_sel_hi:[1,0,1]
	v_pk_fma_f32 v[72:73], v[98:99], s[16:17], v[72:73] op_sel_hi:[1,0,1]
	v_pk_fma_f32 v[70:71], v[84:85], s[16:17], v[70:71] op_sel_hi:[1,0,1]
	v_pk_fma_f32 v[68:69], v[100:101], s[16:17], v[68:69] op_sel_hi:[1,0,1]
	v_pk_fma_f32 v[80:81], v[86:87], s[16:17], v[66:67] op_sel_hi:[1,0,1]
	v_pk_fma_f32 v[82:83], v[102:103], s[16:17], v[64:65] op_sel_hi:[1,0,1]
	v_cvt_pk_bf16_f32 v64, v76, v77
	v_cvt_pk_bf16_f32 v65, v78, v79
	v_cvt_pk_bf16_f32 v66, v72, v73
	v_cvt_pk_bf16_f32 v67, v74, v75
	v_cvt_pk_bf16_f32 v68, v68, v69
	v_cvt_pk_bf16_f32 v69, v70, v71
	v_cvt_pk_bf16_f32 v70, v82, v83
	v_cvt_pk_bf16_f32 v71, v80, v81
	global_store_dwordx4 v[92:93], v[64:67], off
	global_store_dwordx4 v[88:89], v[68:71], off
	v_lshl_add_u64 v[72:73], v[132:133], 0, s[40:41]
	global_load_dwordx4 v[64:67], v[94:95], off
	v_lshl_add_u64 v[68:69], s[10:11], 0, v[72:73]
	global_load_dwordx4 v[68:71], v[68:69], off
	v_lshl_add_u64 v[74:75], v[132:133], 0, s[42:43]
	v_lshl_add_u64 v[76:77], s[12:13], 0, v[90:91]
	v_lshl_add_u64 v[72:73], s[12:13], 0, v[72:73]
	v_lshl_add_u64 v[78:79], s[10:11], 0, v[74:75]
	s_waitcnt vmcnt(1)
	v_lshlrev_b32_e32 v80, 16, v64
	v_and_b32_e32 v81, 0xffff0000, v64
	v_lshlrev_b32_e32 v64, 16, v65
	v_and_b32_e32 v65, 0xffff0000, v65
	v_lshlrev_b32_e32 v82, 16, v66
	v_and_b32_e32 v83, 0xffff0000, v66
	v_lshlrev_b32_e32 v66, 16, v67
	v_and_b32_e32 v67, 0xffff0000, v67
	s_waitcnt vmcnt(0)
	v_lshlrev_b32_e32 v84, 16, v68
	v_and_b32_e32 v85, 0xffff0000, v68
	v_lshlrev_b32_e32 v68, 16, v69
	v_and_b32_e32 v69, 0xffff0000, v69
	v_lshlrev_b32_e32 v86, 16, v70
	v_and_b32_e32 v87, 0xffff0000, v70
	v_lshlrev_b32_e32 v70, 16, v71
	v_and_b32_e32 v71, 0xffff0000, v71
	v_pk_fma_f32 v[62:63], v[64:65], s[16:17], v[62:63] op_sel_hi:[1,0,1]
	v_pk_fma_f32 v[60:61], v[80:81], s[16:17], v[60:61] op_sel_hi:[1,0,1]
	v_pk_fma_f32 v[58:59], v[66:67], s[16:17], v[58:59] op_sel_hi:[1,0,1]
	v_pk_fma_f32 v[56:57], v[82:83], s[16:17], v[56:57] op_sel_hi:[1,0,1]
	v_pk_fma_f32 v[54:55], v[68:69], s[16:17], v[54:55] op_sel_hi:[1,0,1]
	v_pk_fma_f32 v[52:53], v[84:85], s[16:17], v[52:53] op_sel_hi:[1,0,1]
	v_pk_fma_f32 v[64:65], v[70:71], s[16:17], v[50:51] op_sel_hi:[1,0,1]
	v_pk_fma_f32 v[66:67], v[86:87], s[16:17], v[48:49] op_sel_hi:[1,0,1]
	v_cvt_pk_bf16_f32 v48, v60, v61
	v_cvt_pk_bf16_f32 v49, v62, v63
	v_cvt_pk_bf16_f32 v50, v56, v57
	v_cvt_pk_bf16_f32 v51, v58, v59
	v_cvt_pk_bf16_f32 v52, v52, v53
	v_cvt_pk_bf16_f32 v53, v54, v55
	v_cvt_pk_bf16_f32 v54, v66, v67
	v_cvt_pk_bf16_f32 v55, v64, v65
	global_store_dwordx4 v[76:77], v[48:51], off
	global_store_dwordx4 v[72:73], v[52:55], off
	v_lshl_add_u64 v[56:57], v[132:133], 0, s[44:45]
	global_load_dwordx4 v[48:51], v[78:79], off
	v_lshl_add_u64 v[52:53], s[10:11], 0, v[56:57]
	global_load_dwordx4 v[52:55], v[52:53], off
	v_lshl_add_u64 v[60:61], s[12:13], 0, v[74:75]
	v_lshl_add_u64 v[58:59], v[132:133], 0, s[46:47]
	v_lshl_add_u64 v[56:57], s[12:13], 0, v[56:57]
	v_lshl_add_u64 v[62:63], s[10:11], 0, v[58:59]
	s_waitcnt vmcnt(1)
; DI unsigned cvt_pk_bf16(float lo, float hi) { const f32x2_t v = {lo, hi}; return __builtin_bit_cast(unsigned, __builtin_convertvector(v, bf16x2_t)); }
; #define PG8_BAR __builtin_amdgcn_s_barrier()
;     DI int nt(const Unit& u) const { return (u.aux & 8) ? PLED / 64 : ((u.aux & 4) ? (D_ / 2) / 64 : D_ / 64); }
; template <class Epi, class Sched, bool ALIGN_EPI, bool FP8 = false>
; DI void gemm_phase(LAS unsigned char* lds, const Gemm g, const Sched& S, const Epi& E) {
;     ...
;         if (!has_next) break;
; #pragma unroll
;         for (int a = 0; a < 2; ++a)
; #pragma unroll
;             for (int b = 0; b < 2; ++b)
; #pragma unroll
;                 for (int m = 0; m < 4; ++m)
; #pragma unroll
;                     for (int n = 0; n < 2; ++n) acc[a][b][m][n] = (f32x4){0.f, 0.f, 0.f, 0.f};
;         cur = nxt; cA = nA; cB = nB; ++ui;
;         if constexpr (sched_vark<Sched>::value) nt = S.nt(cur);
;         if constexpr (ALIGN_EPI) { if (wr == 1) PG8_BAR; }
;     DI void operator()(const f32x4 (&acc)[2][2][4][2], const Unit& u, int wr, int wc, int fr, int fq) const {
;     ...
;             for (int m = 0; m < 4; ++m) { const size_t r = (size_t)(row0 + ai * HALF + m * 16);
; #pragma unroll
;                 for (int bj = 0; bj < 2; ++bj) { const size_t o = r * D_ + col0 + bj * HALF; f32x4 x0, x1; unpack8f(*(const u32x4*)(R0 + o), x0, x1);
;                     f32x4 v0 = ALPHA * x0 + acc[ai][bj][m][0], v1 = ALPHA * x1 + acc[ai][bj][m][1];
;                     if (HAS_R1) { f32x4 q0, q1; unpack8f(*(const u32x4*)(R1 + o), q0, q1); v0 = v0 + q0; v1 = v1 + q1; }
;                     u32x4 w; w.x = cvt_pk_bf16(v0[0], v0[1]); w.y = cvt_pk_bf16(v0[2], v0[3]); w.z = cvt_pk_bf16(v1[0], v1[1]); w.w = cvt_pk_bf16(v1[2], v1[3]);
;                     *(u32x4*)(Yo + o) = w; }
;                 if (m & 1) asm volatile("" ::: "memory"); }
;     }
	v_lshlrev_b32_e32 v64, 16, v48
	v_and_b32_e32 v65, 0xffff0000, v48
	v_lshlrev_b32_e32 v48, 16, v49
	v_and_b32_e32 v49, 0xffff0000, v49
	v_lshlrev_b32_e32 v66, 16, v50
	v_and_b32_e32 v67, 0xffff0000, v50
	v_lshlrev_b32_e32 v50, 16, v51
	v_and_b32_e32 v51, 0xffff0000, v51
	s_waitcnt vmcnt(0)
	v_lshlrev_b32_e32 v68, 16, v52
	v_and_b32_e32 v69, 0xffff0000, v52
	v_lshlrev_b32_e32 v52, 16, v53
	v_and_b32_e32 v53, 0xffff0000, v53
	v_lshlrev_b32_e32 v70, 16, v54
	v_and_b32_e32 v71, 0xffff0000, v54
	v_lshlrev_b32_e32 v54, 16, v55
	v_and_b32_e32 v55, 0xffff0000, v55
	v_pk_fma_f32 v[46:47], v[48:49], s[16:17], v[46:47] op_sel_hi:[1,0,1]
	v_pk_fma_f32 v[44:45], v[64:65], s[16:17], v[44:45] op_sel_hi:[1,0,1]
	v_pk_fma_f32 v[42:43], v[50:51], s[16:17], v[42:43] op_sel_hi:[1,0,1]
	v_pk_fma_f32 v[40:41], v[66:67], s[16:17], v[40:41] op_sel_hi:[1,0,1]
	v_pk_fma_f32 v[38:39], v[52:53], s[16:17], v[38:39] op_sel_hi:[1,0,1]
	v_pk_fma_f32 v[36:37], v[68:69], s[16:17], v[36:37] op_sel_hi:[1,0,1]
	v_pk_fma_f32 v[48:49], v[54:55], s[16:17], v[34:35] op_sel_hi:[1,0,1]
	v_pk_fma_f32 v[50:51], v[70:71], s[16:17], v[32:33] op_sel_hi:[1,0,1]
	v_cvt_pk_bf16_f32 v32, v44, v45
	v_cvt_pk_bf16_f32 v33, v46, v47
	v_cvt_pk_bf16_f32 v34, v40, v41
	v_cvt_pk_bf16_f32 v35, v42, v43
	v_cvt_pk_bf16_f32 v36, v36, v37
	v_cvt_pk_bf16_f32 v37, v38, v39
	v_cvt_pk_bf16_f32 v38, v50, v51
	v_cvt_pk_bf16_f32 v39, v48, v49
	global_store_dwordx4 v[60:61], v[32:35], off
	global_store_dwordx4 v[56:57], v[36:39], off
	v_lshl_add_u64 v[40:41], v[132:133], 0, s[48:49]
	global_load_dwordx4 v[32:35], v[62:63], off
	v_lshl_add_u64 v[36:37], s[10:11], 0, v[40:41]
	global_load_dwordx4 v[36:39], v[36:37], off
	v_lshl_add_u64 v[42:43], v[132:133], 0, s[50:51]
	v_lshl_add_u64 v[44:45], s[12:13], 0, v[58:59]
	v_lshl_add_u64 v[40:41], s[12:13], 0, v[40:41]
	v_lshl_add_u64 v[46:47], s[10:11], 0, v[42:43]
	s_waitcnt vmcnt(1)
	v_lshlrev_b32_e32 v48, 16, v32
	v_and_b32_e32 v49, 0xffff0000, v32
	v_lshlrev_b32_e32 v32, 16, v33
	v_and_b32_e32 v33, 0xffff0000, v33
	v_lshlrev_b32_e32 v50, 16, v34
	v_and_b32_e32 v51, 0xffff0000, v34
	v_lshlrev_b32_e32 v34, 16, v35
	v_and_b32_e32 v35, 0xffff0000, v35
	s_waitcnt vmcnt(0)
	v_lshlrev_b32_e32 v52, 16, v36
	v_and_b32_e32 v53, 0xffff0000, v36
	v_lshlrev_b32_e32 v36, 16, v37
	v_and_b32_e32 v37, 0xffff0000, v37
	v_lshlrev_b32_e32 v54, 16, v38
	v_and_b32_e32 v55, 0xffff0000, v38
	v_lshlrev_b32_e32 v38, 16, v39
	v_and_b32_e32 v39, 0xffff0000, v39
	v_pk_fma_f32 v[30:31], v[32:33], s[16:17], v[30:31] op_sel_hi:[1,0,1]
	v_pk_fma_f32 v[28:29], v[48:49], s[16:17], v[28:29] op_sel_hi:[1,0,1]
	v_pk_fma_f32 v[26:27], v[34:35], s[16:17], v[26:27] op_sel_hi:[1,0,1]
	v_pk_fma_f32 v[24:25], v[50:51], s[16:17], v[24:25] op_sel_hi:[1,0,1]
	v_pk_fma_f32 v[22:23], v[36:37], s[16:17], v[22:23] op_sel_hi:[1,0,1]
	v_pk_fma_f32 v[20:21], v[52:53], s[16:17], v[20:21] op_sel_hi:[1,0,1]
	v_pk_fma_f32 v[32:33], v[38:39], s[16:17], v[18:19] op_sel_hi:[1,0,1]
	v_pk_fma_f32 v[34:35], v[54:55], s[16:17], v[16:17] op_sel_hi:[1,0,1]
	v_cvt_pk_bf16_f32 v16, v28, v29
	v_cvt_pk_bf16_f32 v17, v30, v31
	v_cvt_pk_bf16_f32 v18, v24, v25
	v_cvt_pk_bf16_f32 v19, v26, v27
	v_cvt_pk_bf16_f32 v20, v20, v21
	v_cvt_pk_bf16_f32 v21, v22, v23
	v_cvt_pk_bf16_f32 v22, v34, v35
	v_cvt_pk_bf16_f32 v23, v32, v33
	global_store_dwordx4 v[44:45], v[16:19], off
	global_store_dwordx4 v[40:41], v[20:23], off
	v_lshl_add_u64 v[24:25], v[132:133], 0, s[52:53]
	global_load_dwordx4 v[16:19], v[46:47], off
	v_lshl_add_u64 v[20:21], s[10:11], 0, v[24:25]
	global_load_dwordx4 v[20:23], v[20:21], off
	v_lshl_add_u64 v[26:27], s[12:13], 0, v[42:43]
	v_lshl_add_u64 v[24:25], s[12:13], 0, v[24:25]
	s_waitcnt vmcnt(1)
	v_lshlrev_b32_e32 v28, 16, v16
	v_and_b32_e32 v29, 0xffff0000, v16
	v_lshlrev_b32_e32 v16, 16, v17
	v_and_b32_e32 v17, 0xffff0000, v17
	v_lshlrev_b32_e32 v30, 16, v18
	v_and_b32_e32 v31, 0xffff0000, v18
	v_lshlrev_b32_e32 v18, 16, v19
	v_and_b32_e32 v19, 0xffff0000, v19
	s_waitcnt vmcnt(0)
	v_lshlrev_b32_e32 v32, 16, v20
	v_and_b32_e32 v33, 0xffff0000, v20
	v_lshlrev_b32_e32 v20, 16, v21
	v_and_b32_e32 v21, 0xffff0000, v21
	v_lshlrev_b32_e32 v34, 16, v22
	v_and_b32_e32 v35, 0xffff0000, v22
	v_lshlrev_b32_e32 v22, 16, v23
	v_and_b32_e32 v23, 0xffff0000, v23
	v_pk_fma_f32 v[14:15], v[16:17], s[16:17], v[14:15] op_sel_hi:[1,0,1]
	v_pk_fma_f32 v[12:13], v[28:29], s[16:17], v[12:13] op_sel_hi:[1,0,1]
	v_pk_fma_f32 v[10:11], v[18:19], s[16:17], v[10:11] op_sel_hi:[1,0,1]
	v_pk_fma_f32 v[8:9], v[30:31], s[16:17], v[8:9] op_sel_hi:[1,0,1]
	v_pk_fma_f32 v[6:7], v[20:21], s[16:17], v[6:7] op_sel_hi:[1,0,1]
	v_pk_fma_f32 v[4:5], v[32:33], s[16:17], v[4:5] op_sel_hi:[1,0,1]
	v_pk_fma_f32 v[16:17], v[22:23], s[16:17], v[2:3] op_sel_hi:[1,0,1]
	v_pk_fma_f32 v[18:19], v[34:35], s[16:17], v[0:1] op_sel_hi:[1,0,1]
	v_cvt_pk_bf16_f32 v0, v12, v13
	v_cvt_pk_bf16_f32 v1, v14, v15
	v_cvt_pk_bf16_f32 v2, v8, v9
	v_cvt_pk_bf16_f32 v3, v10, v11
	v_cvt_pk_bf16_f32 v4, v4, v5
	v_cvt_pk_bf16_f32 v5, v6, v7
	v_cvt_pk_bf16_f32 v6, v18, v19
	v_cvt_pk_bf16_f32 v7, v16, v17
	global_store_dwordx4 v[26:27], v[0:3], off
	global_store_dwordx4 v[24:25], v[4:7], off
	s_cbranch_vccnz .LBB0_1297
	s_andn2_b64 vcc, exec, s[8:9]
	s_cbranch_vccnz .LBB0_1296
	s_barrier
	s_branch .LBB0_1296

; #define PG8_STAGE(bufoff, gbase, voff) do { _Pragma("unroll") for (int _i = 0; _i < 2; ++_i) { unsigned keep_; \
;         asm volatile("s_mov_b32 %0, m0\n\ts_mov_b32 m0, %3\n\ts_nop 0\n\tglobal_load_lds_dwordx4 %1, %2\n\ts_mov_b32 m0, %0" : "=&s"(keep_) : "v"((voff)[_i]), "s"((const char*)(gbase)), "s"(ldsbase + (unsigned)((bufoff) + _i * 8192)) : "memory"); } } while (0)
; #define PG8_WAIT_V(n) asm volatile("s_waitcnt vmcnt(" #n ")" ::: "memory")
; #define PG8_WAIT_L(n) asm volatile("s_waitcnt lgkmcnt(" #n ")" ::: "memory")
; #define PG8_BAR __builtin_amdgcn_s_barrier()
; #define PG8_SCHED __builtin_amdgcn_sched_barrier(0)
;     DI int nt(const Unit& u) const { return (u.aux & 8) ? PLED / 64 : ((u.aux & 4) ? (D_ / 2) / 64 : D_ / 64); }
; template <class Epi, class Sched, bool ALIGN_EPI, bool FP8 = false>
; DI void gemm_phase(LAS unsigned char* lds, const Gemm g, const Sched& S, const Epi& E) {
;     ...
;             const bool last = (t == nt - 2);
;             const char* a1 = cA + (size_t)(t + 1) * kstep;
;             const char* a2 = last ? nA : cA + (size_t)(t + 2) * kstep; const char* b2 = last ? nB : cB + (size_t)(t + 2) * kstep;
;             const char* a3 = a2 + kstep; const char* b3 = b2 + kstep;
;             PG8_LDB(B0, 0, 0); PG8_LDB(B1, 0, 1); PG8_SCHED; PG8_LDA(At, 0, 0); PG8_STAGE(PG8_SA(1, 1), a1 + hstepA, voffA);
;             PG8_WAIT_V(8); PG8_WAIT_L(0); PG8_BAR; PG8_MMA(0, 0, At, B0); PG8_MMA(0, 1, At, B1); PG8_BAR; PG8_SCHED;
;             PG8_LDA(At, 0, 1); PG8_STAGE(PG8_SB(0, 0), b2, voffB); PG8_STAGE(PG8_SB(0, 1), b2 + hstepB, voffB); PG8_STAGE(PG8_SA(0, 0), a2, voffA);
;             PG8_WAIT_V(8); PG8_WAIT_L(0); PG8_BAR; PG8_MMA(1, 0, At, B0); PG8_MMA(1, 1, At, B1); PG8_BAR; PG8_SCHED;
.LBB0_1608:
	s_cmp_lg_u32 s99, 0
	s_cbranch_scc1 .Lmy_g0_1608
	ds_read_b128 v[144:147], v133
	ds_read_b128 v[148:151], v133 offset:16
	ds_read_b128 v[152:155], v133 offset:2048
	ds_read_b128 v[156:159], v133 offset:2064
	ds_read_b128 v[160:163], v133 offset:16384
	ds_read_b128 v[164:167], v133 offset:16400
	ds_read_b128 v[168:171], v133 offset:18432
	ds_read_b128 v[172:175], v133 offset:18448
	s_add_u32 s6, s26, 0x100
	s_addc_u32 s7, s27, 0
	s_cmp_eq_u32 s70, 12
	s_cselect_b32 s42, s17, s6
	s_cselect_b32 s43, s15, s7
	s_cselect_b32 s40, s18, s68
	s_cselect_b32 s41, s19, s69
	s_add_u32 s28, s42, 0x80
	s_addc_u32 s29, s43, 0
	ds_read_b128 v[176:179], v132
	ds_read_b128 v[180:183], v132 offset:16
	ds_read_b128 v[184:187], v132 offset:2048
	ds_read_b128 v[188:191], v132 offset:2064
	ds_read_b128 v[192:195], v132 offset:4096
	ds_read_b128 v[196:199], v132 offset:4112
	ds_read_b128 v[200:203], v132 offset:6144
	ds_read_b128 v[204:207], v132 offset:6160
	s_add_u32 s26, s26, 0x40080
	s_addc_u32 s27, s27, 0
	s_mov_b32 s71, m0
	s_mov_b32 m0, s62
	s_nop 0
	global_load_lds_dwordx4 v134, s[26:27]
	s_mov_b32 m0, s71
	s_nop 0
	s_mov_b32 s71, m0
	s_mov_b32 m0, s63
	s_nop 0
	global_load_lds_dwordx4 v136, s[26:27]
	s_mov_b32 m0, s71
	s_waitcnt vmcnt(8)
	s_waitcnt lgkmcnt(0)
	s_mov_b64 exec, 1
	ds_add_u32 v255, v255 offset:4096
	s_mov_b64 exec, -1
	s_setprio 1
	v_mfma_scale_f32_16x16x128_f8f6f4 v[124:127], v[144:151], v[176:183], v[124:127], v140, v140 op_sel_hi:[0,0,0]
	v_mfma_scale_f32_16x16x128_f8f6f4 v[120:123], v[152:159], v[176:183], v[120:123], v140, v140 op_sel_hi:[0,0,0]
	v_mfma_scale_f32_16x16x128_f8f6f4 v[108:111], v[144:151], v[184:191], v[108:111], v140, v140 op_sel_hi:[0,0,0]
	v_mfma_scale_f32_16x16x128_f8f6f4 v[104:107], v[152:159], v[184:191], v[104:107], v140, v140 op_sel_hi:[0,0,0]
	v_mfma_scale_f32_16x16x128_f8f6f4 v[208:211], v[144:151], v[192:199], v[92:95], v140, v140 op_sel_hi:[0,0,0]
	v_mfma_scale_f32_16x16x128_f8f6f4 v[212:215], v[152:159], v[192:199], v[88:91], v140, v140 op_sel_hi:[0,0,0]
	v_mfma_scale_f32_16x16x128_f8f6f4 v[216:219], v[144:151], v[200:207], v[76:79], v140, v140 op_sel_hi:[0,0,0]
	v_mfma_scale_f32_16x16x128_f8f6f4 v[220:223], v[152:159], v[200:207], v[72:75], v140, v140 op_sel_hi:[0,0,0]
	v_mfma_scale_f32_16x16x128_f8f6f4 v[116:119], v[160:167], v[176:183], v[116:119], v141, v140 op_sel_hi:[0,0,0]
	v_mfma_scale_f32_16x16x128_f8f6f4 v[112:115], v[168:175], v[176:183], v[112:115], v141, v140 op_sel_hi:[0,0,0]
	v_mfma_scale_f32_16x16x128_f8f6f4 v[100:103], v[160:167], v[184:191], v[100:103], v141, v140 op_sel_hi:[0,0,0]
	v_mfma_scale_f32_16x16x128_f8f6f4 v[96:99], v[168:175], v[184:191], v[96:99], v141, v140 op_sel_hi:[0,0,0]
	v_mfma_scale_f32_16x16x128_f8f6f4 v[176:179], v[160:167], v[192:199], v[84:87], v141, v140 op_sel_hi:[0,0,0]
	v_mfma_scale_f32_16x16x128_f8f6f4 v[180:183], v[168:175], v[192:199], v[80:83], v141, v140 op_sel_hi:[0,0,0]
	v_mfma_scale_f32_16x16x128_f8f6f4 v[184:187], v[160:167], v[200:207], v[68:71], v141, v140 op_sel_hi:[0,0,0]
	v_mfma_scale_f32_16x16x128_f8f6f4 v[188:191], v[168:175], v[200:207], v[64:67], v141, v140 op_sel_hi:[0,0,0]
	s_setprio 0
	s_barrier
	s_nop 4
	ds_read_b128 v[64:67], v132 offset:16384
	ds_read_b128 v[68:71], v132 offset:16400
	ds_read_b128 v[72:75], v132 offset:18432
	ds_read_b128 v[76:79], v132 offset:18448
	ds_read_b128 v[80:83], v132 offset:20480
	ds_read_b128 v[84:87], v132 offset:20496
	ds_read_b128 v[88:91], v132 offset:22528
	ds_read_b128 v[92:95], v132 offset:22544
	s_mov_b32 s26, m0
	s_mov_b32 m0, s23
	s_nop 0
	global_load_lds_dwordx4 v135, s[40:41]
	s_mov_b32 m0, s26
	s_nop 0
	s_mov_b32 s26, m0
	s_mov_b32 m0, s25
	s_nop 0
	global_load_lds_dwordx4 v137, s[40:41]
	s_mov_b32 m0, s26
	s_add_u32 s26, s40, 0x40000
	s_addc_u32 s27, s41, 0
	s_mov_b32 s71, m0
	s_mov_b32 m0, s48
	s_nop 0
	global_load_lds_dwordx4 v135, s[26:27]
	s_mov_b32 m0, s71
	s_nop 0
	s_mov_b32 s71, m0
	s_mov_b32 m0, s49
	s_nop 0
	global_load_lds_dwordx4 v137, s[26:27]
	s_mov_b32 m0, s71
	s_mov_b32 s26, m0
	s_mov_b32 m0, s44
	s_nop 0
	global_load_lds_dwordx4 v134, s[42:43]
	s_mov_b32 m0, s26
	s_nop 0
	s_mov_b32 s26, m0
	s_mov_b32 m0, s50
	s_nop 0
	global_load_lds_dwordx4 v136, s[42:43]
	s_mov_b32 m0, s26
	s_waitcnt vmcnt(8)
	s_waitcnt lgkmcnt(0)
	s_mov_b64 exec, 1
	ds_add_u32 v255, v255 offset:4096
	s_mov_b64 exec, -1
	s_setprio 1
	v_mfma_scale_f32_16x16x128_f8f6f4 v[60:63], v[144:151], v[64:71], v[60:63], v140, v140 op_sel_hi:[0,0,0]
	v_mfma_scale_f32_16x16x128_f8f6f4 v[56:59], v[152:159], v[64:71], v[56:59], v140, v140 op_sel_hi:[0,0,0]
	v_mfma_scale_f32_16x16x128_f8f6f4 v[192:195], v[144:151], v[72:79], v[44:47], v140, v140 op_sel_hi:[0,0,0]
	v_mfma_scale_f32_16x16x128_f8f6f4 v[196:199], v[152:159], v[72:79], v[40:43], v140, v140 op_sel_hi:[0,0,0]
	v_mfma_scale_f32_16x16x128_f8f6f4 v[200:203], v[144:151], v[80:87], v[28:31], v140, v140 op_sel_hi:[0,0,0]
	v_mfma_scale_f32_16x16x128_f8f6f4 v[204:207], v[152:159], v[80:87], v[24:27], v140, v140 op_sel_hi:[0,0,0]
	v_mfma_scale_f32_16x16x128_f8f6f4 v[224:227], v[144:151], v[88:95], v[12:15], v140, v140 op_sel_hi:[0,0,0]
	v_mfma_scale_f32_16x16x128_f8f6f4 v[228:231], v[152:159], v[88:95], v[8:11], v140, v140 op_sel_hi:[0,0,0]
	v_mfma_scale_f32_16x16x128_f8f6f4 v[52:55], v[160:167], v[64:71], v[52:55], v141, v140 op_sel_hi:[0,0,0]
	v_mfma_scale_f32_16x16x128_f8f6f4 v[48:51], v[168:175], v[64:71], v[48:51], v141, v140 op_sel_hi:[0,0,0]
	v_mfma_scale_f32_16x16x128_f8f6f4 v[232:235], v[160:167], v[72:79], v[36:39], v141, v140 op_sel_hi:[0,0,0]
	v_mfma_scale_f32_16x16x128_f8f6f4 v[236:239], v[168:175], v[72:79], v[32:35], v141, v140 op_sel_hi:[0,0,0]
	v_mfma_scale_f32_16x16x128_f8f6f4 v[240:243], v[160:167], v[80:87], v[20:23], v141, v140 op_sel_hi:[0,0,0]
	v_mfma_scale_f32_16x16x128_f8f6f4 v[244:247], v[168:175], v[80:87], v[16:19], v141, v140 op_sel_hi:[0,0,0]
	v_mfma_scale_f32_16x16x128_f8f6f4 v[248:251], v[160:167], v[88:95], v[4:7], v141, v140 op_sel_hi:[0,0,0]
	v_mfma_scale_f32_16x16x128_f8f6f4 v[128:131], v[168:175], v[88:95], v[0:3], v141, v140 op_sel_hi:[0,0,0]
	s_setprio 0
	s_barrier
; #define PG8_STAGE(bufoff, gbase, voff) do { _Pragma("unroll") for (int _i = 0; _i < 2; ++_i) { unsigned keep_; \
;         asm volatile("s_mov_b32 %0, m0\n\ts_mov_b32 m0, %3\n\ts_nop 0\n\tglobal_load_lds_dwordx4 %1, %2\n\ts_mov_b32 m0, %0" : "=&s"(keep_) : "v"((voff)[_i]), "s"((const char*)(gbase)), "s"(ldsbase + (unsigned)((bufoff) + _i * 8192)) : "memory"); } } while (0)
; #define PG8_WAIT_V(n) asm volatile("s_waitcnt vmcnt(" #n ")" ::: "memory")
; #define PG8_WAIT_L(n) asm volatile("s_waitcnt lgkmcnt(" #n ")" ::: "memory")
; #define PG8_BAR __builtin_amdgcn_s_barrier()
; #define PG8_SCHED __builtin_amdgcn_sched_barrier(0)
; template <class Epi, class Sched, bool ALIGN_EPI, bool FP8 = false>
; DI void gemm_phase(LAS unsigned char* lds, const Gemm g, const Sched& S, const Epi& E) {
;     ...
;             PG8_LDB(B0, 1, 0); PG8_LDB(B1, 1, 1); PG8_SCHED; PG8_LDA(At, 1, 0); PG8_STAGE(PG8_SA(0, 1), a2 + hstepA, voffA);
;             PG8_WAIT_V(8); PG8_WAIT_L(0); PG8_BAR; PG8_MMA(0, 0, At, B0); PG8_MMA(0, 1, At, B1); PG8_BAR; PG8_SCHED;
;             PG8_LDA(At, 1, 1); PG8_STAGE(PG8_SB(1, 0), b3, voffB); PG8_STAGE(PG8_SB(1, 1), b3 + hstepB, voffB); PG8_STAGE(PG8_SA(1, 0), a3, voffA);
;             PG8_WAIT_V(8); PG8_WAIT_L(0); PG8_BAR; PG8_MMA(1, 0, At, B0); PG8_MMA(1, 1, At, B1); PG8_BAR; PG8_SCHED;
;         }
	s_nop 4
	ds_read_b128 v[0:3], v133 offset:32768
	ds_read_b128 v[4:7], v133 offset:32784
	ds_read_b128 v[16:19], v133 offset:34816
	ds_read_b128 v[20:23], v133 offset:34832
	ds_read_b128 v[144:147], v133 offset:49152
	ds_read_b128 v[148:151], v133 offset:49168
	ds_read_b128 v[152:155], v133 offset:51200
	ds_read_b128 v[156:159], v133 offset:51216
	ds_read_b128 v[8:11], v132 offset:32768
	ds_read_b128 v[12:15], v132 offset:32784
	ds_read_b128 v[24:27], v132 offset:34816
	ds_read_b128 v[28:31], v132 offset:34832
	ds_read_b128 v[32:35], v132 offset:36864
	ds_read_b128 v[36:39], v132 offset:36880
	ds_read_b128 v[40:43], v132 offset:38912
	ds_read_b128 v[44:47], v132 offset:38928
	s_add_u32 s26, s42, 0x40000
	s_addc_u32 s27, s43, 0
	s_mov_b32 s42, m0
	s_mov_b32 m0, s51
	s_nop 0
	global_load_lds_dwordx4 v134, s[26:27]
	s_mov_b32 m0, s42
	s_nop 0
	s_mov_b32 s42, m0
	s_mov_b32 m0, s52
	s_nop 0
	global_load_lds_dwordx4 v136, s[26:27]
	s_mov_b32 m0, s42
	s_waitcnt vmcnt(8)
	s_waitcnt lgkmcnt(0)
	s_mov_b64 exec, 1
	ds_add_u32 v255, v255 offset:4096
	s_mov_b64 exec, -1
	s_setprio 1
	v_mfma_scale_f32_16x16x128_f8f6f4 v[124:127], v[0:7], v[8:15], v[124:127], v140, v140 op_sel_hi:[0,0,0]
	v_mfma_scale_f32_16x16x128_f8f6f4 v[120:123], v[16:23], v[8:15], v[120:123], v140, v140 op_sel_hi:[0,0,0]
	v_mfma_scale_f32_16x16x128_f8f6f4 v[108:111], v[0:7], v[24:31], v[108:111], v140, v140 op_sel_hi:[0,0,0]
	v_mfma_scale_f32_16x16x128_f8f6f4 v[104:107], v[16:23], v[24:31], v[104:107], v140, v140 op_sel_hi:[0,0,0]
	v_mfma_scale_f32_16x16x128_f8f6f4 v[92:95], v[0:7], v[32:39], v[208:211], v140, v140 op_sel_hi:[0,0,0]
	v_mfma_scale_f32_16x16x128_f8f6f4 v[88:91], v[16:23], v[32:39], v[212:215], v140, v140 op_sel_hi:[0,0,0]
	v_mfma_scale_f32_16x16x128_f8f6f4 v[76:79], v[0:7], v[40:47], v[216:219], v140, v140 op_sel_hi:[0,0,0]
	v_mfma_scale_f32_16x16x128_f8f6f4 v[72:75], v[16:23], v[40:47], v[220:223], v140, v140 op_sel_hi:[0,0,0]
	v_mfma_scale_f32_16x16x128_f8f6f4 v[116:119], v[144:151], v[8:15], v[116:119], v141, v140 op_sel_hi:[0,0,0]
	v_mfma_scale_f32_16x16x128_f8f6f4 v[112:115], v[152:159], v[8:15], v[112:115], v141, v140 op_sel_hi:[0,0,0]
	v_mfma_scale_f32_16x16x128_f8f6f4 v[100:103], v[144:151], v[24:31], v[100:103], v141, v140 op_sel_hi:[0,0,0]
	v_mfma_scale_f32_16x16x128_f8f6f4 v[96:99], v[152:159], v[24:31], v[96:99], v141, v140 op_sel_hi:[0,0,0]
	v_mfma_scale_f32_16x16x128_f8f6f4 v[84:87], v[144:151], v[32:39], v[176:179], v141, v140 op_sel_hi:[0,0,0]
	v_mfma_scale_f32_16x16x128_f8f6f4 v[80:83], v[152:159], v[32:39], v[180:183], v141, v140 op_sel_hi:[0,0,0]
	v_mfma_scale_f32_16x16x128_f8f6f4 v[68:71], v[144:151], v[40:47], v[184:187], v141, v140 op_sel_hi:[0,0,0]
	v_mfma_scale_f32_16x16x128_f8f6f4 v[64:67], v[152:159], v[40:47], v[188:191], v141, v140 op_sel_hi:[0,0,0]
	s_setprio 0
	s_barrier
	ds_read_b128 v[32:35], v132 offset:49152
	ds_read_b128 v[36:39], v132 offset:49168
	ds_read_b128 v[160:163], v132 offset:51200
	ds_read_b128 v[164:167], v132 offset:51216
	ds_read_b128 v[168:171], v132 offset:53248
	ds_read_b128 v[172:175], v132 offset:53264
	ds_read_b128 v[176:179], v132 offset:55296
	ds_read_b128 v[180:183], v132 offset:55312
	s_add_u32 s26, s40, 0x80
	s_addc_u32 s27, s41, 0
	s_mov_b32 s42, m0
	s_mov_b32 m0, s56
	s_nop 0
	global_load_lds_dwordx4 v135, s[26:27]
	s_mov_b32 m0, s42
	s_nop 0
	s_mov_b32 s42, m0
	s_mov_b32 m0, s57
	s_nop 0
	global_load_lds_dwordx4 v137, s[26:27]
	s_mov_b32 m0, s42
	s_add_u32 s26, s40, 0x40080
	s_addc_u32 s27, s41, 0
	s_mov_b32 s40, m0
	s_mov_b32 m0, s60
	s_nop 0
	global_load_lds_dwordx4 v135, s[26:27]
	s_mov_b32 m0, s40
	s_nop 0
	s_mov_b32 s40, m0
	s_mov_b32 m0, s61
	s_nop 0
	global_load_lds_dwordx4 v137, s[26:27]
	s_mov_b32 m0, s40
	s_mov_b32 s26, m0
	s_mov_b32 m0, s58
	s_nop 0
	global_load_lds_dwordx4 v134, s[28:29]
	s_mov_b32 m0, s26
	s_nop 0
	s_mov_b32 s26, m0
	s_mov_b32 m0, s59
	s_nop 0
	global_load_lds_dwordx4 v136, s[28:29]
	s_mov_b32 m0, s26
	s_waitcnt vmcnt(8)
	s_waitcnt lgkmcnt(0)
	s_mov_b64 exec, 1
	ds_add_u32 v255, v255 offset:4096
	s_mov_b64 exec, -1
	s_setprio 1
	v_mfma_scale_f32_16x16x128_f8f6f4 v[60:63], v[0:7], v[32:39], v[60:63], v140, v140 op_sel_hi:[0,0,0]
	v_mfma_scale_f32_16x16x128_f8f6f4 v[56:59], v[16:23], v[32:39], v[56:59], v140, v140 op_sel_hi:[0,0,0]
	v_mfma_scale_f32_16x16x128_f8f6f4 v[44:47], v[0:7], v[160:167], v[192:195], v140, v140 op_sel_hi:[0,0,0]
	v_mfma_scale_f32_16x16x128_f8f6f4 v[40:43], v[16:23], v[160:167], v[196:199], v140, v140 op_sel_hi:[0,0,0]
	v_mfma_scale_f32_16x16x128_f8f6f4 v[28:31], v[0:7], v[168:175], v[200:203], v140, v140 op_sel_hi:[0,0,0]
	v_mfma_scale_f32_16x16x128_f8f6f4 v[24:27], v[16:23], v[168:175], v[204:207], v140, v140 op_sel_hi:[0,0,0]
	v_mfma_scale_f32_16x16x128_f8f6f4 v[12:15], v[0:7], v[176:183], v[224:227], v140, v140 op_sel_hi:[0,0,0]
	v_mfma_scale_f32_16x16x128_f8f6f4 v[8:11], v[16:23], v[176:183], v[228:231], v140, v140 op_sel_hi:[0,0,0]
	v_mfma_scale_f32_16x16x128_f8f6f4 v[52:55], v[144:151], v[32:39], v[52:55], v141, v140 op_sel_hi:[0,0,0]
	v_mfma_scale_f32_16x16x128_f8f6f4 v[48:51], v[152:159], v[32:39], v[48:51], v141, v140 op_sel_hi:[0,0,0]
	v_mfma_scale_f32_16x16x128_f8f6f4 v[36:39], v[144:151], v[160:167], v[232:235], v141, v140 op_sel_hi:[0,0,0]
	v_mfma_scale_f32_16x16x128_f8f6f4 v[32:35], v[152:159], v[160:167], v[236:239], v141, v140 op_sel_hi:[0,0,0]
	v_mfma_scale_f32_16x16x128_f8f6f4 v[20:23], v[144:151], v[168:175], v[240:243], v141, v140 op_sel_hi:[0,0,0]
	v_mfma_scale_f32_16x16x128_f8f6f4 v[16:19], v[152:159], v[168:175], v[244:247], v141, v140 op_sel_hi:[0,0,0]
	v_mfma_scale_f32_16x16x128_f8f6f4 v[4:7], v[144:151], v[176:183], v[248:251], v141, v140 op_sel_hi:[0,0,0]
	v_mfma_scale_f32_16x16x128_f8f6f4 v[0:3], v[152:159], v[176:183], v[128:131], v141, v140 op_sel_hi:[0,0,0]
	s_setprio 0
	s_barrier
	s_add_i32 s70, s70, 2
	s_add_u32 s68, s68, 0x100
	s_addc_u32 s69, s69, 0
	s_cmp_gt_u32 s70, 13
	s_mov_b64 s[26:27], s[6:7]
	s_cbranch_scc0 .LBB0_1608
	s_branch .Lmy_ex_1608
; #define PG8_STAGE(bufoff, gbase, voff) do { _Pragma("unroll") for (int _i = 0; _i < 2; ++_i) { unsigned keep_; \
;         asm volatile("s_mov_b32 %0, m0\n\ts_mov_b32 m0, %3\n\ts_nop 0\n\tglobal_load_lds_dwordx4 %1, %2\n\ts_mov_b32 m0, %0" : "=&s"(keep_) : "v"((voff)[_i]), "s"((const char*)(gbase)), "s"(ldsbase + (unsigned)((bufoff) + _i * 8192)) : "memory"); } } while (0)
; #define PG8_WAIT_V(n) asm volatile("s_waitcnt vmcnt(" #n ")" ::: "memory")
; #define PG8_WAIT_L(n) asm volatile("s_waitcnt lgkmcnt(" #n ")" ::: "memory")
; #define PG8_BAR __builtin_amdgcn_s_barrier()
; #define PG8_SCHED __builtin_amdgcn_sched_barrier(0)
;     DI int nt(const Unit& u) const { return (u.aux & 8) ? PLED / 64 : ((u.aux & 4) ? (D_ / 2) / 64 : D_ / 64); }
; template <class Epi, class Sched, bool ALIGN_EPI, bool FP8 = false>
; DI void gemm_phase(LAS unsigned char* lds, const Gemm g, const Sched& S, const Epi& E) {
;     ...
;             const bool last = (t == nt - 2);
;             const char* a1 = cA + (size_t)(t + 1) * kstep;
;             const char* a2 = last ? nA : cA + (size_t)(t + 2) * kstep; const char* b2 = last ? nB : cB + (size_t)(t + 2) * kstep;
;             const char* a3 = a2 + kstep; const char* b3 = b2 + kstep;
;             PG8_LDB(B0, 0, 0); PG8_LDB(B1, 0, 1); PG8_SCHED; PG8_LDA(At, 0, 0); PG8_STAGE(PG8_SA(1, 1), a1 + hstepA, voffA);
;             PG8_WAIT_V(8); PG8_WAIT_L(0); PG8_BAR; PG8_MMA(0, 0, At, B0); PG8_MMA(0, 1, At, B1); PG8_BAR; PG8_SCHED;
.Lmy_g0_1608:
	ds_read_b128 v[144:147], v133
	ds_read_b128 v[148:151], v133 offset:16
	ds_read_b128 v[152:155], v133 offset:2048
	ds_read_b128 v[156:159], v133 offset:2064
	ds_read_b128 v[160:163], v133 offset:16384
	ds_read_b128 v[164:167], v133 offset:16400
	ds_read_b128 v[168:171], v133 offset:18432
	ds_read_b128 v[172:175], v133 offset:18448
	s_add_u32 s6, s26, 0x100
	s_addc_u32 s7, s27, 0
	s_cmp_eq_u32 s70, 12
	s_cselect_b32 s42, s17, s6
	s_cselect_b32 s43, s15, s7
	s_cselect_b32 s40, s18, s68
	s_cselect_b32 s41, s19, s69
	s_add_u32 s28, s42, 0x80
	s_addc_u32 s29, s43, 0
	ds_read_b128 v[176:179], v132
	ds_read_b128 v[180:183], v132 offset:16
	ds_read_b128 v[184:187], v132 offset:2048
	ds_read_b128 v[188:191], v132 offset:2064
	ds_read_b128 v[192:195], v132 offset:4096
	ds_read_b128 v[196:199], v132 offset:4112
	ds_read_b128 v[200:203], v132 offset:6144
	ds_read_b128 v[204:207], v132 offset:6160
	s_add_u32 s26, s26, 0x40080
	s_addc_u32 s27, s27, 0
	s_mov_b32 s71, m0
	s_mov_b32 m0, s62
	s_nop 0
	global_load_lds_dwordx4 v134, s[26:27]
	s_mov_b32 m0, s71
	s_nop 0
	s_mov_b32 s71, m0
	s_mov_b32 m0, s63
	s_nop 0
	global_load_lds_dwordx4 v136, s[26:27]
	s_mov_b32 m0, s71
	s_waitcnt vmcnt(8)
	s_waitcnt lgkmcnt(0)
	s_barrier
	s_setprio 1
	v_mfma_scale_f32_16x16x128_f8f6f4 v[124:127], v[144:151], v[176:183], v[124:127], v140, v140 op_sel_hi:[0,0,0]
	v_mfma_scale_f32_16x16x128_f8f6f4 v[120:123], v[152:159], v[176:183], v[120:123], v140, v140 op_sel_hi:[0,0,0]
	v_mfma_scale_f32_16x16x128_f8f6f4 v[108:111], v[144:151], v[184:191], v[108:111], v140, v140 op_sel_hi:[0,0,0]
	v_mfma_scale_f32_16x16x128_f8f6f4 v[104:107], v[152:159], v[184:191], v[104:107], v140, v140 op_sel_hi:[0,0,0]
	v_mfma_scale_f32_16x16x128_f8f6f4 v[208:211], v[144:151], v[192:199], v[92:95], v140, v140 op_sel_hi:[0,0,0]
	v_mfma_scale_f32_16x16x128_f8f6f4 v[212:215], v[152:159], v[192:199], v[88:91], v140, v140 op_sel_hi:[0,0,0]
	v_mfma_scale_f32_16x16x128_f8f6f4 v[216:219], v[144:151], v[200:207], v[76:79], v140, v140 op_sel_hi:[0,0,0]
	v_mfma_scale_f32_16x16x128_f8f6f4 v[220:223], v[152:159], v[200:207], v[72:75], v140, v140 op_sel_hi:[0,0,0]
	v_mfma_scale_f32_16x16x128_f8f6f4 v[116:119], v[160:167], v[176:183], v[116:119], v141, v140 op_sel_hi:[0,0,0]
	v_mfma_scale_f32_16x16x128_f8f6f4 v[112:115], v[168:175], v[176:183], v[112:115], v141, v140 op_sel_hi:[0,0,0]
	v_mfma_scale_f32_16x16x128_f8f6f4 v[100:103], v[160:167], v[184:191], v[100:103], v141, v140 op_sel_hi:[0,0,0]
	v_mfma_scale_f32_16x16x128_f8f6f4 v[96:99], v[168:175], v[184:191], v[96:99], v141, v140 op_sel_hi:[0,0,0]
	v_mfma_scale_f32_16x16x128_f8f6f4 v[176:179], v[160:167], v[192:199], v[84:87], v141, v140 op_sel_hi:[0,0,0]
	v_mfma_scale_f32_16x16x128_f8f6f4 v[180:183], v[168:175], v[192:199], v[80:83], v141, v140 op_sel_hi:[0,0,0]
	ds_read_b32 v255, v255 offset:4096
	v_mfma_scale_f32_16x16x128_f8f6f4 v[184:187], v[160:167], v[200:207], v[68:71], v141, v140 op_sel_hi:[0,0,0]
	v_mfma_scale_f32_16x16x128_f8f6f4 v[188:191], v[168:175], v[200:207], v[64:67], v141, v140 op_sel_hi:[0,0,0]
	s_add_u32 s98, s98, 0x80000
	s_waitcnt lgkmcnt(0)
	v_readfirstlane_b32 s101, v255
	v_mov_b32_e32 v255, 0x20000
	s_cmp_ge_u32 s101, s98
	s_cbranch_scc1 .Lmy_g_44

; #define PG8_STAGE(bufoff, gbase, voff) do { _Pragma("unroll") for (int _i = 0; _i < 2; ++_i) { unsigned keep_; \
;         asm volatile("s_mov_b32 %0, m0\n\ts_mov_b32 m0, %3\n\ts_nop 0\n\tglobal_load_lds_dwordx4 %1, %2\n\ts_mov_b32 m0, %0" : "=&s"(keep_) : "v"((voff)[_i]), "s"((const char*)(gbase)), "s"(ldsbase + (unsigned)((bufoff) + _i * 8192)) : "memory"); } } while (0)
; #define PG8_WAIT_V(n) asm volatile("s_waitcnt vmcnt(" #n ")" ::: "memory")
; #define PG8_WAIT_L(n) asm volatile("s_waitcnt lgkmcnt(" #n ")" ::: "memory")
; #define PG8_BAR __builtin_amdgcn_s_barrier()
; #define PG8_SCHED __builtin_amdgcn_sched_barrier(0)
; template <class Epi, class Sched, bool ALIGN_EPI, bool FP8 = false>
; DI void gemm_phase(LAS unsigned char* lds, const Gemm g, const Sched& S, const Epi& E) {
;     ...
;             PG8_LDA(At, 0, 1); PG8_STAGE(PG8_SB(0, 0), b2, voffB); PG8_STAGE(PG8_SB(0, 1), b2 + hstepB, voffB); PG8_STAGE(PG8_SA(0, 0), a2, voffA);
;             PG8_WAIT_V(8); PG8_WAIT_L(0); PG8_BAR; PG8_MMA(1, 0, At, B0); PG8_MMA(1, 1, At, B1); PG8_BAR; PG8_SCHED;
.Lmy_g_44:
	s_setprio 0
	s_nop 4
	ds_read_b128 v[64:67], v132 offset:16384
	ds_read_b128 v[68:71], v132 offset:16400
	ds_read_b128 v[72:75], v132 offset:18432
	ds_read_b128 v[76:79], v132 offset:18448
	ds_read_b128 v[80:83], v132 offset:20480
	ds_read_b128 v[84:87], v132 offset:20496
	ds_read_b128 v[88:91], v132 offset:22528
	ds_read_b128 v[92:95], v132 offset:22544
	s_mov_b32 s26, m0
	s_mov_b32 m0, s23
	s_nop 0
	global_load_lds_dwordx4 v135, s[40:41]
	s_mov_b32 m0, s26
	s_nop 0
	s_mov_b32 s26, m0
	s_mov_b32 m0, s25
	s_nop 0
	global_load_lds_dwordx4 v137, s[40:41]
	s_mov_b32 m0, s26
	s_add_u32 s26, s40, 0x40000
	s_addc_u32 s27, s41, 0
	s_mov_b32 s71, m0
	s_mov_b32 m0, s48
	s_nop 0
	global_load_lds_dwordx4 v135, s[26:27]
	s_mov_b32 m0, s71
	s_nop 0
	s_mov_b32 s71, m0
	s_mov_b32 m0, s49
	s_nop 0
	global_load_lds_dwordx4 v137, s[26:27]
	s_mov_b32 m0, s71
	s_mov_b32 s26, m0
	s_mov_b32 m0, s44
	s_nop 0
	global_load_lds_dwordx4 v134, s[42:43]
	s_mov_b32 m0, s26
	s_nop 0
	s_mov_b32 s26, m0
	s_mov_b32 m0, s50
	s_nop 0
	global_load_lds_dwordx4 v136, s[42:43]
	s_mov_b32 m0, s26
	s_waitcnt vmcnt(8)
	s_waitcnt lgkmcnt(0)
	s_barrier
	s_setprio 1
	v_mfma_scale_f32_16x16x128_f8f6f4 v[60:63], v[144:151], v[64:71], v[60:63], v140, v140 op_sel_hi:[0,0,0]
	v_mfma_scale_f32_16x16x128_f8f6f4 v[56:59], v[152:159], v[64:71], v[56:59], v140, v140 op_sel_hi:[0,0,0]
	v_mfma_scale_f32_16x16x128_f8f6f4 v[192:195], v[144:151], v[72:79], v[44:47], v140, v140 op_sel_hi:[0,0,0]
	v_mfma_scale_f32_16x16x128_f8f6f4 v[196:199], v[152:159], v[72:79], v[40:43], v140, v140 op_sel_hi:[0,0,0]
	v_mfma_scale_f32_16x16x128_f8f6f4 v[200:203], v[144:151], v[80:87], v[28:31], v140, v140 op_sel_hi:[0,0,0]
	v_mfma_scale_f32_16x16x128_f8f6f4 v[204:207], v[152:159], v[80:87], v[24:27], v140, v140 op_sel_hi:[0,0,0]
	v_mfma_scale_f32_16x16x128_f8f6f4 v[224:227], v[144:151], v[88:95], v[12:15], v140, v140 op_sel_hi:[0,0,0]
	v_mfma_scale_f32_16x16x128_f8f6f4 v[228:231], v[152:159], v[88:95], v[8:11], v140, v140 op_sel_hi:[0,0,0]
	v_mfma_scale_f32_16x16x128_f8f6f4 v[52:55], v[160:167], v[64:71], v[52:55], v141, v140 op_sel_hi:[0,0,0]
	v_mfma_scale_f32_16x16x128_f8f6f4 v[48:51], v[168:175], v[64:71], v[48:51], v141, v140 op_sel_hi:[0,0,0]
	v_mfma_scale_f32_16x16x128_f8f6f4 v[232:235], v[160:167], v[72:79], v[36:39], v141, v140 op_sel_hi:[0,0,0]
	v_mfma_scale_f32_16x16x128_f8f6f4 v[236:239], v[168:175], v[72:79], v[32:35], v141, v140 op_sel_hi:[0,0,0]
	v_mfma_scale_f32_16x16x128_f8f6f4 v[240:243], v[160:167], v[80:87], v[20:23], v141, v140 op_sel_hi:[0,0,0]
	v_mfma_scale_f32_16x16x128_f8f6f4 v[244:247], v[168:175], v[80:87], v[16:19], v141, v140 op_sel_hi:[0,0,0]
	ds_read_b32 v255, v255 offset:4096
	v_mfma_scale_f32_16x16x128_f8f6f4 v[248:251], v[160:167], v[88:95], v[4:7], v141, v140 op_sel_hi:[0,0,0]
	v_mfma_scale_f32_16x16x128_f8f6f4 v[128:131], v[168:175], v[88:95], v[0:3], v141, v140 op_sel_hi:[0,0,0]
	s_add_u32 s98, s98, 0x80000
	s_waitcnt lgkmcnt(0)
	v_readfirstlane_b32 s101, v255
	v_mov_b32_e32 v255, 0x20000
	s_cmp_ge_u32 s101, s98
	s_cbranch_scc1 .Lmy_g_45

; #define PG8_STAGE(bufoff, gbase, voff) do { _Pragma("unroll") for (int _i = 0; _i < 2; ++_i) { unsigned keep_; \
;         asm volatile("s_mov_b32 %0, m0\n\ts_mov_b32 m0, %3\n\ts_nop 0\n\tglobal_load_lds_dwordx4 %1, %2\n\ts_mov_b32 m0, %0" : "=&s"(keep_) : "v"((voff)[_i]), "s"((const char*)(gbase)), "s"(ldsbase + (unsigned)((bufoff) + _i * 8192)) : "memory"); } } while (0)
; #define PG8_WAIT_V(n) asm volatile("s_waitcnt vmcnt(" #n ")" ::: "memory")
; #define PG8_WAIT_L(n) asm volatile("s_waitcnt lgkmcnt(" #n ")" ::: "memory")
; #define PG8_BAR __builtin_amdgcn_s_barrier()
; #define PG8_SCHED __builtin_amdgcn_sched_barrier(0)
; template <class Epi, class Sched, bool ALIGN_EPI, bool FP8 = false>
; DI void gemm_phase(LAS unsigned char* lds, const Gemm g, const Sched& S, const Epi& E) {
;     ...
;             PG8_LDB(B0, 1, 0); PG8_LDB(B1, 1, 1); PG8_SCHED; PG8_LDA(At, 1, 0); PG8_STAGE(PG8_SA(0, 1), a2 + hstepA, voffA);
;             PG8_WAIT_V(8); PG8_WAIT_L(0); PG8_BAR; PG8_MMA(0, 0, At, B0); PG8_MMA(0, 1, At, B1); PG8_BAR; PG8_SCHED;
.Lmy_g_45:
	s_setprio 0
	s_nop 4
	ds_read_b128 v[0:3], v133 offset:32768
	ds_read_b128 v[4:7], v133 offset:32784
	ds_read_b128 v[16:19], v133 offset:34816
	ds_read_b128 v[20:23], v133 offset:34832
	ds_read_b128 v[144:147], v133 offset:49152
	ds_read_b128 v[148:151], v133 offset:49168
	ds_read_b128 v[152:155], v133 offset:51200
	ds_read_b128 v[156:159], v133 offset:51216
	ds_read_b128 v[8:11], v132 offset:32768
	ds_read_b128 v[12:15], v132 offset:32784
	ds_read_b128 v[24:27], v132 offset:34816
	ds_read_b128 v[28:31], v132 offset:34832
	ds_read_b128 v[32:35], v132 offset:36864
	ds_read_b128 v[36:39], v132 offset:36880
	ds_read_b128 v[40:43], v132 offset:38912
	ds_read_b128 v[44:47], v132 offset:38928
	s_add_u32 s26, s42, 0x40000
	s_addc_u32 s27, s43, 0
	s_mov_b32 s42, m0
	s_mov_b32 m0, s51
	s_nop 0
	global_load_lds_dwordx4 v134, s[26:27]
	s_mov_b32 m0, s42
	s_nop 0
	s_mov_b32 s42, m0
	s_mov_b32 m0, s52
	s_nop 0
	global_load_lds_dwordx4 v136, s[26:27]
	s_mov_b32 m0, s42
	s_waitcnt vmcnt(8)
	s_waitcnt lgkmcnt(0)
	s_barrier
	s_setprio 1
	v_mfma_scale_f32_16x16x128_f8f6f4 v[124:127], v[0:7], v[8:15], v[124:127], v140, v140 op_sel_hi:[0,0,0]
	v_mfma_scale_f32_16x16x128_f8f6f4 v[120:123], v[16:23], v[8:15], v[120:123], v140, v140 op_sel_hi:[0,0,0]
	v_mfma_scale_f32_16x16x128_f8f6f4 v[108:111], v[0:7], v[24:31], v[108:111], v140, v140 op_sel_hi:[0,0,0]
	v_mfma_scale_f32_16x16x128_f8f6f4 v[104:107], v[16:23], v[24:31], v[104:107], v140, v140 op_sel_hi:[0,0,0]
	v_mfma_scale_f32_16x16x128_f8f6f4 v[92:95], v[0:7], v[32:39], v[208:211], v140, v140 op_sel_hi:[0,0,0]
	v_mfma_scale_f32_16x16x128_f8f6f4 v[88:91], v[16:23], v[32:39], v[212:215], v140, v140 op_sel_hi:[0,0,0]
	v_mfma_scale_f32_16x16x128_f8f6f4 v[76:79], v[0:7], v[40:47], v[216:219], v140, v140 op_sel_hi:[0,0,0]
	v_mfma_scale_f32_16x16x128_f8f6f4 v[72:75], v[16:23], v[40:47], v[220:223], v140, v140 op_sel_hi:[0,0,0]
	v_mfma_scale_f32_16x16x128_f8f6f4 v[116:119], v[144:151], v[8:15], v[116:119], v141, v140 op_sel_hi:[0,0,0]
	v_mfma_scale_f32_16x16x128_f8f6f4 v[112:115], v[152:159], v[8:15], v[112:115], v141, v140 op_sel_hi:[0,0,0]
	v_mfma_scale_f32_16x16x128_f8f6f4 v[100:103], v[144:151], v[24:31], v[100:103], v141, v140 op_sel_hi:[0,0,0]
	v_mfma_scale_f32_16x16x128_f8f6f4 v[96:99], v[152:159], v[24:31], v[96:99], v141, v140 op_sel_hi:[0,0,0]
	v_mfma_scale_f32_16x16x128_f8f6f4 v[84:87], v[144:151], v[32:39], v[176:179], v141, v140 op_sel_hi:[0,0,0]
	v_mfma_scale_f32_16x16x128_f8f6f4 v[80:83], v[152:159], v[32:39], v[180:183], v141, v140 op_sel_hi:[0,0,0]
	ds_read_b32 v255, v255 offset:4096
	v_mfma_scale_f32_16x16x128_f8f6f4 v[68:71], v[144:151], v[40:47], v[184:187], v141, v140 op_sel_hi:[0,0,0]
	v_mfma_scale_f32_16x16x128_f8f6f4 v[64:67], v[152:159], v[40:47], v[188:191], v141, v140 op_sel_hi:[0,0,0]
	s_add_u32 s98, s98, 0x80000
	s_waitcnt lgkmcnt(0)
	v_readfirstlane_b32 s101, v255
	v_mov_b32_e32 v255, 0x20000
	s_cmp_ge_u32 s101, s98
	s_cbranch_scc1 .Lmy_g_46

; #define PG8_STAGE(bufoff, gbase, voff) do { _Pragma("unroll") for (int _i = 0; _i < 2; ++_i) { unsigned keep_; \
;         asm volatile("s_mov_b32 %0, m0\n\ts_mov_b32 m0, %3\n\ts_nop 0\n\tglobal_load_lds_dwordx4 %1, %2\n\ts_mov_b32 m0, %0" : "=&s"(keep_) : "v"((voff)[_i]), "s"((const char*)(gbase)), "s"(ldsbase + (unsigned)((bufoff) + _i * 8192)) : "memory"); } } while (0)
; #define PG8_WAIT_V(n) asm volatile("s_waitcnt vmcnt(" #n ")" ::: "memory")
; #define PG8_WAIT_L(n) asm volatile("s_waitcnt lgkmcnt(" #n ")" ::: "memory")
; #define PG8_BAR __builtin_amdgcn_s_barrier()
; #define PG8_SCHED __builtin_amdgcn_sched_barrier(0)
; template <class Epi, class Sched, bool ALIGN_EPI, bool FP8 = false>
; DI void gemm_phase(LAS unsigned char* lds, const Gemm g, const Sched& S, const Epi& E) {
;     ...
;             PG8_LDA(At, 1, 1); PG8_STAGE(PG8_SB(1, 0), b3, voffB); PG8_STAGE(PG8_SB(1, 1), b3 + hstepB, voffB); PG8_STAGE(PG8_SA(1, 0), a3, voffA);
;             PG8_WAIT_V(8); PG8_WAIT_L(0); PG8_BAR; PG8_MMA(1, 0, At, B0); PG8_MMA(1, 1, At, B1); PG8_BAR; PG8_SCHED;
.Lmy_g_46:
	s_setprio 0
	ds_read_b128 v[32:35], v132 offset:49152
	ds_read_b128 v[36:39], v132 offset:49168
	ds_read_b128 v[160:163], v132 offset:51200
	ds_read_b128 v[164:167], v132 offset:51216
	ds_read_b128 v[168:171], v132 offset:53248
	ds_read_b128 v[172:175], v132 offset:53264
	ds_read_b128 v[176:179], v132 offset:55296
	ds_read_b128 v[180:183], v132 offset:55312
	s_add_u32 s26, s40, 0x80
	s_addc_u32 s27, s41, 0
	s_mov_b32 s42, m0
	s_mov_b32 m0, s56
	s_nop 0
	global_load_lds_dwordx4 v135, s[26:27]
	s_mov_b32 m0, s42
	s_nop 0
	s_mov_b32 s42, m0
	s_mov_b32 m0, s57
	s_nop 0
	global_load_lds_dwordx4 v137, s[26:27]
	s_mov_b32 m0, s42
	s_add_u32 s26, s40, 0x40080
	s_addc_u32 s27, s41, 0
	s_mov_b32 s40, m0
	s_mov_b32 m0, s60
	s_nop 0
	global_load_lds_dwordx4 v135, s[26:27]
	s_mov_b32 m0, s40
	s_nop 0
	s_mov_b32 s40, m0
	s_mov_b32 m0, s61
	s_nop 0
	global_load_lds_dwordx4 v137, s[26:27]
	s_mov_b32 m0, s40
	s_mov_b32 s26, m0
	s_mov_b32 m0, s58
	s_nop 0
	global_load_lds_dwordx4 v134, s[28:29]
	s_mov_b32 m0, s26
	s_nop 0
	s_mov_b32 s26, m0
	s_mov_b32 m0, s59
	s_nop 0
	global_load_lds_dwordx4 v136, s[28:29]
	s_mov_b32 m0, s26
	s_waitcnt vmcnt(8)
	s_waitcnt lgkmcnt(0)
	s_barrier
	s_setprio 1
	v_mfma_scale_f32_16x16x128_f8f6f4 v[60:63], v[0:7], v[32:39], v[60:63], v140, v140 op_sel_hi:[0,0,0]
	v_mfma_scale_f32_16x16x128_f8f6f4 v[56:59], v[16:23], v[32:39], v[56:59], v140, v140 op_sel_hi:[0,0,0]
	v_mfma_scale_f32_16x16x128_f8f6f4 v[44:47], v[0:7], v[160:167], v[192:195], v140, v140 op_sel_hi:[0,0,0]
	v_mfma_scale_f32_16x16x128_f8f6f4 v[40:43], v[16:23], v[160:167], v[196:199], v140, v140 op_sel_hi:[0,0,0]
	v_mfma_scale_f32_16x16x128_f8f6f4 v[28:31], v[0:7], v[168:175], v[200:203], v140, v140 op_sel_hi:[0,0,0]
	v_mfma_scale_f32_16x16x128_f8f6f4 v[24:27], v[16:23], v[168:175], v[204:207], v140, v140 op_sel_hi:[0,0,0]
	v_mfma_scale_f32_16x16x128_f8f6f4 v[12:15], v[0:7], v[176:183], v[224:227], v140, v140 op_sel_hi:[0,0,0]
	v_mfma_scale_f32_16x16x128_f8f6f4 v[8:11], v[16:23], v[176:183], v[228:231], v140, v140 op_sel_hi:[0,0,0]
	v_mfma_scale_f32_16x16x128_f8f6f4 v[52:55], v[144:151], v[32:39], v[52:55], v141, v140 op_sel_hi:[0,0,0]
	v_mfma_scale_f32_16x16x128_f8f6f4 v[48:51], v[152:159], v[32:39], v[48:51], v141, v140 op_sel_hi:[0,0,0]
	v_mfma_scale_f32_16x16x128_f8f6f4 v[36:39], v[144:151], v[160:167], v[232:235], v141, v140 op_sel_hi:[0,0,0]
	v_mfma_scale_f32_16x16x128_f8f6f4 v[32:35], v[152:159], v[160:167], v[236:239], v141, v140 op_sel_hi:[0,0,0]
	v_mfma_scale_f32_16x16x128_f8f6f4 v[20:23], v[144:151], v[168:175], v[240:243], v141, v140 op_sel_hi:[0,0,0]
	v_mfma_scale_f32_16x16x128_f8f6f4 v[16:19], v[152:159], v[168:175], v[244:247], v141, v140 op_sel_hi:[0,0,0]
	ds_read_b32 v255, v255 offset:4096
	v_mfma_scale_f32_16x16x128_f8f6f4 v[4:7], v[144:151], v[176:183], v[248:251], v141, v140 op_sel_hi:[0,0,0]
	v_mfma_scale_f32_16x16x128_f8f6f4 v[0:3], v[152:159], v[176:183], v[128:131], v141, v140 op_sel_hi:[0,0,0]
	s_add_u32 s98, s98, 0x80000
	s_waitcnt lgkmcnt(0)
	v_readfirstlane_b32 s101, v255
	v_mov_b32_e32 v255, 0x20000
	s_cmp_ge_u32 s101, s98
	s_cbranch_scc1 .Lmy_g_47

; #define PG8_WAIT_V(n) asm volatile("s_waitcnt vmcnt(" #n ")" ::: "memory")
; #define PG8_WAIT_L(n) asm volatile("s_waitcnt lgkmcnt(" #n ")" ::: "memory")
; #define PG8_BAR __builtin_amdgcn_s_barrier()
; #define PG8_SCHED __builtin_amdgcn_sched_barrier(0)
; template <class Epi, class Sched, bool ALIGN_EPI, bool FP8 = false>
; DI void gemm_phase(LAS unsigned char* lds, const Gemm g, const Sched& S, const Epi& E) {
;     ...
;             PG8_WAIT_V(8); PG8_WAIT_L(0); PG8_BAR; PG8_MMA(1, 0, At, B0); PG8_MMA(1, 1, At, B1); PG8_BAR; PG8_SCHED;
;         }
;         if constexpr (ALIGN_EPI) { if (wr == 0) PG8_BAR; }
;         E(acc, cur, wr, wc, fr, fq);
.Lmy_g_47:
	s_setprio 0
	s_add_i32 s70, s70, 2
	s_add_u32 s68, s68, 0x100
	s_addc_u32 s69, s69, 0
	s_cmp_gt_u32 s70, 13
	s_mov_b64 s[26:27], s[6:7]
	s_cbranch_scc0 .Lmy_g0_1608
.Lmy_ex_1608:
	s_and_b64 vcc, exec, s[12:13]
	s_cbranch_vccz .LBB0_1611
	s_barrier

; #define PG8_STAGE(bufoff, gbase, voff) do { _Pragma("unroll") for (int _i = 0; _i < 2; ++_i) { unsigned keep_; \
;         asm volatile("s_mov_b32 %0, m0\n\ts_mov_b32 m0, %3\n\ts_nop 0\n\tglobal_load_lds_dwordx4 %1, %2\n\ts_mov_b32 m0, %0" : "=&s"(keep_) : "v"((voff)[_i]), "s"((const char*)(gbase)), "s"(ldsbase + (unsigned)((bufoff) + _i * 8192)) : "memory"); } } while (0)
; #define PG8_WAIT_V(n) asm volatile("s_waitcnt vmcnt(" #n ")" ::: "memory")
; #define PG8_WAIT_L(n) asm volatile("s_waitcnt lgkmcnt(" #n ")" ::: "memory")
; #define PG8_BAR __builtin_amdgcn_s_barrier()
; #define PG8_SCHED __builtin_amdgcn_sched_barrier(0)
;     DI int nt(const Unit& u) const { return (u.aux & 8) ? PLED / 64 : ((u.aux & 4) ? (D_ / 2) / 64 : D_ / 64); }
; template <class Epi, class Sched, bool ALIGN_EPI, bool FP8 = false>
; DI void gemm_phase(LAS unsigned char* lds, const Gemm g, const Sched& S, const Epi& E) {
;     ...
;             const bool last = (t == nt - 2);
;             const char* a1 = cA + (size_t)(t + 1) * kstep;
;             const char* a2 = last ? nA : cA + (size_t)(t + 2) * kstep; const char* b2 = last ? nB : cB + (size_t)(t + 2) * kstep;
;             const char* a3 = a2 + kstep; const char* b3 = b2 + kstep;
;             PG8_LDB(B0, 0, 0); PG8_LDB(B1, 0, 1); PG8_SCHED; PG8_LDA(At, 0, 0); PG8_STAGE(PG8_SA(1, 1), a1 + hstepA, voffA);
;             PG8_WAIT_V(8); PG8_WAIT_L(0); PG8_BAR; PG8_MMA(0, 0, At, B0); PG8_MMA(0, 1, At, B1); PG8_BAR; PG8_SCHED;
;             PG8_LDA(At, 0, 1); PG8_STAGE(PG8_SB(0, 0), b2, voffB); PG8_STAGE(PG8_SB(0, 1), b2 + hstepB, voffB); PG8_STAGE(PG8_SA(0, 0), a2, voffA);
;             PG8_WAIT_V(8); PG8_WAIT_L(0); PG8_BAR; PG8_MMA(1, 0, At, B0); PG8_MMA(1, 1, At, B1); PG8_BAR; PG8_SCHED;
.LBB0_1685:
	s_cmp_lg_u32 s99, 0
	s_cbranch_scc1 .Lmy_g0_1685
	ds_read_b128 v[140:143], v131
	ds_read_b128 v[144:147], v131 offset:16
	ds_read_b128 v[148:151], v131 offset:2048
	ds_read_b128 v[152:155], v131 offset:2064
	ds_read_b128 v[156:159], v131 offset:16384
	ds_read_b128 v[160:163], v131 offset:16400
	ds_read_b128 v[164:167], v131 offset:18432
	ds_read_b128 v[168:171], v131 offset:18448
	s_add_u32 s46, s44, 0x100
	s_addc_u32 s47, s45, 0
	s_cmp_eq_u32 s92, 52
	s_cselect_b32 s52, s6, s46
	s_cselect_b32 s53, s7, s47
	s_cselect_b32 s50, s42, s90
	s_cselect_b32 s51, s43, s91
	s_add_u32 s48, s52, 0x80
	s_addc_u32 s49, s53, 0
	ds_read_b128 v[172:175], v130
	ds_read_b128 v[176:179], v130 offset:16
	ds_read_b128 v[180:183], v130 offset:2048
	ds_read_b128 v[184:187], v130 offset:2064
	ds_read_b128 v[188:191], v130 offset:4096
	ds_read_b128 v[192:195], v130 offset:4112
	ds_read_b128 v[196:199], v130 offset:6144
	ds_read_b128 v[200:203], v130 offset:6160
	s_add_u32 s44, s44, 0xe0080
	s_addc_u32 s45, s45, 0
	s_mov_b32 s93, m0
	s_mov_b32 m0, s73
	s_nop 0
	global_load_lds_dwordx4 v132, s[44:45]
	s_mov_b32 m0, s93
	s_nop 0
	s_mov_b32 s93, m0
	s_mov_b32 m0, s74
	s_nop 0
	global_load_lds_dwordx4 v134, s[44:45]
	s_mov_b32 m0, s93
	s_waitcnt vmcnt(8)
	s_waitcnt lgkmcnt(0)
	s_mov_b64 exec, 1
	ds_add_u32 v255, v255 offset:4096
	s_mov_b64 exec, -1
	s_setprio 1
	v_mfma_scale_f32_16x16x128_f8f6f4 v[124:127], v[140:147], v[172:179], v[124:127], v138, v138 op_sel_hi:[0,0,0]
	v_mfma_scale_f32_16x16x128_f8f6f4 v[120:123], v[148:155], v[172:179], v[120:123], v138, v138 op_sel_hi:[0,0,0]
	v_mfma_scale_f32_16x16x128_f8f6f4 v[116:119], v[140:147], v[180:187], v[116:119], v138, v138 op_sel_hi:[0,0,0]
	v_mfma_scale_f32_16x16x128_f8f6f4 v[112:115], v[148:155], v[180:187], v[112:115], v138, v138 op_sel_hi:[0,0,0]
	v_mfma_scale_f32_16x16x128_f8f6f4 v[100:103], v[140:147], v[188:195], v[100:103], v138, v138 op_sel_hi:[0,0,0]
	v_mfma_scale_f32_16x16x128_f8f6f4 v[96:99], v[148:155], v[188:195], v[96:99], v138, v138 op_sel_hi:[0,0,0]
	v_mfma_scale_f32_16x16x128_f8f6f4 v[204:207], v[140:147], v[196:203], v[84:87], v138, v138 op_sel_hi:[0,0,0]
	v_mfma_scale_f32_16x16x128_f8f6f4 v[208:211], v[148:155], v[196:203], v[80:83], v138, v138 op_sel_hi:[0,0,0]
	v_mfma_scale_f32_16x16x128_f8f6f4 v[108:111], v[156:163], v[172:179], v[108:111], v138, v138 op_sel_hi:[0,0,0]
	v_mfma_scale_f32_16x16x128_f8f6f4 v[104:107], v[164:171], v[172:179], v[104:107], v138, v138 op_sel_hi:[0,0,0]
	v_mfma_scale_f32_16x16x128_f8f6f4 v[172:175], v[156:163], v[180:187], v[92:95], v138, v138 op_sel_hi:[0,0,0]
	v_mfma_scale_f32_16x16x128_f8f6f4 v[176:179], v[164:171], v[180:187], v[88:91], v138, v138 op_sel_hi:[0,0,0]
	v_mfma_scale_f32_16x16x128_f8f6f4 v[180:183], v[156:163], v[188:195], v[76:79], v138, v138 op_sel_hi:[0,0,0]
	v_mfma_scale_f32_16x16x128_f8f6f4 v[184:187], v[164:171], v[188:195], v[72:75], v138, v138 op_sel_hi:[0,0,0]
	v_mfma_scale_f32_16x16x128_f8f6f4 v[188:191], v[156:163], v[196:203], v[68:71], v138, v138 op_sel_hi:[0,0,0]
	v_mfma_scale_f32_16x16x128_f8f6f4 v[192:195], v[164:171], v[196:203], v[64:67], v138, v138 op_sel_hi:[0,0,0]
	s_setprio 0
	s_barrier
	s_nop 4
	ds_read_b128 v[64:67], v130 offset:16384
	ds_read_b128 v[68:71], v130 offset:16400
	ds_read_b128 v[72:75], v130 offset:18432
	ds_read_b128 v[76:79], v130 offset:18448
	ds_read_b128 v[80:83], v130 offset:20480
	ds_read_b128 v[84:87], v130 offset:20496
	ds_read_b128 v[88:91], v130 offset:22528
	ds_read_b128 v[92:95], v130 offset:22544
	s_mov_b32 s44, m0
	s_mov_b32 m0, s57
	s_nop 0
	global_load_lds_dwordx4 v133, s[50:51]
	s_mov_b32 m0, s44
	s_nop 0
	s_mov_b32 s44, m0
	s_mov_b32 m0, s58
	s_nop 0
	global_load_lds_dwordx4 v135, s[50:51]
	s_mov_b32 m0, s44
	s_add_u32 s44, s50, 0xe0000
	s_addc_u32 s45, s51, 0
	s_mov_b32 s93, m0
	s_mov_b32 m0, s59
	s_nop 0
	global_load_lds_dwordx4 v133, s[44:45]
	s_mov_b32 m0, s93
	s_nop 0
	s_mov_b32 s93, m0
	s_mov_b32 m0, s60
	s_nop 0
	global_load_lds_dwordx4 v135, s[44:45]
	s_mov_b32 m0, s93
	s_mov_b32 s44, m0
	s_mov_b32 m0, s54
	s_nop 0
	global_load_lds_dwordx4 v132, s[52:53]
	s_mov_b32 m0, s44
	s_nop 0
	s_mov_b32 s44, m0
	s_mov_b32 m0, s61
	s_nop 0
	global_load_lds_dwordx4 v134, s[52:53]
	s_mov_b32 m0, s44
	s_waitcnt vmcnt(8)
	s_waitcnt lgkmcnt(0)
	s_mov_b64 exec, 1
	ds_add_u32 v255, v255 offset:4096
	s_mov_b64 exec, -1
	s_setprio 1
	v_mfma_scale_f32_16x16x128_f8f6f4 v[60:63], v[140:147], v[64:71], v[60:63], v138, v138 op_sel_hi:[0,0,0]
	v_mfma_scale_f32_16x16x128_f8f6f4 v[56:59], v[148:155], v[64:71], v[56:59], v138, v138 op_sel_hi:[0,0,0]
	v_mfma_scale_f32_16x16x128_f8f6f4 v[52:55], v[140:147], v[72:79], v[52:55], v138, v138 op_sel_hi:[0,0,0]
	v_mfma_scale_f32_16x16x128_f8f6f4 v[48:51], v[148:155], v[72:79], v[48:51], v138, v138 op_sel_hi:[0,0,0]
	v_mfma_scale_f32_16x16x128_f8f6f4 v[196:199], v[140:147], v[80:87], v[36:39], v138, v138 op_sel_hi:[0,0,0]
	v_mfma_scale_f32_16x16x128_f8f6f4 v[200:203], v[148:155], v[80:87], v[32:35], v138, v138 op_sel_hi:[0,0,0]
	v_mfma_scale_f32_16x16x128_f8f6f4 v[212:215], v[140:147], v[88:95], v[20:23], v138, v138 op_sel_hi:[0,0,0]
	v_mfma_scale_f32_16x16x128_f8f6f4 v[216:219], v[148:155], v[88:95], v[16:19], v138, v138 op_sel_hi:[0,0,0]
	v_mfma_scale_f32_16x16x128_f8f6f4 v[220:223], v[156:163], v[64:71], v[44:47], v138, v138 op_sel_hi:[0,0,0]
	v_mfma_scale_f32_16x16x128_f8f6f4 v[224:227], v[164:171], v[64:71], v[40:43], v138, v138 op_sel_hi:[0,0,0]
	v_mfma_scale_f32_16x16x128_f8f6f4 v[228:231], v[156:163], v[72:79], v[28:31], v138, v138 op_sel_hi:[0,0,0]
	v_mfma_scale_f32_16x16x128_f8f6f4 v[232:235], v[164:171], v[72:79], v[24:27], v138, v138 op_sel_hi:[0,0,0]
	v_mfma_scale_f32_16x16x128_f8f6f4 v[236:239], v[156:163], v[80:87], v[12:15], v138, v138 op_sel_hi:[0,0,0]
	v_mfma_scale_f32_16x16x128_f8f6f4 v[240:243], v[164:171], v[80:87], v[8:11], v138, v138 op_sel_hi:[0,0,0]
	v_mfma_scale_f32_16x16x128_f8f6f4 v[244:247], v[156:163], v[88:95], v[4:7], v138, v138 op_sel_hi:[0,0,0]
	v_mfma_scale_f32_16x16x128_f8f6f4 v[248:251], v[164:171], v[88:95], v[0:3], v138, v138 op_sel_hi:[0,0,0]
	s_setprio 0
	s_barrier
; #define PG8_STAGE(bufoff, gbase, voff) do { _Pragma("unroll") for (int _i = 0; _i < 2; ++_i) { unsigned keep_; \
;         asm volatile("s_mov_b32 %0, m0\n\ts_mov_b32 m0, %3\n\ts_nop 0\n\tglobal_load_lds_dwordx4 %1, %2\n\ts_mov_b32 m0, %0" : "=&s"(keep_) : "v"((voff)[_i]), "s"((const char*)(gbase)), "s"(ldsbase + (unsigned)((bufoff) + _i * 8192)) : "memory"); } } while (0)
; #define PG8_WAIT_V(n) asm volatile("s_waitcnt vmcnt(" #n ")" ::: "memory")
; #define PG8_WAIT_L(n) asm volatile("s_waitcnt lgkmcnt(" #n ")" ::: "memory")
; #define PG8_BAR __builtin_amdgcn_s_barrier()
; #define PG8_SCHED __builtin_amdgcn_sched_barrier(0)
; template <class Epi, class Sched, bool ALIGN_EPI, bool FP8 = false>
; DI void gemm_phase(LAS unsigned char* lds, const Gemm g, const Sched& S, const Epi& E) {
;     ...
;             PG8_LDB(B0, 1, 0); PG8_LDB(B1, 1, 1); PG8_SCHED; PG8_LDA(At, 1, 0); PG8_STAGE(PG8_SA(0, 1), a2 + hstepA, voffA);
;             PG8_WAIT_V(8); PG8_WAIT_L(0); PG8_BAR; PG8_MMA(0, 0, At, B0); PG8_MMA(0, 1, At, B1); PG8_BAR; PG8_SCHED;
;             PG8_LDA(At, 1, 1); PG8_STAGE(PG8_SB(1, 0), b3, voffB); PG8_STAGE(PG8_SB(1, 1), b3 + hstepB, voffB); PG8_STAGE(PG8_SA(1, 0), a3, voffA);
;             PG8_WAIT_V(8); PG8_WAIT_L(0); PG8_BAR; PG8_MMA(1, 0, At, B0); PG8_MMA(1, 1, At, B1); PG8_BAR; PG8_SCHED;
;         }
	s_nop 4
	ds_read_b128 v[0:3], v131 offset:32768
	ds_read_b128 v[4:7], v131 offset:32784
	ds_read_b128 v[8:11], v131 offset:34816
	ds_read_b128 v[12:15], v131 offset:34832
	ds_read_b128 v[140:143], v131 offset:49152
	ds_read_b128 v[144:147], v131 offset:49168
	ds_read_b128 v[148:151], v131 offset:51200
	ds_read_b128 v[152:155], v131 offset:51216
	ds_read_b128 v[16:19], v130 offset:32768
	ds_read_b128 v[20:23], v130 offset:32784
	ds_read_b128 v[24:27], v130 offset:34816
	ds_read_b128 v[28:31], v130 offset:34832
	ds_read_b128 v[32:35], v130 offset:36864
	ds_read_b128 v[36:39], v130 offset:36880
	ds_read_b128 v[40:43], v130 offset:38912
	ds_read_b128 v[44:47], v130 offset:38928
	s_add_u32 s44, s52, 0xe0000
	s_addc_u32 s45, s53, 0
	s_mov_b32 s52, m0
	s_mov_b32 m0, s62
	s_nop 0
	global_load_lds_dwordx4 v132, s[44:45]
	s_mov_b32 m0, s52
	s_nop 0
	s_mov_b32 s52, m0
	s_mov_b32 m0, s63
	s_nop 0
	global_load_lds_dwordx4 v134, s[44:45]
	s_mov_b32 m0, s52
	s_waitcnt vmcnt(8)
	s_waitcnt lgkmcnt(0)
	s_mov_b64 exec, 1
	ds_add_u32 v255, v255 offset:4096
	s_mov_b64 exec, -1
	s_setprio 1
	v_mfma_scale_f32_16x16x128_f8f6f4 v[124:127], v[0:7], v[16:23], v[124:127], v138, v138 op_sel_hi:[0,0,0]
	v_mfma_scale_f32_16x16x128_f8f6f4 v[120:123], v[8:15], v[16:23], v[120:123], v138, v138 op_sel_hi:[0,0,0]
	v_mfma_scale_f32_16x16x128_f8f6f4 v[116:119], v[0:7], v[24:31], v[116:119], v138, v138 op_sel_hi:[0,0,0]
	v_mfma_scale_f32_16x16x128_f8f6f4 v[112:115], v[8:15], v[24:31], v[112:115], v138, v138 op_sel_hi:[0,0,0]
	v_mfma_scale_f32_16x16x128_f8f6f4 v[100:103], v[0:7], v[32:39], v[100:103], v138, v138 op_sel_hi:[0,0,0]
	v_mfma_scale_f32_16x16x128_f8f6f4 v[96:99], v[8:15], v[32:39], v[96:99], v138, v138 op_sel_hi:[0,0,0]
	v_mfma_scale_f32_16x16x128_f8f6f4 v[84:87], v[0:7], v[40:47], v[204:207], v138, v138 op_sel_hi:[0,0,0]
	v_mfma_scale_f32_16x16x128_f8f6f4 v[80:83], v[8:15], v[40:47], v[208:211], v138, v138 op_sel_hi:[0,0,0]
	v_mfma_scale_f32_16x16x128_f8f6f4 v[108:111], v[140:147], v[16:23], v[108:111], v138, v138 op_sel_hi:[0,0,0]
	v_mfma_scale_f32_16x16x128_f8f6f4 v[104:107], v[148:155], v[16:23], v[104:107], v138, v138 op_sel_hi:[0,0,0]
	v_mfma_scale_f32_16x16x128_f8f6f4 v[92:95], v[140:147], v[24:31], v[172:175], v138, v138 op_sel_hi:[0,0,0]
	v_mfma_scale_f32_16x16x128_f8f6f4 v[88:91], v[148:155], v[24:31], v[176:179], v138, v138 op_sel_hi:[0,0,0]
	v_mfma_scale_f32_16x16x128_f8f6f4 v[76:79], v[140:147], v[32:39], v[180:183], v138, v138 op_sel_hi:[0,0,0]
	v_mfma_scale_f32_16x16x128_f8f6f4 v[72:75], v[148:155], v[32:39], v[184:187], v138, v138 op_sel_hi:[0,0,0]
	v_mfma_scale_f32_16x16x128_f8f6f4 v[68:71], v[140:147], v[40:47], v[188:191], v138, v138 op_sel_hi:[0,0,0]
	v_mfma_scale_f32_16x16x128_f8f6f4 v[64:67], v[148:155], v[40:47], v[192:195], v138, v138 op_sel_hi:[0,0,0]
	s_setprio 0
	s_barrier
	ds_read_b128 v[24:27], v130 offset:49152
	ds_read_b128 v[28:31], v130 offset:49168
	ds_read_b128 v[156:159], v130 offset:51200
	ds_read_b128 v[160:163], v130 offset:51216
	ds_read_b128 v[164:167], v130 offset:53248
	ds_read_b128 v[168:171], v130 offset:53264
	ds_read_b128 v[172:175], v130 offset:55296
	ds_read_b128 v[176:179], v130 offset:55312
	s_add_u32 s44, s50, 0x80
	s_addc_u32 s45, s51, 0
	s_mov_b32 s52, m0
	s_mov_b32 m0, s67
	s_nop 0
	global_load_lds_dwordx4 v133, s[44:45]
	s_mov_b32 m0, s52
	s_nop 0
	s_mov_b32 s52, m0
	s_mov_b32 m0, s68
	s_nop 0
	global_load_lds_dwordx4 v135, s[44:45]
	s_mov_b32 m0, s52
	s_add_u32 s44, s50, 0xe0080
	s_addc_u32 s45, s51, 0
	s_mov_b32 s50, m0
	s_mov_b32 m0, s71
	s_nop 0
	global_load_lds_dwordx4 v133, s[44:45]
	s_mov_b32 m0, s50
	s_nop 0
	s_mov_b32 s50, m0
	s_mov_b32 m0, s72
	s_nop 0
	global_load_lds_dwordx4 v135, s[44:45]
	s_mov_b32 m0, s50
	s_mov_b32 s44, m0
	s_mov_b32 m0, s69
	s_nop 0
	global_load_lds_dwordx4 v132, s[48:49]
	s_mov_b32 m0, s44
	s_nop 0
	s_mov_b32 s44, m0
	s_mov_b32 m0, s70
	s_nop 0
	global_load_lds_dwordx4 v134, s[48:49]
	s_mov_b32 m0, s44
	s_waitcnt vmcnt(8)
	s_waitcnt lgkmcnt(0)
	s_mov_b64 exec, 1
	ds_add_u32 v255, v255 offset:4096
	s_mov_b64 exec, -1
	s_setprio 1
	v_mfma_scale_f32_16x16x128_f8f6f4 v[60:63], v[0:7], v[24:31], v[60:63], v138, v138 op_sel_hi:[0,0,0]
	v_mfma_scale_f32_16x16x128_f8f6f4 v[56:59], v[8:15], v[24:31], v[56:59], v138, v138 op_sel_hi:[0,0,0]
	v_mfma_scale_f32_16x16x128_f8f6f4 v[52:55], v[0:7], v[156:163], v[52:55], v138, v138 op_sel_hi:[0,0,0]
	v_mfma_scale_f32_16x16x128_f8f6f4 v[48:51], v[8:15], v[156:163], v[48:51], v138, v138 op_sel_hi:[0,0,0]
	v_mfma_scale_f32_16x16x128_f8f6f4 v[36:39], v[0:7], v[164:171], v[196:199], v138, v138 op_sel_hi:[0,0,0]
	v_mfma_scale_f32_16x16x128_f8f6f4 v[32:35], v[8:15], v[164:171], v[200:203], v138, v138 op_sel_hi:[0,0,0]
	v_mfma_scale_f32_16x16x128_f8f6f4 v[20:23], v[0:7], v[172:179], v[212:215], v138, v138 op_sel_hi:[0,0,0]
	v_mfma_scale_f32_16x16x128_f8f6f4 v[16:19], v[8:15], v[172:179], v[216:219], v138, v138 op_sel_hi:[0,0,0]
	v_mfma_scale_f32_16x16x128_f8f6f4 v[44:47], v[140:147], v[24:31], v[220:223], v138, v138 op_sel_hi:[0,0,0]
	v_mfma_scale_f32_16x16x128_f8f6f4 v[40:43], v[148:155], v[24:31], v[224:227], v138, v138 op_sel_hi:[0,0,0]
	v_mfma_scale_f32_16x16x128_f8f6f4 v[28:31], v[140:147], v[156:163], v[228:231], v138, v138 op_sel_hi:[0,0,0]
	v_mfma_scale_f32_16x16x128_f8f6f4 v[24:27], v[148:155], v[156:163], v[232:235], v138, v138 op_sel_hi:[0,0,0]
	v_mfma_scale_f32_16x16x128_f8f6f4 v[12:15], v[140:147], v[164:171], v[236:239], v138, v138 op_sel_hi:[0,0,0]
	v_mfma_scale_f32_16x16x128_f8f6f4 v[8:11], v[148:155], v[164:171], v[240:243], v138, v138 op_sel_hi:[0,0,0]
	v_mfma_scale_f32_16x16x128_f8f6f4 v[4:7], v[140:147], v[172:179], v[244:247], v138, v138 op_sel_hi:[0,0,0]
	v_mfma_scale_f32_16x16x128_f8f6f4 v[0:3], v[148:155], v[172:179], v[248:251], v138, v138 op_sel_hi:[0,0,0]
	s_setprio 0
	s_barrier
	s_add_i32 s92, s92, 2
	s_add_u32 s90, s90, 0x100
	s_addc_u32 s91, s91, 0
	s_cmp_gt_u32 s92, 53
	s_mov_b64 s[44:45], s[46:47]
	s_cbranch_scc0 .LBB0_1685
	s_branch .Lmy_ex_1685
; #define PG8_STAGE(bufoff, gbase, voff) do { _Pragma("unroll") for (int _i = 0; _i < 2; ++_i) { unsigned keep_; \
;         asm volatile("s_mov_b32 %0, m0\n\ts_mov_b32 m0, %3\n\ts_nop 0\n\tglobal_load_lds_dwordx4 %1, %2\n\ts_mov_b32 m0, %0" : "=&s"(keep_) : "v"((voff)[_i]), "s"((const char*)(gbase)), "s"(ldsbase + (unsigned)((bufoff) + _i * 8192)) : "memory"); } } while (0)
; #define PG8_WAIT_V(n) asm volatile("s_waitcnt vmcnt(" #n ")" ::: "memory")
; #define PG8_WAIT_L(n) asm volatile("s_waitcnt lgkmcnt(" #n ")" ::: "memory")
; #define PG8_BAR __builtin_amdgcn_s_barrier()
; #define PG8_SCHED __builtin_amdgcn_sched_barrier(0)
;     DI int nt(const Unit& u) const { return (u.aux & 8) ? PLED / 64 : ((u.aux & 4) ? (D_ / 2) / 64 : D_ / 64); }
; template <class Epi, class Sched, bool ALIGN_EPI, bool FP8 = false>
; DI void gemm_phase(LAS unsigned char* lds, const Gemm g, const Sched& S, const Epi& E) {
;     ...
;             const bool last = (t == nt - 2);
;             const char* a1 = cA + (size_t)(t + 1) * kstep;
;             const char* a2 = last ? nA : cA + (size_t)(t + 2) * kstep; const char* b2 = last ? nB : cB + (size_t)(t + 2) * kstep;
;             const char* a3 = a2 + kstep; const char* b3 = b2 + kstep;
;             PG8_LDB(B0, 0, 0); PG8_LDB(B1, 0, 1); PG8_SCHED; PG8_LDA(At, 0, 0); PG8_STAGE(PG8_SA(1, 1), a1 + hstepA, voffA);
;             PG8_WAIT_V(8); PG8_WAIT_L(0); PG8_BAR; PG8_MMA(0, 0, At, B0); PG8_MMA(0, 1, At, B1); PG8_BAR; PG8_SCHED;
.Lmy_g0_1685:
	ds_read_b128 v[140:143], v131
	ds_read_b128 v[144:147], v131 offset:16
	ds_read_b128 v[148:151], v131 offset:2048
	ds_read_b128 v[152:155], v131 offset:2064
	ds_read_b128 v[156:159], v131 offset:16384
	ds_read_b128 v[160:163], v131 offset:16400
	ds_read_b128 v[164:167], v131 offset:18432
	ds_read_b128 v[168:171], v131 offset:18448
	s_add_u32 s46, s44, 0x100
	s_addc_u32 s47, s45, 0
	s_cmp_eq_u32 s92, 52
	s_cselect_b32 s52, s6, s46
	s_cselect_b32 s53, s7, s47
	s_cselect_b32 s50, s42, s90
	s_cselect_b32 s51, s43, s91
	s_add_u32 s48, s52, 0x80
	s_addc_u32 s49, s53, 0
	ds_read_b128 v[172:175], v130
	ds_read_b128 v[176:179], v130 offset:16
	ds_read_b128 v[180:183], v130 offset:2048
	ds_read_b128 v[184:187], v130 offset:2064
	ds_read_b128 v[188:191], v130 offset:4096
	ds_read_b128 v[192:195], v130 offset:4112
	ds_read_b128 v[196:199], v130 offset:6144
	ds_read_b128 v[200:203], v130 offset:6160
	s_add_u32 s44, s44, 0xe0080
	s_addc_u32 s45, s45, 0
	s_mov_b32 s93, m0
	s_mov_b32 m0, s73
	s_nop 0
	global_load_lds_dwordx4 v132, s[44:45]
	s_mov_b32 m0, s93
	s_nop 0
	s_mov_b32 s93, m0
	s_mov_b32 m0, s74
	s_nop 0
	global_load_lds_dwordx4 v134, s[44:45]
	s_mov_b32 m0, s93
	s_waitcnt vmcnt(8)
	s_waitcnt lgkmcnt(0)
	s_barrier
	s_setprio 1
	v_mfma_scale_f32_16x16x128_f8f6f4 v[124:127], v[140:147], v[172:179], v[124:127], v138, v138 op_sel_hi:[0,0,0]
	v_mfma_scale_f32_16x16x128_f8f6f4 v[120:123], v[148:155], v[172:179], v[120:123], v138, v138 op_sel_hi:[0,0,0]
	v_mfma_scale_f32_16x16x128_f8f6f4 v[116:119], v[140:147], v[180:187], v[116:119], v138, v138 op_sel_hi:[0,0,0]
	v_mfma_scale_f32_16x16x128_f8f6f4 v[112:115], v[148:155], v[180:187], v[112:115], v138, v138 op_sel_hi:[0,0,0]
	v_mfma_scale_f32_16x16x128_f8f6f4 v[100:103], v[140:147], v[188:195], v[100:103], v138, v138 op_sel_hi:[0,0,0]
	v_mfma_scale_f32_16x16x128_f8f6f4 v[96:99], v[148:155], v[188:195], v[96:99], v138, v138 op_sel_hi:[0,0,0]
	v_mfma_scale_f32_16x16x128_f8f6f4 v[204:207], v[140:147], v[196:203], v[84:87], v138, v138 op_sel_hi:[0,0,0]
	v_mfma_scale_f32_16x16x128_f8f6f4 v[208:211], v[148:155], v[196:203], v[80:83], v138, v138 op_sel_hi:[0,0,0]
	v_mfma_scale_f32_16x16x128_f8f6f4 v[108:111], v[156:163], v[172:179], v[108:111], v138, v138 op_sel_hi:[0,0,0]
	v_mfma_scale_f32_16x16x128_f8f6f4 v[104:107], v[164:171], v[172:179], v[104:107], v138, v138 op_sel_hi:[0,0,0]
	v_mfma_scale_f32_16x16x128_f8f6f4 v[172:175], v[156:163], v[180:187], v[92:95], v138, v138 op_sel_hi:[0,0,0]
	v_mfma_scale_f32_16x16x128_f8f6f4 v[176:179], v[164:171], v[180:187], v[88:91], v138, v138 op_sel_hi:[0,0,0]
	v_mfma_scale_f32_16x16x128_f8f6f4 v[180:183], v[156:163], v[188:195], v[76:79], v138, v138 op_sel_hi:[0,0,0]
	v_mfma_scale_f32_16x16x128_f8f6f4 v[184:187], v[164:171], v[188:195], v[72:75], v138, v138 op_sel_hi:[0,0,0]
	ds_read_b32 v255, v255 offset:4096
	v_mfma_scale_f32_16x16x128_f8f6f4 v[188:191], v[156:163], v[196:203], v[68:71], v138, v138 op_sel_hi:[0,0,0]
	v_mfma_scale_f32_16x16x128_f8f6f4 v[192:195], v[164:171], v[196:203], v[64:67], v138, v138 op_sel_hi:[0,0,0]
	s_add_u32 s98, s98, 0x80000
	s_waitcnt lgkmcnt(0)
	v_readfirstlane_b32 s101, v255
	v_mov_b32_e32 v255, 0x20000
	s_cmp_ge_u32 s101, s98
	s_cbranch_scc1 .Lmy_g_48

; #define PG8_STAGE(bufoff, gbase, voff) do { _Pragma("unroll") for (int _i = 0; _i < 2; ++_i) { unsigned keep_; \
;         asm volatile("s_mov_b32 %0, m0\n\ts_mov_b32 m0, %3\n\ts_nop 0\n\tglobal_load_lds_dwordx4 %1, %2\n\ts_mov_b32 m0, %0" : "=&s"(keep_) : "v"((voff)[_i]), "s"((const char*)(gbase)), "s"(ldsbase + (unsigned)((bufoff) + _i * 8192)) : "memory"); } } while (0)
; #define PG8_WAIT_V(n) asm volatile("s_waitcnt vmcnt(" #n ")" ::: "memory")
; #define PG8_WAIT_L(n) asm volatile("s_waitcnt lgkmcnt(" #n ")" ::: "memory")
; #define PG8_BAR __builtin_amdgcn_s_barrier()
; #define PG8_SCHED __builtin_amdgcn_sched_barrier(0)
; template <class Epi, class Sched, bool ALIGN_EPI, bool FP8 = false>
; DI void gemm_phase(LAS unsigned char* lds, const Gemm g, const Sched& S, const Epi& E) {
;     ...
;             PG8_LDA(At, 0, 1); PG8_STAGE(PG8_SB(0, 0), b2, voffB); PG8_STAGE(PG8_SB(0, 1), b2 + hstepB, voffB); PG8_STAGE(PG8_SA(0, 0), a2, voffA);
;             PG8_WAIT_V(8); PG8_WAIT_L(0); PG8_BAR; PG8_MMA(1, 0, At, B0); PG8_MMA(1, 1, At, B1); PG8_BAR; PG8_SCHED;
.Lmy_g_48:
	s_setprio 0
	s_nop 4
	ds_read_b128 v[64:67], v130 offset:16384
	ds_read_b128 v[68:71], v130 offset:16400
	ds_read_b128 v[72:75], v130 offset:18432
	ds_read_b128 v[76:79], v130 offset:18448
	ds_read_b128 v[80:83], v130 offset:20480
	ds_read_b128 v[84:87], v130 offset:20496
	ds_read_b128 v[88:91], v130 offset:22528
	ds_read_b128 v[92:95], v130 offset:22544
	s_mov_b32 s44, m0
	s_mov_b32 m0, s57
	s_nop 0
	global_load_lds_dwordx4 v133, s[50:51]
	s_mov_b32 m0, s44
	s_nop 0
	s_mov_b32 s44, m0
	s_mov_b32 m0, s58
	s_nop 0
	global_load_lds_dwordx4 v135, s[50:51]
	s_mov_b32 m0, s44
	s_add_u32 s44, s50, 0xe0000
	s_addc_u32 s45, s51, 0
	s_mov_b32 s93, m0
	s_mov_b32 m0, s59
	s_nop 0
	global_load_lds_dwordx4 v133, s[44:45]
	s_mov_b32 m0, s93
	s_nop 0
	s_mov_b32 s93, m0
	s_mov_b32 m0, s60
	s_nop 0
	global_load_lds_dwordx4 v135, s[44:45]
	s_mov_b32 m0, s93
	s_mov_b32 s44, m0
	s_mov_b32 m0, s54
	s_nop 0
	global_load_lds_dwordx4 v132, s[52:53]
	s_mov_b32 m0, s44
	s_nop 0
	s_mov_b32 s44, m0
	s_mov_b32 m0, s61
	s_nop 0
	global_load_lds_dwordx4 v134, s[52:53]
	s_mov_b32 m0, s44
	s_waitcnt vmcnt(8)
	s_waitcnt lgkmcnt(0)
	s_barrier
	s_setprio 1
	v_mfma_scale_f32_16x16x128_f8f6f4 v[60:63], v[140:147], v[64:71], v[60:63], v138, v138 op_sel_hi:[0,0,0]
	v_mfma_scale_f32_16x16x128_f8f6f4 v[56:59], v[148:155], v[64:71], v[56:59], v138, v138 op_sel_hi:[0,0,0]
	v_mfma_scale_f32_16x16x128_f8f6f4 v[52:55], v[140:147], v[72:79], v[52:55], v138, v138 op_sel_hi:[0,0,0]
	v_mfma_scale_f32_16x16x128_f8f6f4 v[48:51], v[148:155], v[72:79], v[48:51], v138, v138 op_sel_hi:[0,0,0]
	v_mfma_scale_f32_16x16x128_f8f6f4 v[196:199], v[140:147], v[80:87], v[36:39], v138, v138 op_sel_hi:[0,0,0]
	v_mfma_scale_f32_16x16x128_f8f6f4 v[200:203], v[148:155], v[80:87], v[32:35], v138, v138 op_sel_hi:[0,0,0]
	v_mfma_scale_f32_16x16x128_f8f6f4 v[212:215], v[140:147], v[88:95], v[20:23], v138, v138 op_sel_hi:[0,0,0]
	v_mfma_scale_f32_16x16x128_f8f6f4 v[216:219], v[148:155], v[88:95], v[16:19], v138, v138 op_sel_hi:[0,0,0]
	v_mfma_scale_f32_16x16x128_f8f6f4 v[220:223], v[156:163], v[64:71], v[44:47], v138, v138 op_sel_hi:[0,0,0]
	v_mfma_scale_f32_16x16x128_f8f6f4 v[224:227], v[164:171], v[64:71], v[40:43], v138, v138 op_sel_hi:[0,0,0]
	v_mfma_scale_f32_16x16x128_f8f6f4 v[228:231], v[156:163], v[72:79], v[28:31], v138, v138 op_sel_hi:[0,0,0]
	v_mfma_scale_f32_16x16x128_f8f6f4 v[232:235], v[164:171], v[72:79], v[24:27], v138, v138 op_sel_hi:[0,0,0]
	v_mfma_scale_f32_16x16x128_f8f6f4 v[236:239], v[156:163], v[80:87], v[12:15], v138, v138 op_sel_hi:[0,0,0]
	v_mfma_scale_f32_16x16x128_f8f6f4 v[240:243], v[164:171], v[80:87], v[8:11], v138, v138 op_sel_hi:[0,0,0]
	ds_read_b32 v255, v255 offset:4096
	v_mfma_scale_f32_16x16x128_f8f6f4 v[244:247], v[156:163], v[88:95], v[4:7], v138, v138 op_sel_hi:[0,0,0]
	v_mfma_scale_f32_16x16x128_f8f6f4 v[248:251], v[164:171], v[88:95], v[0:3], v138, v138 op_sel_hi:[0,0,0]
	s_add_u32 s98, s98, 0x80000
	s_waitcnt lgkmcnt(0)
	v_readfirstlane_b32 s101, v255
	v_mov_b32_e32 v255, 0x20000
	s_cmp_ge_u32 s101, s98
	s_cbranch_scc1 .Lmy_g_49

; #define PG8_STAGE(bufoff, gbase, voff) do { _Pragma("unroll") for (int _i = 0; _i < 2; ++_i) { unsigned keep_; \
;         asm volatile("s_mov_b32 %0, m0\n\ts_mov_b32 m0, %3\n\ts_nop 0\n\tglobal_load_lds_dwordx4 %1, %2\n\ts_mov_b32 m0, %0" : "=&s"(keep_) : "v"((voff)[_i]), "s"((const char*)(gbase)), "s"(ldsbase + (unsigned)((bufoff) + _i * 8192)) : "memory"); } } while (0)
; #define PG8_WAIT_V(n) asm volatile("s_waitcnt vmcnt(" #n ")" ::: "memory")
; #define PG8_WAIT_L(n) asm volatile("s_waitcnt lgkmcnt(" #n ")" ::: "memory")
; #define PG8_BAR __builtin_amdgcn_s_barrier()
; #define PG8_SCHED __builtin_amdgcn_sched_barrier(0)
; template <class Epi, class Sched, bool ALIGN_EPI, bool FP8 = false>
; DI void gemm_phase(LAS unsigned char* lds, const Gemm g, const Sched& S, const Epi& E) {
;     ...
;             PG8_LDB(B0, 1, 0); PG8_LDB(B1, 1, 1); PG8_SCHED; PG8_LDA(At, 1, 0); PG8_STAGE(PG8_SA(0, 1), a2 + hstepA, voffA);
;             PG8_WAIT_V(8); PG8_WAIT_L(0); PG8_BAR; PG8_MMA(0, 0, At, B0); PG8_MMA(0, 1, At, B1); PG8_BAR; PG8_SCHED;
.Lmy_g_49:
	s_setprio 0
	s_nop 4
	ds_read_b128 v[0:3], v131 offset:32768
	ds_read_b128 v[4:7], v131 offset:32784
	ds_read_b128 v[8:11], v131 offset:34816
	ds_read_b128 v[12:15], v131 offset:34832
	ds_read_b128 v[140:143], v131 offset:49152
	ds_read_b128 v[144:147], v131 offset:49168
	ds_read_b128 v[148:151], v131 offset:51200
	ds_read_b128 v[152:155], v131 offset:51216
	ds_read_b128 v[16:19], v130 offset:32768
	ds_read_b128 v[20:23], v130 offset:32784
	ds_read_b128 v[24:27], v130 offset:34816
	ds_read_b128 v[28:31], v130 offset:34832
	ds_read_b128 v[32:35], v130 offset:36864
	ds_read_b128 v[36:39], v130 offset:36880
	ds_read_b128 v[40:43], v130 offset:38912
	ds_read_b128 v[44:47], v130 offset:38928
	s_add_u32 s44, s52, 0xe0000
	s_addc_u32 s45, s53, 0
	s_mov_b32 s52, m0
	s_mov_b32 m0, s62
	s_nop 0
	global_load_lds_dwordx4 v132, s[44:45]
	s_mov_b32 m0, s52
	s_nop 0
	s_mov_b32 s52, m0
	s_mov_b32 m0, s63
	s_nop 0
	global_load_lds_dwordx4 v134, s[44:45]
	s_mov_b32 m0, s52
	s_waitcnt vmcnt(8)
	s_waitcnt lgkmcnt(0)
	s_barrier
	s_setprio 1
	v_mfma_scale_f32_16x16x128_f8f6f4 v[124:127], v[0:7], v[16:23], v[124:127], v138, v138 op_sel_hi:[0,0,0]
	v_mfma_scale_f32_16x16x128_f8f6f4 v[120:123], v[8:15], v[16:23], v[120:123], v138, v138 op_sel_hi:[0,0,0]
	v_mfma_scale_f32_16x16x128_f8f6f4 v[116:119], v[0:7], v[24:31], v[116:119], v138, v138 op_sel_hi:[0,0,0]
	v_mfma_scale_f32_16x16x128_f8f6f4 v[112:115], v[8:15], v[24:31], v[112:115], v138, v138 op_sel_hi:[0,0,0]
	v_mfma_scale_f32_16x16x128_f8f6f4 v[100:103], v[0:7], v[32:39], v[100:103], v138, v138 op_sel_hi:[0,0,0]
	v_mfma_scale_f32_16x16x128_f8f6f4 v[96:99], v[8:15], v[32:39], v[96:99], v138, v138 op_sel_hi:[0,0,0]
	v_mfma_scale_f32_16x16x128_f8f6f4 v[84:87], v[0:7], v[40:47], v[204:207], v138, v138 op_sel_hi:[0,0,0]
	v_mfma_scale_f32_16x16x128_f8f6f4 v[80:83], v[8:15], v[40:47], v[208:211], v138, v138 op_sel_hi:[0,0,0]
	v_mfma_scale_f32_16x16x128_f8f6f4 v[108:111], v[140:147], v[16:23], v[108:111], v138, v138 op_sel_hi:[0,0,0]
	v_mfma_scale_f32_16x16x128_f8f6f4 v[104:107], v[148:155], v[16:23], v[104:107], v138, v138 op_sel_hi:[0,0,0]
	v_mfma_scale_f32_16x16x128_f8f6f4 v[92:95], v[140:147], v[24:31], v[172:175], v138, v138 op_sel_hi:[0,0,0]
	v_mfma_scale_f32_16x16x128_f8f6f4 v[88:91], v[148:155], v[24:31], v[176:179], v138, v138 op_sel_hi:[0,0,0]
	v_mfma_scale_f32_16x16x128_f8f6f4 v[76:79], v[140:147], v[32:39], v[180:183], v138, v138 op_sel_hi:[0,0,0]
	v_mfma_scale_f32_16x16x128_f8f6f4 v[72:75], v[148:155], v[32:39], v[184:187], v138, v138 op_sel_hi:[0,0,0]
	ds_read_b32 v255, v255 offset:4096
	v_mfma_scale_f32_16x16x128_f8f6f4 v[68:71], v[140:147], v[40:47], v[188:191], v138, v138 op_sel_hi:[0,0,0]
	v_mfma_scale_f32_16x16x128_f8f6f4 v[64:67], v[148:155], v[40:47], v[192:195], v138, v138 op_sel_hi:[0,0,0]
	s_add_u32 s98, s98, 0x80000
	s_waitcnt lgkmcnt(0)
	v_readfirstlane_b32 s101, v255
	v_mov_b32_e32 v255, 0x20000
	s_cmp_ge_u32 s101, s98
	s_cbranch_scc1 .Lmy_g_50

; #define PG8_STAGE(bufoff, gbase, voff) do { _Pragma("unroll") for (int _i = 0; _i < 2; ++_i) { unsigned keep_; \
;         asm volatile("s_mov_b32 %0, m0\n\ts_mov_b32 m0, %3\n\ts_nop 0\n\tglobal_load_lds_dwordx4 %1, %2\n\ts_mov_b32 m0, %0" : "=&s"(keep_) : "v"((voff)[_i]), "s"((const char*)(gbase)), "s"(ldsbase + (unsigned)((bufoff) + _i * 8192)) : "memory"); } } while (0)
; #define PG8_WAIT_V(n) asm volatile("s_waitcnt vmcnt(" #n ")" ::: "memory")
; #define PG8_WAIT_L(n) asm volatile("s_waitcnt lgkmcnt(" #n ")" ::: "memory")
; #define PG8_BAR __builtin_amdgcn_s_barrier()
; #define PG8_SCHED __builtin_amdgcn_sched_barrier(0)
; template <class Epi, class Sched, bool ALIGN_EPI, bool FP8 = false>
; DI void gemm_phase(LAS unsigned char* lds, const Gemm g, const Sched& S, const Epi& E) {
;     ...
;             PG8_LDA(At, 1, 1); PG8_STAGE(PG8_SB(1, 0), b3, voffB); PG8_STAGE(PG8_SB(1, 1), b3 + hstepB, voffB); PG8_STAGE(PG8_SA(1, 0), a3, voffA);
;             PG8_WAIT_V(8); PG8_WAIT_L(0); PG8_BAR; PG8_MMA(1, 0, At, B0); PG8_MMA(1, 1, At, B1); PG8_BAR; PG8_SCHED;
.Lmy_g_50:
	s_setprio 0
	ds_read_b128 v[24:27], v130 offset:49152
	ds_read_b128 v[28:31], v130 offset:49168
	ds_read_b128 v[156:159], v130 offset:51200
	ds_read_b128 v[160:163], v130 offset:51216
	ds_read_b128 v[164:167], v130 offset:53248
	ds_read_b128 v[168:171], v130 offset:53264
	ds_read_b128 v[172:175], v130 offset:55296
	ds_read_b128 v[176:179], v130 offset:55312
	s_add_u32 s44, s50, 0x80
	s_addc_u32 s45, s51, 0
	s_mov_b32 s52, m0
	s_mov_b32 m0, s67
	s_nop 0
	global_load_lds_dwordx4 v133, s[44:45]
	s_mov_b32 m0, s52
	s_nop 0
	s_mov_b32 s52, m0
	s_mov_b32 m0, s68
	s_nop 0
	global_load_lds_dwordx4 v135, s[44:45]
	s_mov_b32 m0, s52
	s_add_u32 s44, s50, 0xe0080
	s_addc_u32 s45, s51, 0
	s_mov_b32 s50, m0
	s_mov_b32 m0, s71
	s_nop 0
	global_load_lds_dwordx4 v133, s[44:45]
	s_mov_b32 m0, s50
	s_nop 0
	s_mov_b32 s50, m0
	s_mov_b32 m0, s72
	s_nop 0
	global_load_lds_dwordx4 v135, s[44:45]
	s_mov_b32 m0, s50
	s_mov_b32 s44, m0
	s_mov_b32 m0, s69
	s_nop 0
	global_load_lds_dwordx4 v132, s[48:49]
	s_mov_b32 m0, s44
	s_nop 0
	s_mov_b32 s44, m0
	s_mov_b32 m0, s70
	s_nop 0
	global_load_lds_dwordx4 v134, s[48:49]
	s_mov_b32 m0, s44
	s_waitcnt vmcnt(8)
	s_waitcnt lgkmcnt(0)
	s_barrier
	s_setprio 1
	v_mfma_scale_f32_16x16x128_f8f6f4 v[60:63], v[0:7], v[24:31], v[60:63], v138, v138 op_sel_hi:[0,0,0]
	v_mfma_scale_f32_16x16x128_f8f6f4 v[56:59], v[8:15], v[24:31], v[56:59], v138, v138 op_sel_hi:[0,0,0]
	v_mfma_scale_f32_16x16x128_f8f6f4 v[52:55], v[0:7], v[156:163], v[52:55], v138, v138 op_sel_hi:[0,0,0]
	v_mfma_scale_f32_16x16x128_f8f6f4 v[48:51], v[8:15], v[156:163], v[48:51], v138, v138 op_sel_hi:[0,0,0]
	v_mfma_scale_f32_16x16x128_f8f6f4 v[36:39], v[0:7], v[164:171], v[196:199], v138, v138 op_sel_hi:[0,0,0]
	v_mfma_scale_f32_16x16x128_f8f6f4 v[32:35], v[8:15], v[164:171], v[200:203], v138, v138 op_sel_hi:[0,0,0]
	v_mfma_scale_f32_16x16x128_f8f6f4 v[20:23], v[0:7], v[172:179], v[212:215], v138, v138 op_sel_hi:[0,0,0]
	v_mfma_scale_f32_16x16x128_f8f6f4 v[16:19], v[8:15], v[172:179], v[216:219], v138, v138 op_sel_hi:[0,0,0]
	v_mfma_scale_f32_16x16x128_f8f6f4 v[44:47], v[140:147], v[24:31], v[220:223], v138, v138 op_sel_hi:[0,0,0]
	v_mfma_scale_f32_16x16x128_f8f6f4 v[40:43], v[148:155], v[24:31], v[224:227], v138, v138 op_sel_hi:[0,0,0]
	v_mfma_scale_f32_16x16x128_f8f6f4 v[28:31], v[140:147], v[156:163], v[228:231], v138, v138 op_sel_hi:[0,0,0]
	v_mfma_scale_f32_16x16x128_f8f6f4 v[24:27], v[148:155], v[156:163], v[232:235], v138, v138 op_sel_hi:[0,0,0]
	v_mfma_scale_f32_16x16x128_f8f6f4 v[12:15], v[140:147], v[164:171], v[236:239], v138, v138 op_sel_hi:[0,0,0]
	v_mfma_scale_f32_16x16x128_f8f6f4 v[8:11], v[148:155], v[164:171], v[240:243], v138, v138 op_sel_hi:[0,0,0]
	ds_read_b32 v255, v255 offset:4096
	v_mfma_scale_f32_16x16x128_f8f6f4 v[4:7], v[140:147], v[172:179], v[244:247], v138, v138 op_sel_hi:[0,0,0]
	v_mfma_scale_f32_16x16x128_f8f6f4 v[0:3], v[148:155], v[172:179], v[248:251], v138, v138 op_sel_hi:[0,0,0]
	s_add_u32 s98, s98, 0x80000
	s_waitcnt lgkmcnt(0)
	v_readfirstlane_b32 s101, v255
	v_mov_b32_e32 v255, 0x20000
	s_cmp_ge_u32 s101, s98
	s_cbranch_scc1 .Lmy_g_51

; #define PG8_WAIT_V(n) asm volatile("s_waitcnt vmcnt(" #n ")" ::: "memory")
; #define PG8_WAIT_L(n) asm volatile("s_waitcnt lgkmcnt(" #n ")" ::: "memory")
; #define PG8_BAR __builtin_amdgcn_s_barrier()
; #define PG8_SCHED __builtin_amdgcn_sched_barrier(0)
; template <class Epi, class Sched, bool ALIGN_EPI, bool FP8 = false>
; DI void gemm_phase(LAS unsigned char* lds, const Gemm g, const Sched& S, const Epi& E) {
;     ...
;             PG8_WAIT_V(8); PG8_WAIT_L(0); PG8_BAR; PG8_MMA(1, 0, At, B0); PG8_MMA(1, 1, At, B1); PG8_BAR; PG8_SCHED;
;         }
.Lmy_g_51:
	s_setprio 0
	s_add_i32 s92, s92, 2
	s_add_u32 s90, s90, 0x100
	s_addc_u32 s91, s91, 0
	s_cmp_gt_u32 s92, 53
	s_mov_b64 s[44:45], s[46:47]
	s_cbranch_scc0 .Lmy_g0_1685

; #define PG8_STAGE(bufoff, gbase, voff) do { _Pragma("unroll") for (int _i = 0; _i < 2; ++_i) { unsigned keep_; \
;         asm volatile("s_mov_b32 %0, m0\n\ts_mov_b32 m0, %3\n\ts_nop 0\n\tglobal_load_lds_dwordx4 %1, %2\n\ts_mov_b32 m0, %0" : "=&s"(keep_) : "v"((voff)[_i]), "s"((const char*)(gbase)), "s"(ldsbase + (unsigned)((bufoff) + _i * 8192)) : "memory"); } } while (0)
; #define PG8_WAIT_V(n) asm volatile("s_waitcnt vmcnt(" #n ")" ::: "memory")
; #define PG8_WAIT_L(n) asm volatile("s_waitcnt lgkmcnt(" #n ")" ::: "memory")
; #define PG8_BAR __builtin_amdgcn_s_barrier()
; #define PG8_SCHED __builtin_amdgcn_sched_barrier(0)
;     DI int nt(const Unit& u) const { return (u.aux & 8) ? PLED / 64 : ((u.aux & 4) ? (D_ / 2) / 64 : D_ / 64); }
; template <class Epi, class Sched, bool ALIGN_EPI, bool FP8 = false>
; DI void gemm_phase(LAS unsigned char* lds, const Gemm g, const Sched& S, const Epi& E) {
;     ...
;             const bool last = (t == nt - 2);
;             const char* a1 = cA + (size_t)(t + 1) * kstep;
;             const char* a2 = last ? nA : cA + (size_t)(t + 2) * kstep; const char* b2 = last ? nB : cB + (size_t)(t + 2) * kstep;
;             const char* a3 = a2 + kstep; const char* b3 = b2 + kstep;
;             PG8_LDB(B0, 0, 0); PG8_LDB(B1, 0, 1); PG8_SCHED; PG8_LDA(At, 0, 0); PG8_STAGE(PG8_SA(1, 1), a1 + hstepA, voffA);
;             PG8_WAIT_V(8); PG8_WAIT_L(0); PG8_BAR; PG8_MMA(0, 0, At, B0); PG8_MMA(0, 1, At, B1); PG8_BAR; PG8_SCHED;
;             PG8_LDA(At, 0, 1); PG8_STAGE(PG8_SB(0, 0), b2, voffB); PG8_STAGE(PG8_SB(0, 1), b2 + hstepB, voffB); PG8_STAGE(PG8_SA(0, 0), a2, voffA);
.LBB0_1710:
	s_cmp_lg_u32 s99, 0
	s_cbranch_scc1 .Lmy_g0_1710
	ds_read_b128 v[146:149], v140
	ds_read_b128 v[150:153], v140 offset:1024
	ds_read_b128 v[154:157], v140 offset:2048
	ds_read_b128 v[158:161], v140 offset:3072
	ds_read_b128 v[162:165], v141
	ds_read_b128 v[166:169], v141 offset:1024
	ds_read_b128 v[170:173], v141 offset:2048
	ds_read_b128 v[174:177], v141 offset:3072
	s_add_u32 s64, s62, 0x100
	s_addc_u32 s65, s63, 0
	s_cmp_eq_u32 vcc_lo, 28
	s_cselect_b32 s70, s94, s64
	s_cselect_b32 s71, s55, s65
	s_cselect_b32 s68, s95, s96
	s_cselect_b32 s69, s53, s97
	s_add_u32 s66, s70, 0x80
	s_addc_u32 s67, s71, 0
	ds_read_b128 v[178:181], v142
	ds_read_b128 v[182:185], v142 offset:1024
	ds_read_b128 v[186:189], v142 offset:2048
	ds_read_b128 v[190:193], v142 offset:3072
	ds_read_b128 v[194:197], v142 offset:4096
	ds_read_b128 v[198:201], v142 offset:5120
	ds_read_b128 v[202:205], v142 offset:6144
	ds_read_b128 v[206:209], v142 offset:7168
	s_add_u32 s62, s62, 0x80080
	s_addc_u32 s63, s63, 0
	s_mov_b32 vcc_hi, m0
	s_mov_b32 m0, s89
	s_nop 0
	global_load_lds_dwordx4 v134, s[62:63]
	s_mov_b32 m0, vcc_hi
	s_nop 0
	s_mov_b32 vcc_hi, m0
	s_mov_b32 m0, s90
	s_nop 0
	global_load_lds_dwordx4 v136, s[62:63]
	s_mov_b32 m0, vcc_hi
	s_waitcnt vmcnt(8)
	s_waitcnt lgkmcnt(0)
	s_mov_b64 exec, 1
	ds_add_u32 v255, v255 offset:4096
	s_mov_b64 exec, -1
	s_setprio 1
	v_mfma_f32_16x16x32_bf16 v[124:127], v[146:149], v[178:181], v[124:127]
	v_mfma_f32_16x16x32_bf16 v[120:123], v[154:157], v[178:181], v[120:123]
	v_mfma_f32_16x16x32_bf16 v[108:111], v[146:149], v[186:189], v[108:111]
	v_mfma_f32_16x16x32_bf16 v[104:107], v[154:157], v[186:189], v[104:107]
	v_mfma_f32_16x16x32_bf16 v[92:95], v[146:149], v[194:197], v[92:95]
	v_mfma_f32_16x16x32_bf16 v[88:91], v[154:157], v[194:197], v[88:91]
	v_mfma_f32_16x16x32_bf16 v[76:79], v[146:149], v[202:205], v[76:79]
	v_mfma_f32_16x16x32_bf16 v[72:75], v[154:157], v[202:205], v[72:75]
	v_mfma_f32_16x16x32_bf16 v[124:127], v[150:153], v[182:185], v[124:127]
	v_mfma_f32_16x16x32_bf16 v[120:123], v[158:161], v[182:185], v[120:123]
	v_mfma_f32_16x16x32_bf16 v[108:111], v[150:153], v[190:193], v[108:111]
	v_mfma_f32_16x16x32_bf16 v[104:107], v[158:161], v[190:193], v[104:107]
	v_mfma_f32_16x16x32_bf16 v[92:95], v[150:153], v[198:201], v[92:95]
	v_mfma_f32_16x16x32_bf16 v[88:91], v[158:161], v[198:201], v[88:91]
	v_mfma_f32_16x16x32_bf16 v[76:79], v[150:153], v[206:209], v[76:79]
	v_mfma_f32_16x16x32_bf16 v[72:75], v[158:161], v[206:209], v[72:75]
	v_mfma_f32_16x16x32_bf16 v[116:119], v[162:165], v[178:181], v[116:119]
	v_mfma_f32_16x16x32_bf16 v[112:115], v[170:173], v[178:181], v[112:115]
	v_mfma_f32_16x16x32_bf16 v[100:103], v[162:165], v[186:189], v[100:103]
	v_mfma_f32_16x16x32_bf16 v[96:99], v[170:173], v[186:189], v[96:99]
	v_mfma_f32_16x16x32_bf16 v[84:87], v[162:165], v[194:197], v[84:87]
	v_mfma_f32_16x16x32_bf16 v[80:83], v[170:173], v[194:197], v[80:83]
	v_mfma_f32_16x16x32_bf16 v[68:71], v[162:165], v[202:205], v[68:71]
	v_mfma_f32_16x16x32_bf16 v[64:67], v[170:173], v[202:205], v[64:67]
	v_mfma_f32_16x16x32_bf16 v[116:119], v[166:169], v[182:185], v[116:119]
	v_mfma_f32_16x16x32_bf16 v[112:115], v[174:177], v[182:185], v[112:115]
	v_mfma_f32_16x16x32_bf16 v[100:103], v[166:169], v[190:193], v[100:103]
	v_mfma_f32_16x16x32_bf16 v[96:99], v[174:177], v[190:193], v[96:99]
	v_mfma_f32_16x16x32_bf16 v[84:87], v[166:169], v[198:201], v[84:87]
	v_mfma_f32_16x16x32_bf16 v[80:83], v[174:177], v[198:201], v[80:83]
	v_mfma_f32_16x16x32_bf16 v[68:71], v[166:169], v[206:209], v[68:71]
	v_mfma_f32_16x16x32_bf16 v[64:67], v[174:177], v[206:209], v[64:67]
	s_setprio 0
	s_barrier
	ds_read_b128 v[178:181], v142 offset:16384
	ds_read_b128 v[182:185], v142 offset:17408
	ds_read_b128 v[186:189], v142 offset:18432
	ds_read_b128 v[190:193], v142 offset:19456
	ds_read_b128 v[194:197], v142 offset:20480
	ds_read_b128 v[198:201], v142 offset:21504
	ds_read_b128 v[202:205], v142 offset:22528
	ds_read_b128 v[206:209], v142 offset:23552
	s_mov_b32 s62, m0
	s_mov_b32 m0, s61
	s_nop 0
	global_load_lds_dwordx4 v135, s[68:69]
	s_mov_b32 m0, s62
	s_nop 0
	s_mov_b32 s62, m0
	s_mov_b32 m0, s75
	s_nop 0
	global_load_lds_dwordx4 v137, s[68:69]
	s_mov_b32 m0, s62
	s_add_u32 s62, s68, 0x80000
	s_addc_u32 s63, s69, 0
	s_mov_b32 vcc_hi, m0
	s_mov_b32 m0, s77
	s_nop 0
	global_load_lds_dwordx4 v135, s[62:63]
	s_mov_b32 m0, vcc_hi
	s_nop 0
	s_mov_b32 vcc_hi, m0
	s_mov_b32 m0, s79
	s_nop 0
	global_load_lds_dwordx4 v137, s[62:63]
	s_mov_b32 m0, vcc_hi
	s_mov_b32 s62, m0
	s_mov_b32 m0, s74
	s_nop 0
	global_load_lds_dwordx4 v134, s[70:71]
	s_mov_b32 m0, s62
	s_nop 0
	s_mov_b32 s62, m0
	s_mov_b32 m0, s80
	s_nop 0
	global_load_lds_dwordx4 v136, s[70:71]
	s_mov_b32 m0, s62
	s_waitcnt vmcnt(8)
	s_waitcnt lgkmcnt(0)
; #define PG8_STAGE(bufoff, gbase, voff) do { _Pragma("unroll") for (int _i = 0; _i < 2; ++_i) { unsigned keep_; \
;         asm volatile("s_mov_b32 %0, m0\n\ts_mov_b32 m0, %3\n\ts_nop 0\n\tglobal_load_lds_dwordx4 %1, %2\n\ts_mov_b32 m0, %0" : "=&s"(keep_) : "v"((voff)[_i]), "s"((const char*)(gbase)), "s"(ldsbase + (unsigned)((bufoff) + _i * 8192)) : "memory"); } } while (0)
; #define PG8_WAIT_V(n) asm volatile("s_waitcnt vmcnt(" #n ")" ::: "memory")
; #define PG8_WAIT_L(n) asm volatile("s_waitcnt lgkmcnt(" #n ")" ::: "memory")
; #define PG8_BAR __builtin_amdgcn_s_barrier()
; #define PG8_SCHED __builtin_amdgcn_sched_barrier(0)
; template <class Epi, class Sched, bool ALIGN_EPI, bool FP8 = false>
; DI void gemm_phase(LAS unsigned char* lds, const Gemm g, const Sched& S, const Epi& E) {
;     ...
;             PG8_WAIT_V(8); PG8_WAIT_L(0); PG8_BAR; PG8_MMA(1, 0, At, B0); PG8_MMA(1, 1, At, B1); PG8_BAR; PG8_SCHED;
;             PG8_LDB(B0, 1, 0); PG8_LDB(B1, 1, 1); PG8_SCHED; PG8_LDA(At, 1, 0); PG8_STAGE(PG8_SA(0, 1), a2 + hstepA, voffA);
;             PG8_WAIT_V(8); PG8_WAIT_L(0); PG8_BAR; PG8_MMA(0, 0, At, B0); PG8_MMA(0, 1, At, B1); PG8_BAR; PG8_SCHED;
;             PG8_LDA(At, 1, 1); PG8_STAGE(PG8_SB(1, 0), b3, voffB); PG8_STAGE(PG8_SB(1, 1), b3 + hstepB, voffB); PG8_STAGE(PG8_SA(1, 0), a3, voffA);
	s_mov_b64 exec, 1
	ds_add_u32 v255, v255 offset:4096
	s_mov_b64 exec, -1
	s_setprio 1
	v_mfma_f32_16x16x32_bf16 v[60:63], v[146:149], v[178:181], v[60:63]
	v_mfma_f32_16x16x32_bf16 v[56:59], v[154:157], v[178:181], v[56:59]
	v_mfma_f32_16x16x32_bf16 v[44:47], v[146:149], v[186:189], v[44:47]
	v_mfma_f32_16x16x32_bf16 v[40:43], v[154:157], v[186:189], v[40:43]
	v_mfma_f32_16x16x32_bf16 v[28:31], v[146:149], v[194:197], v[28:31]
	v_mfma_f32_16x16x32_bf16 v[24:27], v[154:157], v[194:197], v[24:27]
	v_mfma_f32_16x16x32_bf16 v[12:15], v[146:149], v[202:205], v[12:15]
	v_mfma_f32_16x16x32_bf16 v[8:11], v[154:157], v[202:205], v[8:11]
	v_mfma_f32_16x16x32_bf16 v[60:63], v[150:153], v[182:185], v[60:63]
	v_mfma_f32_16x16x32_bf16 v[56:59], v[158:161], v[182:185], v[56:59]
	v_mfma_f32_16x16x32_bf16 v[44:47], v[150:153], v[190:193], v[44:47]
	v_mfma_f32_16x16x32_bf16 v[40:43], v[158:161], v[190:193], v[40:43]
	v_mfma_f32_16x16x32_bf16 v[28:31], v[150:153], v[198:201], v[28:31]
	v_mfma_f32_16x16x32_bf16 v[24:27], v[158:161], v[198:201], v[24:27]
	v_mfma_f32_16x16x32_bf16 v[12:15], v[150:153], v[206:209], v[12:15]
	v_mfma_f32_16x16x32_bf16 v[8:11], v[158:161], v[206:209], v[8:11]
	v_mfma_f32_16x16x32_bf16 v[52:55], v[162:165], v[178:181], v[52:55]
	v_mfma_f32_16x16x32_bf16 v[48:51], v[170:173], v[178:181], v[48:51]
	v_mfma_f32_16x16x32_bf16 v[36:39], v[162:165], v[186:189], v[36:39]
	v_mfma_f32_16x16x32_bf16 v[32:35], v[170:173], v[186:189], v[32:35]
	v_mfma_f32_16x16x32_bf16 v[20:23], v[162:165], v[194:197], v[20:23]
	v_mfma_f32_16x16x32_bf16 v[16:19], v[170:173], v[194:197], v[16:19]
	v_mfma_f32_16x16x32_bf16 v[4:7], v[162:165], v[202:205], v[4:7]
	v_mfma_f32_16x16x32_bf16 v[0:3], v[170:173], v[202:205], v[0:3]
	v_mfma_f32_16x16x32_bf16 v[52:55], v[166:169], v[182:185], v[52:55]
	v_mfma_f32_16x16x32_bf16 v[48:51], v[174:177], v[182:185], v[48:51]
	v_mfma_f32_16x16x32_bf16 v[36:39], v[166:169], v[190:193], v[36:39]
	v_mfma_f32_16x16x32_bf16 v[32:35], v[174:177], v[190:193], v[32:35]
	v_mfma_f32_16x16x32_bf16 v[20:23], v[166:169], v[198:201], v[20:23]
	v_mfma_f32_16x16x32_bf16 v[16:19], v[174:177], v[198:201], v[16:19]
	v_mfma_f32_16x16x32_bf16 v[4:7], v[166:169], v[206:209], v[4:7]
	v_mfma_f32_16x16x32_bf16 v[0:3], v[174:177], v[206:209], v[0:3]
	s_setprio 0
	s_barrier
	ds_read_b128 v[146:149], v143
	ds_read_b128 v[150:153], v143 offset:1024
	ds_read_b128 v[154:157], v143 offset:2048
	ds_read_b128 v[158:161], v143 offset:3072
	ds_read_b128 v[162:165], v144
	ds_read_b128 v[166:169], v144 offset:1024
	ds_read_b128 v[170:173], v144 offset:2048
	ds_read_b128 v[174:177], v144 offset:3072
	ds_read_b128 v[178:181], v142 offset:32768
	ds_read_b128 v[182:185], v142 offset:33792
	ds_read_b128 v[186:189], v142 offset:34816
	ds_read_b128 v[190:193], v142 offset:35840
	ds_read_b128 v[194:197], v142 offset:36864
	ds_read_b128 v[198:201], v142 offset:37888
	ds_read_b128 v[202:205], v142 offset:38912
	ds_read_b128 v[206:209], v142 offset:39936
	s_add_u32 s62, s70, 0x80000
	s_addc_u32 s63, s71, 0
	s_mov_b32 s70, m0
	s_mov_b32 m0, s81
	s_nop 0
	global_load_lds_dwordx4 v134, s[62:63]
	s_mov_b32 m0, s70
	s_nop 0
	s_mov_b32 s70, m0
	s_mov_b32 m0, s82
	s_nop 0
	global_load_lds_dwordx4 v136, s[62:63]
	s_mov_b32 m0, s70
	s_waitcnt vmcnt(8)
	s_waitcnt lgkmcnt(0)
	s_mov_b64 exec, 1
	ds_add_u32 v255, v255 offset:4096
	s_mov_b64 exec, -1
	s_setprio 1
	v_mfma_f32_16x16x32_bf16 v[124:127], v[146:149], v[178:181], v[124:127]
	v_mfma_f32_16x16x32_bf16 v[120:123], v[154:157], v[178:181], v[120:123]
	v_mfma_f32_16x16x32_bf16 v[108:111], v[146:149], v[186:189], v[108:111]
	v_mfma_f32_16x16x32_bf16 v[104:107], v[154:157], v[186:189], v[104:107]
	v_mfma_f32_16x16x32_bf16 v[92:95], v[146:149], v[194:197], v[92:95]
	v_mfma_f32_16x16x32_bf16 v[88:91], v[154:157], v[194:197], v[88:91]
	v_mfma_f32_16x16x32_bf16 v[76:79], v[146:149], v[202:205], v[76:79]
	v_mfma_f32_16x16x32_bf16 v[72:75], v[154:157], v[202:205], v[72:75]
	v_mfma_f32_16x16x32_bf16 v[124:127], v[150:153], v[182:185], v[124:127]
	v_mfma_f32_16x16x32_bf16 v[120:123], v[158:161], v[182:185], v[120:123]
	v_mfma_f32_16x16x32_bf16 v[108:111], v[150:153], v[190:193], v[108:111]
	v_mfma_f32_16x16x32_bf16 v[104:107], v[158:161], v[190:193], v[104:107]
	v_mfma_f32_16x16x32_bf16 v[92:95], v[150:153], v[198:201], v[92:95]
	v_mfma_f32_16x16x32_bf16 v[88:91], v[158:161], v[198:201], v[88:91]
	v_mfma_f32_16x16x32_bf16 v[76:79], v[150:153], v[206:209], v[76:79]
	v_mfma_f32_16x16x32_bf16 v[72:75], v[158:161], v[206:209], v[72:75]
	v_mfma_f32_16x16x32_bf16 v[116:119], v[162:165], v[178:181], v[116:119]
	v_mfma_f32_16x16x32_bf16 v[112:115], v[170:173], v[178:181], v[112:115]
	v_mfma_f32_16x16x32_bf16 v[100:103], v[162:165], v[186:189], v[100:103]
	v_mfma_f32_16x16x32_bf16 v[96:99], v[170:173], v[186:189], v[96:99]
	v_mfma_f32_16x16x32_bf16 v[84:87], v[162:165], v[194:197], v[84:87]
	v_mfma_f32_16x16x32_bf16 v[80:83], v[170:173], v[194:197], v[80:83]
	v_mfma_f32_16x16x32_bf16 v[68:71], v[162:165], v[202:205], v[68:71]
	v_mfma_f32_16x16x32_bf16 v[64:67], v[170:173], v[202:205], v[64:67]
	v_mfma_f32_16x16x32_bf16 v[116:119], v[166:169], v[182:185], v[116:119]
	v_mfma_f32_16x16x32_bf16 v[112:115], v[174:177], v[182:185], v[112:115]
	v_mfma_f32_16x16x32_bf16 v[100:103], v[166:169], v[190:193], v[100:103]
	v_mfma_f32_16x16x32_bf16 v[96:99], v[174:177], v[190:193], v[96:99]
	v_mfma_f32_16x16x32_bf16 v[84:87], v[166:169], v[198:201], v[84:87]
	v_mfma_f32_16x16x32_bf16 v[80:83], v[174:177], v[198:201], v[80:83]
	v_mfma_f32_16x16x32_bf16 v[68:71], v[166:169], v[206:209], v[68:71]
	v_mfma_f32_16x16x32_bf16 v[64:67], v[174:177], v[206:209], v[64:67]
	s_setprio 0
	s_barrier
; #define PG8_STAGE(bufoff, gbase, voff) do { _Pragma("unroll") for (int _i = 0; _i < 2; ++_i) { unsigned keep_; \
;         asm volatile("s_mov_b32 %0, m0\n\ts_mov_b32 m0, %3\n\ts_nop 0\n\tglobal_load_lds_dwordx4 %1, %2\n\ts_mov_b32 m0, %0" : "=&s"(keep_) : "v"((voff)[_i]), "s"((const char*)(gbase)), "s"(ldsbase + (unsigned)((bufoff) + _i * 8192)) : "memory"); } } while (0)
; #define PG8_WAIT_V(n) asm volatile("s_waitcnt vmcnt(" #n ")" ::: "memory")
; #define PG8_WAIT_L(n) asm volatile("s_waitcnt lgkmcnt(" #n ")" ::: "memory")
; #define PG8_BAR __builtin_amdgcn_s_barrier()
; #define PG8_SCHED __builtin_amdgcn_sched_barrier(0)
; template <class Epi, class Sched, bool ALIGN_EPI, bool FP8 = false>
; DI void gemm_phase(LAS unsigned char* lds, const Gemm g, const Sched& S, const Epi& E) {
;     ...
;             PG8_LDA(At, 1, 1); PG8_STAGE(PG8_SB(1, 0), b3, voffB); PG8_STAGE(PG8_SB(1, 1), b3 + hstepB, voffB); PG8_STAGE(PG8_SA(1, 0), a3, voffA);
;             PG8_WAIT_V(8); PG8_WAIT_L(0); PG8_BAR; PG8_MMA(1, 0, At, B0); PG8_MMA(1, 1, At, B1); PG8_BAR; PG8_SCHED;
;         }
	ds_read_b128 v[178:181], v142 offset:49152
	ds_read_b128 v[182:185], v142 offset:50176
	ds_read_b128 v[186:189], v142 offset:51200
	ds_read_b128 v[190:193], v142 offset:52224
	ds_read_b128 v[194:197], v142 offset:53248
	ds_read_b128 v[198:201], v142 offset:54272
	ds_read_b128 v[202:205], v142 offset:55296
	ds_read_b128 v[206:209], v142 offset:56320
	s_add_u32 s62, s68, 0x80
	s_addc_u32 s63, s69, 0
	s_mov_b32 s70, m0
	s_mov_b32 m0, s83
	s_nop 0
	global_load_lds_dwordx4 v135, s[62:63]
	s_mov_b32 m0, s70
	s_nop 0
	s_mov_b32 s70, m0
	s_mov_b32 m0, s84
	s_nop 0
	global_load_lds_dwordx4 v137, s[62:63]
	s_mov_b32 m0, s70
	s_add_u32 s62, s68, 0x80080
	s_addc_u32 s63, s69, 0
	s_mov_b32 s68, m0
	s_mov_b32 m0, s87
	s_nop 0
	global_load_lds_dwordx4 v135, s[62:63]
	s_mov_b32 m0, s68
	s_nop 0
	s_mov_b32 s68, m0
	s_mov_b32 m0, s88
	s_nop 0
	global_load_lds_dwordx4 v137, s[62:63]
	s_mov_b32 m0, s68
	s_mov_b32 s62, m0
	s_mov_b32 m0, s85
	s_nop 0
	global_load_lds_dwordx4 v134, s[66:67]
	s_mov_b32 m0, s62
	s_nop 0
	s_mov_b32 s62, m0
	s_mov_b32 m0, s86
	s_nop 0
	global_load_lds_dwordx4 v136, s[66:67]
	s_mov_b32 m0, s62
	s_waitcnt vmcnt(8)
	s_waitcnt lgkmcnt(0)
	s_mov_b64 exec, 1
	ds_add_u32 v255, v255 offset:4096
	s_mov_b64 exec, -1
	s_setprio 1
	v_mfma_f32_16x16x32_bf16 v[60:63], v[146:149], v[178:181], v[60:63]
	v_mfma_f32_16x16x32_bf16 v[56:59], v[154:157], v[178:181], v[56:59]
	v_mfma_f32_16x16x32_bf16 v[44:47], v[146:149], v[186:189], v[44:47]
	v_mfma_f32_16x16x32_bf16 v[40:43], v[154:157], v[186:189], v[40:43]
	v_mfma_f32_16x16x32_bf16 v[28:31], v[146:149], v[194:197], v[28:31]
	v_mfma_f32_16x16x32_bf16 v[24:27], v[154:157], v[194:197], v[24:27]
	v_mfma_f32_16x16x32_bf16 v[12:15], v[146:149], v[202:205], v[12:15]
	v_mfma_f32_16x16x32_bf16 v[8:11], v[154:157], v[202:205], v[8:11]
	v_mfma_f32_16x16x32_bf16 v[60:63], v[150:153], v[182:185], v[60:63]
	v_mfma_f32_16x16x32_bf16 v[56:59], v[158:161], v[182:185], v[56:59]
	v_mfma_f32_16x16x32_bf16 v[44:47], v[150:153], v[190:193], v[44:47]
	v_mfma_f32_16x16x32_bf16 v[40:43], v[158:161], v[190:193], v[40:43]
	v_mfma_f32_16x16x32_bf16 v[28:31], v[150:153], v[198:201], v[28:31]
	v_mfma_f32_16x16x32_bf16 v[24:27], v[158:161], v[198:201], v[24:27]
	v_mfma_f32_16x16x32_bf16 v[12:15], v[150:153], v[206:209], v[12:15]
	v_mfma_f32_16x16x32_bf16 v[8:11], v[158:161], v[206:209], v[8:11]
	v_mfma_f32_16x16x32_bf16 v[52:55], v[162:165], v[178:181], v[52:55]
	v_mfma_f32_16x16x32_bf16 v[48:51], v[170:173], v[178:181], v[48:51]
	v_mfma_f32_16x16x32_bf16 v[36:39], v[162:165], v[186:189], v[36:39]
	v_mfma_f32_16x16x32_bf16 v[32:35], v[170:173], v[186:189], v[32:35]
	v_mfma_f32_16x16x32_bf16 v[20:23], v[162:165], v[194:197], v[20:23]
	v_mfma_f32_16x16x32_bf16 v[16:19], v[170:173], v[194:197], v[16:19]
	v_mfma_f32_16x16x32_bf16 v[4:7], v[162:165], v[202:205], v[4:7]
	v_mfma_f32_16x16x32_bf16 v[0:3], v[170:173], v[202:205], v[0:3]
	v_mfma_f32_16x16x32_bf16 v[52:55], v[166:169], v[182:185], v[52:55]
	v_mfma_f32_16x16x32_bf16 v[48:51], v[174:177], v[182:185], v[48:51]
	v_mfma_f32_16x16x32_bf16 v[36:39], v[166:169], v[190:193], v[36:39]
	v_mfma_f32_16x16x32_bf16 v[32:35], v[174:177], v[190:193], v[32:35]
	v_mfma_f32_16x16x32_bf16 v[20:23], v[166:169], v[198:201], v[20:23]
	v_mfma_f32_16x16x32_bf16 v[16:19], v[174:177], v[198:201], v[16:19]
	v_mfma_f32_16x16x32_bf16 v[4:7], v[166:169], v[206:209], v[4:7]
	v_mfma_f32_16x16x32_bf16 v[0:3], v[174:177], v[206:209], v[0:3]
	s_setprio 0
	s_barrier
	s_add_i32 vcc_lo, vcc_lo, 2
	s_add_u32 s96, s96, 0x100
	s_addc_u32 s97, s97, 0
	s_cmp_gt_u32 vcc_lo, 29
	s_mov_b64 s[62:63], s[64:65]
	s_cbranch_scc0 .LBB0_1710
	s_branch .Lmy_ex_1710
; #define PG8_STAGE(bufoff, gbase, voff) do { _Pragma("unroll") for (int _i = 0; _i < 2; ++_i) { unsigned keep_; \
;         asm volatile("s_mov_b32 %0, m0\n\ts_mov_b32 m0, %3\n\ts_nop 0\n\tglobal_load_lds_dwordx4 %1, %2\n\ts_mov_b32 m0, %0" : "=&s"(keep_) : "v"((voff)[_i]), "s"((const char*)(gbase)), "s"(ldsbase + (unsigned)((bufoff) + _i * 8192)) : "memory"); } } while (0)
; #define PG8_WAIT_V(n) asm volatile("s_waitcnt vmcnt(" #n ")" ::: "memory")
; #define PG8_WAIT_L(n) asm volatile("s_waitcnt lgkmcnt(" #n ")" ::: "memory")
; #define PG8_BAR __builtin_amdgcn_s_barrier()
; #define PG8_SCHED __builtin_amdgcn_sched_barrier(0)
;     DI int nt(const Unit& u) const { return (u.aux & 8) ? PLED / 64 : ((u.aux & 4) ? (D_ / 2) / 64 : D_ / 64); }
; template <class Epi, class Sched, bool ALIGN_EPI, bool FP8 = false>
; DI void gemm_phase(LAS unsigned char* lds, const Gemm g, const Sched& S, const Epi& E) {
;     ...
;             const bool last = (t == nt - 2);
;             const char* a1 = cA + (size_t)(t + 1) * kstep;
;             const char* a2 = last ? nA : cA + (size_t)(t + 2) * kstep; const char* b2 = last ? nB : cB + (size_t)(t + 2) * kstep;
;             const char* a3 = a2 + kstep; const char* b3 = b2 + kstep;
;             PG8_LDB(B0, 0, 0); PG8_LDB(B1, 0, 1); PG8_SCHED; PG8_LDA(At, 0, 0); PG8_STAGE(PG8_SA(1, 1), a1 + hstepA, voffA);
;             PG8_WAIT_V(8); PG8_WAIT_L(0); PG8_BAR; PG8_MMA(0, 0, At, B0); PG8_MMA(0, 1, At, B1); PG8_BAR; PG8_SCHED;
.Lmy_g0_1710:
	ds_read_b128 v[146:149], v140
	ds_read_b128 v[150:153], v140 offset:1024
	ds_read_b128 v[154:157], v140 offset:2048
	ds_read_b128 v[158:161], v140 offset:3072
	ds_read_b128 v[162:165], v141
	ds_read_b128 v[166:169], v141 offset:1024
	ds_read_b128 v[170:173], v141 offset:2048
	ds_read_b128 v[174:177], v141 offset:3072
	s_add_u32 s64, s62, 0x100
	s_addc_u32 s65, s63, 0
	s_cmp_eq_u32 vcc_lo, 28
	s_cselect_b32 s70, s94, s64
	s_cselect_b32 s71, s55, s65
	s_cselect_b32 s68, s95, s96
	s_cselect_b32 s69, s53, s97
	s_add_u32 s66, s70, 0x80
	s_addc_u32 s67, s71, 0
	ds_read_b128 v[178:181], v142
	ds_read_b128 v[182:185], v142 offset:1024
	ds_read_b128 v[186:189], v142 offset:2048
	ds_read_b128 v[190:193], v142 offset:3072
	ds_read_b128 v[194:197], v142 offset:4096
	ds_read_b128 v[198:201], v142 offset:5120
	ds_read_b128 v[202:205], v142 offset:6144
	ds_read_b128 v[206:209], v142 offset:7168
	s_add_u32 s62, s62, 0x80080
	s_addc_u32 s63, s63, 0
	s_mov_b32 vcc_hi, m0
	s_mov_b32 m0, s89
	s_nop 0
	global_load_lds_dwordx4 v134, s[62:63]
	s_mov_b32 m0, vcc_hi
	s_nop 0
	s_mov_b32 vcc_hi, m0
	s_mov_b32 m0, s90
	s_nop 0
	global_load_lds_dwordx4 v136, s[62:63]
	s_mov_b32 m0, vcc_hi
	s_waitcnt vmcnt(8)
	s_waitcnt lgkmcnt(0)
	s_barrier
	s_setprio 1
	v_mfma_f32_16x16x32_bf16 v[124:127], v[146:149], v[178:181], v[124:127]
	v_mfma_f32_16x16x32_bf16 v[120:123], v[154:157], v[178:181], v[120:123]
	v_mfma_f32_16x16x32_bf16 v[108:111], v[146:149], v[186:189], v[108:111]
	v_mfma_f32_16x16x32_bf16 v[104:107], v[154:157], v[186:189], v[104:107]
	v_mfma_f32_16x16x32_bf16 v[92:95], v[146:149], v[194:197], v[92:95]
	v_mfma_f32_16x16x32_bf16 v[88:91], v[154:157], v[194:197], v[88:91]
	v_mfma_f32_16x16x32_bf16 v[76:79], v[146:149], v[202:205], v[76:79]
	v_mfma_f32_16x16x32_bf16 v[72:75], v[154:157], v[202:205], v[72:75]
	v_mfma_f32_16x16x32_bf16 v[124:127], v[150:153], v[182:185], v[124:127]
	v_mfma_f32_16x16x32_bf16 v[120:123], v[158:161], v[182:185], v[120:123]
	v_mfma_f32_16x16x32_bf16 v[108:111], v[150:153], v[190:193], v[108:111]
	v_mfma_f32_16x16x32_bf16 v[104:107], v[158:161], v[190:193], v[104:107]
	v_mfma_f32_16x16x32_bf16 v[92:95], v[150:153], v[198:201], v[92:95]
	v_mfma_f32_16x16x32_bf16 v[88:91], v[158:161], v[198:201], v[88:91]
	v_mfma_f32_16x16x32_bf16 v[76:79], v[150:153], v[206:209], v[76:79]
	v_mfma_f32_16x16x32_bf16 v[72:75], v[158:161], v[206:209], v[72:75]
	v_mfma_f32_16x16x32_bf16 v[116:119], v[162:165], v[178:181], v[116:119]
	v_mfma_f32_16x16x32_bf16 v[112:115], v[170:173], v[178:181], v[112:115]
	v_mfma_f32_16x16x32_bf16 v[100:103], v[162:165], v[186:189], v[100:103]
	v_mfma_f32_16x16x32_bf16 v[96:99], v[170:173], v[186:189], v[96:99]
	v_mfma_f32_16x16x32_bf16 v[84:87], v[162:165], v[194:197], v[84:87]
	v_mfma_f32_16x16x32_bf16 v[80:83], v[170:173], v[194:197], v[80:83]
	v_mfma_f32_16x16x32_bf16 v[68:71], v[162:165], v[202:205], v[68:71]
	v_mfma_f32_16x16x32_bf16 v[64:67], v[170:173], v[202:205], v[64:67]
	v_mfma_f32_16x16x32_bf16 v[116:119], v[166:169], v[182:185], v[116:119]
	v_mfma_f32_16x16x32_bf16 v[112:115], v[174:177], v[182:185], v[112:115]
	v_mfma_f32_16x16x32_bf16 v[100:103], v[166:169], v[190:193], v[100:103]
	v_mfma_f32_16x16x32_bf16 v[96:99], v[174:177], v[190:193], v[96:99]
	ds_read_b32 v255, v255 offset:4096
	v_mfma_f32_16x16x32_bf16 v[84:87], v[166:169], v[198:201], v[84:87]
	v_mfma_f32_16x16x32_bf16 v[80:83], v[174:177], v[198:201], v[80:83]
	v_mfma_f32_16x16x32_bf16 v[68:71], v[166:169], v[206:209], v[68:71]
	v_mfma_f32_16x16x32_bf16 v[64:67], v[174:177], v[206:209], v[64:67]
	s_add_u32 s98, s98, 0x80000
	s_waitcnt lgkmcnt(0)
	v_readfirstlane_b32 s101, v255
	v_mov_b32_e32 v255, 0x20000
	s_cmp_ge_u32 s101, s98
	s_cbranch_scc1 .Lmy_g_52

; #define PG8_STAGE(bufoff, gbase, voff) do { _Pragma("unroll") for (int _i = 0; _i < 2; ++_i) { unsigned keep_; \
;         asm volatile("s_mov_b32 %0, m0\n\ts_mov_b32 m0, %3\n\ts_nop 0\n\tglobal_load_lds_dwordx4 %1, %2\n\ts_mov_b32 m0, %0" : "=&s"(keep_) : "v"((voff)[_i]), "s"((const char*)(gbase)), "s"(ldsbase + (unsigned)((bufoff) + _i * 8192)) : "memory"); } } while (0)
; #define PG8_WAIT_V(n) asm volatile("s_waitcnt vmcnt(" #n ")" ::: "memory")
; #define PG8_WAIT_L(n) asm volatile("s_waitcnt lgkmcnt(" #n ")" ::: "memory")
; #define PG8_BAR __builtin_amdgcn_s_barrier()
; #define PG8_SCHED __builtin_amdgcn_sched_barrier(0)
; template <class Epi, class Sched, bool ALIGN_EPI, bool FP8 = false>
; DI void gemm_phase(LAS unsigned char* lds, const Gemm g, const Sched& S, const Epi& E) {
;     ...
;             PG8_LDA(At, 0, 1); PG8_STAGE(PG8_SB(0, 0), b2, voffB); PG8_STAGE(PG8_SB(0, 1), b2 + hstepB, voffB); PG8_STAGE(PG8_SA(0, 0), a2, voffA);
;             PG8_WAIT_V(8); PG8_WAIT_L(0); PG8_BAR; PG8_MMA(1, 0, At, B0); PG8_MMA(1, 1, At, B1); PG8_BAR; PG8_SCHED;
.Lmy_g_52:
	s_setprio 0
	ds_read_b128 v[178:181], v142 offset:16384
	ds_read_b128 v[182:185], v142 offset:17408
	ds_read_b128 v[186:189], v142 offset:18432
	ds_read_b128 v[190:193], v142 offset:19456
	ds_read_b128 v[194:197], v142 offset:20480
	ds_read_b128 v[198:201], v142 offset:21504
	ds_read_b128 v[202:205], v142 offset:22528
	ds_read_b128 v[206:209], v142 offset:23552
	s_mov_b32 s62, m0
	s_mov_b32 m0, s61
	s_nop 0
	global_load_lds_dwordx4 v135, s[68:69]
	s_mov_b32 m0, s62
	s_nop 0
	s_mov_b32 s62, m0
	s_mov_b32 m0, s75
	s_nop 0
	global_load_lds_dwordx4 v137, s[68:69]
	s_mov_b32 m0, s62
	s_add_u32 s62, s68, 0x80000
	s_addc_u32 s63, s69, 0
	s_mov_b32 vcc_hi, m0
	s_mov_b32 m0, s77
	s_nop 0
	global_load_lds_dwordx4 v135, s[62:63]
	s_mov_b32 m0, vcc_hi
	s_nop 0
	s_mov_b32 vcc_hi, m0
	s_mov_b32 m0, s79
	s_nop 0
	global_load_lds_dwordx4 v137, s[62:63]
	s_mov_b32 m0, vcc_hi
	s_mov_b32 s62, m0
	s_mov_b32 m0, s74
	s_nop 0
	global_load_lds_dwordx4 v134, s[70:71]
	s_mov_b32 m0, s62
	s_nop 0
	s_mov_b32 s62, m0
	s_mov_b32 m0, s80
	s_nop 0
	global_load_lds_dwordx4 v136, s[70:71]
	s_mov_b32 m0, s62
	s_waitcnt vmcnt(8)
	s_waitcnt lgkmcnt(0)
	s_barrier
	s_setprio 1
	v_mfma_f32_16x16x32_bf16 v[60:63], v[146:149], v[178:181], v[60:63]
	v_mfma_f32_16x16x32_bf16 v[56:59], v[154:157], v[178:181], v[56:59]
	v_mfma_f32_16x16x32_bf16 v[44:47], v[146:149], v[186:189], v[44:47]
	v_mfma_f32_16x16x32_bf16 v[40:43], v[154:157], v[186:189], v[40:43]
	v_mfma_f32_16x16x32_bf16 v[28:31], v[146:149], v[194:197], v[28:31]
	v_mfma_f32_16x16x32_bf16 v[24:27], v[154:157], v[194:197], v[24:27]
	v_mfma_f32_16x16x32_bf16 v[12:15], v[146:149], v[202:205], v[12:15]
	v_mfma_f32_16x16x32_bf16 v[8:11], v[154:157], v[202:205], v[8:11]
	v_mfma_f32_16x16x32_bf16 v[60:63], v[150:153], v[182:185], v[60:63]
	v_mfma_f32_16x16x32_bf16 v[56:59], v[158:161], v[182:185], v[56:59]
	v_mfma_f32_16x16x32_bf16 v[44:47], v[150:153], v[190:193], v[44:47]
	v_mfma_f32_16x16x32_bf16 v[40:43], v[158:161], v[190:193], v[40:43]
	v_mfma_f32_16x16x32_bf16 v[28:31], v[150:153], v[198:201], v[28:31]
	v_mfma_f32_16x16x32_bf16 v[24:27], v[158:161], v[198:201], v[24:27]
	v_mfma_f32_16x16x32_bf16 v[12:15], v[150:153], v[206:209], v[12:15]
	v_mfma_f32_16x16x32_bf16 v[8:11], v[158:161], v[206:209], v[8:11]
	v_mfma_f32_16x16x32_bf16 v[52:55], v[162:165], v[178:181], v[52:55]
	v_mfma_f32_16x16x32_bf16 v[48:51], v[170:173], v[178:181], v[48:51]
	v_mfma_f32_16x16x32_bf16 v[36:39], v[162:165], v[186:189], v[36:39]
	v_mfma_f32_16x16x32_bf16 v[32:35], v[170:173], v[186:189], v[32:35]
	v_mfma_f32_16x16x32_bf16 v[20:23], v[162:165], v[194:197], v[20:23]
	v_mfma_f32_16x16x32_bf16 v[16:19], v[170:173], v[194:197], v[16:19]
	v_mfma_f32_16x16x32_bf16 v[4:7], v[162:165], v[202:205], v[4:7]
	v_mfma_f32_16x16x32_bf16 v[0:3], v[170:173], v[202:205], v[0:3]
	v_mfma_f32_16x16x32_bf16 v[52:55], v[166:169], v[182:185], v[52:55]
	v_mfma_f32_16x16x32_bf16 v[48:51], v[174:177], v[182:185], v[48:51]
	v_mfma_f32_16x16x32_bf16 v[36:39], v[166:169], v[190:193], v[36:39]
	v_mfma_f32_16x16x32_bf16 v[32:35], v[174:177], v[190:193], v[32:35]
	ds_read_b32 v255, v255 offset:4096
	v_mfma_f32_16x16x32_bf16 v[20:23], v[166:169], v[198:201], v[20:23]
	v_mfma_f32_16x16x32_bf16 v[16:19], v[174:177], v[198:201], v[16:19]
	v_mfma_f32_16x16x32_bf16 v[4:7], v[166:169], v[206:209], v[4:7]
	v_mfma_f32_16x16x32_bf16 v[0:3], v[174:177], v[206:209], v[0:3]
	s_add_u32 s98, s98, 0x80000
	s_waitcnt lgkmcnt(0)
	v_readfirstlane_b32 s101, v255
	v_mov_b32_e32 v255, 0x20000
	s_cmp_ge_u32 s101, s98
	s_cbranch_scc1 .Lmy_g_53

; #define PG8_STAGE(bufoff, gbase, voff) do { _Pragma("unroll") for (int _i = 0; _i < 2; ++_i) { unsigned keep_; \
;         asm volatile("s_mov_b32 %0, m0\n\ts_mov_b32 m0, %3\n\ts_nop 0\n\tglobal_load_lds_dwordx4 %1, %2\n\ts_mov_b32 m0, %0" : "=&s"(keep_) : "v"((voff)[_i]), "s"((const char*)(gbase)), "s"(ldsbase + (unsigned)((bufoff) + _i * 8192)) : "memory"); } } while (0)
; #define PG8_WAIT_V(n) asm volatile("s_waitcnt vmcnt(" #n ")" ::: "memory")
; #define PG8_WAIT_L(n) asm volatile("s_waitcnt lgkmcnt(" #n ")" ::: "memory")
; #define PG8_BAR __builtin_amdgcn_s_barrier()
; #define PG8_SCHED __builtin_amdgcn_sched_barrier(0)
; template <class Epi, class Sched, bool ALIGN_EPI, bool FP8 = false>
; DI void gemm_phase(LAS unsigned char* lds, const Gemm g, const Sched& S, const Epi& E) {
;     ...
;             PG8_LDB(B0, 1, 0); PG8_LDB(B1, 1, 1); PG8_SCHED; PG8_LDA(At, 1, 0); PG8_STAGE(PG8_SA(0, 1), a2 + hstepA, voffA);
;             PG8_WAIT_V(8); PG8_WAIT_L(0); PG8_BAR; PG8_MMA(0, 0, At, B0); PG8_MMA(0, 1, At, B1); PG8_BAR; PG8_SCHED;
.Lmy_g_53:
	s_setprio 0
	ds_read_b128 v[146:149], v143
	ds_read_b128 v[150:153], v143 offset:1024
	ds_read_b128 v[154:157], v143 offset:2048
	ds_read_b128 v[158:161], v143 offset:3072
	ds_read_b128 v[162:165], v144
	ds_read_b128 v[166:169], v144 offset:1024
	ds_read_b128 v[170:173], v144 offset:2048
	ds_read_b128 v[174:177], v144 offset:3072
	ds_read_b128 v[178:181], v142 offset:32768
	ds_read_b128 v[182:185], v142 offset:33792
	ds_read_b128 v[186:189], v142 offset:34816
	ds_read_b128 v[190:193], v142 offset:35840
	ds_read_b128 v[194:197], v142 offset:36864
	ds_read_b128 v[198:201], v142 offset:37888
	ds_read_b128 v[202:205], v142 offset:38912
	ds_read_b128 v[206:209], v142 offset:39936
	s_add_u32 s62, s70, 0x80000
	s_addc_u32 s63, s71, 0
	s_mov_b32 s70, m0
	s_mov_b32 m0, s81
	s_nop 0
	global_load_lds_dwordx4 v134, s[62:63]
	s_mov_b32 m0, s70
	s_nop 0
	s_mov_b32 s70, m0
	s_mov_b32 m0, s82
	s_nop 0
	global_load_lds_dwordx4 v136, s[62:63]
	s_mov_b32 m0, s70
	s_waitcnt vmcnt(8)
	s_waitcnt lgkmcnt(0)
	s_barrier
	s_setprio 1
	v_mfma_f32_16x16x32_bf16 v[124:127], v[146:149], v[178:181], v[124:127]
	v_mfma_f32_16x16x32_bf16 v[120:123], v[154:157], v[178:181], v[120:123]
	v_mfma_f32_16x16x32_bf16 v[108:111], v[146:149], v[186:189], v[108:111]
	v_mfma_f32_16x16x32_bf16 v[104:107], v[154:157], v[186:189], v[104:107]
	v_mfma_f32_16x16x32_bf16 v[92:95], v[146:149], v[194:197], v[92:95]
	v_mfma_f32_16x16x32_bf16 v[88:91], v[154:157], v[194:197], v[88:91]
	v_mfma_f32_16x16x32_bf16 v[76:79], v[146:149], v[202:205], v[76:79]
	v_mfma_f32_16x16x32_bf16 v[72:75], v[154:157], v[202:205], v[72:75]
	v_mfma_f32_16x16x32_bf16 v[124:127], v[150:153], v[182:185], v[124:127]
	v_mfma_f32_16x16x32_bf16 v[120:123], v[158:161], v[182:185], v[120:123]
	v_mfma_f32_16x16x32_bf16 v[108:111], v[150:153], v[190:193], v[108:111]
	v_mfma_f32_16x16x32_bf16 v[104:107], v[158:161], v[190:193], v[104:107]
	v_mfma_f32_16x16x32_bf16 v[92:95], v[150:153], v[198:201], v[92:95]
	v_mfma_f32_16x16x32_bf16 v[88:91], v[158:161], v[198:201], v[88:91]
	v_mfma_f32_16x16x32_bf16 v[76:79], v[150:153], v[206:209], v[76:79]
	v_mfma_f32_16x16x32_bf16 v[72:75], v[158:161], v[206:209], v[72:75]
	v_mfma_f32_16x16x32_bf16 v[116:119], v[162:165], v[178:181], v[116:119]
	v_mfma_f32_16x16x32_bf16 v[112:115], v[170:173], v[178:181], v[112:115]
	v_mfma_f32_16x16x32_bf16 v[100:103], v[162:165], v[186:189], v[100:103]
	v_mfma_f32_16x16x32_bf16 v[96:99], v[170:173], v[186:189], v[96:99]
	v_mfma_f32_16x16x32_bf16 v[84:87], v[162:165], v[194:197], v[84:87]
	v_mfma_f32_16x16x32_bf16 v[80:83], v[170:173], v[194:197], v[80:83]
	v_mfma_f32_16x16x32_bf16 v[68:71], v[162:165], v[202:205], v[68:71]
	v_mfma_f32_16x16x32_bf16 v[64:67], v[170:173], v[202:205], v[64:67]
	v_mfma_f32_16x16x32_bf16 v[116:119], v[166:169], v[182:185], v[116:119]
	v_mfma_f32_16x16x32_bf16 v[112:115], v[174:177], v[182:185], v[112:115]
	v_mfma_f32_16x16x32_bf16 v[100:103], v[166:169], v[190:193], v[100:103]
	v_mfma_f32_16x16x32_bf16 v[96:99], v[174:177], v[190:193], v[96:99]
	ds_read_b32 v255, v255 offset:4096
	v_mfma_f32_16x16x32_bf16 v[84:87], v[166:169], v[198:201], v[84:87]
	v_mfma_f32_16x16x32_bf16 v[80:83], v[174:177], v[198:201], v[80:83]
	v_mfma_f32_16x16x32_bf16 v[68:71], v[166:169], v[206:209], v[68:71]
	v_mfma_f32_16x16x32_bf16 v[64:67], v[174:177], v[206:209], v[64:67]
	s_add_u32 s98, s98, 0x80000
	s_waitcnt lgkmcnt(0)
	v_readfirstlane_b32 s101, v255
	v_mov_b32_e32 v255, 0x20000
	s_cmp_ge_u32 s101, s98
	s_cbranch_scc1 .Lmy_g_54

; #define PG8_STAGE(bufoff, gbase, voff) do { _Pragma("unroll") for (int _i = 0; _i < 2; ++_i) { unsigned keep_; \
;         asm volatile("s_mov_b32 %0, m0\n\ts_mov_b32 m0, %3\n\ts_nop 0\n\tglobal_load_lds_dwordx4 %1, %2\n\ts_mov_b32 m0, %0" : "=&s"(keep_) : "v"((voff)[_i]), "s"((const char*)(gbase)), "s"(ldsbase + (unsigned)((bufoff) + _i * 8192)) : "memory"); } } while (0)
; #define PG8_WAIT_V(n) asm volatile("s_waitcnt vmcnt(" #n ")" ::: "memory")
; #define PG8_WAIT_L(n) asm volatile("s_waitcnt lgkmcnt(" #n ")" ::: "memory")
; #define PG8_BAR __builtin_amdgcn_s_barrier()
; #define PG8_SCHED __builtin_amdgcn_sched_barrier(0)
; template <class Epi, class Sched, bool ALIGN_EPI, bool FP8 = false>
; DI void gemm_phase(LAS unsigned char* lds, const Gemm g, const Sched& S, const Epi& E) {
;     ...
;             PG8_LDA(At, 1, 1); PG8_STAGE(PG8_SB(1, 0), b3, voffB); PG8_STAGE(PG8_SB(1, 1), b3 + hstepB, voffB); PG8_STAGE(PG8_SA(1, 0), a3, voffA);
;             PG8_WAIT_V(8); PG8_WAIT_L(0); PG8_BAR; PG8_MMA(1, 0, At, B0); PG8_MMA(1, 1, At, B1); PG8_BAR; PG8_SCHED;
.Lmy_g_54:
	s_setprio 0
	ds_read_b128 v[178:181], v142 offset:49152
	ds_read_b128 v[182:185], v142 offset:50176
	ds_read_b128 v[186:189], v142 offset:51200
	ds_read_b128 v[190:193], v142 offset:52224
	ds_read_b128 v[194:197], v142 offset:53248
	ds_read_b128 v[198:201], v142 offset:54272
	ds_read_b128 v[202:205], v142 offset:55296
	ds_read_b128 v[206:209], v142 offset:56320
	s_add_u32 s62, s68, 0x80
	s_addc_u32 s63, s69, 0
	s_mov_b32 s70, m0
	s_mov_b32 m0, s83
	s_nop 0
	global_load_lds_dwordx4 v135, s[62:63]
	s_mov_b32 m0, s70
	s_nop 0
	s_mov_b32 s70, m0
	s_mov_b32 m0, s84
	s_nop 0
	global_load_lds_dwordx4 v137, s[62:63]
	s_mov_b32 m0, s70
	s_add_u32 s62, s68, 0x80080
	s_addc_u32 s63, s69, 0
	s_mov_b32 s68, m0
	s_mov_b32 m0, s87
	s_nop 0
	global_load_lds_dwordx4 v135, s[62:63]
	s_mov_b32 m0, s68
	s_nop 0
	s_mov_b32 s68, m0
	s_mov_b32 m0, s88
	s_nop 0
	global_load_lds_dwordx4 v137, s[62:63]
	s_mov_b32 m0, s68
	s_mov_b32 s62, m0
	s_mov_b32 m0, s85
	s_nop 0
	global_load_lds_dwordx4 v134, s[66:67]
	s_mov_b32 m0, s62
	s_nop 0
	s_mov_b32 s62, m0
	s_mov_b32 m0, s86
	s_nop 0
	global_load_lds_dwordx4 v136, s[66:67]
	s_mov_b32 m0, s62
	s_waitcnt vmcnt(8)
	s_waitcnt lgkmcnt(0)
	s_barrier
	s_setprio 1
	v_mfma_f32_16x16x32_bf16 v[60:63], v[146:149], v[178:181], v[60:63]
	v_mfma_f32_16x16x32_bf16 v[56:59], v[154:157], v[178:181], v[56:59]
	v_mfma_f32_16x16x32_bf16 v[44:47], v[146:149], v[186:189], v[44:47]
	v_mfma_f32_16x16x32_bf16 v[40:43], v[154:157], v[186:189], v[40:43]
	v_mfma_f32_16x16x32_bf16 v[28:31], v[146:149], v[194:197], v[28:31]
	v_mfma_f32_16x16x32_bf16 v[24:27], v[154:157], v[194:197], v[24:27]
	v_mfma_f32_16x16x32_bf16 v[12:15], v[146:149], v[202:205], v[12:15]
	v_mfma_f32_16x16x32_bf16 v[8:11], v[154:157], v[202:205], v[8:11]
	v_mfma_f32_16x16x32_bf16 v[60:63], v[150:153], v[182:185], v[60:63]
	v_mfma_f32_16x16x32_bf16 v[56:59], v[158:161], v[182:185], v[56:59]
	v_mfma_f32_16x16x32_bf16 v[44:47], v[150:153], v[190:193], v[44:47]
	v_mfma_f32_16x16x32_bf16 v[40:43], v[158:161], v[190:193], v[40:43]
	v_mfma_f32_16x16x32_bf16 v[28:31], v[150:153], v[198:201], v[28:31]
	v_mfma_f32_16x16x32_bf16 v[24:27], v[158:161], v[198:201], v[24:27]
	v_mfma_f32_16x16x32_bf16 v[12:15], v[150:153], v[206:209], v[12:15]
	v_mfma_f32_16x16x32_bf16 v[8:11], v[158:161], v[206:209], v[8:11]
	v_mfma_f32_16x16x32_bf16 v[52:55], v[162:165], v[178:181], v[52:55]
	v_mfma_f32_16x16x32_bf16 v[48:51], v[170:173], v[178:181], v[48:51]
	v_mfma_f32_16x16x32_bf16 v[36:39], v[162:165], v[186:189], v[36:39]
	v_mfma_f32_16x16x32_bf16 v[32:35], v[170:173], v[186:189], v[32:35]
	v_mfma_f32_16x16x32_bf16 v[20:23], v[162:165], v[194:197], v[20:23]
	v_mfma_f32_16x16x32_bf16 v[16:19], v[170:173], v[194:197], v[16:19]
	v_mfma_f32_16x16x32_bf16 v[4:7], v[162:165], v[202:205], v[4:7]
	v_mfma_f32_16x16x32_bf16 v[0:3], v[170:173], v[202:205], v[0:3]
	v_mfma_f32_16x16x32_bf16 v[52:55], v[166:169], v[182:185], v[52:55]
	v_mfma_f32_16x16x32_bf16 v[48:51], v[174:177], v[182:185], v[48:51]
	v_mfma_f32_16x16x32_bf16 v[36:39], v[166:169], v[190:193], v[36:39]
	v_mfma_f32_16x16x32_bf16 v[32:35], v[174:177], v[190:193], v[32:35]
	ds_read_b32 v255, v255 offset:4096
	v_mfma_f32_16x16x32_bf16 v[20:23], v[166:169], v[198:201], v[20:23]
	v_mfma_f32_16x16x32_bf16 v[16:19], v[174:177], v[198:201], v[16:19]
	v_mfma_f32_16x16x32_bf16 v[4:7], v[166:169], v[206:209], v[4:7]
	v_mfma_f32_16x16x32_bf16 v[0:3], v[174:177], v[206:209], v[0:3]
	s_add_u32 s98, s98, 0x80000
	s_waitcnt lgkmcnt(0)
	v_readfirstlane_b32 s101, v255
	v_mov_b32_e32 v255, 0x20000
	s_cmp_ge_u32 s101, s98
	s_cbranch_scc1 .Lmy_g_55

; #define PG8_BAR __builtin_amdgcn_s_barrier()
; template <class Epi, class Sched, bool ALIGN_EPI, bool FP8 = false>
; DI void gemm_phase(LAS unsigned char* lds, const Gemm g, const Sched& S, const Epi& E) {
;     ...
;         for (int t = 0; t < nt; t += 2) {
;             if constexpr (Epi::MID) { if (t == (nt >> 1)) E.mid(acc, cur, wr, wc, fr, fq); }
;             const bool last = (t == nt - 2);
;             const char* a1 = cA + (size_t)(t + 1) * kstep;
;             const char* a2 = last ? nA : cA + (size_t)(t + 2) * kstep; const char* b2 = last ? nB : cB + (size_t)(t + 2) * kstep;
;             const char* a3 = a2 + kstep; const char* b3 = b2 + kstep;
;             PG8_LDB(B0, 0, 0); PG8_LDB(B1, 0, 1); PG8_SCHED; PG8_LDA(At, 0, 0); PG8_STAGE(PG8_SA(1, 1), a1 + hstepA, voffA);
;             PG8_WAIT_V(8); PG8_WAIT_L(0); PG8_BAR; PG8_MMA(0, 0, At, B0); PG8_MMA(0, 1, At, B1); PG8_BAR; PG8_SCHED;
;             PG8_LDA(At, 0, 1); PG8_STAGE(PG8_SB(0, 0), b2, voffB); PG8_STAGE(PG8_SB(0, 1), b2 + hstepB, voffB); PG8_STAGE(PG8_SA(0, 0), a2, voffA);
;             PG8_WAIT_V(8); PG8_WAIT_L(0); PG8_BAR; PG8_MMA(1, 0, At, B0); PG8_MMA(1, 1, At, B1); PG8_BAR; PG8_SCHED;
;             PG8_LDB(B0, 1, 0); PG8_LDB(B1, 1, 1); PG8_SCHED; PG8_LDA(At, 1, 0); PG8_STAGE(PG8_SA(0, 1), a2 + hstepA, voffA);
;     DI void operator()(const f32x4 (&acc)[2][2][4][2], const Unit& u, int wr, int wc, int fr, int fq) const {
;         int row0 = u.pm * BM + wr * 64 + fr; asm volatile("" : "+v"(row0));
;         const int col0 = u.pn * BM + wc * 32 + 8 * fq;
; #pragma unroll
;         for (int ai = 0; ai < 2; ++ai)
; #pragma unroll
;             for (int m = 0; m < 4; ++m) { const size_t r = (size_t)(row0 + ai * HALF + m * 16);
; #pragma unroll
;                 for (int bj = 0; bj < 2; ++bj) { const size_t o = r * D_ + col0 + bj * HALF; f32x4 p0, p1; unpack8f(*(const u32x4*)(PWB + o), p0, p1);
;                     const f32x4 a0 = acc[ai][bj][m][0], a1 = acc[ai][bj][m][1];
;                     u32x4 w; w.x = cvt_pk_bf16(sig_(a0[0]) * p0[0], sig_(a0[1]) * p0[1]); w.y = cvt_pk_bf16(sig_(a0[2]) * p0[2], sig_(a0[3]) * p0[3]);
;                     w.z = cvt_pk_bf16(sig_(a1[0]) * p1[0], sig_(a1[1]) * p1[1]); w.w = cvt_pk_bf16(sig_(a1[2]) * p1[2], sig_(a1[3]) * p1[3]);
;                     *(u32x4*)(PLEB + o) = w; }
;                 if (m & 1) asm volatile("" ::: "memory"); }
;     }
.Lmy_g_55:
	s_setprio 0
	s_add_i32 vcc_lo, vcc_lo, 2
	s_add_u32 s96, s96, 0x100
	s_addc_u32 s97, s97, 0
	s_cmp_gt_u32 vcc_lo, 29
	s_mov_b64 s[62:63], s[64:65]
	s_cbranch_scc0 .Lmy_g0_1710
.Lmy_ex_1710:
	s_and_b64 vcc, exec, s[14:15]
	s_cbranch_vccz .LBB0_1713
	s_barrier
.LBB0_1713:
	v_lshl_add_u32 v132, s60, 8, v138
	v_lshl_or_b32 v146, s93, 8, v139
	v_ashrrev_i32_e32 v133, 31, v132
	v_ashrrev_i32_e32 v147, 31, v146
	v_lshlrev_b64 v[132:133], 11, v[132:133]
	v_lshl_add_u64 v[132:133], v[132:133], 0, v[146:147]
	v_lshlrev_b64 v[132:133], 1, v[132:133]
	v_lshl_add_u64 v[146:147], s[10:11], 0, v[132:133]
	v_or_b32_e32 v154, 0x100, v132
	v_mov_b32_e32 v155, v133
	global_load_dwordx4 v[146:149], v[146:147], off
	v_lshl_add_u64 v[150:151], s[10:11], 0, v[154:155]
	global_load_dwordx4 v[150:153], v[150:151], off
	v_mul_f32_e32 v124, 0xbfb8aa3b, v124
	v_mul_f32_e32 v125, 0xbfb8aa3b, v125
	v_mul_f32_e32 v126, 0xbfb8aa3b, v126
	v_mul_f32_e32 v127, 0xbfb8aa3b, v127
	v_mul_f32_e32 v120, 0xbfb8aa3b, v120
	v_mul_f32_e32 v121, 0xbfb8aa3b, v121
	v_mul_f32_e32 v122, 0xbfb8aa3b, v122
	v_mul_f32_e32 v123, 0xbfb8aa3b, v123
	v_mul_f32_e32 v116, 0xbfb8aa3b, v116
	v_mul_f32_e32 v117, 0xbfb8aa3b, v117
	v_mul_f32_e32 v118, 0xbfb8aa3b, v118
	v_mul_f32_e32 v119, 0xbfb8aa3b, v119
	v_exp_f32_e32 v124, v124
	v_exp_f32_e32 v125, v125
	v_exp_f32_e32 v126, v126
	v_exp_f32_e32 v127, v127
	v_exp_f32_e32 v120, v120
	v_exp_f32_e32 v121, v121
	v_exp_f32_e32 v122, v122
	v_exp_f32_e32 v123, v123
	v_exp_f32_e32 v116, v116
	v_exp_f32_e32 v117, v117
	v_exp_f32_e32 v118, v118
	v_exp_f32_e32 v119, v119
	v_mul_f32_e32 v112, 0xbfb8aa3b, v112
	v_mul_f32_e32 v113, 0xbfb8aa3b, v113
	v_exp_f32_e32 v145, v112
	v_exp_f32_e32 v160, v113
	v_add_f32_e32 v112, 1.0, v124
	v_add_f32_e32 v113, 1.0, v125
	v_add_f32_e32 v124, 1.0, v126
	v_add_f32_e32 v125, 1.0, v127
	v_add_f32_e32 v120, 1.0, v120
	v_add_f32_e32 v121, 1.0, v121
	v_add_f32_e32 v122, 1.0, v122
	v_add_f32_e32 v123, 1.0, v123
	v_add_f32_e32 v126, 1.0, v116
	v_add_f32_e32 v127, 1.0, v117
	v_add_f32_e32 v156, 1.0, v118
	v_add_f32_e32 v157, 1.0, v119
	v_rcp_f32_e32 v112, v112
	v_rcp_f32_e32 v113, v113
	v_rcp_f32_e32 v116, v124
	v_rcp_f32_e32 v117, v125
	v_rcp_f32_e32 v118, v120
	v_rcp_f32_e32 v119, v121
	v_rcp_f32_e32 v120, v122
	v_rcp_f32_e32 v121, v123
	v_rcp_f32_e32 v124, v126
	v_rcp_f32_e32 v125, v127
	v_rcp_f32_e32 v126, v156
	v_rcp_f32_e32 v127, v157
	v_lshl_add_u64 v[122:123], s[12:13], 0, v[132:133]
	v_mul_f32_e32 v114, 0xbfb8aa3b, v114
	v_mul_f32_e32 v108, 0xbfb8aa3b, v108
	v_mul_f32_e32 v109, 0xbfb8aa3b, v109
	v_mul_f32_e32 v110, 0xbfb8aa3b, v110
	v_mul_f32_e32 v111, 0xbfb8aa3b, v111
	v_mul_f32_e32 v100, 0xbfb8aa3b, v100
	v_exp_f32_e32 v108, v108
	v_exp_f32_e32 v109, v109
	v_mul_f32_e32 v104, 0xbfb8aa3b, v104
	v_mul_f32_e32 v105, 0xbfb8aa3b, v105
	v_exp_f32_e32 v110, v110
	v_exp_f32_e32 v111, v111
	v_exp_f32_e32 v100, v100
	v_mul_f32_e32 v106, 0xbfb8aa3b, v106
	v_mul_f32_e32 v107, 0xbfb8aa3b, v107
	v_exp_f32_e32 v104, v104
	v_exp_f32_e32 v105, v105
	v_mul_f32_e32 v101, 0xbfb8aa3b, v101
	v_exp_f32_e32 v106, v106
	v_exp_f32_e32 v107, v107
	v_mul_f32_e32 v102, 0xbfb8aa3b, v102
	v_mul_f32_e32 v103, 0xbfb8aa3b, v103
	v_exp_f32_e32 v102, v102
	v_exp_f32_e32 v103, v103
	s_waitcnt vmcnt(1)
	v_lshlrev_b32_e32 v156, 16, v146
	v_and_b32_e32 v157, 0xffff0000, v146
	v_lshlrev_b32_e32 v146, 16, v147
	v_and_b32_e32 v147, 0xffff0000, v147
	v_lshlrev_b32_e32 v158, 16, v148
	v_and_b32_e32 v159, 0xffff0000, v148
	v_lshlrev_b32_e32 v148, 16, v149
	v_and_b32_e32 v149, 0xffff0000, v149
	v_pk_mul_f32 v[112:113], v[112:113], v[156:157]
	v_pk_mul_f32 v[146:147], v[116:117], v[146:147]
	v_pk_mul_f32 v[118:119], v[118:119], v[158:159]
	v_pk_mul_f32 v[120:121], v[120:121], v[148:149]
	s_waitcnt vmcnt(0)
	v_lshlrev_b32_e32 v148, 16, v150
	v_and_b32_e32 v149, 0xffff0000, v150
	v_lshlrev_b32_e32 v150, 16, v151
	v_and_b32_e32 v151, 0xffff0000, v151
	v_cvt_pk_bf16_f32 v116, v112, v113
	v_cvt_pk_bf16_f32 v117, v146, v147
	v_cvt_pk_bf16_f32 v118, v118, v119
	v_cvt_pk_bf16_f32 v119, v120, v121
	v_pk_mul_f32 v[112:113], v[124:125], v[148:149]
	v_pk_mul_f32 v[120:121], v[126:127], v[150:151]
	global_store_dwordx4 v[122:123], v[116:119], off
	v_cvt_pk_bf16_f32 v112, v112, v113
	v_cvt_pk_bf16_f32 v113, v120, v121
	v_add_f32_e32 v116, 1.0, v145
	v_add_f32_e32 v117, 1.0, v160
	v_exp_f32_e32 v120, v114
	v_mul_f32_e32 v114, 0xbfb8aa3b, v115
	v_rcp_f32_e32 v116, v116
	v_rcp_f32_e32 v117, v117
	v_exp_f32_e32 v121, v114
	v_lshlrev_b32_e32 v118, 16, v152
	v_and_b32_e32 v119, 0xffff0000, v152
	v_pk_mul_f32 v[114:115], v[116:117], v[118:119]
	v_add_f32_e32 v116, 1.0, v120
	v_add_f32_e32 v117, 1.0, v121
	v_rcp_f32_e32 v116, v116
	v_rcp_f32_e32 v117, v117
	v_lshlrev_b32_e32 v118, 16, v153
	v_and_b32_e32 v119, 0xffff0000, v153
	v_cvt_pk_bf16_f32 v114, v114, v115
	v_pk_mul_f32 v[116:117], v[116:117], v[118:119]
	v_lshl_add_u64 v[120:121], v[132:133], 0, s[16:17]
	v_cvt_pk_bf16_f32 v115, v116, v117
	v_lshl_add_u64 v[116:117], s[12:13], 0, v[154:155]
	global_store_dwordx4 v[116:117], v[112:115], off
	v_lshl_add_u64 v[122:123], v[132:133], 0, s[18:19]
	v_lshl_add_u64 v[116:117], s[10:11], 0, v[122:123]
	v_lshl_add_u64 v[112:113], s[10:11], 0, v[120:121]
	global_load_dwordx4 v[112:115], v[112:113], off
	v_exp_f32_e32 v145, v101
	global_load_dwordx4 v[116:119], v[116:117], off
	v_add_f32_e32 v101, 1.0, v108
	v_add_f32_e32 v108, 1.0, v109
	v_add_f32_e32 v109, 1.0, v110
	v_add_f32_e32 v110, 1.0, v111
	v_add_f32_e32 v127, 1.0, v100
	v_rcp_f32_e32 v100, v101
	v_rcp_f32_e32 v101, v108
	v_add_f32_e32 v111, 1.0, v104
	v_add_f32_e32 v124, 1.0, v105
	v_rcp_f32_e32 v104, v109
	v_rcp_f32_e32 v105, v110
; DI unsigned cvt_pk_bf16(float lo, float hi) { const f32x2_t v = {lo, hi}; return __builtin_bit_cast(unsigned, __builtin_convertvector(v, bf16x2_t)); }
; DI float sig_(float x) { return __builtin_amdgcn_rcpf(1.0f + __builtin_amdgcn_exp2f(-1.4426950408889634f * x)); }
;     DI void operator()(const f32x4 (&acc)[2][2][4][2], const Unit& u, int wr, int wc, int fr, int fq) const {
;     ...
;             for (int m = 0; m < 4; ++m) { const size_t r = (size_t)(row0 + ai * HALF + m * 16);
; #pragma unroll
;                 for (int bj = 0; bj < 2; ++bj) { const size_t o = r * D_ + col0 + bj * HALF; f32x4 p0, p1; unpack8f(*(const u32x4*)(PWB + o), p0, p1);
;                     const f32x4 a0 = acc[ai][bj][m][0], a1 = acc[ai][bj][m][1];
;                     u32x4 w; w.x = cvt_pk_bf16(sig_(a0[0]) * p0[0], sig_(a0[1]) * p0[1]); w.y = cvt_pk_bf16(sig_(a0[2]) * p0[2], sig_(a0[3]) * p0[3]);
;                     w.z = cvt_pk_bf16(sig_(a1[0]) * p1[0], sig_(a1[1]) * p1[1]); w.w = cvt_pk_bf16(sig_(a1[2]) * p1[2], sig_(a1[3]) * p1[3]);
;                     *(u32x4*)(PLEB + o) = w; }
;                 if (m & 1) asm volatile("" ::: "memory"); }
;     }
	v_add_f32_e32 v125, 1.0, v106
	v_add_f32_e32 v126, 1.0, v107
	v_mul_f32_e32 v96, 0xbfb8aa3b, v96
	v_mul_f32_e32 v97, 0xbfb8aa3b, v97
	v_rcp_f32_e32 v106, v111
	v_rcp_f32_e32 v107, v124
	v_rcp_f32_e32 v108, v125
	v_rcp_f32_e32 v109, v126
	v_exp_f32_e32 v96, v96
	v_exp_f32_e32 v97, v97
	v_mul_f32_e32 v98, 0xbfb8aa3b, v98
	v_mul_f32_e32 v99, 0xbfb8aa3b, v99
	v_add_f32_e32 v102, 1.0, v102
	v_add_f32_e32 v103, 1.0, v103
	v_exp_f32_e32 v98, v98
	v_exp_f32_e32 v99, v99
	v_rcp_f32_e32 v110, v127
	v_rcp_f32_e32 v102, v102
	v_rcp_f32_e32 v103, v103
	v_add_f32_e32 v96, 1.0, v96
	v_add_f32_e32 v97, 1.0, v97
	v_lshl_add_u64 v[120:121], s[12:13], 0, v[120:121]
	v_rcp_f32_e32 v96, v96
	v_rcp_f32_e32 v97, v97
	v_add_f32_e32 v98, 1.0, v98
	v_add_f32_e32 v99, 1.0, v99
	v_rcp_f32_e32 v98, v98
	v_rcp_f32_e32 v99, v99
	v_mul_f32_e32 v92, 0xbfb8aa3b, v92
	v_mul_f32_e32 v93, 0xbfb8aa3b, v93
	v_mul_f32_e32 v94, 0xbfb8aa3b, v94
	v_mul_f32_e32 v95, 0xbfb8aa3b, v95
	v_mul_f32_e32 v88, 0xbfb8aa3b, v88
	v_mul_f32_e32 v89, 0xbfb8aa3b, v89
	v_exp_f32_e32 v92, v92
	v_exp_f32_e32 v93, v93
	v_exp_f32_e32 v94, v94
	v_exp_f32_e32 v95, v95
	v_exp_f32_e32 v88, v88
	v_exp_f32_e32 v89, v89
	v_add_f32_e32 v92, 1.0, v92
	v_add_f32_e32 v93, 1.0, v93
	v_add_f32_e32 v94, 1.0, v94
	v_add_f32_e32 v95, 1.0, v95
	v_mul_f32_e32 v90, 0xbfb8aa3b, v90
	v_mul_f32_e32 v84, 0xbfb8aa3b, v84
	v_mul_f32_e32 v85, 0xbfb8aa3b, v85
	v_exp_f32_e32 v84, v84
	v_exp_f32_e32 v85, v85
	v_mul_f32_e32 v86, 0xbfb8aa3b, v86
	v_mul_f32_e32 v87, 0xbfb8aa3b, v87
	v_exp_f32_e32 v86, v86
	v_exp_f32_e32 v87, v87
	v_mul_f32_e32 v80, 0xbfb8aa3b, v80
	v_mul_f32_e32 v81, 0xbfb8aa3b, v81
	v_exp_f32_e32 v80, v80
	v_exp_f32_e32 v81, v81
	v_add_f32_e32 v84, 1.0, v84
	v_add_f32_e32 v85, 1.0, v85
	v_mul_f32_e32 v82, 0xbfb8aa3b, v82
	v_mul_f32_e32 v83, 0xbfb8aa3b, v83
	v_rcp_f32_e32 v84, v84
	v_rcp_f32_e32 v85, v85
	v_add_f32_e32 v86, 1.0, v86
	v_add_f32_e32 v87, 1.0, v87
	v_exp_f32_e32 v82, v82
	s_waitcnt vmcnt(1)
	v_lshlrev_b32_e32 v124, 16, v112
	v_and_b32_e32 v125, 0xffff0000, v112
	v_lshlrev_b32_e32 v112, 16, v113
	v_and_b32_e32 v113, 0xffff0000, v113
	v_pk_mul_f32 v[100:101], v[100:101], v[124:125]
	v_pk_mul_f32 v[112:113], v[104:105], v[112:113]
	v_cvt_pk_bf16_f32 v104, v100, v101
	v_add_f32_e32 v100, 1.0, v145
	v_lshlrev_b32_e32 v126, 16, v114
	v_and_b32_e32 v127, 0xffff0000, v114
	v_lshlrev_b32_e32 v114, 16, v115
	v_and_b32_e32 v115, 0xffff0000, v115
	v_rcp_f32_e32 v111, v100
	v_pk_mul_f32 v[106:107], v[106:107], v[126:127]
	v_pk_mul_f32 v[108:109], v[108:109], v[114:115]
	v_cvt_pk_bf16_f32 v105, v112, v113
	v_cvt_pk_bf16_f32 v106, v106, v107
	v_cvt_pk_bf16_f32 v107, v108, v109
	global_store_dwordx4 v[120:121], v[104:107], off
	s_waitcnt vmcnt(1)
	v_lshlrev_b32_e32 v100, 16, v116
	v_and_b32_e32 v101, 0xffff0000, v116
	v_lshlrev_b32_e32 v104, 16, v117
	v_and_b32_e32 v105, 0xffff0000, v117
	v_pk_mul_f32 v[100:101], v[110:111], v[100:101]
	v_pk_mul_f32 v[102:103], v[102:103], v[104:105]
	v_cvt_pk_bf16_f32 v100, v100, v101
	v_cvt_pk_bf16_f32 v101, v102, v103
	v_lshlrev_b32_e32 v102, 16, v118
	v_and_b32_e32 v103, 0xffff0000, v118
	v_pk_mul_f32 v[96:97], v[96:97], v[102:103]
	v_lshl_add_u64 v[104:105], v[132:133], 0, s[20:21]
	v_cvt_pk_bf16_f32 v102, v96, v97
	v_lshlrev_b32_e32 v96, 16, v119
	v_and_b32_e32 v97, 0xffff0000, v119
	v_pk_mul_f32 v[96:97], v[98:99], v[96:97]
	v_lshl_add_u64 v[106:107], v[132:133], 0, s[22:23]
	v_cvt_pk_bf16_f32 v103, v96, v97
	v_lshl_add_u64 v[96:97], s[12:13], 0, v[122:123]
	global_store_dwordx4 v[96:97], v[100:103], off
	v_lshl_add_u64 v[96:97], s[10:11], 0, v[104:105]
	global_load_dwordx4 v[96:99], v[96:97], off
	v_lshl_add_u64 v[100:101], s[10:11], 0, v[106:107]
	global_load_dwordx4 v[100:103], v[100:101], off
	v_add_f32_e32 v108, 1.0, v88
	v_add_f32_e32 v109, 1.0, v89
	v_rcp_f32_e32 v88, v92
	v_rcp_f32_e32 v89, v93
	v_rcp_f32_e32 v92, v94
	v_rcp_f32_e32 v93, v95
	v_rcp_f32_e32 v94, v108
	v_rcp_f32_e32 v95, v109
	v_exp_f32_e32 v83, v83
	v_rcp_f32_e32 v86, v86
	v_rcp_f32_e32 v87, v87
	v_add_f32_e32 v80, 1.0, v80
	v_add_f32_e32 v81, 1.0, v81
	v_rcp_f32_e32 v80, v80
	v_rcp_f32_e32 v81, v81
	v_add_f32_e32 v82, 1.0, v82
	v_add_f32_e32 v83, 1.0, v83
	v_rcp_f32_e32 v82, v82
	v_rcp_f32_e32 v83, v83
	v_mul_f32_e32 v76, 0xbfb8aa3b, v76
	v_mul_f32_e32 v77, 0xbfb8aa3b, v77
	v_mul_f32_e32 v78, 0xbfb8aa3b, v78
	v_mul_f32_e32 v79, 0xbfb8aa3b, v79
	v_exp_f32_e32 v76, v76
	v_exp_f32_e32 v77, v77
	v_exp_f32_e32 v78, v78
	v_exp_f32_e32 v79, v79
	v_mul_f32_e32 v72, 0xbfb8aa3b, v72
	v_mul_f32_e32 v73, 0xbfb8aa3b, v73
	v_exp_f32_e32 v72, v72
	v_exp_f32_e32 v73, v73
	v_mul_f32_e32 v74, 0xbfb8aa3b, v74
	v_mul_f32_e32 v75, 0xbfb8aa3b, v75
	v_add_f32_e32 v76, 1.0, v76
	v_add_f32_e32 v77, 1.0, v77
	v_add_f32_e32 v78, 1.0, v78
	v_add_f32_e32 v79, 1.0, v79
	v_exp_f32_e32 v74, v74
	v_exp_f32_e32 v75, v75
	v_rcp_f32_e32 v76, v76
	v_rcp_f32_e32 v77, v77
	v_rcp_f32_e32 v78, v78
	v_rcp_f32_e32 v79, v79
	v_add_f32_e32 v72, 1.0, v72
	v_add_f32_e32 v73, 1.0, v73
	v_mul_f32_e32 v68, 0xbfb8aa3b, v68
	v_mul_f32_e32 v69, 0xbfb8aa3b, v69
	v_rcp_f32_e32 v72, v72
	v_rcp_f32_e32 v73, v73
	v_exp_f32_e32 v68, v68
	v_exp_f32_e32 v69, v69
	v_mul_f32_e32 v70, 0xbfb8aa3b, v70
	v_mul_f32_e32 v71, 0xbfb8aa3b, v71
	v_add_f32_e32 v74, 1.0, v74
	v_add_f32_e32 v75, 1.0, v75
	v_exp_f32_e32 v70, v70
	v_exp_f32_e32 v71, v71
	v_rcp_f32_e32 v74, v74
	v_rcp_f32_e32 v75, v75
	v_mul_f32_e32 v64, 0xbfb8aa3b, v64
	v_mul_f32_e32 v65, 0xbfb8aa3b, v65
	v_exp_f32_e32 v64, v64
	v_exp_f32_e32 v65, v65
	v_add_f32_e32 v68, 1.0, v68
	v_add_f32_e32 v69, 1.0, v69
	v_mul_f32_e32 v66, 0xbfb8aa3b, v66
	v_mul_f32_e32 v67, 0xbfb8aa3b, v67
	v_rcp_f32_e32 v68, v68
	v_rcp_f32_e32 v69, v69
	v_add_f32_e32 v70, 1.0, v70
	v_add_f32_e32 v71, 1.0, v71
	v_exp_f32_e32 v66, v66
	v_exp_f32_e32 v67, v67
	v_rcp_f32_e32 v70, v70
	v_rcp_f32_e32 v71, v71
	v_add_f32_e32 v64, 1.0, v64
	v_add_f32_e32 v65, 1.0, v65
	s_waitcnt vmcnt(1)
; DI unsigned cvt_pk_bf16(float lo, float hi) { const f32x2_t v = {lo, hi}; return __builtin_bit_cast(unsigned, __builtin_convertvector(v, bf16x2_t)); }
; DI float sig_(float x) { return __builtin_amdgcn_rcpf(1.0f + __builtin_amdgcn_exp2f(-1.4426950408889634f * x)); }
;     DI void operator()(const f32x4 (&acc)[2][2][4][2], const Unit& u, int wr, int wc, int fr, int fq) const {
;     ...
;             for (int m = 0; m < 4; ++m) { const size_t r = (size_t)(row0 + ai * HALF + m * 16);
; #pragma unroll
;                 for (int bj = 0; bj < 2; ++bj) { const size_t o = r * D_ + col0 + bj * HALF; f32x4 p0, p1; unpack8f(*(const u32x4*)(PWB + o), p0, p1);
;                     const f32x4 a0 = acc[ai][bj][m][0], a1 = acc[ai][bj][m][1];
;                     u32x4 w; w.x = cvt_pk_bf16(sig_(a0[0]) * p0[0], sig_(a0[1]) * p0[1]); w.y = cvt_pk_bf16(sig_(a0[2]) * p0[2], sig_(a0[3]) * p0[3]);
;                     w.z = cvt_pk_bf16(sig_(a1[0]) * p1[0], sig_(a1[1]) * p1[1]); w.w = cvt_pk_bf16(sig_(a1[2]) * p1[2], sig_(a1[3]) * p1[3]);
;                     *(u32x4*)(PLEB + o) = w; }
;                 if (m & 1) asm volatile("" ::: "memory"); }
;     }
	v_lshlrev_b32_e32 v108, 16, v96
	v_and_b32_e32 v109, 0xffff0000, v96
	v_lshlrev_b32_e32 v96, 16, v97
	v_and_b32_e32 v97, 0xffff0000, v97
	v_pk_mul_f32 v[88:89], v[88:89], v[108:109]
	v_pk_mul_f32 v[92:93], v[92:93], v[96:97]
	v_cvt_pk_bf16_f32 v88, v88, v89
	v_cvt_pk_bf16_f32 v89, v92, v93
	v_exp_f32_e32 v92, v90
	v_mul_f32_e32 v90, 0xbfb8aa3b, v91
	v_exp_f32_e32 v93, v90
	v_lshlrev_b32_e32 v110, 16, v98
	v_add_f32_e32 v92, 1.0, v92
	v_rcp_f32_e32 v92, v92
	v_add_f32_e32 v93, 1.0, v93
	v_rcp_f32_e32 v93, v93
	v_and_b32_e32 v111, 0xffff0000, v98
	v_pk_mul_f32 v[90:91], v[94:95], v[110:111]
	v_lshlrev_b32_e32 v94, 16, v99
	v_and_b32_e32 v95, 0xffff0000, v99
	v_pk_mul_f32 v[92:93], v[92:93], v[94:95]
	v_cvt_pk_bf16_f32 v90, v90, v91
	v_cvt_pk_bf16_f32 v91, v92, v93
	v_lshl_add_u64 v[92:93], s[12:13], 0, v[104:105]
	global_store_dwordx4 v[92:93], v[88:91], off
	v_rcp_f32_e32 v64, v64
	v_rcp_f32_e32 v65, v65
	s_waitcnt vmcnt(1)
	v_lshlrev_b32_e32 v88, 16, v100
	v_and_b32_e32 v89, 0xffff0000, v100
	v_pk_mul_f32 v[84:85], v[84:85], v[88:89]
	v_lshlrev_b32_e32 v88, 16, v101
	v_and_b32_e32 v89, 0xffff0000, v101
	v_pk_mul_f32 v[86:87], v[86:87], v[88:89]
	v_cvt_pk_bf16_f32 v84, v84, v85
	v_cvt_pk_bf16_f32 v85, v86, v87
	v_lshlrev_b32_e32 v86, 16, v102
	v_and_b32_e32 v87, 0xffff0000, v102
	v_pk_mul_f32 v[80:81], v[80:81], v[86:87]
	v_lshl_add_u64 v[88:89], v[132:133], 0, s[24:25]
	v_cvt_pk_bf16_f32 v86, v80, v81
	v_lshlrev_b32_e32 v80, 16, v103
	v_and_b32_e32 v81, 0xffff0000, v103
	v_pk_mul_f32 v[80:81], v[82:83], v[80:81]
	v_lshl_add_u64 v[90:91], v[132:133], 0, s[26:27]
	v_cvt_pk_bf16_f32 v87, v80, v81
	v_lshl_add_u64 v[80:81], s[12:13], 0, v[106:107]
	global_store_dwordx4 v[80:81], v[84:87], off
	v_lshl_add_u64 v[80:81], s[10:11], 0, v[88:89]
	global_load_dwordx4 v[80:83], v[80:81], off
	v_lshl_add_u64 v[84:85], s[10:11], 0, v[90:91]
	global_load_dwordx4 v[84:87], v[84:85], off
	v_add_f32_e32 v66, 1.0, v66
	v_add_f32_e32 v67, 1.0, v67
	v_rcp_f32_e32 v66, v66
	v_rcp_f32_e32 v67, v67
	v_mul_f32_e32 v60, 0xbfb8aa3b, v60
	v_mul_f32_e32 v61, 0xbfb8aa3b, v61
	v_mul_f32_e32 v62, 0xbfb8aa3b, v62
	v_mul_f32_e32 v63, 0xbfb8aa3b, v63
	v_exp_f32_e32 v60, v60
	v_exp_f32_e32 v61, v61
	v_exp_f32_e32 v62, v62
	v_exp_f32_e32 v63, v63
	v_mul_f32_e32 v56, 0xbfb8aa3b, v56
	v_mul_f32_e32 v57, 0xbfb8aa3b, v57
	v_exp_f32_e32 v56, v56
	v_exp_f32_e32 v57, v57
	v_mul_f32_e32 v58, 0xbfb8aa3b, v58
	v_mul_f32_e32 v59, 0xbfb8aa3b, v59
	v_add_f32_e32 v60, 1.0, v60
	v_add_f32_e32 v61, 1.0, v61
	v_add_f32_e32 v62, 1.0, v62
	v_add_f32_e32 v63, 1.0, v63
	v_exp_f32_e32 v58, v58
	v_exp_f32_e32 v59, v59
	v_rcp_f32_e32 v60, v60
	v_rcp_f32_e32 v61, v61
	v_rcp_f32_e32 v62, v62
	v_rcp_f32_e32 v63, v63
	v_add_f32_e32 v56, 1.0, v56
	v_add_f32_e32 v57, 1.0, v57
	v_mul_f32_e32 v52, 0xbfb8aa3b, v52
	v_mul_f32_e32 v53, 0xbfb8aa3b, v53
	v_rcp_f32_e32 v56, v56
	v_rcp_f32_e32 v57, v57
	v_exp_f32_e32 v52, v52
	v_exp_f32_e32 v53, v53
	v_mul_f32_e32 v54, 0xbfb8aa3b, v54
	v_mul_f32_e32 v55, 0xbfb8aa3b, v55
	v_add_f32_e32 v58, 1.0, v58
	v_add_f32_e32 v59, 1.0, v59
	v_exp_f32_e32 v54, v54
	v_exp_f32_e32 v55, v55
	v_rcp_f32_e32 v58, v58
	v_rcp_f32_e32 v59, v59
	v_mul_f32_e32 v48, 0xbfb8aa3b, v48
	v_mul_f32_e32 v49, 0xbfb8aa3b, v49
	v_exp_f32_e32 v48, v48
	v_exp_f32_e32 v49, v49
	v_add_f32_e32 v52, 1.0, v52
	v_add_f32_e32 v53, 1.0, v53
	v_mul_f32_e32 v50, 0xbfb8aa3b, v50
	v_mul_f32_e32 v51, 0xbfb8aa3b, v51
	v_rcp_f32_e32 v52, v52
	v_rcp_f32_e32 v53, v53
	v_add_f32_e32 v54, 1.0, v54
	v_add_f32_e32 v55, 1.0, v55
	v_exp_f32_e32 v50, v50
	v_exp_f32_e32 v51, v51
	v_rcp_f32_e32 v54, v54
	v_rcp_f32_e32 v55, v55
	v_add_f32_e32 v48, 1.0, v48
	v_add_f32_e32 v49, 1.0, v49
	v_rcp_f32_e32 v48, v48
	v_rcp_f32_e32 v49, v49
	v_add_f32_e32 v50, 1.0, v50
	v_add_f32_e32 v51, 1.0, v51
	v_rcp_f32_e32 v50, v50
	v_rcp_f32_e32 v51, v51
	v_mul_f32_e32 v44, 0xbfb8aa3b, v44
	v_mul_f32_e32 v45, 0xbfb8aa3b, v45
	v_mul_f32_e32 v46, 0xbfb8aa3b, v46
	v_mul_f32_e32 v47, 0xbfb8aa3b, v47
	v_exp_f32_e32 v44, v44
	v_exp_f32_e32 v45, v45
	v_exp_f32_e32 v46, v46
	v_exp_f32_e32 v47, v47
	v_mul_f32_e32 v40, 0xbfb8aa3b, v40
	s_waitcnt vmcnt(1)
	v_lshlrev_b32_e32 v92, 16, v80
	v_and_b32_e32 v93, 0xffff0000, v80
	v_lshlrev_b32_e32 v80, 16, v81
	v_and_b32_e32 v81, 0xffff0000, v81
	v_pk_mul_f32 v[76:77], v[76:77], v[92:93]
	v_pk_mul_f32 v[78:79], v[78:79], v[80:81]
	v_cvt_pk_bf16_f32 v76, v76, v77
	v_cvt_pk_bf16_f32 v77, v78, v79
	v_lshlrev_b32_e32 v78, 16, v82
	v_and_b32_e32 v79, 0xffff0000, v82
	v_pk_mul_f32 v[72:73], v[72:73], v[78:79]
	v_mul_f32_e32 v41, 0xbfb8aa3b, v41
	v_cvt_pk_bf16_f32 v78, v72, v73
	v_lshlrev_b32_e32 v72, 16, v83
	v_and_b32_e32 v73, 0xffff0000, v83
	v_pk_mul_f32 v[72:73], v[74:75], v[72:73]
	v_lshl_add_u64 v[74:75], v[132:133], 0, s[28:29]
	v_cvt_pk_bf16_f32 v79, v72, v73
	v_lshl_add_u64 v[72:73], s[12:13], 0, v[88:89]
	global_store_dwordx4 v[72:73], v[76:79], off
	s_waitcnt vmcnt(1)
; DI unsigned cvt_pk_bf16(float lo, float hi) { const f32x2_t v = {lo, hi}; return __builtin_bit_cast(unsigned, __builtin_convertvector(v, bf16x2_t)); }
; DI float sig_(float x) { return __builtin_amdgcn_rcpf(1.0f + __builtin_amdgcn_exp2f(-1.4426950408889634f * x)); }
;     DI void operator()(const f32x4 (&acc)[2][2][4][2], const Unit& u, int wr, int wc, int fr, int fq) const {
;     ...
;             for (int m = 0; m < 4; ++m) { const size_t r = (size_t)(row0 + ai * HALF + m * 16);
; #pragma unroll
;                 for (int bj = 0; bj < 2; ++bj) { const size_t o = r * D_ + col0 + bj * HALF; f32x4 p0, p1; unpack8f(*(const u32x4*)(PWB + o), p0, p1);
;                     const f32x4 a0 = acc[ai][bj][m][0], a1 = acc[ai][bj][m][1];
;                     u32x4 w; w.x = cvt_pk_bf16(sig_(a0[0]) * p0[0], sig_(a0[1]) * p0[1]); w.y = cvt_pk_bf16(sig_(a0[2]) * p0[2], sig_(a0[3]) * p0[3]);
;                     w.z = cvt_pk_bf16(sig_(a1[0]) * p1[0], sig_(a1[1]) * p1[1]); w.w = cvt_pk_bf16(sig_(a1[2]) * p1[2], sig_(a1[3]) * p1[3]);
;                     *(u32x4*)(PLEB + o) = w; }
;                 if (m & 1) asm volatile("" ::: "memory"); }
;     }
	v_lshlrev_b32_e32 v72, 16, v84
	v_and_b32_e32 v73, 0xffff0000, v84
	v_pk_mul_f32 v[68:69], v[68:69], v[72:73]
	v_lshlrev_b32_e32 v72, 16, v85
	v_and_b32_e32 v73, 0xffff0000, v85
	v_pk_mul_f32 v[70:71], v[70:71], v[72:73]
	v_cvt_pk_bf16_f32 v68, v68, v69
	v_cvt_pk_bf16_f32 v69, v70, v71
	v_lshlrev_b32_e32 v70, 16, v86
	v_and_b32_e32 v71, 0xffff0000, v86
	v_pk_mul_f32 v[64:65], v[64:65], v[70:71]
	v_lshl_add_u64 v[72:73], v[132:133], 0, s[4:5]
	v_cvt_pk_bf16_f32 v70, v64, v65
	v_lshlrev_b32_e32 v64, 16, v87
	v_and_b32_e32 v65, 0xffff0000, v87
	v_pk_mul_f32 v[64:65], v[66:67], v[64:65]
	v_exp_f32_e32 v40, v40
	v_cvt_pk_bf16_f32 v71, v64, v65
	v_lshl_add_u64 v[64:65], s[12:13], 0, v[90:91]
	global_store_dwordx4 v[64:65], v[68:71], off
	v_lshl_add_u64 v[64:65], s[10:11], 0, v[72:73]
	global_load_dwordx4 v[64:67], v[64:65], off
	v_lshl_add_u64 v[68:69], s[10:11], 0, v[74:75]
	global_load_dwordx4 v[68:71], v[68:69], off
	v_exp_f32_e32 v41, v41
	v_mul_f32_e32 v42, 0xbfb8aa3b, v42
	v_mul_f32_e32 v43, 0xbfb8aa3b, v43
	v_add_f32_e32 v44, 1.0, v44
	v_add_f32_e32 v45, 1.0, v45
	v_add_f32_e32 v46, 1.0, v46
	v_add_f32_e32 v47, 1.0, v47
	v_exp_f32_e32 v42, v42
	v_exp_f32_e32 v43, v43
	v_rcp_f32_e32 v44, v44
	v_rcp_f32_e32 v45, v45
	v_rcp_f32_e32 v46, v46
	v_rcp_f32_e32 v47, v47
	v_add_f32_e32 v40, 1.0, v40
	v_add_f32_e32 v41, 1.0, v41
	v_mul_f32_e32 v36, 0xbfb8aa3b, v36
	v_mul_f32_e32 v37, 0xbfb8aa3b, v37
	v_rcp_f32_e32 v40, v40
	v_rcp_f32_e32 v41, v41
	v_exp_f32_e32 v36, v36
	v_exp_f32_e32 v37, v37
	v_mul_f32_e32 v38, 0xbfb8aa3b, v38
	v_mul_f32_e32 v39, 0xbfb8aa3b, v39
	v_add_f32_e32 v42, 1.0, v42
	v_add_f32_e32 v43, 1.0, v43
	v_exp_f32_e32 v38, v38
	v_exp_f32_e32 v39, v39
	v_rcp_f32_e32 v42, v42
	v_rcp_f32_e32 v43, v43
	v_mul_f32_e32 v32, 0xbfb8aa3b, v32
	v_mul_f32_e32 v33, 0xbfb8aa3b, v33
	v_exp_f32_e32 v32, v32
	v_exp_f32_e32 v33, v33
	v_add_f32_e32 v36, 1.0, v36
	v_add_f32_e32 v37, 1.0, v37
	v_mul_f32_e32 v34, 0xbfb8aa3b, v34
	v_mul_f32_e32 v35, 0xbfb8aa3b, v35
	v_rcp_f32_e32 v36, v36
	v_rcp_f32_e32 v37, v37
	v_add_f32_e32 v38, 1.0, v38
	v_add_f32_e32 v39, 1.0, v39
	v_exp_f32_e32 v34, v34
	v_exp_f32_e32 v35, v35
	v_rcp_f32_e32 v38, v38
	v_rcp_f32_e32 v39, v39
	v_add_f32_e32 v32, 1.0, v32
	v_add_f32_e32 v33, 1.0, v33
	v_rcp_f32_e32 v32, v32
	v_rcp_f32_e32 v33, v33
	v_add_f32_e32 v34, 1.0, v34
	v_add_f32_e32 v35, 1.0, v35
	v_rcp_f32_e32 v34, v34
	v_rcp_f32_e32 v35, v35
	v_mul_f32_e32 v28, 0xbfb8aa3b, v28
	v_mul_f32_e32 v29, 0xbfb8aa3b, v29
	v_mul_f32_e32 v30, 0xbfb8aa3b, v30
	v_mul_f32_e32 v31, 0xbfb8aa3b, v31
	v_exp_f32_e32 v28, v28
	v_exp_f32_e32 v29, v29
	v_exp_f32_e32 v30, v30
	v_exp_f32_e32 v31, v31
	v_mul_f32_e32 v24, 0xbfb8aa3b, v24
	v_mul_f32_e32 v25, 0xbfb8aa3b, v25
	v_exp_f32_e32 v24, v24
	v_exp_f32_e32 v25, v25
	v_mul_f32_e32 v26, 0xbfb8aa3b, v26
	v_mul_f32_e32 v27, 0xbfb8aa3b, v27
	v_add_f32_e32 v28, 1.0, v28
	v_add_f32_e32 v29, 1.0, v29
	v_add_f32_e32 v30, 1.0, v30
	v_add_f32_e32 v31, 1.0, v31
	v_exp_f32_e32 v26, v26
	v_exp_f32_e32 v27, v27
	v_rcp_f32_e32 v28, v28
	v_rcp_f32_e32 v29, v29
	v_rcp_f32_e32 v30, v30
	v_rcp_f32_e32 v31, v31
	s_waitcnt vmcnt(1)
	v_lshlrev_b32_e32 v76, 16, v64
	v_and_b32_e32 v77, 0xffff0000, v64
	v_lshlrev_b32_e32 v64, 16, v65
	v_and_b32_e32 v65, 0xffff0000, v65
	v_pk_mul_f32 v[60:61], v[60:61], v[76:77]
	v_pk_mul_f32 v[62:63], v[62:63], v[64:65]
	v_cvt_pk_bf16_f32 v60, v60, v61
	v_cvt_pk_bf16_f32 v61, v62, v63
	v_lshlrev_b32_e32 v62, 16, v66
	v_and_b32_e32 v63, 0xffff0000, v66
	v_pk_mul_f32 v[56:57], v[56:57], v[62:63]
	v_add_f32_e32 v24, 1.0, v24
	v_cvt_pk_bf16_f32 v62, v56, v57
	v_lshlrev_b32_e32 v56, 16, v67
	v_and_b32_e32 v57, 0xffff0000, v67
	v_pk_mul_f32 v[56:57], v[58:59], v[56:57]
	v_lshl_add_u64 v[58:59], v[132:133], 0, s[42:43]
	v_cvt_pk_bf16_f32 v63, v56, v57
	v_lshl_add_u64 v[56:57], s[12:13], 0, v[72:73]
	global_store_dwordx4 v[56:57], v[60:63], off
	s_waitcnt vmcnt(1)
	v_lshlrev_b32_e32 v56, 16, v68
	v_and_b32_e32 v57, 0xffff0000, v68
	v_pk_mul_f32 v[52:53], v[52:53], v[56:57]
	v_lshlrev_b32_e32 v56, 16, v69
	v_and_b32_e32 v57, 0xffff0000, v69
	v_pk_mul_f32 v[54:55], v[54:55], v[56:57]
	v_cvt_pk_bf16_f32 v52, v52, v53
	v_cvt_pk_bf16_f32 v53, v54, v55
	v_lshlrev_b32_e32 v54, 16, v70
	v_and_b32_e32 v55, 0xffff0000, v70
	v_pk_mul_f32 v[48:49], v[48:49], v[54:55]
	v_lshl_add_u64 v[56:57], v[132:133], 0, s[40:41]
	v_cvt_pk_bf16_f32 v54, v48, v49
	v_lshlrev_b32_e32 v48, 16, v71
	v_and_b32_e32 v49, 0xffff0000, v71
	v_pk_mul_f32 v[48:49], v[50:51], v[48:49]
	v_add_f32_e32 v25, 1.0, v25
	v_cvt_pk_bf16_f32 v55, v48, v49
	v_lshl_add_u64 v[48:49], s[12:13], 0, v[74:75]
	global_store_dwordx4 v[48:49], v[52:55], off
	v_lshl_add_u64 v[48:49], s[10:11], 0, v[56:57]
	global_load_dwordx4 v[48:51], v[48:49], off
	v_lshl_add_u64 v[52:53], s[10:11], 0, v[58:59]
	global_load_dwordx4 v[52:55], v[52:53], off
	v_mul_f32_e32 v20, 0xbfb8aa3b, v20
	v_mul_f32_e32 v21, 0xbfb8aa3b, v21
	v_rcp_f32_e32 v24, v24
	v_rcp_f32_e32 v25, v25
	v_exp_f32_e32 v20, v20
	v_exp_f32_e32 v21, v21
	v_mul_f32_e32 v22, 0xbfb8aa3b, v22
	v_mul_f32_e32 v23, 0xbfb8aa3b, v23
	v_add_f32_e32 v26, 1.0, v26
	v_add_f32_e32 v27, 1.0, v27
	v_exp_f32_e32 v22, v22
	v_exp_f32_e32 v23, v23
	v_rcp_f32_e32 v26, v26
	v_rcp_f32_e32 v27, v27
	v_mul_f32_e32 v16, 0xbfb8aa3b, v16
	v_mul_f32_e32 v17, 0xbfb8aa3b, v17
	v_exp_f32_e32 v16, v16
	v_exp_f32_e32 v17, v17
	v_add_f32_e32 v20, 1.0, v20
	v_add_f32_e32 v21, 1.0, v21
	v_mul_f32_e32 v18, 0xbfb8aa3b, v18
	v_mul_f32_e32 v19, 0xbfb8aa3b, v19
	v_rcp_f32_e32 v20, v20
	v_rcp_f32_e32 v21, v21
	v_add_f32_e32 v22, 1.0, v22
	v_add_f32_e32 v23, 1.0, v23
	v_exp_f32_e32 v18, v18
	v_exp_f32_e32 v19, v19
	v_rcp_f32_e32 v22, v22
	v_rcp_f32_e32 v23, v23
	v_add_f32_e32 v16, 1.0, v16
	v_add_f32_e32 v17, 1.0, v17
	v_rcp_f32_e32 v16, v16
	v_rcp_f32_e32 v17, v17
	v_add_f32_e32 v18, 1.0, v18
	v_add_f32_e32 v19, 1.0, v19
	v_rcp_f32_e32 v18, v18
	v_rcp_f32_e32 v19, v19
	v_mul_f32_e32 v12, 0xbfb8aa3b, v12
	v_mul_f32_e32 v13, 0xbfb8aa3b, v13
	v_mul_f32_e32 v14, 0xbfb8aa3b, v14
	v_mul_f32_e32 v15, 0xbfb8aa3b, v15
	v_exp_f32_e32 v12, v12
	v_exp_f32_e32 v13, v13
	v_exp_f32_e32 v14, v14
	v_exp_f32_e32 v15, v15
	v_mul_f32_e32 v8, 0xbfb8aa3b, v8
	v_mul_f32_e32 v9, 0xbfb8aa3b, v9
	v_exp_f32_e32 v8, v8
	v_exp_f32_e32 v9, v9
	v_mul_f32_e32 v10, 0xbfb8aa3b, v10
	v_mul_f32_e32 v11, 0xbfb8aa3b, v11
	v_add_f32_e32 v12, 1.0, v12
	v_add_f32_e32 v13, 1.0, v13
	v_add_f32_e32 v14, 1.0, v14
	v_add_f32_e32 v15, 1.0, v15
	v_exp_f32_e32 v10, v10
	v_exp_f32_e32 v11, v11
	v_rcp_f32_e32 v12, v12
	v_rcp_f32_e32 v13, v13
	v_rcp_f32_e32 v14, v14
	v_rcp_f32_e32 v15, v15
	v_add_f32_e32 v8, 1.0, v8
	v_add_f32_e32 v9, 1.0, v9
	v_mul_f32_e32 v4, 0xbfb8aa3b, v4
	v_mul_f32_e32 v5, 0xbfb8aa3b, v5
	v_rcp_f32_e32 v8, v8
	v_rcp_f32_e32 v9, v9
	v_exp_f32_e32 v4, v4
	v_exp_f32_e32 v5, v5
	v_mul_f32_e32 v6, 0xbfb8aa3b, v6
	v_mul_f32_e32 v7, 0xbfb8aa3b, v7
	v_add_f32_e32 v10, 1.0, v10
	v_add_f32_e32 v11, 1.0, v11
	v_exp_f32_e32 v6, v6
	v_exp_f32_e32 v7, v7
	v_rcp_f32_e32 v10, v10
	s_waitcnt vmcnt(1)
; DI unsigned cvt_pk_bf16(float lo, float hi) { const f32x2_t v = {lo, hi}; return __builtin_bit_cast(unsigned, __builtin_convertvector(v, bf16x2_t)); }
; #define PG8_WAIT_V(n) asm volatile("s_waitcnt vmcnt(" #n ")" ::: "memory")
; #define PG8_BAR __builtin_amdgcn_s_barrier()
;     DI int nt(const Unit& u) const { return (u.aux & 8) ? PLED / 64 : ((u.aux & 4) ? (D_ / 2) / 64 : D_ / 64); }
; DI float sig_(float x) { return __builtin_amdgcn_rcpf(1.0f + __builtin_amdgcn_exp2f(-1.4426950408889634f * x)); }
; template <class Epi, class Sched, bool ALIGN_EPI, bool FP8 = false>
; DI void gemm_phase(LAS unsigned char* lds, const Gemm g, const Sched& S, const Epi& E) {
;     ...
;         if (!has_next) break;
; #pragma unroll
;         for (int a = 0; a < 2; ++a)
; #pragma unroll
;             for (int b = 0; b < 2; ++b)
; #pragma unroll
;                 for (int m = 0; m < 4; ++m)
; #pragma unroll
;                     for (int n = 0; n < 2; ++n) acc[a][b][m][n] = (f32x4){0.f, 0.f, 0.f, 0.f};
;         cur = nxt; cA = nA; cB = nB; ++ui;
;         if constexpr (sched_vark<Sched>::value) nt = S.nt(cur);
;         if constexpr (ALIGN_EPI) { if (wr == 1) PG8_BAR; }
;     }
;     PG8_WAIT_V(0);
;     if constexpr (!ALIGN_EPI) { if (wr == 0) PG8_BAR; }
;     PG8_BAR;
;     DI void operator()(const f32x4 (&acc)[2][2][4][2], const Unit& u, int wr, int wc, int fr, int fq) const {
;     ...
;             for (int m = 0; m < 4; ++m) { const size_t r = (size_t)(row0 + ai * HALF + m * 16);
; #pragma unroll
;                 for (int bj = 0; bj < 2; ++bj) { const size_t o = r * D_ + col0 + bj * HALF; f32x4 p0, p1; unpack8f(*(const u32x4*)(PWB + o), p0, p1);
;                     const f32x4 a0 = acc[ai][bj][m][0], a1 = acc[ai][bj][m][1];
;                     u32x4 w; w.x = cvt_pk_bf16(sig_(a0[0]) * p0[0], sig_(a0[1]) * p0[1]); w.y = cvt_pk_bf16(sig_(a0[2]) * p0[2], sig_(a0[3]) * p0[3]);
;                     w.z = cvt_pk_bf16(sig_(a1[0]) * p1[0], sig_(a1[1]) * p1[1]); w.w = cvt_pk_bf16(sig_(a1[2]) * p1[2], sig_(a1[3]) * p1[3]);
;                     *(u32x4*)(PLEB + o) = w; }
;                 if (m & 1) asm volatile("" ::: "memory"); }
;     }
	v_lshlrev_b32_e32 v60, 16, v48
	v_and_b32_e32 v61, 0xffff0000, v48
	v_lshlrev_b32_e32 v48, 16, v49
	v_and_b32_e32 v49, 0xffff0000, v49
	v_pk_mul_f32 v[44:45], v[44:45], v[60:61]
	v_pk_mul_f32 v[46:47], v[46:47], v[48:49]
	v_cvt_pk_bf16_f32 v44, v44, v45
	v_cvt_pk_bf16_f32 v45, v46, v47
	v_lshlrev_b32_e32 v46, 16, v50
	v_and_b32_e32 v47, 0xffff0000, v50
	v_pk_mul_f32 v[40:41], v[40:41], v[46:47]
	v_rcp_f32_e32 v11, v11
	v_cvt_pk_bf16_f32 v46, v40, v41
	v_lshlrev_b32_e32 v40, 16, v51
	v_and_b32_e32 v41, 0xffff0000, v51
	v_pk_mul_f32 v[40:41], v[42:43], v[40:41]
	v_lshl_add_u64 v[42:43], v[132:133], 0, s[46:47]
	v_cvt_pk_bf16_f32 v47, v40, v41
	v_lshl_add_u64 v[40:41], s[12:13], 0, v[56:57]
	global_store_dwordx4 v[40:41], v[44:47], off
	s_waitcnt vmcnt(1)
	v_lshlrev_b32_e32 v40, 16, v52
	v_and_b32_e32 v41, 0xffff0000, v52
	v_pk_mul_f32 v[36:37], v[36:37], v[40:41]
	v_lshlrev_b32_e32 v40, 16, v53
	v_and_b32_e32 v41, 0xffff0000, v53
	v_pk_mul_f32 v[38:39], v[38:39], v[40:41]
	v_cvt_pk_bf16_f32 v36, v36, v37
	v_cvt_pk_bf16_f32 v37, v38, v39
	v_lshlrev_b32_e32 v38, 16, v54
	v_and_b32_e32 v39, 0xffff0000, v54
	v_pk_mul_f32 v[32:33], v[32:33], v[38:39]
	v_lshl_add_u64 v[40:41], v[132:133], 0, s[44:45]
	v_cvt_pk_bf16_f32 v38, v32, v33
	v_lshlrev_b32_e32 v32, 16, v55
	v_and_b32_e32 v33, 0xffff0000, v55
	v_pk_mul_f32 v[32:33], v[34:35], v[32:33]
	v_mul_f32_e32 v0, 0xbfb8aa3b, v0
	v_cvt_pk_bf16_f32 v39, v32, v33
	v_lshl_add_u64 v[32:33], s[12:13], 0, v[58:59]
	global_store_dwordx4 v[32:33], v[36:39], off
	v_lshl_add_u64 v[32:33], s[10:11], 0, v[40:41]
	global_load_dwordx4 v[32:35], v[32:33], off
	v_lshl_add_u64 v[36:37], s[10:11], 0, v[42:43]
	global_load_dwordx4 v[36:39], v[36:37], off
	v_mul_f32_e32 v1, 0xbfb8aa3b, v1
	v_exp_f32_e32 v0, v0
	v_exp_f32_e32 v1, v1
	v_add_f32_e32 v4, 1.0, v4
	v_add_f32_e32 v5, 1.0, v5
	v_mul_f32_e32 v2, 0xbfb8aa3b, v2
	v_mul_f32_e32 v3, 0xbfb8aa3b, v3
	v_rcp_f32_e32 v4, v4
	v_rcp_f32_e32 v5, v5
	v_add_f32_e32 v6, 1.0, v6
	v_add_f32_e32 v7, 1.0, v7
	v_exp_f32_e32 v2, v2
	v_exp_f32_e32 v3, v3
	v_rcp_f32_e32 v6, v6
	v_rcp_f32_e32 v7, v7
	v_add_f32_e32 v0, 1.0, v0
	v_add_f32_e32 v1, 1.0, v1
	v_rcp_f32_e32 v0, v0
	v_rcp_f32_e32 v1, v1
	v_add_f32_e32 v2, 1.0, v2
	v_add_f32_e32 v3, 1.0, v3
	v_rcp_f32_e32 v2, v2
	v_rcp_f32_e32 v3, v3
	s_andn2_b64 vcc, exec, s[2:3]
	s_mov_b64 s[2:3], -1
	s_waitcnt vmcnt(1)
	v_lshlrev_b32_e32 v44, 16, v32
	v_and_b32_e32 v45, 0xffff0000, v32
	v_lshlrev_b32_e32 v32, 16, v33
	v_and_b32_e32 v33, 0xffff0000, v33
	v_pk_mul_f32 v[28:29], v[28:29], v[44:45]
	v_pk_mul_f32 v[30:31], v[30:31], v[32:33]
	v_cvt_pk_bf16_f32 v28, v28, v29
	v_cvt_pk_bf16_f32 v29, v30, v31
	v_lshlrev_b32_e32 v30, 16, v34
	v_and_b32_e32 v31, 0xffff0000, v34
	v_pk_mul_f32 v[24:25], v[24:25], v[30:31]
	s_nop 0
	v_cvt_pk_bf16_f32 v30, v24, v25
	v_lshlrev_b32_e32 v24, 16, v35
	v_and_b32_e32 v25, 0xffff0000, v35
	v_pk_mul_f32 v[24:25], v[26:27], v[24:25]
	v_lshl_add_u64 v[26:27], v[132:133], 0, s[50:51]
	v_cvt_pk_bf16_f32 v31, v24, v25
	v_lshl_add_u64 v[24:25], s[12:13], 0, v[40:41]
	global_store_dwordx4 v[24:25], v[28:31], off
	s_waitcnt vmcnt(1)
	v_lshlrev_b32_e32 v24, 16, v36
	v_and_b32_e32 v25, 0xffff0000, v36
	v_pk_mul_f32 v[20:21], v[20:21], v[24:25]
	v_lshlrev_b32_e32 v24, 16, v37
	v_and_b32_e32 v25, 0xffff0000, v37
	v_pk_mul_f32 v[22:23], v[22:23], v[24:25]
	v_cvt_pk_bf16_f32 v20, v20, v21
	v_cvt_pk_bf16_f32 v21, v22, v23
	v_lshlrev_b32_e32 v22, 16, v38
	v_and_b32_e32 v23, 0xffff0000, v38
	v_pk_mul_f32 v[16:17], v[16:17], v[22:23]
	v_lshl_add_u64 v[24:25], v[132:133], 0, s[48:49]
	v_cvt_pk_bf16_f32 v22, v16, v17
	v_lshlrev_b32_e32 v16, 16, v39
	v_and_b32_e32 v17, 0xffff0000, v39
	v_pk_mul_f32 v[16:17], v[18:19], v[16:17]
	s_nop 0
	v_cvt_pk_bf16_f32 v23, v16, v17
	v_lshl_add_u64 v[16:17], s[12:13], 0, v[42:43]
	global_store_dwordx4 v[16:17], v[20:23], off
	v_lshl_add_u64 v[16:17], s[10:11], 0, v[24:25]
	global_load_dwordx4 v[16:19], v[16:17], off
	v_lshl_add_u64 v[20:21], s[10:11], 0, v[26:27]
	global_load_dwordx4 v[20:23], v[20:21], off
	s_waitcnt vmcnt(1)
	v_lshlrev_b32_e32 v28, 16, v16
	v_and_b32_e32 v29, 0xffff0000, v16
	v_lshlrev_b32_e32 v16, 16, v17
	v_and_b32_e32 v17, 0xffff0000, v17
	v_pk_mul_f32 v[12:13], v[12:13], v[28:29]
	v_pk_mul_f32 v[14:15], v[14:15], v[16:17]
	v_cvt_pk_bf16_f32 v12, v12, v13
	v_cvt_pk_bf16_f32 v13, v14, v15
	v_lshlrev_b32_e32 v14, 16, v18
	v_and_b32_e32 v15, 0xffff0000, v18
	v_pk_mul_f32 v[8:9], v[8:9], v[14:15]
	s_nop 0
	v_cvt_pk_bf16_f32 v14, v8, v9
	v_lshlrev_b32_e32 v8, 16, v19
	v_and_b32_e32 v9, 0xffff0000, v19
	v_pk_mul_f32 v[8:9], v[10:11], v[8:9]
	s_nop 0
	v_cvt_pk_bf16_f32 v15, v8, v9
	v_lshl_add_u64 v[8:9], s[12:13], 0, v[24:25]
	global_store_dwordx4 v[8:9], v[12:15], off
	s_waitcnt vmcnt(1)
	v_lshlrev_b32_e32 v8, 16, v20
	v_and_b32_e32 v9, 0xffff0000, v20
	v_pk_mul_f32 v[4:5], v[4:5], v[8:9]
	v_lshlrev_b32_e32 v8, 16, v21
	v_and_b32_e32 v9, 0xffff0000, v21
	v_pk_mul_f32 v[6:7], v[6:7], v[8:9]
	v_cvt_pk_bf16_f32 v4, v4, v5
	v_cvt_pk_bf16_f32 v5, v6, v7
	v_lshlrev_b32_e32 v6, 16, v22
	v_and_b32_e32 v7, 0xffff0000, v22
	v_pk_mul_f32 v[0:1], v[0:1], v[6:7]
	s_nop 0
	v_cvt_pk_bf16_f32 v6, v0, v1
	v_lshlrev_b32_e32 v0, 16, v23
	v_and_b32_e32 v1, 0xffff0000, v23
	v_pk_mul_f32 v[0:1], v[2:3], v[0:1]
	s_nop 0
	v_cvt_pk_bf16_f32 v7, v0, v1
	v_lshl_add_u64 v[0:1], s[12:13], 0, v[26:27]
	global_store_dwordx4 v[0:1], v[4:7], off
	s_cbranch_vccnz .LBB0_1702
	s_andn2_b64 vcc, exec, s[6:7]
	s_cbranch_vccnz .LBB0_1701
	s_barrier
	s_branch .LBB0_1701

; #define LAS __attribute__((address_space(3)))
; __global__ void __launch_bounds__(512, 2) mk_fwd(FArgs args) {
;     extern __shared__ __attribute__((aligned(16))) unsigned char lds_raw[];
;     LAS unsigned char* lds = (LAS unsigned char*)lds_raw;
	.amdhsa_kernel _Z6mk_fwd5FArgs
		.amdhsa_group_segment_fixed_size 0
		.amdhsa_private_segment_fixed_size 0
		.amdhsa_kernarg_size 456
		.amdhsa_user_sgpr_count 2
		.amdhsa_user_sgpr_dispatch_ptr 0
		.amdhsa_user_sgpr_queue_ptr 0
		.amdhsa_user_sgpr_kernarg_segment_ptr 1
		.amdhsa_user_sgpr_dispatch_id 0
		.amdhsa_user_sgpr_kernarg_preload_length 0
		.amdhsa_user_sgpr_kernarg_preload_offset 0
		.amdhsa_user_sgpr_private_segment_size 0
		.amdhsa_uses_dynamic_stack 0
		.amdhsa_enable_private_segment 0
		.amdhsa_system_sgpr_workgroup_id_x 1
		.amdhsa_system_sgpr_workgroup_id_y 0
		.amdhsa_system_sgpr_workgroup_id_z 0
		.amdhsa_system_sgpr_workgroup_info 0
		.amdhsa_system_vgpr_workitem_id 0
		.amdhsa_next_free_vgpr 256
		.amdhsa_next_free_sgpr 102
		.amdhsa_accum_offset 256
		.amdhsa_reserve_vcc 1
		.amdhsa_float_round_mode_32 0
		.amdhsa_float_round_mode_16_64 0
		.amdhsa_float_denorm_mode_32 3
		.amdhsa_float_denorm_mode_16_64 3
		.amdhsa_dx10_clamp 1
		.amdhsa_ieee_mode 1
		.amdhsa_fp16_overflow 0
		.amdhsa_tg_split 0
		.amdhsa_exception_fp_ieee_invalid_op 0
		.amdhsa_exception_fp_denorm_src 0
		.amdhsa_exception_fp_ieee_div_zero 0
		.amdhsa_exception_fp_ieee_overflow 0
		.amdhsa_exception_fp_ieee_underflow 0
		.amdhsa_exception_fp_ieee_inexact 0
		.amdhsa_exception_int_div_zero 0
	.end_amdhsa_kernel

; #define LAS __attribute__((address_space(3)))
; __global__ void __launch_bounds__(512, 2) mk_fwd(FArgs args) {
;     extern __shared__ __attribute__((aligned(16))) unsigned char lds_raw[];
;     LAS unsigned char* lds = (LAS unsigned char*)lds_raw;
amdhsa.kernels:
  - .agpr_count:     0
    .args:
      - .offset:         0
        .size:           200
        .value_kind:     by_value
      - .offset:         200
        .size:           4
        .value_kind:     hidden_block_count_x
      - .offset:         204
        .size:           4
        .value_kind:     hidden_block_count_y
      - .offset:         208
        .size:           4
        .value_kind:     hidden_block_count_z
      - .offset:         212
        .size:           2
        .value_kind:     hidden_group_size_x
      - .offset:         214
        .size:           2
        .value_kind:     hidden_group_size_y
      - .offset:         216
        .size:           2
        .value_kind:     hidden_group_size_z
      - .offset:         218
        .size:           2
        .value_kind:     hidden_remainder_x
      - .offset:         220
        .size:           2
        .value_kind:     hidden_remainder_y
      - .offset:         222
        .size:           2
        .value_kind:     hidden_remainder_z
      - .offset:         240
        .size:           8
        .value_kind:     hidden_global_offset_x
      - .offset:         248
        .size:           8
        .value_kind:     hidden_global_offset_y
      - .offset:         256
        .size:           8
        .value_kind:     hidden_global_offset_z
      - .offset:         264
        .size:           2
        .value_kind:     hidden_grid_dims
      - .offset:         320
        .size:           4
        .value_kind:     hidden_dynamic_lds_size
    .group_segment_fixed_size: 0
    .kernarg_segment_align: 8
    .kernarg_segment_size: 456
    .language:       OpenCL C
    .language_version:
      - 2
      - 0
    .max_flat_workgroup_size: 512
    .name:           _Z6mk_fwd5FArgs
    .private_segment_fixed_size: 0
    .sgpr_count:     108
    .sgpr_spill_count: 6
    .symbol:         _Z6mk_fwd5FArgs.kd
    .uniform_work_group_size: 1
    .uses_dynamic_stack: false
    .vgpr_count:     256
    .vgpr_spill_count: 0
    .wavefront_size: 64
